# expert-weight conversion loops: transpose of item A no longer waits for item B's just-issued loads (counted vmcnt per path)
# baseline (speedup 1.0000x reference)
; #define GAS __attribute__((address_space(1)))
; #define LAS __attribute__((address_space(3)))
; #define LDS_WAIT() asm volatile("s_waitcnt lgkmcnt(0)" ::: "memory")
; __device__ __forceinline__ void p8_issue(const TItem8& t, f32x4 (&v)[16], int lane) {
;     const GAS f32x4* src = (const GAS f32x4*)((const GAS float*)t.src + (size_t)(lane >> 3) * t.N + 4 * (lane & 7));
; #pragma unroll
;     for (int i = 0; i < 16; ++i) v[i] = __builtin_nontemporal_load(src + (size_t)(2 * i) * t.N);
; }
; __device__ __forceinline__ void p8_finish(const TItem8& t, const f32x4 (&v)[16], LAS float* scr, int lane) {
; #pragma unroll
;     for (int i = 0; i < 16; ++i) *(LAS f32x4*)(scr + (8 * i + (lane >> 3)) * 32 + (((lane & 7) ^ (i & 7)) << 2)) = v[i] * W8_SCALE;
;     LDS_WAIT(); asm volatile("" ::: "memory");
; __device__ __forceinline__ void p8_convert(Frame& F, const Args& args, int lo, int hi, int gw, int NGW, int nlight) {
;     ...
;         for (;;) {
;             int nx = item_of(++idx); bool has = nx < hi;
;             if (has) { cb = p8_decode(args, ws, nx); p8_issue(cb, vb, F.lane); }
;             p8_finish(ca, va, scr, F.lane);
.LBB0_324:
	s_lshl_b64 s[10:11], s[14:15], 11
	s_add_u32 s4, s54, s10
	v_mul_u32_u24_e32 v66, s56, v1
	s_addc_u32 s11, s55, s11
	v_lshlrev_b32_e32 v140, 2, v66
	s_add_u32 s10, s4, s18
	v_lshl_add_u64 v[66:67], s[16:17], 0, v[140:141]
	v_mov_b32_e32 v143, v141
	s_addc_u32 s11, s11, s19
	v_lshl_add_u64 v[66:67], v[66:67], 0, v[142:143]
	s_lshl_b32 s4, s56, 5
	v_lshl_add_u64 v[74:75], v[66:67], 0, s[4:5]
	global_load_dwordx4 v[66:69], v[66:67], off nt
	s_nop 0
	global_load_dwordx4 v[70:73], v[74:75], off nt
	v_lshl_add_u64 v[74:75], v[74:75], 0, s[4:5]
	v_lshl_add_u64 v[82:83], v[74:75], 0, s[4:5]
	global_load_dwordx4 v[74:77], v[74:75], off nt
	s_nop 0
	global_load_dwordx4 v[78:81], v[82:83], off nt
	v_lshl_add_u64 v[82:83], v[82:83], 0, s[4:5]
	v_lshl_add_u64 v[90:91], v[82:83], 0, s[4:5]
	global_load_dwordx4 v[82:85], v[82:83], off nt
	s_nop 0
	global_load_dwordx4 v[86:89], v[90:91], off nt
	v_lshl_add_u64 v[90:91], v[90:91], 0, s[4:5]
	v_lshl_add_u64 v[98:99], v[90:91], 0, s[4:5]
	v_lshl_add_u64 v[102:103], v[98:99], 0, s[4:5]
	v_lshl_add_u64 v[106:107], v[102:103], 0, s[4:5]
	v_lshl_add_u64 v[110:111], v[106:107], 0, s[4:5]
	v_lshl_add_u64 v[114:115], v[110:111], 0, s[4:5]
	v_lshl_add_u64 v[118:119], v[114:115], 0, s[4:5]
	v_lshl_add_u64 v[122:123], v[118:119], 0, s[4:5]
	v_lshl_add_u64 v[126:127], v[122:123], 0, s[4:5]
	global_load_dwordx4 v[90:93], v[90:91], off nt
	s_nop 0
	global_load_dwordx4 v[94:97], v[98:99], off nt
	s_nop 0
	global_load_dwordx4 v[98:101], v[102:103], off nt
	s_nop 0
	global_load_dwordx4 v[102:105], v[106:107], off nt
	s_nop 0
	global_load_dwordx4 v[106:109], v[110:111], off nt
	s_nop 0
	global_load_dwordx4 v[110:113], v[114:115], off nt
	s_nop 0
	global_load_dwordx4 v[114:117], v[118:119], off nt
	s_nop 0
	global_load_dwordx4 v[118:121], v[122:123], off nt
	s_nop 0
	global_load_dwordx4 v[122:125], v[126:127], off nt
	v_lshl_add_u64 v[126:127], v[126:127], 0, s[4:5]
	global_load_dwordx4 v[126:129], v[126:127], off nt
	s_waitcnt vmcnt(31)
	v_pk_mul_f32 v[194:195], v[4:5], s[6:7] op_sel_hi:[1,0]
	v_pk_mul_f32 v[192:193], v[2:3], s[6:7] op_sel_hi:[1,0]
	ds_write_b128 v146, v[192:195]
	s_waitcnt vmcnt(30)
	v_pk_mul_f32 v[194:195], v[8:9], s[6:7] op_sel_hi:[1,0]
	v_pk_mul_f32 v[192:193], v[6:7], s[6:7] op_sel_hi:[1,0]
	ds_write_b128 v147, v[192:195] offset:1024
	s_waitcnt vmcnt(29)
	v_pk_mul_f32 v[194:195], v[12:13], s[6:7] op_sel_hi:[1,0]
	v_pk_mul_f32 v[192:193], v[10:11], s[6:7] op_sel_hi:[1,0]
	ds_write_b128 v148, v[192:195] offset:2048
	s_waitcnt vmcnt(28)
	v_pk_mul_f32 v[194:195], v[16:17], s[6:7] op_sel_hi:[1,0]
	v_pk_mul_f32 v[192:193], v[14:15], s[6:7] op_sel_hi:[1,0]
	ds_write_b128 v149, v[192:195] offset:3072
	s_waitcnt vmcnt(27)
	v_pk_mul_f32 v[194:195], v[20:21], s[6:7] op_sel_hi:[1,0]
	v_pk_mul_f32 v[192:193], v[18:19], s[6:7] op_sel_hi:[1,0]
	ds_write_b128 v150, v[192:195] offset:4096
	s_waitcnt vmcnt(26)
	v_pk_mul_f32 v[194:195], v[24:25], s[6:7] op_sel_hi:[1,0]
	v_pk_mul_f32 v[192:193], v[22:23], s[6:7] op_sel_hi:[1,0]
	ds_write_b128 v151, v[192:195] offset:5120
	s_waitcnt vmcnt(25)
	v_pk_mul_f32 v[194:195], v[28:29], s[6:7] op_sel_hi:[1,0]
	v_pk_mul_f32 v[192:193], v[26:27], s[6:7] op_sel_hi:[1,0]
	ds_write_b128 v152, v[192:195] offset:6144
	s_waitcnt vmcnt(24)
	v_pk_mul_f32 v[194:195], v[32:33], s[6:7] op_sel_hi:[1,0]
	v_pk_mul_f32 v[192:193], v[30:31], s[6:7] op_sel_hi:[1,0]
	ds_write_b128 v153, v[192:195] offset:7168
	s_waitcnt vmcnt(23)
	v_pk_mul_f32 v[194:195], v[36:37], s[6:7] op_sel_hi:[1,0]
	v_pk_mul_f32 v[192:193], v[34:35], s[6:7] op_sel_hi:[1,0]
	ds_write_b128 v146, v[192:195] offset:8192
	s_waitcnt vmcnt(22)
	v_pk_mul_f32 v[194:195], v[40:41], s[6:7] op_sel_hi:[1,0]
	v_pk_mul_f32 v[192:193], v[38:39], s[6:7] op_sel_hi:[1,0]
	ds_write_b128 v147, v[192:195] offset:9216
	s_waitcnt vmcnt(21)
	v_pk_mul_f32 v[194:195], v[44:45], s[6:7] op_sel_hi:[1,0]
	v_pk_mul_f32 v[192:193], v[42:43], s[6:7] op_sel_hi:[1,0]
	ds_write_b128 v148, v[192:195] offset:10240
	s_waitcnt vmcnt(20)
	v_pk_mul_f32 v[194:195], v[48:49], s[6:7] op_sel_hi:[1,0]
	v_pk_mul_f32 v[192:193], v[46:47], s[6:7] op_sel_hi:[1,0]
	ds_write_b128 v149, v[192:195] offset:11264
	s_waitcnt vmcnt(19)
	v_pk_mul_f32 v[194:195], v[52:53], s[6:7] op_sel_hi:[1,0]
	v_pk_mul_f32 v[192:193], v[50:51], s[6:7] op_sel_hi:[1,0]
	ds_write_b128 v150, v[192:195] offset:12288
	s_waitcnt vmcnt(18)
	v_pk_mul_f32 v[194:195], v[56:57], s[6:7] op_sel_hi:[1,0]
	v_pk_mul_f32 v[192:193], v[54:55], s[6:7] op_sel_hi:[1,0]
	ds_write_b128 v151, v[192:195] offset:13312
	s_waitcnt vmcnt(17)
	v_pk_mul_f32 v[194:195], v[60:61], s[6:7] op_sel_hi:[1,0]
	v_pk_mul_f32 v[192:193], v[58:59], s[6:7] op_sel_hi:[1,0]
	ds_write_b128 v152, v[192:195] offset:14336
	s_waitcnt vmcnt(16)
	v_pk_mul_f32 v[194:195], v[64:65], s[6:7] op_sel_hi:[1,0]
	v_pk_mul_f32 v[192:193], v[62:63], s[6:7] op_sel_hi:[1,0]
	ds_write_b128 v153, v[192:195] offset:15360
	s_branch .Lcv1_11_325

; #define GAS __attribute__((address_space(1)))
; __device__ __forceinline__ void p8_finish(const TItem8& t, const f32x4 (&v)[16], LAS float* scr, int lane) {
;     ...
;     const int c = lane & 7;
; #pragma unroll
;     for (int j = 0; j < 4; ++j) { const int n = (lane >> 3) + 8 * j; float x[16];
; #pragma unroll
;         for (int i = 0; i < 16; ++i) { const int k = 16 * c + i; x[i] = scr[k * 32 + ((((n >> 2) ^ ((k >> 3) & 7)) << 2) | (n & 3))]; }
;         int w[4];
; #pragma unroll
;         for (int g = 0; g < 4; ++g) { int q = 0; q = __builtin_amdgcn_cvt_pk_fp8_f32(fminf(fmaxf(x[4 * g], -448.f), 448.f), fminf(fmaxf(x[4 * g + 1], -448.f), 448.f), q, false);
;             q = __builtin_amdgcn_cvt_pk_fp8_f32(fminf(fmaxf(x[4 * g + 2], -448.f), 448.f), fminf(fmaxf(x[4 * g + 3], -448.f), 448.f), q, true); w[g] = q; }
;         v4u o; o.x = (unsigned)w[0]; o.y = (unsigned)w[1]; o.z = (unsigned)w[2]; o.w = (unsigned)w[3];
;         __builtin_nontemporal_store(o, (GAS v4u*)(t.dst + (size_t)n * t.Kd + 16 * c)); }
.Lcv1_11_325:
	s_waitcnt lgkmcnt(0)
	ds_read2_b32 v[192:193], v154 offset1:32
	ds_read2_b32 v[194:195], v154 offset0:64 offset1:96
	ds_read2_b32 v[196:197], v154 offset0:128 offset1:160
	ds_read2_b32 v[198:199], v154 offset0:192 offset1:224
	ds_read_b32 v140, v155
	ds_read_b32 v143, v156
	ds_read_b32 v200, v157
	ds_read_b32 v201, v158
	ds_read_b32 v202, v159
	ds_read_b32 v203, v160
	ds_read_b32 v204, v161
	ds_read_b32 v205, v162
	s_waitcnt lgkmcnt(11)
	v_max_f32_e32 v192, v192, v192
	v_med3_f32 v206, v192, s7, v191
	v_max_f32_e32 v192, v193, v193
	v_med3_f32 v193, v192, s7, v191
	v_mov_b32_e32 v192, 0
	v_cvt_pk_fp8_f32 v192, v206, v193
	s_waitcnt lgkmcnt(10)
	v_max_f32_e32 v193, v194, v194
	v_max_f32_e32 v194, v195, v195
	v_med3_f32 v193, v193, s7, v191
	v_med3_f32 v194, v194, s7, v191
	v_cvt_pk_fp8_f32 v192, v193, v194 op_sel:[0,0,1]
	s_waitcnt lgkmcnt(9)
	v_max_f32_e32 v193, v196, v196
	v_med3_f32 v194, v193, s7, v191
	v_max_f32_e32 v193, v197, v197
	v_med3_f32 v195, v193, s7, v191
	v_mov_b32_e32 v193, 0
	v_cvt_pk_fp8_f32 v193, v194, v195
	s_waitcnt lgkmcnt(8)
	v_max_f32_e32 v194, v198, v198
	v_max_f32_e32 v195, v199, v199
	v_med3_f32 v194, v194, s7, v191
	v_med3_f32 v195, v195, s7, v191
	s_waitcnt lgkmcnt(7)
	v_max_f32_e32 v140, v140, v140
	s_waitcnt lgkmcnt(6)
	v_max_f32_e32 v143, v143, v143
	v_cvt_pk_fp8_f32 v193, v194, v195 op_sel:[0,0,1]
	v_med3_f32 v140, v140, s7, v191
	v_med3_f32 v143, v143, s7, v191
	v_mov_b32_e32 v194, 0
	v_cvt_pk_fp8_f32 v194, v140, v143
	s_waitcnt lgkmcnt(5)
	v_max_f32_e32 v140, v200, v200
	s_waitcnt lgkmcnt(4)
	v_max_f32_e32 v143, v201, v201
	v_med3_f32 v140, v140, s7, v191
	v_med3_f32 v143, v143, s7, v191
	v_cvt_pk_fp8_f32 v194, v140, v143 op_sel:[0,0,1]
	s_waitcnt lgkmcnt(3)
	v_max_f32_e32 v140, v202, v202
	s_waitcnt lgkmcnt(2)
	v_max_f32_e32 v143, v203, v203
	v_med3_f32 v140, v140, s7, v191
	v_med3_f32 v143, v143, s7, v191
	v_mov_b32_e32 v195, 0
	v_cvt_pk_fp8_f32 v195, v140, v143
	s_waitcnt lgkmcnt(1)
	v_max_f32_e32 v140, v204, v204
	s_waitcnt lgkmcnt(0)
	v_max_f32_e32 v143, v205, v205
	v_med3_f32 v140, v140, s7, v191
	v_med3_f32 v143, v143, s7, v191
	v_cvt_pk_fp8_f32 v195, v140, v143 op_sel:[0,0,1]
	ds_read2_b32 v[196:197], v163 offset1:32
	ds_read2_b32 v[198:199], v163 offset0:64 offset1:96
	ds_read2_b32 v[200:201], v163 offset0:128 offset1:160
	ds_read2_b32 v[202:203], v163 offset0:192 offset1:224
	ds_read_b32 v140, v164
	ds_read_b32 v143, v165
	ds_read_b32 v204, v166
	ds_read_b32 v205, v167
	ds_read_b32 v206, v168
	ds_read_b32 v207, v169
	ds_read_b32 v208, v170
	ds_read_b32 v209, v171
	s_waitcnt lgkmcnt(11)
	v_max_f32_e32 v196, v196, v196
	v_med3_f32 v210, v196, s7, v191
	v_max_f32_e32 v196, v197, v197
	v_med3_f32 v197, v196, s7, v191
	v_mov_b32_e32 v196, 0
	v_cvt_pk_fp8_f32 v196, v210, v197
	s_waitcnt lgkmcnt(10)
	v_max_f32_e32 v197, v198, v198
	v_max_f32_e32 v198, v199, v199
	v_med3_f32 v197, v197, s7, v191
	v_med3_f32 v198, v198, s7, v191
	v_cvt_pk_fp8_f32 v196, v197, v198 op_sel:[0,0,1]
	s_waitcnt lgkmcnt(9)
	v_max_f32_e32 v197, v200, v200
	v_med3_f32 v198, v197, s7, v191
	v_max_f32_e32 v197, v201, v201
	v_med3_f32 v199, v197, s7, v191
	v_mov_b32_e32 v197, 0
	v_cvt_pk_fp8_f32 v197, v198, v199
	s_waitcnt lgkmcnt(8)
	v_max_f32_e32 v198, v202, v202
	v_max_f32_e32 v199, v203, v203
	v_med3_f32 v198, v198, s7, v191
	v_med3_f32 v199, v199, s7, v191
	s_waitcnt lgkmcnt(7)
	v_max_f32_e32 v140, v140, v140
	s_waitcnt lgkmcnt(6)
	v_max_f32_e32 v143, v143, v143
	v_cvt_pk_fp8_f32 v197, v198, v199 op_sel:[0,0,1]
	v_med3_f32 v140, v140, s7, v191
	v_med3_f32 v143, v143, s7, v191
	v_mov_b32_e32 v198, 0
	v_cvt_pk_fp8_f32 v198, v140, v143
	s_waitcnt lgkmcnt(5)
	v_max_f32_e32 v140, v204, v204
	s_waitcnt lgkmcnt(4)
	v_max_f32_e32 v143, v205, v205
	v_med3_f32 v140, v140, s7, v191
	v_med3_f32 v143, v143, s7, v191
	v_cvt_pk_fp8_f32 v198, v140, v143 op_sel:[0,0,1]
	s_waitcnt lgkmcnt(3)
	v_max_f32_e32 v140, v206, v206
	s_waitcnt lgkmcnt(2)
	v_max_f32_e32 v143, v207, v207
	v_med3_f32 v140, v140, s7, v191
	v_med3_f32 v143, v143, s7, v191
	v_mov_b32_e32 v199, 0
	v_cvt_pk_fp8_f32 v199, v140, v143
	s_waitcnt lgkmcnt(1)
	v_max_f32_e32 v140, v208, v208
	s_waitcnt lgkmcnt(0)
	v_max_f32_e32 v143, v209, v209
	v_med3_f32 v140, v140, s7, v191
	v_med3_f32 v143, v143, s7, v191
	v_cvt_pk_fp8_f32 v199, v140, v143 op_sel:[0,0,1]
	v_lshl_add_u64 v[144:145], s[8:9], 0, v[130:131]
	v_lshl_add_u64 v[200:201], v[144:145], 0, v[132:133]
	global_store_dwordx4 v[200:201], v[192:195], off nt
	s_andn2_b64 vcc, exec, s[12:13]
	s_mov_b64 s[12:13], 0
	v_lshl_add_u64 v[192:193], v[144:145], 0, v[134:135]
	global_store_dwordx4 v[192:193], v[196:199], off nt
	ds_read2_b32 v[192:193], v172 offset1:32
	ds_read2_b32 v[194:195], v172 offset0:64 offset1:96
	ds_read2_b32 v[196:197], v172 offset0:128 offset1:160
	ds_read2_b32 v[198:199], v172 offset0:192 offset1:224
	ds_read_b32 v140, v173
	ds_read_b32 v143, v174
	ds_read_b32 v200, v175
	ds_read_b32 v201, v176
	ds_read_b32 v202, v177
	ds_read_b32 v203, v178
	ds_read_b32 v204, v179
	ds_read_b32 v205, v180
	s_waitcnt lgkmcnt(11)
; #define GAS __attribute__((address_space(1)))
; #define LDS_WAIT() asm volatile("s_waitcnt lgkmcnt(0)" ::: "memory")
; __device__ __forceinline__ void p8_finish(const TItem8& t, const f32x4 (&v)[16], LAS float* scr, int lane) {
;     ...
;     const int c = lane & 7;
; #pragma unroll
;     for (int j = 0; j < 4; ++j) { const int n = (lane >> 3) + 8 * j; float x[16];
; #pragma unroll
;         for (int i = 0; i < 16; ++i) { const int k = 16 * c + i; x[i] = scr[k * 32 + ((((n >> 2) ^ ((k >> 3) & 7)) << 2) | (n & 3))]; }
;         int w[4];
; #pragma unroll
;         for (int g = 0; g < 4; ++g) { int q = 0; q = __builtin_amdgcn_cvt_pk_fp8_f32(fminf(fmaxf(x[4 * g], -448.f), 448.f), fminf(fmaxf(x[4 * g + 1], -448.f), 448.f), q, false);
;             q = __builtin_amdgcn_cvt_pk_fp8_f32(fminf(fmaxf(x[4 * g + 2], -448.f), 448.f), fminf(fmaxf(x[4 * g + 3], -448.f), 448.f), q, true); w[g] = q; }
;         v4u o; o.x = (unsigned)w[0]; o.y = (unsigned)w[1]; o.z = (unsigned)w[2]; o.w = (unsigned)w[3];
;         __builtin_nontemporal_store(o, (GAS v4u*)(t.dst + (size_t)n * t.Kd + 16 * c)); }
;     LDS_WAIT(); asm volatile("" ::: "memory");
; __device__ __forceinline__ void p8_convert(Frame& F, const Args& args, int lo, int hi, int gw, int NGW, int nlight) {
;     ...
;         for (;;) {
;             int nx = item_of(++idx); bool has = nx < hi;
;             if (has) { cb = p8_decode(args, ws, nx); p8_issue(cb, vb, F.lane); }
;             p8_finish(ca, va, scr, F.lane);
;             if (!has) break;
;             nx = item_of(++idx); has = nx < hi;
;             if (has) { ca = p8_decode(args, ws, nx); p8_issue(ca, va, F.lane); }
	v_max_f32_e32 v192, v192, v192
	v_med3_f32 v206, v192, s7, v191
	v_max_f32_e32 v192, v193, v193
	v_med3_f32 v193, v192, s7, v191
	v_mov_b32_e32 v192, 0
	v_cvt_pk_fp8_f32 v192, v206, v193
	s_waitcnt lgkmcnt(10)
	v_max_f32_e32 v193, v194, v194
	v_max_f32_e32 v194, v195, v195
	v_med3_f32 v193, v193, s7, v191
	v_med3_f32 v194, v194, s7, v191
	v_cvt_pk_fp8_f32 v192, v193, v194 op_sel:[0,0,1]
	s_waitcnt lgkmcnt(9)
	v_max_f32_e32 v193, v196, v196
	v_med3_f32 v194, v193, s7, v191
	v_max_f32_e32 v193, v197, v197
	v_med3_f32 v195, v193, s7, v191
	v_mov_b32_e32 v193, 0
	v_cvt_pk_fp8_f32 v193, v194, v195
	s_waitcnt lgkmcnt(8)
	v_max_f32_e32 v194, v198, v198
	v_max_f32_e32 v195, v199, v199
	v_med3_f32 v194, v194, s7, v191
	v_med3_f32 v195, v195, s7, v191
	s_waitcnt lgkmcnt(7)
	v_max_f32_e32 v140, v140, v140
	s_waitcnt lgkmcnt(6)
	v_max_f32_e32 v143, v143, v143
	v_cvt_pk_fp8_f32 v193, v194, v195 op_sel:[0,0,1]
	v_med3_f32 v140, v140, s7, v191
	v_med3_f32 v143, v143, s7, v191
	v_mov_b32_e32 v194, 0
	v_cvt_pk_fp8_f32 v194, v140, v143
	s_waitcnt lgkmcnt(5)
	v_max_f32_e32 v140, v200, v200
	s_waitcnt lgkmcnt(4)
	v_max_f32_e32 v143, v201, v201
	v_med3_f32 v140, v140, s7, v191
	v_med3_f32 v143, v143, s7, v191
	v_cvt_pk_fp8_f32 v194, v140, v143 op_sel:[0,0,1]
	s_waitcnt lgkmcnt(3)
	v_max_f32_e32 v140, v202, v202
	s_waitcnt lgkmcnt(2)
	v_max_f32_e32 v143, v203, v203
	v_med3_f32 v140, v140, s7, v191
	v_med3_f32 v143, v143, s7, v191
	v_mov_b32_e32 v195, 0
	v_cvt_pk_fp8_f32 v195, v140, v143
	s_waitcnt lgkmcnt(1)
	v_max_f32_e32 v140, v204, v204
	s_waitcnt lgkmcnt(0)
	v_max_f32_e32 v143, v205, v205
	v_med3_f32 v140, v140, s7, v191
	v_med3_f32 v143, v143, s7, v191
	v_cvt_pk_fp8_f32 v195, v140, v143 op_sel:[0,0,1]
	ds_read2_b32 v[196:197], v181 offset1:32
	ds_read2_b32 v[198:199], v181 offset0:64 offset1:96
	ds_read2_b32 v[200:201], v181 offset0:128 offset1:160
	ds_read2_b32 v[202:203], v181 offset0:192 offset1:224
	ds_read_b32 v140, v182
	ds_read_b32 v143, v183
	ds_read_b32 v204, v184
	ds_read_b32 v205, v185
	ds_read_b32 v206, v186
	ds_read_b32 v207, v187
	ds_read_b32 v208, v188
	ds_read_b32 v209, v189
	s_waitcnt lgkmcnt(11)
	v_max_f32_e32 v196, v196, v196
	v_med3_f32 v210, v196, s7, v191
	v_max_f32_e32 v196, v197, v197
	v_med3_f32 v197, v196, s7, v191
	v_mov_b32_e32 v196, 0
	v_cvt_pk_fp8_f32 v196, v210, v197
	s_waitcnt lgkmcnt(10)
	v_max_f32_e32 v197, v198, v198
	v_max_f32_e32 v198, v199, v199
	v_med3_f32 v197, v197, s7, v191
	v_med3_f32 v198, v198, s7, v191
	v_cvt_pk_fp8_f32 v196, v197, v198 op_sel:[0,0,1]
	s_waitcnt lgkmcnt(9)
	v_max_f32_e32 v197, v200, v200
	v_med3_f32 v198, v197, s7, v191
	v_max_f32_e32 v197, v201, v201
	v_med3_f32 v199, v197, s7, v191
	v_mov_b32_e32 v197, 0
	v_cvt_pk_fp8_f32 v197, v198, v199
	s_waitcnt lgkmcnt(8)
	v_max_f32_e32 v198, v202, v202
	v_max_f32_e32 v199, v203, v203
	v_med3_f32 v198, v198, s7, v191
	v_med3_f32 v199, v199, s7, v191
	s_waitcnt lgkmcnt(7)
	v_max_f32_e32 v140, v140, v140
	s_waitcnt lgkmcnt(6)
	v_max_f32_e32 v143, v143, v143
	v_cvt_pk_fp8_f32 v197, v198, v199 op_sel:[0,0,1]
	v_med3_f32 v140, v140, s7, v191
	v_med3_f32 v143, v143, s7, v191
	v_mov_b32_e32 v198, 0
	v_cvt_pk_fp8_f32 v198, v140, v143
	s_waitcnt lgkmcnt(5)
	v_max_f32_e32 v140, v204, v204
	s_waitcnt lgkmcnt(4)
	v_max_f32_e32 v143, v205, v205
	v_med3_f32 v140, v140, s7, v191
	v_med3_f32 v143, v143, s7, v191
	v_cvt_pk_fp8_f32 v198, v140, v143 op_sel:[0,0,1]
	s_waitcnt lgkmcnt(3)
	v_max_f32_e32 v140, v206, v206
	s_waitcnt lgkmcnt(2)
	v_max_f32_e32 v143, v207, v207
	v_med3_f32 v140, v140, s7, v191
	v_med3_f32 v143, v143, s7, v191
	v_mov_b32_e32 v199, 0
	v_cvt_pk_fp8_f32 v199, v140, v143
	s_waitcnt lgkmcnt(1)
	v_max_f32_e32 v140, v208, v208
	s_waitcnt lgkmcnt(0)
	v_max_f32_e32 v143, v209, v209
	v_med3_f32 v140, v140, s7, v191
	v_med3_f32 v143, v143, s7, v191
	v_cvt_pk_fp8_f32 v199, v140, v143 op_sel:[0,0,1]
	v_lshl_add_u64 v[200:201], v[144:145], 0, v[136:137]
	v_lshl_add_u64 v[144:145], v[144:145], 0, v[138:139]
	global_store_dwordx4 v[200:201], v[192:195], off nt
	global_store_dwordx4 v[144:145], v[196:199], off nt
	s_waitcnt lgkmcnt(0)
	s_cbranch_vccnz .LBB0_314
	s_add_i32 s25, s25, 2
	s_mul_i32 s4, s25, s22
	s_add_i32 s4, s4, s24
	s_cmpk_lt_i32 s4, 0x6acd
	s_cselect_b64 s[12:13], -1, 0
	s_cmpk_gt_i32 s4, 0x6acc
	s_cbranch_scc1 .LBB0_336
	s_mul_hi_i32 s8, s4, 0x2aaaaaab
	s_lshr_b32 s9, s8, 31
	s_ashr_i32 s8, s8, 9
	s_add_i32 s8, s8, s9
	s_mul_i32 s9, s8, 0xc00
	s_sub_i32 s26, s4, s9
	s_cmpk_gt_i32 s26, 0x7ff
	s_mov_b64 s[56:57], -1
	s_cbranch_scc0 .LBB0_329
	s_ashr_i32 s9, s8, 31
	s_lshl_b64 s[18:19], s[8:9], 22
	s_lshl_b64 s[14:15], s[8:9], 24
	s_add_u32 s9, s42, s14
	s_addc_u32 s16, s43, s15
	s_lshl_b32 s4, s26, 1
	s_and_b32 s4, s4, 0x7fffff80
	s_addk_i32 s4, 0xf000
	s_lshl_b64 s[14:15], s[4:5], 13
	s_add_u32 s9, s9, s14
	s_addc_u32 s17, s16, s15
	s_lshl_b32 s14, s26, 5
	s_and_b32 s14, s14, 0x7e0
	s_lshl_b32 s16, s14, 2
	s_add_u32 s16, s9, s16
	s_addc_u32 s17, s17, 0
	s_add_u32 s54, s2, s18
	s_mov_b32 s15, s5
	s_addc_u32 s55, s3, s19
	s_mov_b64 s[56:57], 0
	s_mov_b64 s[18:19], s[4:5]

; #define GAS __attribute__((address_space(1)))
; #define LAS __attribute__((address_space(3)))
; #define LDS_WAIT() asm volatile("s_waitcnt lgkmcnt(0)" ::: "memory")
; __device__ __forceinline__ void p8_issue(const TItem8& t, f32x4 (&v)[16], int lane) {
;     const GAS f32x4* src = (const GAS f32x4*)((const GAS float*)t.src + (size_t)(lane >> 3) * t.N + 4 * (lane & 7));
; #pragma unroll
;     for (int i = 0; i < 16; ++i) v[i] = __builtin_nontemporal_load(src + (size_t)(2 * i) * t.N);
; }
; __device__ __forceinline__ void p8_finish(const TItem8& t, const f32x4 (&v)[16], LAS float* scr, int lane) {
; #pragma unroll
;     for (int i = 0; i < 16; ++i) *(LAS f32x4*)(scr + (8 * i + (lane >> 3)) * 32 + (((lane & 7) ^ (i & 7)) << 2)) = v[i] * W8_SCALE;
;     LDS_WAIT(); asm volatile("" ::: "memory");
; __device__ __forceinline__ void p8_convert(Frame& F, const Args& args, int lo, int hi, int gw, int NGW, int nlight) {
;     ...
;             nx = item_of(++idx); has = nx < hi;
;             if (has) { ca = p8_decode(args, ws, nx); p8_issue(ca, va, F.lane); }
;             p8_finish(cb, vb, scr, F.lane);
.LBB0_335:
	s_lshl_b64 s[8:9], s[14:15], 11
	s_add_u32 s4, s54, s8
	v_mul_u32_u24_e32 v2, s56, v1
	s_addc_u32 s9, s55, s9
	v_lshlrev_b32_e32 v140, 2, v2
	s_add_u32 s8, s4, s18
	v_lshl_add_u64 v[2:3], s[16:17], 0, v[140:141]
	v_mov_b32_e32 v143, v141
	s_addc_u32 s9, s9, s19
	v_lshl_add_u64 v[2:3], v[2:3], 0, v[142:143]
	s_lshl_b32 s4, s56, 5
	v_lshl_add_u64 v[10:11], v[2:3], 0, s[4:5]
	global_load_dwordx4 v[2:5], v[2:3], off nt
	s_nop 0
	global_load_dwordx4 v[6:9], v[10:11], off nt
	v_lshl_add_u64 v[10:11], v[10:11], 0, s[4:5]
	v_lshl_add_u64 v[18:19], v[10:11], 0, s[4:5]
	global_load_dwordx4 v[10:13], v[10:11], off nt
	s_nop 0
	global_load_dwordx4 v[14:17], v[18:19], off nt
	v_lshl_add_u64 v[18:19], v[18:19], 0, s[4:5]
	v_lshl_add_u64 v[26:27], v[18:19], 0, s[4:5]
	global_load_dwordx4 v[18:21], v[18:19], off nt
	s_nop 0
	global_load_dwordx4 v[22:25], v[26:27], off nt
	v_lshl_add_u64 v[26:27], v[26:27], 0, s[4:5]
	v_lshl_add_u64 v[34:35], v[26:27], 0, s[4:5]
	v_lshl_add_u64 v[38:39], v[34:35], 0, s[4:5]
	v_lshl_add_u64 v[42:43], v[38:39], 0, s[4:5]
	v_lshl_add_u64 v[46:47], v[42:43], 0, s[4:5]
	v_lshl_add_u64 v[50:51], v[46:47], 0, s[4:5]
	v_lshl_add_u64 v[54:55], v[50:51], 0, s[4:5]
	v_lshl_add_u64 v[58:59], v[54:55], 0, s[4:5]
	v_lshl_add_u64 v[62:63], v[58:59], 0, s[4:5]
	global_load_dwordx4 v[26:29], v[26:27], off nt
	s_nop 0
	global_load_dwordx4 v[30:33], v[34:35], off nt
	s_nop 0
	global_load_dwordx4 v[34:37], v[38:39], off nt
	s_nop 0
	global_load_dwordx4 v[38:41], v[42:43], off nt
	s_nop 0
	global_load_dwordx4 v[42:45], v[46:47], off nt
	s_nop 0
	global_load_dwordx4 v[46:49], v[50:51], off nt
	s_nop 0
	global_load_dwordx4 v[50:53], v[54:55], off nt
	s_nop 0
	global_load_dwordx4 v[54:57], v[58:59], off nt
	s_nop 0
	global_load_dwordx4 v[58:61], v[62:63], off nt
	v_lshl_add_u64 v[62:63], v[62:63], 0, s[4:5]
	global_load_dwordx4 v[62:65], v[62:63], off nt
	s_waitcnt vmcnt(35)
	v_pk_mul_f32 v[194:195], v[68:69], s[6:7] op_sel_hi:[1,0]
	v_pk_mul_f32 v[192:193], v[66:67], s[6:7] op_sel_hi:[1,0]
	ds_write_b128 v146, v[192:195]
	s_waitcnt vmcnt(34)
	v_pk_mul_f32 v[194:195], v[72:73], s[6:7] op_sel_hi:[1,0]
	v_pk_mul_f32 v[192:193], v[70:71], s[6:7] op_sel_hi:[1,0]
	ds_write_b128 v147, v[192:195] offset:1024
	s_waitcnt vmcnt(33)
	v_pk_mul_f32 v[194:195], v[76:77], s[6:7] op_sel_hi:[1,0]
	v_pk_mul_f32 v[192:193], v[74:75], s[6:7] op_sel_hi:[1,0]
	ds_write_b128 v148, v[192:195] offset:2048
	s_waitcnt vmcnt(32)
	v_pk_mul_f32 v[194:195], v[80:81], s[6:7] op_sel_hi:[1,0]
	v_pk_mul_f32 v[192:193], v[78:79], s[6:7] op_sel_hi:[1,0]
	ds_write_b128 v149, v[192:195] offset:3072
	s_waitcnt vmcnt(31)
	v_pk_mul_f32 v[194:195], v[84:85], s[6:7] op_sel_hi:[1,0]
	v_pk_mul_f32 v[192:193], v[82:83], s[6:7] op_sel_hi:[1,0]
	ds_write_b128 v150, v[192:195] offset:4096
	s_waitcnt vmcnt(30)
	v_pk_mul_f32 v[194:195], v[88:89], s[6:7] op_sel_hi:[1,0]
	v_pk_mul_f32 v[192:193], v[86:87], s[6:7] op_sel_hi:[1,0]
	ds_write_b128 v151, v[192:195] offset:5120
	s_waitcnt vmcnt(29)
	v_pk_mul_f32 v[194:195], v[92:93], s[6:7] op_sel_hi:[1,0]
	v_pk_mul_f32 v[192:193], v[90:91], s[6:7] op_sel_hi:[1,0]
	ds_write_b128 v152, v[192:195] offset:6144
	s_waitcnt vmcnt(28)
	v_pk_mul_f32 v[194:195], v[96:97], s[6:7] op_sel_hi:[1,0]
	v_pk_mul_f32 v[192:193], v[94:95], s[6:7] op_sel_hi:[1,0]
	ds_write_b128 v153, v[192:195] offset:7168
	s_waitcnt vmcnt(27)
	v_pk_mul_f32 v[194:195], v[100:101], s[6:7] op_sel_hi:[1,0]
	v_pk_mul_f32 v[192:193], v[98:99], s[6:7] op_sel_hi:[1,0]
	ds_write_b128 v146, v[192:195] offset:8192
	s_waitcnt vmcnt(26)
	v_pk_mul_f32 v[194:195], v[104:105], s[6:7] op_sel_hi:[1,0]
	v_pk_mul_f32 v[192:193], v[102:103], s[6:7] op_sel_hi:[1,0]
	ds_write_b128 v147, v[192:195] offset:9216
	s_waitcnt vmcnt(25)
	v_pk_mul_f32 v[194:195], v[108:109], s[6:7] op_sel_hi:[1,0]
	v_pk_mul_f32 v[192:193], v[106:107], s[6:7] op_sel_hi:[1,0]
	ds_write_b128 v148, v[192:195] offset:10240
	s_waitcnt vmcnt(24)
	v_pk_mul_f32 v[194:195], v[112:113], s[6:7] op_sel_hi:[1,0]
	v_pk_mul_f32 v[192:193], v[110:111], s[6:7] op_sel_hi:[1,0]
	ds_write_b128 v149, v[192:195] offset:11264
	s_waitcnt vmcnt(23)
	v_pk_mul_f32 v[194:195], v[116:117], s[6:7] op_sel_hi:[1,0]
	v_pk_mul_f32 v[192:193], v[114:115], s[6:7] op_sel_hi:[1,0]
	ds_write_b128 v150, v[192:195] offset:12288
	s_waitcnt vmcnt(22)
	v_pk_mul_f32 v[194:195], v[120:121], s[6:7] op_sel_hi:[1,0]
	v_pk_mul_f32 v[192:193], v[118:119], s[6:7] op_sel_hi:[1,0]
	ds_write_b128 v151, v[192:195] offset:13312
	s_waitcnt vmcnt(21)
	v_pk_mul_f32 v[194:195], v[124:125], s[6:7] op_sel_hi:[1,0]
	v_pk_mul_f32 v[192:193], v[122:123], s[6:7] op_sel_hi:[1,0]
	ds_write_b128 v152, v[192:195] offset:14336
	s_waitcnt vmcnt(20)
	v_pk_mul_f32 v[194:195], v[128:129], s[6:7] op_sel_hi:[1,0]
	v_pk_mul_f32 v[192:193], v[126:127], s[6:7] op_sel_hi:[1,0]
	ds_write_b128 v153, v[192:195] offset:15360
	s_branch .Lcv2_11_325
; #define GAS __attribute__((address_space(1)))
; #define LAS __attribute__((address_space(3)))
; #define LDS_WAIT() asm volatile("s_waitcnt lgkmcnt(0)" ::: "memory")
; __device__ __forceinline__ void p8_finish(const TItem8& t, const f32x4 (&v)[16], LAS float* scr, int lane) {
;     ...
;     for (int i = 0; i < 16; ++i) *(LAS f32x4*)(scr + (8 * i + (lane >> 3)) * 32 + (((lane & 7) ^ (i & 7)) << 2)) = v[i] * W8_SCALE;
;     LDS_WAIT(); asm volatile("" ::: "memory");
;     const int c = lane & 7;
; #pragma unroll
;     for (int j = 0; j < 4; ++j) { const int n = (lane >> 3) + 8 * j; float x[16];
; #pragma unroll
;         for (int i = 0; i < 16; ++i) { const int k = 16 * c + i; x[i] = scr[k * 32 + ((((n >> 2) ^ ((k >> 3) & 7)) << 2) | (n & 3))]; }
;         int w[4];
; #pragma unroll
;         for (int g = 0; g < 4; ++g) { int q = 0; q = __builtin_amdgcn_cvt_pk_fp8_f32(fminf(fmaxf(x[4 * g], -448.f), 448.f), fminf(fmaxf(x[4 * g + 1], -448.f), 448.f), q, false);
;             q = __builtin_amdgcn_cvt_pk_fp8_f32(fminf(fmaxf(x[4 * g + 2], -448.f), 448.f), fminf(fmaxf(x[4 * g + 3], -448.f), 448.f), q, true); w[g] = q; }
;         v4u o; o.x = (unsigned)w[0]; o.y = (unsigned)w[1]; o.z = (unsigned)w[2]; o.w = (unsigned)w[3];
;         __builtin_nontemporal_store(o, (GAS v4u*)(t.dst + (size_t)n * t.Kd + 16 * c)); }
.LBB0_336:
	s_waitcnt vmcnt(19)
	v_pk_mul_f32 v[194:195], v[68:69], s[6:7] op_sel_hi:[1,0]
	v_pk_mul_f32 v[192:193], v[66:67], s[6:7] op_sel_hi:[1,0]
	ds_write_b128 v146, v[192:195]
	s_waitcnt vmcnt(18)
	v_pk_mul_f32 v[194:195], v[72:73], s[6:7] op_sel_hi:[1,0]
	v_pk_mul_f32 v[192:193], v[70:71], s[6:7] op_sel_hi:[1,0]
	ds_write_b128 v147, v[192:195] offset:1024
	s_waitcnt vmcnt(17)
	v_pk_mul_f32 v[194:195], v[76:77], s[6:7] op_sel_hi:[1,0]
	v_pk_mul_f32 v[192:193], v[74:75], s[6:7] op_sel_hi:[1,0]
	ds_write_b128 v148, v[192:195] offset:2048
	s_waitcnt vmcnt(16)
	v_pk_mul_f32 v[194:195], v[80:81], s[6:7] op_sel_hi:[1,0]
	v_pk_mul_f32 v[192:193], v[78:79], s[6:7] op_sel_hi:[1,0]
	ds_write_b128 v149, v[192:195] offset:3072
	s_waitcnt vmcnt(15)
	v_pk_mul_f32 v[194:195], v[84:85], s[6:7] op_sel_hi:[1,0]
	v_pk_mul_f32 v[192:193], v[82:83], s[6:7] op_sel_hi:[1,0]
	ds_write_b128 v150, v[192:195] offset:4096
	s_waitcnt vmcnt(14)
	v_pk_mul_f32 v[194:195], v[88:89], s[6:7] op_sel_hi:[1,0]
	v_pk_mul_f32 v[192:193], v[86:87], s[6:7] op_sel_hi:[1,0]
	ds_write_b128 v151, v[192:195] offset:5120
	s_waitcnt vmcnt(13)
	v_pk_mul_f32 v[194:195], v[92:93], s[6:7] op_sel_hi:[1,0]
	v_pk_mul_f32 v[192:193], v[90:91], s[6:7] op_sel_hi:[1,0]
	ds_write_b128 v152, v[192:195] offset:6144
	s_waitcnt vmcnt(12)
	v_pk_mul_f32 v[194:195], v[96:97], s[6:7] op_sel_hi:[1,0]
	v_pk_mul_f32 v[192:193], v[94:95], s[6:7] op_sel_hi:[1,0]
	ds_write_b128 v153, v[192:195] offset:7168
	s_waitcnt vmcnt(11)
	v_pk_mul_f32 v[194:195], v[100:101], s[6:7] op_sel_hi:[1,0]
	v_pk_mul_f32 v[192:193], v[98:99], s[6:7] op_sel_hi:[1,0]
	ds_write_b128 v146, v[192:195] offset:8192
	s_waitcnt vmcnt(10)
	v_pk_mul_f32 v[194:195], v[104:105], s[6:7] op_sel_hi:[1,0]
	v_pk_mul_f32 v[192:193], v[102:103], s[6:7] op_sel_hi:[1,0]
	ds_write_b128 v147, v[192:195] offset:9216
	s_waitcnt vmcnt(9)
	v_pk_mul_f32 v[194:195], v[108:109], s[6:7] op_sel_hi:[1,0]
	v_pk_mul_f32 v[192:193], v[106:107], s[6:7] op_sel_hi:[1,0]
	ds_write_b128 v148, v[192:195] offset:10240
	s_waitcnt vmcnt(8)
	v_pk_mul_f32 v[194:195], v[112:113], s[6:7] op_sel_hi:[1,0]
	v_pk_mul_f32 v[192:193], v[110:111], s[6:7] op_sel_hi:[1,0]
	ds_write_b128 v149, v[192:195] offset:11264
	s_waitcnt vmcnt(7)
	v_pk_mul_f32 v[194:195], v[116:117], s[6:7] op_sel_hi:[1,0]
	v_pk_mul_f32 v[192:193], v[114:115], s[6:7] op_sel_hi:[1,0]
	ds_write_b128 v150, v[192:195] offset:12288
	s_waitcnt vmcnt(6)
	v_pk_mul_f32 v[194:195], v[120:121], s[6:7] op_sel_hi:[1,0]
	v_pk_mul_f32 v[192:193], v[118:119], s[6:7] op_sel_hi:[1,0]
	ds_write_b128 v151, v[192:195] offset:13312
	s_waitcnt vmcnt(5)
	v_pk_mul_f32 v[194:195], v[124:125], s[6:7] op_sel_hi:[1,0]
	v_pk_mul_f32 v[192:193], v[122:123], s[6:7] op_sel_hi:[1,0]
	ds_write_b128 v152, v[192:195] offset:14336
	s_waitcnt vmcnt(4)
	v_pk_mul_f32 v[194:195], v[128:129], s[6:7] op_sel_hi:[1,0]
	v_pk_mul_f32 v[192:193], v[126:127], s[6:7] op_sel_hi:[1,0]
	ds_write_b128 v153, v[192:195] offset:15360
.Lcv2_11_325:
	s_waitcnt lgkmcnt(0)
	ds_read2_b32 v[192:193], v154 offset1:32
	ds_read2_b32 v[194:195], v154 offset0:64 offset1:96
	ds_read2_b32 v[196:197], v154 offset0:128 offset1:160
	ds_read2_b32 v[198:199], v154 offset0:192 offset1:224
	ds_read_b32 v140, v155
	ds_read_b32 v143, v156
	ds_read_b32 v200, v157
	ds_read_b32 v201, v158
	ds_read_b32 v202, v159
	ds_read_b32 v203, v160
	ds_read_b32 v204, v161
	ds_read_b32 v205, v162
	s_waitcnt lgkmcnt(11)
	v_max_f32_e32 v192, v192, v192
	v_med3_f32 v206, v192, s7, v191
	v_max_f32_e32 v192, v193, v193
	v_med3_f32 v193, v192, s7, v191
	v_mov_b32_e32 v192, v141
	v_cvt_pk_fp8_f32 v192, v206, v193
	s_waitcnt lgkmcnt(10)
	v_max_f32_e32 v193, v194, v194
	v_max_f32_e32 v194, v195, v195
	v_med3_f32 v193, v193, s7, v191
	v_med3_f32 v194, v194, s7, v191
	v_cvt_pk_fp8_f32 v192, v193, v194 op_sel:[0,0,1]
	s_waitcnt lgkmcnt(9)
	v_max_f32_e32 v193, v196, v196
	v_med3_f32 v194, v193, s7, v191
	v_max_f32_e32 v193, v197, v197
	v_med3_f32 v195, v193, s7, v191
	v_mov_b32_e32 v193, v141
	v_cvt_pk_fp8_f32 v193, v194, v195
	s_waitcnt lgkmcnt(8)
	v_max_f32_e32 v194, v198, v198
	v_max_f32_e32 v195, v199, v199
	v_med3_f32 v194, v194, s7, v191
	v_med3_f32 v195, v195, s7, v191
	s_waitcnt lgkmcnt(7)
	v_max_f32_e32 v140, v140, v140
	s_waitcnt lgkmcnt(6)
	v_max_f32_e32 v143, v143, v143
	v_cvt_pk_fp8_f32 v193, v194, v195 op_sel:[0,0,1]
	v_med3_f32 v140, v140, s7, v191
	v_med3_f32 v143, v143, s7, v191
	v_mov_b32_e32 v194, v141
	v_cvt_pk_fp8_f32 v194, v140, v143
	s_waitcnt lgkmcnt(5)
	v_max_f32_e32 v140, v200, v200
	s_waitcnt lgkmcnt(4)
	v_max_f32_e32 v143, v201, v201
	v_med3_f32 v140, v140, s7, v191
	v_med3_f32 v143, v143, s7, v191
	v_cvt_pk_fp8_f32 v194, v140, v143 op_sel:[0,0,1]
	s_waitcnt lgkmcnt(3)
	v_max_f32_e32 v140, v202, v202
	s_waitcnt lgkmcnt(2)
	v_max_f32_e32 v143, v203, v203
	v_med3_f32 v140, v140, s7, v191
	v_med3_f32 v143, v143, s7, v191
	v_mov_b32_e32 v195, v141
	v_cvt_pk_fp8_f32 v195, v140, v143
	s_waitcnt lgkmcnt(1)
	v_max_f32_e32 v140, v204, v204
	s_waitcnt lgkmcnt(0)
	v_max_f32_e32 v143, v205, v205
	v_med3_f32 v140, v140, s7, v191
	v_med3_f32 v143, v143, s7, v191
	v_cvt_pk_fp8_f32 v195, v140, v143 op_sel:[0,0,1]
	ds_read2_b32 v[196:197], v163 offset1:32
	ds_read2_b32 v[198:199], v163 offset0:64 offset1:96
	ds_read2_b32 v[200:201], v163 offset0:128 offset1:160
	ds_read2_b32 v[202:203], v163 offset0:192 offset1:224
	ds_read_b32 v140, v164
	ds_read_b32 v143, v165
	ds_read_b32 v204, v166
	ds_read_b32 v205, v167
	ds_read_b32 v206, v168
	ds_read_b32 v207, v169
	ds_read_b32 v208, v170
	ds_read_b32 v209, v171
	s_waitcnt lgkmcnt(11)
; #define GAS __attribute__((address_space(1)))
; __device__ __forceinline__ void p8_finish(const TItem8& t, const f32x4 (&v)[16], LAS float* scr, int lane) {
;     ...
;     const int c = lane & 7;
; #pragma unroll
;     for (int j = 0; j < 4; ++j) { const int n = (lane >> 3) + 8 * j; float x[16];
; #pragma unroll
;         for (int i = 0; i < 16; ++i) { const int k = 16 * c + i; x[i] = scr[k * 32 + ((((n >> 2) ^ ((k >> 3) & 7)) << 2) | (n & 3))]; }
;         int w[4];
; #pragma unroll
;         for (int g = 0; g < 4; ++g) { int q = 0; q = __builtin_amdgcn_cvt_pk_fp8_f32(fminf(fmaxf(x[4 * g], -448.f), 448.f), fminf(fmaxf(x[4 * g + 1], -448.f), 448.f), q, false);
;             q = __builtin_amdgcn_cvt_pk_fp8_f32(fminf(fmaxf(x[4 * g + 2], -448.f), 448.f), fminf(fmaxf(x[4 * g + 3], -448.f), 448.f), q, true); w[g] = q; }
;         v4u o; o.x = (unsigned)w[0]; o.y = (unsigned)w[1]; o.z = (unsigned)w[2]; o.w = (unsigned)w[3];
;         __builtin_nontemporal_store(o, (GAS v4u*)(t.dst + (size_t)n * t.Kd + 16 * c)); }
	v_max_f32_e32 v196, v196, v196
	v_med3_f32 v210, v196, s7, v191
	v_max_f32_e32 v196, v197, v197
	v_med3_f32 v197, v196, s7, v191
	v_mov_b32_e32 v196, v141
	v_cvt_pk_fp8_f32 v196, v210, v197
	s_waitcnt lgkmcnt(10)
	v_max_f32_e32 v197, v198, v198
	v_max_f32_e32 v198, v199, v199
	v_med3_f32 v197, v197, s7, v191
	v_med3_f32 v198, v198, s7, v191
	v_cvt_pk_fp8_f32 v196, v197, v198 op_sel:[0,0,1]
	s_waitcnt lgkmcnt(9)
	v_max_f32_e32 v197, v200, v200
	v_med3_f32 v198, v197, s7, v191
	v_max_f32_e32 v197, v201, v201
	v_med3_f32 v199, v197, s7, v191
	v_mov_b32_e32 v197, v141
	v_cvt_pk_fp8_f32 v197, v198, v199
	s_waitcnt lgkmcnt(8)
	v_max_f32_e32 v198, v202, v202
	v_max_f32_e32 v199, v203, v203
	v_med3_f32 v198, v198, s7, v191
	v_med3_f32 v199, v199, s7, v191
	s_waitcnt lgkmcnt(7)
	v_max_f32_e32 v140, v140, v140
	s_waitcnt lgkmcnt(6)
	v_max_f32_e32 v143, v143, v143
	v_cvt_pk_fp8_f32 v197, v198, v199 op_sel:[0,0,1]
	v_med3_f32 v140, v140, s7, v191
	v_med3_f32 v143, v143, s7, v191
	v_mov_b32_e32 v198, v141
	v_cvt_pk_fp8_f32 v198, v140, v143
	s_waitcnt lgkmcnt(5)
	v_max_f32_e32 v140, v204, v204
	s_waitcnt lgkmcnt(4)
	v_max_f32_e32 v143, v205, v205
	v_med3_f32 v140, v140, s7, v191
	v_med3_f32 v143, v143, s7, v191
	v_cvt_pk_fp8_f32 v198, v140, v143 op_sel:[0,0,1]
	s_waitcnt lgkmcnt(3)
	v_max_f32_e32 v140, v206, v206
	s_waitcnt lgkmcnt(2)
	v_max_f32_e32 v143, v207, v207
	v_med3_f32 v140, v140, s7, v191
	v_med3_f32 v143, v143, s7, v191
	v_mov_b32_e32 v199, v141
	v_cvt_pk_fp8_f32 v199, v140, v143
	s_waitcnt lgkmcnt(1)
	v_max_f32_e32 v140, v208, v208
	s_waitcnt lgkmcnt(0)
	v_max_f32_e32 v143, v209, v209
	v_med3_f32 v140, v140, s7, v191
	v_med3_f32 v143, v143, s7, v191
	v_cvt_pk_fp8_f32 v199, v140, v143 op_sel:[0,0,1]
	v_lshl_add_u64 v[144:145], s[10:11], 0, v[130:131]
	v_lshl_add_u64 v[200:201], v[144:145], 0, v[132:133]
	global_store_dwordx4 v[200:201], v[192:195], off nt
	s_nop 1
	v_lshl_add_u64 v[192:193], v[144:145], 0, v[134:135]
	global_store_dwordx4 v[192:193], v[196:199], off nt
	ds_read2_b32 v[192:193], v172 offset1:32
	ds_read2_b32 v[194:195], v172 offset0:64 offset1:96
	ds_read2_b32 v[196:197], v172 offset0:128 offset1:160
	ds_read2_b32 v[198:199], v172 offset0:192 offset1:224
	ds_read_b32 v140, v173
	ds_read_b32 v143, v174
	ds_read_b32 v200, v175
	ds_read_b32 v201, v176
	ds_read_b32 v202, v177
	ds_read_b32 v203, v178
	ds_read_b32 v204, v179
	ds_read_b32 v205, v180
	s_waitcnt lgkmcnt(11)
	v_max_f32_e32 v192, v192, v192
	v_med3_f32 v206, v192, s7, v191
	v_max_f32_e32 v192, v193, v193
	v_med3_f32 v193, v192, s7, v191
	v_mov_b32_e32 v192, v141
	v_cvt_pk_fp8_f32 v192, v206, v193
	s_waitcnt lgkmcnt(10)
	v_max_f32_e32 v193, v194, v194
	v_max_f32_e32 v194, v195, v195
	v_med3_f32 v193, v193, s7, v191
	v_med3_f32 v194, v194, s7, v191
	v_cvt_pk_fp8_f32 v192, v193, v194 op_sel:[0,0,1]
	s_waitcnt lgkmcnt(9)
	v_max_f32_e32 v193, v196, v196
	v_med3_f32 v194, v193, s7, v191
	v_max_f32_e32 v193, v197, v197
	v_med3_f32 v195, v193, s7, v191
	v_mov_b32_e32 v193, v141
	v_cvt_pk_fp8_f32 v193, v194, v195
	s_waitcnt lgkmcnt(8)
	v_max_f32_e32 v194, v198, v198
	v_max_f32_e32 v195, v199, v199
	v_med3_f32 v194, v194, s7, v191
	v_med3_f32 v195, v195, s7, v191
	s_waitcnt lgkmcnt(7)
	v_max_f32_e32 v140, v140, v140
	s_waitcnt lgkmcnt(6)
	v_max_f32_e32 v143, v143, v143
	v_cvt_pk_fp8_f32 v193, v194, v195 op_sel:[0,0,1]
	v_med3_f32 v140, v140, s7, v191
	v_med3_f32 v143, v143, s7, v191
	v_mov_b32_e32 v194, v141
	v_cvt_pk_fp8_f32 v194, v140, v143
	s_waitcnt lgkmcnt(5)
	v_max_f32_e32 v140, v200, v200
	s_waitcnt lgkmcnt(4)
	v_max_f32_e32 v143, v201, v201
	v_med3_f32 v140, v140, s7, v191
	v_med3_f32 v143, v143, s7, v191
	v_cvt_pk_fp8_f32 v194, v140, v143 op_sel:[0,0,1]
	s_waitcnt lgkmcnt(3)
	v_max_f32_e32 v140, v202, v202
	s_waitcnt lgkmcnt(2)
	v_max_f32_e32 v143, v203, v203
	v_med3_f32 v140, v140, s7, v191
	v_med3_f32 v143, v143, s7, v191
	v_mov_b32_e32 v195, v141
	v_cvt_pk_fp8_f32 v195, v140, v143
	s_waitcnt lgkmcnt(1)
	v_max_f32_e32 v140, v204, v204
	s_waitcnt lgkmcnt(0)
	v_max_f32_e32 v143, v205, v205
	v_med3_f32 v140, v140, s7, v191
	v_med3_f32 v143, v143, s7, v191
	v_cvt_pk_fp8_f32 v195, v140, v143 op_sel:[0,0,1]
	ds_read2_b32 v[196:197], v181 offset1:32
	ds_read2_b32 v[198:199], v181 offset0:64 offset1:96
	ds_read2_b32 v[200:201], v181 offset0:128 offset1:160
	ds_read2_b32 v[202:203], v181 offset0:192 offset1:224
	ds_read_b32 v140, v182
	ds_read_b32 v143, v183
	ds_read_b32 v204, v184
	ds_read_b32 v205, v185
	ds_read_b32 v206, v186
	ds_read_b32 v207, v187
	ds_read_b32 v208, v188
	ds_read_b32 v209, v189
	s_waitcnt lgkmcnt(11)
	v_max_f32_e32 v196, v196, v196
	v_med3_f32 v210, v196, s7, v191
	v_max_f32_e32 v196, v197, v197
	v_med3_f32 v197, v196, s7, v191
	v_mov_b32_e32 v196, v141
	v_cvt_pk_fp8_f32 v196, v210, v197
	s_waitcnt lgkmcnt(10)
	v_max_f32_e32 v197, v198, v198
	v_max_f32_e32 v198, v199, v199
	v_med3_f32 v197, v197, s7, v191
	v_med3_f32 v198, v198, s7, v191
	v_cvt_pk_fp8_f32 v196, v197, v198 op_sel:[0,0,1]
	s_waitcnt lgkmcnt(9)
	v_max_f32_e32 v197, v200, v200
	v_med3_f32 v198, v197, s7, v191
	v_max_f32_e32 v197, v201, v201
	v_med3_f32 v199, v197, s7, v191
	v_mov_b32_e32 v197, v141
	v_cvt_pk_fp8_f32 v197, v198, v199
	s_waitcnt lgkmcnt(8)
	v_max_f32_e32 v198, v202, v202
	v_max_f32_e32 v199, v203, v203
	v_med3_f32 v198, v198, s7, v191
	v_med3_f32 v199, v199, s7, v191
	s_waitcnt lgkmcnt(7)
	v_max_f32_e32 v140, v140, v140
	s_waitcnt lgkmcnt(6)
	v_max_f32_e32 v143, v143, v143
	v_cvt_pk_fp8_f32 v197, v198, v199 op_sel:[0,0,1]
	v_med3_f32 v140, v140, s7, v191
	v_med3_f32 v143, v143, s7, v191
	v_mov_b32_e32 v198, v141
	v_cvt_pk_fp8_f32 v198, v140, v143
	s_waitcnt lgkmcnt(5)
	v_max_f32_e32 v140, v204, v204
	s_waitcnt lgkmcnt(4)
	v_max_f32_e32 v143, v205, v205
	v_med3_f32 v140, v140, s7, v191
	v_med3_f32 v143, v143, s7, v191
	v_cvt_pk_fp8_f32 v198, v140, v143 op_sel:[0,0,1]
	s_waitcnt lgkmcnt(3)
	v_max_f32_e32 v140, v206, v206
	s_waitcnt lgkmcnt(2)
	v_max_f32_e32 v143, v207, v207
	v_med3_f32 v140, v140, s7, v191
	v_med3_f32 v143, v143, s7, v191
	v_mov_b32_e32 v199, v141
	v_cvt_pk_fp8_f32 v199, v140, v143
	s_waitcnt lgkmcnt(1)
	v_max_f32_e32 v140, v208, v208
	s_waitcnt lgkmcnt(0)
	v_max_f32_e32 v143, v209, v209
	v_med3_f32 v140, v140, s7, v191
	v_med3_f32 v143, v143, s7, v191
	v_cvt_pk_fp8_f32 v199, v140, v143 op_sel:[0,0,1]
	v_lshl_add_u64 v[200:201], v[144:145], 0, v[136:137]
	v_lshl_add_u64 v[144:145], v[144:145], 0, v[138:139]
	global_store_dwordx4 v[200:201], v[192:195], off nt
	global_store_dwordx4 v[144:145], v[196:199], off nt
	s_waitcnt lgkmcnt(0)
	s_xor_b64 s[12:13], s[12:13], -1
	s_andn2_b64 vcc, exec, s[12:13]
	s_cbranch_vccnz .LBB0_315

; #define GAS __attribute__((address_space(1)))
; __device__ __forceinline__ void p8_finish(const TItem8& t, const f32x4 (&v)[16], LAS float* scr, int lane) {
;     ...
;     for (int j = 0; j < 4; ++j) { const int n = (lane >> 3) + 8 * j; float x[16];
; #pragma unroll
;         for (int i = 0; i < 16; ++i) { const int k = 16 * c + i; x[i] = scr[k * 32 + ((((n >> 2) ^ ((k >> 3) & 7)) << 2) | (n & 3))]; }
;         int w[4];
; #pragma unroll
;         for (int g = 0; g < 4; ++g) { int q = 0; q = __builtin_amdgcn_cvt_pk_fp8_f32(fminf(fmaxf(x[4 * g], -448.f), 448.f), fminf(fmaxf(x[4 * g + 1], -448.f), 448.f), q, false);
;             q = __builtin_amdgcn_cvt_pk_fp8_f32(fminf(fmaxf(x[4 * g + 2], -448.f), 448.f), fminf(fmaxf(x[4 * g + 3], -448.f), 448.f), q, true); w[g] = q; }
;         v4u o; o.x = (unsigned)w[0]; o.y = (unsigned)w[1]; o.z = (unsigned)w[2]; o.w = (unsigned)w[3];
;         __builtin_nontemporal_store(o, (GAS v4u*)(t.dst + (size_t)n * t.Kd + 16 * c)); }
.Lcv1_10_353:
	s_waitcnt lgkmcnt(0)
	ds_read2_b32 v[192:193], v154 offset1:32
	ds_read2_b32 v[194:195], v154 offset0:64 offset1:96
	ds_read2_b32 v[196:197], v154 offset0:128 offset1:160
	ds_read2_b32 v[198:199], v154 offset0:192 offset1:224
	ds_read_b32 v140, v155
	ds_read_b32 v143, v156
	ds_read_b32 v200, v157
	ds_read_b32 v201, v158
	ds_read_b32 v202, v159
	ds_read_b32 v203, v160
	ds_read_b32 v204, v161
	ds_read_b32 v205, v162
	s_waitcnt lgkmcnt(11)
	v_max_f32_e32 v192, v192, v192
	v_med3_f32 v206, v192, s7, v191
	v_max_f32_e32 v192, v193, v193
	v_med3_f32 v193, v192, s7, v191
	v_mov_b32_e32 v192, 0
	v_cvt_pk_fp8_f32 v192, v206, v193
	s_waitcnt lgkmcnt(10)
	v_max_f32_e32 v193, v194, v194
	v_max_f32_e32 v194, v195, v195
	v_med3_f32 v193, v193, s7, v191
	v_med3_f32 v194, v194, s7, v191
	v_cvt_pk_fp8_f32 v192, v193, v194 op_sel:[0,0,1]
	s_waitcnt lgkmcnt(9)
	v_max_f32_e32 v193, v196, v196
	v_med3_f32 v194, v193, s7, v191
	v_max_f32_e32 v193, v197, v197
	v_med3_f32 v195, v193, s7, v191
	v_mov_b32_e32 v193, 0
	v_cvt_pk_fp8_f32 v193, v194, v195
	s_waitcnt lgkmcnt(8)
	v_max_f32_e32 v194, v198, v198
	v_max_f32_e32 v195, v199, v199
	v_med3_f32 v194, v194, s7, v191
	v_med3_f32 v195, v195, s7, v191
	s_waitcnt lgkmcnt(7)
	v_max_f32_e32 v140, v140, v140
	s_waitcnt lgkmcnt(6)
	v_max_f32_e32 v143, v143, v143
	v_cvt_pk_fp8_f32 v193, v194, v195 op_sel:[0,0,1]
	v_med3_f32 v140, v140, s7, v191
	v_med3_f32 v143, v143, s7, v191
	v_mov_b32_e32 v194, 0
	v_cvt_pk_fp8_f32 v194, v140, v143
	s_waitcnt lgkmcnt(5)
	v_max_f32_e32 v140, v200, v200
	s_waitcnt lgkmcnt(4)
	v_max_f32_e32 v143, v201, v201
	v_med3_f32 v140, v140, s7, v191
	v_med3_f32 v143, v143, s7, v191
	v_cvt_pk_fp8_f32 v194, v140, v143 op_sel:[0,0,1]
	s_waitcnt lgkmcnt(3)
	v_max_f32_e32 v140, v202, v202
	s_waitcnt lgkmcnt(2)
	v_max_f32_e32 v143, v203, v203
	v_med3_f32 v140, v140, s7, v191
	v_med3_f32 v143, v143, s7, v191
	v_mov_b32_e32 v195, 0
	v_cvt_pk_fp8_f32 v195, v140, v143
	s_waitcnt lgkmcnt(1)
	v_max_f32_e32 v140, v204, v204
	s_waitcnt lgkmcnt(0)
	v_max_f32_e32 v143, v205, v205
	v_med3_f32 v140, v140, s7, v191
	v_med3_f32 v143, v143, s7, v191
	v_cvt_pk_fp8_f32 v195, v140, v143 op_sel:[0,0,1]
	ds_read2_b32 v[196:197], v163 offset1:32
	ds_read2_b32 v[198:199], v163 offset0:64 offset1:96
	ds_read2_b32 v[200:201], v163 offset0:128 offset1:160
	ds_read2_b32 v[202:203], v163 offset0:192 offset1:224
	ds_read_b32 v140, v164
	ds_read_b32 v143, v165
	ds_read_b32 v204, v166
	ds_read_b32 v205, v167
	ds_read_b32 v206, v168
	ds_read_b32 v207, v169
	ds_read_b32 v208, v170
	ds_read_b32 v209, v171
	s_waitcnt lgkmcnt(11)
	v_max_f32_e32 v196, v196, v196
	v_med3_f32 v210, v196, s7, v191
	v_max_f32_e32 v196, v197, v197
	v_med3_f32 v197, v196, s7, v191
	v_mov_b32_e32 v196, 0
	v_cvt_pk_fp8_f32 v196, v210, v197
	s_waitcnt lgkmcnt(10)
	v_max_f32_e32 v197, v198, v198
	v_max_f32_e32 v198, v199, v199
	v_med3_f32 v197, v197, s7, v191
	v_med3_f32 v198, v198, s7, v191
	v_cvt_pk_fp8_f32 v196, v197, v198 op_sel:[0,0,1]
	s_waitcnt lgkmcnt(9)
	v_max_f32_e32 v197, v200, v200
	v_med3_f32 v198, v197, s7, v191
	v_max_f32_e32 v197, v201, v201
	v_med3_f32 v199, v197, s7, v191
	v_mov_b32_e32 v197, 0
	v_cvt_pk_fp8_f32 v197, v198, v199
	s_waitcnt lgkmcnt(8)
	v_max_f32_e32 v198, v202, v202
	v_max_f32_e32 v199, v203, v203
	v_med3_f32 v198, v198, s7, v191
	v_med3_f32 v199, v199, s7, v191
	s_waitcnt lgkmcnt(7)
	v_max_f32_e32 v140, v140, v140
	s_waitcnt lgkmcnt(6)
	v_max_f32_e32 v143, v143, v143
	v_cvt_pk_fp8_f32 v197, v198, v199 op_sel:[0,0,1]
	v_med3_f32 v140, v140, s7, v191
	v_med3_f32 v143, v143, s7, v191
	v_mov_b32_e32 v198, 0
	v_cvt_pk_fp8_f32 v198, v140, v143
	s_waitcnt lgkmcnt(5)
	v_max_f32_e32 v140, v204, v204
	s_waitcnt lgkmcnt(4)
	v_max_f32_e32 v143, v205, v205
	v_med3_f32 v140, v140, s7, v191
	v_med3_f32 v143, v143, s7, v191
	v_cvt_pk_fp8_f32 v198, v140, v143 op_sel:[0,0,1]
	s_waitcnt lgkmcnt(3)
	v_max_f32_e32 v140, v206, v206
	s_waitcnt lgkmcnt(2)
	v_max_f32_e32 v143, v207, v207
	v_med3_f32 v140, v140, s7, v191
	v_med3_f32 v143, v143, s7, v191
	v_mov_b32_e32 v199, 0
	v_cvt_pk_fp8_f32 v199, v140, v143
	s_waitcnt lgkmcnt(1)
	v_max_f32_e32 v140, v208, v208
	s_waitcnt lgkmcnt(0)
	v_max_f32_e32 v143, v209, v209
	v_med3_f32 v140, v140, s7, v191
	v_med3_f32 v143, v143, s7, v191
	v_cvt_pk_fp8_f32 v199, v140, v143 op_sel:[0,0,1]
	v_lshl_add_u64 v[144:145], s[8:9], 0, v[130:131]
	v_lshl_add_u64 v[200:201], v[144:145], 0, v[132:133]
	global_store_dwordx4 v[200:201], v[192:195], off nt
	s_andn2_b64 vcc, exec, s[12:13]
	s_mov_b64 s[12:13], 0
	v_lshl_add_u64 v[192:193], v[144:145], 0, v[134:135]
	global_store_dwordx4 v[192:193], v[196:199], off nt
	ds_read2_b32 v[192:193], v172 offset1:32
	ds_read2_b32 v[194:195], v172 offset0:64 offset1:96
	ds_read2_b32 v[196:197], v172 offset0:128 offset1:160
	ds_read2_b32 v[198:199], v172 offset0:192 offset1:224
	ds_read_b32 v140, v173
	ds_read_b32 v143, v174
	ds_read_b32 v200, v175
	ds_read_b32 v201, v176
	ds_read_b32 v202, v177
	ds_read_b32 v203, v178
	ds_read_b32 v204, v179
	ds_read_b32 v205, v180
	s_waitcnt lgkmcnt(11)
; #define GAS __attribute__((address_space(1)))
; __device__ __forceinline__ TItem8 p8_decode(const Args& args, unsigned char* ws, int it) {
;     TItem8 t;
;     if (it >= P8_N) { const int j = it - P8_N; it = (P8_E0 + j / P8_DN1) * (P8_GU1 + P8_DN1) + P8_GU1 + j % P8_DN1; }
;     else if (it >= P8_E0 * (P8_GU1 + P8_DN1)) { const int r = it - P8_E0 * (P8_GU1 + P8_DN1); it = (P8_E0 + r / P8_GU1) * (P8_GU1 + P8_DN1) + r % P8_GU1; }
;     const int e = it / (P8_GU1 + P8_DN1), q = it % (P8_GU1 + P8_DN1);
;     if (q < P8_GU1) { const int kb = q / 128, nb = q % 128, n0 = nb * 32;
;         const int dr = (n0 < DE) ? (256 * (n0 / 128) + (n0 % 128)) : (256 * ((n0 - DE) / 128) + 128 + ((n0 - DE) % 128));
;         t.src = args.in[25] + (size_t)e * D * 2 * DE + (size_t)(kb * 128) * (2 * DE) + n0; t.N = 2 * DE; t.dst = ws + WS_WGU + (size_t)e * 2 * DE * D + (size_t)dr * D + kb * 128; t.Kd = D; }
; __device__ __forceinline__ void p8_finish(const TItem8& t, const f32x4 (&v)[16], LAS float* scr, int lane) {
;     ...
;     for (int j = 0; j < 4; ++j) { const int n = (lane >> 3) + 8 * j; float x[16];
; #pragma unroll
;         for (int i = 0; i < 16; ++i) { const int k = 16 * c + i; x[i] = scr[k * 32 + ((((n >> 2) ^ ((k >> 3) & 7)) << 2) | (n & 3))]; }
;         int w[4];
; #pragma unroll
;         for (int g = 0; g < 4; ++g) { int q = 0; q = __builtin_amdgcn_cvt_pk_fp8_f32(fminf(fmaxf(x[4 * g], -448.f), 448.f), fminf(fmaxf(x[4 * g + 1], -448.f), 448.f), q, false);
;             q = __builtin_amdgcn_cvt_pk_fp8_f32(fminf(fmaxf(x[4 * g + 2], -448.f), 448.f), fminf(fmaxf(x[4 * g + 3], -448.f), 448.f), q, true); w[g] = q; }
;         v4u o; o.x = (unsigned)w[0]; o.y = (unsigned)w[1]; o.z = (unsigned)w[2]; o.w = (unsigned)w[3];
;         __builtin_nontemporal_store(o, (GAS v4u*)(t.dst + (size_t)n * t.Kd + 16 * c)); }
	v_max_f32_e32 v192, v192, v192
	v_med3_f32 v206, v192, s7, v191
	v_max_f32_e32 v192, v193, v193
	v_med3_f32 v193, v192, s7, v191
	v_mov_b32_e32 v192, 0
	v_cvt_pk_fp8_f32 v192, v206, v193
	s_waitcnt lgkmcnt(10)
	v_max_f32_e32 v193, v194, v194
	v_max_f32_e32 v194, v195, v195
	v_med3_f32 v193, v193, s7, v191
	v_med3_f32 v194, v194, s7, v191
	v_cvt_pk_fp8_f32 v192, v193, v194 op_sel:[0,0,1]
	s_waitcnt lgkmcnt(9)
	v_max_f32_e32 v193, v196, v196
	v_med3_f32 v194, v193, s7, v191
	v_max_f32_e32 v193, v197, v197
	v_med3_f32 v195, v193, s7, v191
	v_mov_b32_e32 v193, 0
	v_cvt_pk_fp8_f32 v193, v194, v195
	s_waitcnt lgkmcnt(8)
	v_max_f32_e32 v194, v198, v198
	v_max_f32_e32 v195, v199, v199
	v_med3_f32 v194, v194, s7, v191
	v_med3_f32 v195, v195, s7, v191
	s_waitcnt lgkmcnt(7)
	v_max_f32_e32 v140, v140, v140
	s_waitcnt lgkmcnt(6)
	v_max_f32_e32 v143, v143, v143
	v_cvt_pk_fp8_f32 v193, v194, v195 op_sel:[0,0,1]
	v_med3_f32 v140, v140, s7, v191
	v_med3_f32 v143, v143, s7, v191
	v_mov_b32_e32 v194, 0
	v_cvt_pk_fp8_f32 v194, v140, v143
	s_waitcnt lgkmcnt(5)
	v_max_f32_e32 v140, v200, v200
	s_waitcnt lgkmcnt(4)
	v_max_f32_e32 v143, v201, v201
	v_med3_f32 v140, v140, s7, v191
	v_med3_f32 v143, v143, s7, v191
	v_cvt_pk_fp8_f32 v194, v140, v143 op_sel:[0,0,1]
	s_waitcnt lgkmcnt(3)
	v_max_f32_e32 v140, v202, v202
	s_waitcnt lgkmcnt(2)
	v_max_f32_e32 v143, v203, v203
	v_med3_f32 v140, v140, s7, v191
	v_med3_f32 v143, v143, s7, v191
	v_mov_b32_e32 v195, 0
	v_cvt_pk_fp8_f32 v195, v140, v143
	s_waitcnt lgkmcnt(1)
	v_max_f32_e32 v140, v204, v204
	s_waitcnt lgkmcnt(0)
	v_max_f32_e32 v143, v205, v205
	v_med3_f32 v140, v140, s7, v191
	v_med3_f32 v143, v143, s7, v191
	v_cvt_pk_fp8_f32 v195, v140, v143 op_sel:[0,0,1]
	ds_read2_b32 v[196:197], v181 offset1:32
	ds_read2_b32 v[198:199], v181 offset0:64 offset1:96
	ds_read2_b32 v[200:201], v181 offset0:128 offset1:160
	ds_read2_b32 v[202:203], v181 offset0:192 offset1:224
	ds_read_b32 v140, v182
	ds_read_b32 v143, v183
	ds_read_b32 v204, v184
	ds_read_b32 v205, v185
	ds_read_b32 v206, v186
	ds_read_b32 v207, v187
	ds_read_b32 v208, v188
	ds_read_b32 v209, v189
	s_waitcnt lgkmcnt(11)
	v_max_f32_e32 v196, v196, v196
	v_med3_f32 v210, v196, s7, v191
	v_max_f32_e32 v196, v197, v197
	v_med3_f32 v197, v196, s7, v191
	v_mov_b32_e32 v196, 0
	v_cvt_pk_fp8_f32 v196, v210, v197
	s_waitcnt lgkmcnt(10)
	v_max_f32_e32 v197, v198, v198
	v_max_f32_e32 v198, v199, v199
	v_med3_f32 v197, v197, s7, v191
	v_med3_f32 v198, v198, s7, v191
	v_cvt_pk_fp8_f32 v196, v197, v198 op_sel:[0,0,1]
	s_waitcnt lgkmcnt(9)
	v_max_f32_e32 v197, v200, v200
	v_med3_f32 v198, v197, s7, v191
	v_max_f32_e32 v197, v201, v201
	v_med3_f32 v199, v197, s7, v191
	v_mov_b32_e32 v197, 0
	v_cvt_pk_fp8_f32 v197, v198, v199
	s_waitcnt lgkmcnt(8)
	v_max_f32_e32 v198, v202, v202
	v_max_f32_e32 v199, v203, v203
	v_med3_f32 v198, v198, s7, v191
	v_med3_f32 v199, v199, s7, v191
	s_waitcnt lgkmcnt(7)
	v_max_f32_e32 v140, v140, v140
	s_waitcnt lgkmcnt(6)
	v_max_f32_e32 v143, v143, v143
	v_cvt_pk_fp8_f32 v197, v198, v199 op_sel:[0,0,1]
	v_med3_f32 v140, v140, s7, v191
	v_med3_f32 v143, v143, s7, v191
	v_mov_b32_e32 v198, 0
	v_cvt_pk_fp8_f32 v198, v140, v143
	s_waitcnt lgkmcnt(5)
	v_max_f32_e32 v140, v204, v204
	s_waitcnt lgkmcnt(4)
	v_max_f32_e32 v143, v205, v205
	v_med3_f32 v140, v140, s7, v191
	v_med3_f32 v143, v143, s7, v191
	v_cvt_pk_fp8_f32 v198, v140, v143 op_sel:[0,0,1]
	s_waitcnt lgkmcnt(3)
	v_max_f32_e32 v140, v206, v206
	s_waitcnt lgkmcnt(2)
	v_max_f32_e32 v143, v207, v207
	v_med3_f32 v140, v140, s7, v191
	v_med3_f32 v143, v143, s7, v191
	v_mov_b32_e32 v199, 0
	v_cvt_pk_fp8_f32 v199, v140, v143
	s_waitcnt lgkmcnt(1)
	v_max_f32_e32 v140, v208, v208
	s_waitcnt lgkmcnt(0)
	v_max_f32_e32 v143, v209, v209
	v_med3_f32 v140, v140, s7, v191
	v_med3_f32 v143, v143, s7, v191
	v_cvt_pk_fp8_f32 v199, v140, v143 op_sel:[0,0,1]
	v_lshl_add_u64 v[200:201], v[144:145], 0, v[136:137]
	v_lshl_add_u64 v[144:145], v[144:145], 0, v[138:139]
	global_store_dwordx4 v[200:201], v[192:195], off nt
	global_store_dwordx4 v[144:145], v[196:199], off nt
	s_waitcnt lgkmcnt(0)
	s_cbranch_vccnz .LBB0_342
	s_add_i32 s24, s24, 2
	s_mul_i32 s4, s24, s22
	s_add_i32 s4, s4, s23
	s_cmp_lt_i32 s4, 0xc03d
	s_cselect_b64 s[12:13], -1, 0
	s_cmp_gt_i32 s4, 0xc03c
	s_cbranch_scc1 .LBB0_364
	s_mul_hi_i32 s8, s4, 0x2aaaaaab
	s_lshr_b32 s9, s8, 31
	s_ashr_i32 s8, s8, 9
	s_add_i32 s8, s8, s9
	s_mul_i32 s9, s8, 0xc00
	s_sub_i32 s25, s4, s9
	s_cmpk_gt_i32 s25, 0x7ff
	s_mov_b64 s[56:57], -1
	s_cbranch_scc0 .LBB0_357
	s_ashr_i32 s9, s8, 31
	s_lshl_b64 s[18:19], s[8:9], 22
	s_lshl_b64 s[14:15], s[8:9], 24
	s_add_u32 s9, s42, s14
	s_addc_u32 s16, s43, s15
	s_lshl_b32 s4, s25, 1
	s_and_b32 s4, s4, 0x7fffff80
	s_addk_i32 s4, 0xf000
	s_lshl_b64 s[14:15], s[4:5], 13
	s_add_u32 s9, s9, s14
	s_addc_u32 s17, s16, s15
	s_lshl_b32 s14, s25, 5
	s_and_b32 s14, s14, 0x7e0
	s_lshl_b32 s16, s14, 2
	s_add_u32 s16, s9, s16
	s_addc_u32 s17, s17, 0
	s_add_u32 s54, s2, s18
	s_mov_b32 s15, s5
	s_addc_u32 s55, s3, s19
	s_mov_b64 s[56:57], 0
	s_mov_b64 s[18:19], s[4:5]

; #define GAS __attribute__((address_space(1)))
; #define LAS __attribute__((address_space(3)))
; __device__ __forceinline__ void p8_issue(const TItem8& t, f32x4 (&v)[16], int lane) {
;     const GAS f32x4* src = (const GAS f32x4*)((const GAS float*)t.src + (size_t)(lane >> 3) * t.N + 4 * (lane & 7));
; #pragma unroll
;     for (int i = 0; i < 16; ++i) v[i] = __builtin_nontemporal_load(src + (size_t)(2 * i) * t.N);
; }
; __device__ __forceinline__ void p8_finish(const TItem8& t, const f32x4 (&v)[16], LAS float* scr, int lane) {
; #pragma unroll
;     for (int i = 0; i < 16; ++i) *(LAS f32x4*)(scr + (8 * i + (lane >> 3)) * 32 + (((lane & 7) ^ (i & 7)) << 2)) = v[i] * W8_SCALE;
.LBB0_383:
	s_lshl_b64 s[8:9], s[12:13], 11
	s_add_u32 s0, s18, s8
	v_mul_u32_u24_e32 v66, s54, v1
	s_addc_u32 s9, s19, s9
	v_lshlrev_b32_e32 v140, 2, v66
	s_add_u32 s8, s0, s16
	v_lshl_add_u64 v[66:67], s[14:15], 0, v[140:141]
	v_mov_b32_e32 v143, v141
	s_addc_u32 s9, s9, s17
	v_lshl_add_u64 v[66:67], v[66:67], 0, v[142:143]
	s_lshl_b32 s0, s54, 5
	v_lshl_add_u64 v[74:75], v[66:67], 0, s[0:1]
	global_load_dwordx4 v[66:69], v[66:67], off nt
	s_nop 0
	global_load_dwordx4 v[70:73], v[74:75], off nt
	v_lshl_add_u64 v[74:75], v[74:75], 0, s[0:1]
	v_lshl_add_u64 v[82:83], v[74:75], 0, s[0:1]
	global_load_dwordx4 v[74:77], v[74:75], off nt
	s_nop 0
	global_load_dwordx4 v[78:81], v[82:83], off nt
	v_lshl_add_u64 v[82:83], v[82:83], 0, s[0:1]
	v_lshl_add_u64 v[90:91], v[82:83], 0, s[0:1]
	global_load_dwordx4 v[82:85], v[82:83], off nt
	s_nop 0
	global_load_dwordx4 v[86:89], v[90:91], off nt
	v_lshl_add_u64 v[90:91], v[90:91], 0, s[0:1]
	v_lshl_add_u64 v[98:99], v[90:91], 0, s[0:1]
	v_lshl_add_u64 v[102:103], v[98:99], 0, s[0:1]
	v_lshl_add_u64 v[106:107], v[102:103], 0, s[0:1]
	v_lshl_add_u64 v[110:111], v[106:107], 0, s[0:1]
	v_lshl_add_u64 v[114:115], v[110:111], 0, s[0:1]
	v_lshl_add_u64 v[118:119], v[114:115], 0, s[0:1]
	v_lshl_add_u64 v[122:123], v[118:119], 0, s[0:1]
	v_lshl_add_u64 v[126:127], v[122:123], 0, s[0:1]
	global_load_dwordx4 v[90:93], v[90:91], off nt
	s_nop 0
	global_load_dwordx4 v[94:97], v[98:99], off nt
	s_nop 0
	global_load_dwordx4 v[98:101], v[102:103], off nt
	s_nop 0
	global_load_dwordx4 v[102:105], v[106:107], off nt
	s_nop 0
	global_load_dwordx4 v[106:109], v[110:111], off nt
	s_nop 0
	global_load_dwordx4 v[110:113], v[114:115], off nt
	s_nop 0
	global_load_dwordx4 v[114:117], v[118:119], off nt
	s_nop 0
	global_load_dwordx4 v[118:121], v[122:123], off nt
	s_nop 0
	global_load_dwordx4 v[122:125], v[126:127], off nt
	v_lshl_add_u64 v[126:127], v[126:127], 0, s[0:1]
	global_load_dwordx4 v[126:129], v[126:127], off nt
	s_waitcnt vmcnt(31)
	v_pk_mul_f32 v[194:195], v[4:5], s[4:5] op_sel_hi:[1,0]
	v_pk_mul_f32 v[192:193], v[2:3], s[4:5] op_sel_hi:[1,0]
	ds_write_b128 v146, v[192:195]
	s_waitcnt vmcnt(30)
	v_pk_mul_f32 v[194:195], v[8:9], s[4:5] op_sel_hi:[1,0]
	v_pk_mul_f32 v[192:193], v[6:7], s[4:5] op_sel_hi:[1,0]
	ds_write_b128 v147, v[192:195] offset:1024
	s_waitcnt vmcnt(29)
	v_pk_mul_f32 v[194:195], v[12:13], s[4:5] op_sel_hi:[1,0]
	v_pk_mul_f32 v[192:193], v[10:11], s[4:5] op_sel_hi:[1,0]
	ds_write_b128 v148, v[192:195] offset:2048
	s_waitcnt vmcnt(28)
	v_pk_mul_f32 v[194:195], v[16:17], s[4:5] op_sel_hi:[1,0]
	v_pk_mul_f32 v[192:193], v[14:15], s[4:5] op_sel_hi:[1,0]
	ds_write_b128 v149, v[192:195] offset:3072
	s_waitcnt vmcnt(27)
	v_pk_mul_f32 v[194:195], v[20:21], s[4:5] op_sel_hi:[1,0]
	v_pk_mul_f32 v[192:193], v[18:19], s[4:5] op_sel_hi:[1,0]
	ds_write_b128 v150, v[192:195] offset:4096
	s_waitcnt vmcnt(26)
	v_pk_mul_f32 v[194:195], v[24:25], s[4:5] op_sel_hi:[1,0]
	v_pk_mul_f32 v[192:193], v[22:23], s[4:5] op_sel_hi:[1,0]
	ds_write_b128 v151, v[192:195] offset:5120
	s_waitcnt vmcnt(25)
	v_pk_mul_f32 v[194:195], v[28:29], s[4:5] op_sel_hi:[1,0]
	v_pk_mul_f32 v[192:193], v[26:27], s[4:5] op_sel_hi:[1,0]
	ds_write_b128 v152, v[192:195] offset:6144
	s_waitcnt vmcnt(24)
	v_pk_mul_f32 v[194:195], v[32:33], s[4:5] op_sel_hi:[1,0]
	v_pk_mul_f32 v[192:193], v[30:31], s[4:5] op_sel_hi:[1,0]
	ds_write_b128 v153, v[192:195] offset:7168
	s_waitcnt vmcnt(23)
	v_pk_mul_f32 v[194:195], v[36:37], s[4:5] op_sel_hi:[1,0]
	v_pk_mul_f32 v[192:193], v[34:35], s[4:5] op_sel_hi:[1,0]
	ds_write_b128 v146, v[192:195] offset:8192
	s_waitcnt vmcnt(22)
	v_pk_mul_f32 v[194:195], v[40:41], s[4:5] op_sel_hi:[1,0]
	v_pk_mul_f32 v[192:193], v[38:39], s[4:5] op_sel_hi:[1,0]
	ds_write_b128 v147, v[192:195] offset:9216
	s_waitcnt vmcnt(21)
	v_pk_mul_f32 v[194:195], v[44:45], s[4:5] op_sel_hi:[1,0]
	v_pk_mul_f32 v[192:193], v[42:43], s[4:5] op_sel_hi:[1,0]
	ds_write_b128 v148, v[192:195] offset:10240
	s_waitcnt vmcnt(20)
	v_pk_mul_f32 v[194:195], v[48:49], s[4:5] op_sel_hi:[1,0]
	v_pk_mul_f32 v[192:193], v[46:47], s[4:5] op_sel_hi:[1,0]
	ds_write_b128 v149, v[192:195] offset:11264
	s_waitcnt vmcnt(19)
	v_pk_mul_f32 v[194:195], v[52:53], s[4:5] op_sel_hi:[1,0]
	v_pk_mul_f32 v[192:193], v[50:51], s[4:5] op_sel_hi:[1,0]
	ds_write_b128 v150, v[192:195] offset:12288
	s_waitcnt vmcnt(18)
	v_pk_mul_f32 v[194:195], v[56:57], s[4:5] op_sel_hi:[1,0]
	v_pk_mul_f32 v[192:193], v[54:55], s[4:5] op_sel_hi:[1,0]
	ds_write_b128 v151, v[192:195] offset:13312
	s_waitcnt vmcnt(17)
	v_pk_mul_f32 v[194:195], v[60:61], s[4:5] op_sel_hi:[1,0]
	v_pk_mul_f32 v[192:193], v[58:59], s[4:5] op_sel_hi:[1,0]
	ds_write_b128 v152, v[192:195] offset:14336
	s_waitcnt vmcnt(16)
	v_pk_mul_f32 v[194:195], v[64:65], s[4:5] op_sel_hi:[1,0]
	v_pk_mul_f32 v[192:193], v[62:63], s[4:5] op_sel_hi:[1,0]
	ds_write_b128 v153, v[192:195] offset:15360
	s_branch .Lcv1_9_384

; #define GAS __attribute__((address_space(1)))
; __device__ __forceinline__ void p8_finish(const TItem8& t, const f32x4 (&v)[16], LAS float* scr, int lane) {
;     ...
;     for (int j = 0; j < 4; ++j) { const int n = (lane >> 3) + 8 * j; float x[16];
; #pragma unroll
;         for (int i = 0; i < 16; ++i) { const int k = 16 * c + i; x[i] = scr[k * 32 + ((((n >> 2) ^ ((k >> 3) & 7)) << 2) | (n & 3))]; }
;         int w[4];
; #pragma unroll
;         for (int g = 0; g < 4; ++g) { int q = 0; q = __builtin_amdgcn_cvt_pk_fp8_f32(fminf(fmaxf(x[4 * g], -448.f), 448.f), fminf(fmaxf(x[4 * g + 1], -448.f), 448.f), q, false);
;             q = __builtin_amdgcn_cvt_pk_fp8_f32(fminf(fmaxf(x[4 * g + 2], -448.f), 448.f), fminf(fmaxf(x[4 * g + 3], -448.f), 448.f), q, true); w[g] = q; }
;         v4u o; o.x = (unsigned)w[0]; o.y = (unsigned)w[1]; o.z = (unsigned)w[2]; o.w = (unsigned)w[3];
;         __builtin_nontemporal_store(o, (GAS v4u*)(t.dst + (size_t)n * t.Kd + 16 * c)); }
.Lcv1_9_384:
	s_waitcnt lgkmcnt(0)
	ds_read2_b32 v[192:193], v154 offset1:32
	ds_read2_b32 v[194:195], v154 offset0:64 offset1:96
	ds_read2_b32 v[196:197], v154 offset0:128 offset1:160
	ds_read2_b32 v[198:199], v154 offset0:192 offset1:224
	ds_read_b32 v140, v155
	ds_read_b32 v143, v156
	ds_read_b32 v200, v157
	ds_read_b32 v201, v158
	ds_read_b32 v202, v159
	ds_read_b32 v203, v160
	ds_read_b32 v204, v161
	ds_read_b32 v205, v162
	s_waitcnt lgkmcnt(11)
	v_max_f32_e32 v192, v192, v192
	v_med3_f32 v206, v192, s5, v191
	v_max_f32_e32 v192, v193, v193
	v_med3_f32 v193, v192, s5, v191
	v_mov_b32_e32 v192, 0
	v_cvt_pk_fp8_f32 v192, v206, v193
	s_waitcnt lgkmcnt(10)
	v_max_f32_e32 v193, v194, v194
	v_max_f32_e32 v194, v195, v195
	v_med3_f32 v193, v193, s5, v191
	v_med3_f32 v194, v194, s5, v191
	v_cvt_pk_fp8_f32 v192, v193, v194 op_sel:[0,0,1]
	s_waitcnt lgkmcnt(9)
	v_max_f32_e32 v193, v196, v196
	v_med3_f32 v194, v193, s5, v191
	v_max_f32_e32 v193, v197, v197
	v_med3_f32 v195, v193, s5, v191
	v_mov_b32_e32 v193, 0
	v_cvt_pk_fp8_f32 v193, v194, v195
	s_waitcnt lgkmcnt(8)
	v_max_f32_e32 v194, v198, v198
	v_max_f32_e32 v195, v199, v199
	v_med3_f32 v194, v194, s5, v191
	v_med3_f32 v195, v195, s5, v191
	s_waitcnt lgkmcnt(7)
	v_max_f32_e32 v140, v140, v140
	s_waitcnt lgkmcnt(6)
	v_max_f32_e32 v143, v143, v143
	v_cvt_pk_fp8_f32 v193, v194, v195 op_sel:[0,0,1]
	v_med3_f32 v140, v140, s5, v191
	v_med3_f32 v143, v143, s5, v191
	v_mov_b32_e32 v194, 0
	v_cvt_pk_fp8_f32 v194, v140, v143
	s_waitcnt lgkmcnt(5)
	v_max_f32_e32 v140, v200, v200
	s_waitcnt lgkmcnt(4)
	v_max_f32_e32 v143, v201, v201
	v_med3_f32 v140, v140, s5, v191
	v_med3_f32 v143, v143, s5, v191
	v_cvt_pk_fp8_f32 v194, v140, v143 op_sel:[0,0,1]
	s_waitcnt lgkmcnt(3)
	v_max_f32_e32 v140, v202, v202
	s_waitcnt lgkmcnt(2)
	v_max_f32_e32 v143, v203, v203
	v_med3_f32 v140, v140, s5, v191
	v_med3_f32 v143, v143, s5, v191
	v_mov_b32_e32 v195, 0
	v_cvt_pk_fp8_f32 v195, v140, v143
	s_waitcnt lgkmcnt(1)
	v_max_f32_e32 v140, v204, v204
	s_waitcnt lgkmcnt(0)
	v_max_f32_e32 v143, v205, v205
	v_med3_f32 v140, v140, s5, v191
	v_med3_f32 v143, v143, s5, v191
	v_cvt_pk_fp8_f32 v195, v140, v143 op_sel:[0,0,1]
	ds_read2_b32 v[196:197], v163 offset1:32
	ds_read2_b32 v[198:199], v163 offset0:64 offset1:96
	ds_read2_b32 v[200:201], v163 offset0:128 offset1:160
	ds_read2_b32 v[202:203], v163 offset0:192 offset1:224
	ds_read_b32 v140, v164
	ds_read_b32 v143, v165
	ds_read_b32 v204, v166
	ds_read_b32 v205, v167
	ds_read_b32 v206, v168
	ds_read_b32 v207, v169
	ds_read_b32 v208, v170
	ds_read_b32 v209, v171
	s_waitcnt lgkmcnt(11)
	v_max_f32_e32 v196, v196, v196
	v_med3_f32 v210, v196, s5, v191
	v_max_f32_e32 v196, v197, v197
	v_med3_f32 v197, v196, s5, v191
	v_mov_b32_e32 v196, 0
	v_cvt_pk_fp8_f32 v196, v210, v197
	s_waitcnt lgkmcnt(10)
	v_max_f32_e32 v197, v198, v198
	v_max_f32_e32 v198, v199, v199
	v_med3_f32 v197, v197, s5, v191
	v_med3_f32 v198, v198, s5, v191
	v_cvt_pk_fp8_f32 v196, v197, v198 op_sel:[0,0,1]
	s_waitcnt lgkmcnt(9)
	v_max_f32_e32 v197, v200, v200
	v_med3_f32 v198, v197, s5, v191
	v_max_f32_e32 v197, v201, v201
	v_med3_f32 v199, v197, s5, v191
	v_mov_b32_e32 v197, 0
	v_cvt_pk_fp8_f32 v197, v198, v199
	s_waitcnt lgkmcnt(8)
	v_max_f32_e32 v198, v202, v202
	v_max_f32_e32 v199, v203, v203
	v_med3_f32 v198, v198, s5, v191
	v_med3_f32 v199, v199, s5, v191
	s_waitcnt lgkmcnt(7)
	v_max_f32_e32 v140, v140, v140
	s_waitcnt lgkmcnt(6)
	v_max_f32_e32 v143, v143, v143
	v_cvt_pk_fp8_f32 v197, v198, v199 op_sel:[0,0,1]
	v_med3_f32 v140, v140, s5, v191
	v_med3_f32 v143, v143, s5, v191
	v_mov_b32_e32 v198, 0
	v_cvt_pk_fp8_f32 v198, v140, v143
	s_waitcnt lgkmcnt(5)
	v_max_f32_e32 v140, v204, v204
	s_waitcnt lgkmcnt(4)
	v_max_f32_e32 v143, v205, v205
	v_med3_f32 v140, v140, s5, v191
	v_med3_f32 v143, v143, s5, v191
	v_cvt_pk_fp8_f32 v198, v140, v143 op_sel:[0,0,1]
	s_waitcnt lgkmcnt(3)
	v_max_f32_e32 v140, v206, v206
	s_waitcnt lgkmcnt(2)
	v_max_f32_e32 v143, v207, v207
	v_med3_f32 v140, v140, s5, v191
	v_med3_f32 v143, v143, s5, v191
	v_mov_b32_e32 v199, 0
	v_cvt_pk_fp8_f32 v199, v140, v143
	s_waitcnt lgkmcnt(1)
	v_max_f32_e32 v140, v208, v208
	s_waitcnt lgkmcnt(0)
	v_max_f32_e32 v143, v209, v209
	v_med3_f32 v140, v140, s5, v191
	v_med3_f32 v143, v143, s5, v191
	v_cvt_pk_fp8_f32 v199, v140, v143 op_sel:[0,0,1]
	v_lshl_add_u64 v[144:145], s[6:7], 0, v[130:131]
	v_lshl_add_u64 v[200:201], v[144:145], 0, v[132:133]
	global_store_dwordx4 v[200:201], v[192:195], off nt
	s_andn2_b64 vcc, exec, s[10:11]
	s_mov_b64 s[10:11], 0
	v_lshl_add_u64 v[192:193], v[144:145], 0, v[134:135]
	global_store_dwordx4 v[192:193], v[196:199], off nt
	ds_read2_b32 v[192:193], v172 offset1:32
	ds_read2_b32 v[194:195], v172 offset0:64 offset1:96
	ds_read2_b32 v[196:197], v172 offset0:128 offset1:160
	ds_read2_b32 v[198:199], v172 offset0:192 offset1:224
	ds_read_b32 v140, v173
	ds_read_b32 v143, v174
	ds_read_b32 v200, v175
	ds_read_b32 v201, v176
	ds_read_b32 v202, v177
	ds_read_b32 v203, v178
	ds_read_b32 v204, v179
	ds_read_b32 v205, v180
	s_waitcnt lgkmcnt(11)
; #define GAS __attribute__((address_space(1)))
; __device__ __forceinline__ TItem8 p8_decode(const Args& args, unsigned char* ws, int it) {
;     TItem8 t;
;     if (it >= P8_N) { const int j = it - P8_N; it = (P8_E0 + j / P8_DN1) * (P8_GU1 + P8_DN1) + P8_GU1 + j % P8_DN1; }
;     else if (it >= P8_E0 * (P8_GU1 + P8_DN1)) { const int r = it - P8_E0 * (P8_GU1 + P8_DN1); it = (P8_E0 + r / P8_GU1) * (P8_GU1 + P8_DN1) + r % P8_GU1; }
;     const int e = it / (P8_GU1 + P8_DN1), q = it % (P8_GU1 + P8_DN1);
;     if (q < P8_GU1) { const int kb = q / 128, nb = q % 128, n0 = nb * 32;
;         const int dr = (n0 < DE) ? (256 * (n0 / 128) + (n0 % 128)) : (256 * ((n0 - DE) / 128) + 128 + ((n0 - DE) % 128));
;         t.src = args.in[25] + (size_t)e * D * 2 * DE + (size_t)(kb * 128) * (2 * DE) + n0; t.N = 2 * DE; t.dst = ws + WS_WGU + (size_t)e * 2 * DE * D + (size_t)dr * D + kb * 128; t.Kd = D; }
; __device__ __forceinline__ void p8_finish(const TItem8& t, const f32x4 (&v)[16], LAS float* scr, int lane) {
;     ...
;     for (int j = 0; j < 4; ++j) { const int n = (lane >> 3) + 8 * j; float x[16];
; #pragma unroll
;         for (int i = 0; i < 16; ++i) { const int k = 16 * c + i; x[i] = scr[k * 32 + ((((n >> 2) ^ ((k >> 3) & 7)) << 2) | (n & 3))]; }
;         int w[4];
; #pragma unroll
;         for (int g = 0; g < 4; ++g) { int q = 0; q = __builtin_amdgcn_cvt_pk_fp8_f32(fminf(fmaxf(x[4 * g], -448.f), 448.f), fminf(fmaxf(x[4 * g + 1], -448.f), 448.f), q, false);
;             q = __builtin_amdgcn_cvt_pk_fp8_f32(fminf(fmaxf(x[4 * g + 2], -448.f), 448.f), fminf(fmaxf(x[4 * g + 3], -448.f), 448.f), q, true); w[g] = q; }
;         v4u o; o.x = (unsigned)w[0]; o.y = (unsigned)w[1]; o.z = (unsigned)w[2]; o.w = (unsigned)w[3];
;         __builtin_nontemporal_store(o, (GAS v4u*)(t.dst + (size_t)n * t.Kd + 16 * c)); }
	v_max_f32_e32 v192, v192, v192
	v_med3_f32 v206, v192, s5, v191
	v_max_f32_e32 v192, v193, v193
	v_med3_f32 v193, v192, s5, v191
	v_mov_b32_e32 v192, 0
	v_cvt_pk_fp8_f32 v192, v206, v193
	s_waitcnt lgkmcnt(10)
	v_max_f32_e32 v193, v194, v194
	v_max_f32_e32 v194, v195, v195
	v_med3_f32 v193, v193, s5, v191
	v_med3_f32 v194, v194, s5, v191
	v_cvt_pk_fp8_f32 v192, v193, v194 op_sel:[0,0,1]
	s_waitcnt lgkmcnt(9)
	v_max_f32_e32 v193, v196, v196
	v_med3_f32 v194, v193, s5, v191
	v_max_f32_e32 v193, v197, v197
	v_med3_f32 v195, v193, s5, v191
	v_mov_b32_e32 v193, 0
	v_cvt_pk_fp8_f32 v193, v194, v195
	s_waitcnt lgkmcnt(8)
	v_max_f32_e32 v194, v198, v198
	v_max_f32_e32 v195, v199, v199
	v_med3_f32 v194, v194, s5, v191
	v_med3_f32 v195, v195, s5, v191
	s_waitcnt lgkmcnt(7)
	v_max_f32_e32 v140, v140, v140
	s_waitcnt lgkmcnt(6)
	v_max_f32_e32 v143, v143, v143
	v_cvt_pk_fp8_f32 v193, v194, v195 op_sel:[0,0,1]
	v_med3_f32 v140, v140, s5, v191
	v_med3_f32 v143, v143, s5, v191
	v_mov_b32_e32 v194, 0
	v_cvt_pk_fp8_f32 v194, v140, v143
	s_waitcnt lgkmcnt(5)
	v_max_f32_e32 v140, v200, v200
	s_waitcnt lgkmcnt(4)
	v_max_f32_e32 v143, v201, v201
	v_med3_f32 v140, v140, s5, v191
	v_med3_f32 v143, v143, s5, v191
	v_cvt_pk_fp8_f32 v194, v140, v143 op_sel:[0,0,1]
	s_waitcnt lgkmcnt(3)
	v_max_f32_e32 v140, v202, v202
	s_waitcnt lgkmcnt(2)
	v_max_f32_e32 v143, v203, v203
	v_med3_f32 v140, v140, s5, v191
	v_med3_f32 v143, v143, s5, v191
	v_mov_b32_e32 v195, 0
	v_cvt_pk_fp8_f32 v195, v140, v143
	s_waitcnt lgkmcnt(1)
	v_max_f32_e32 v140, v204, v204
	s_waitcnt lgkmcnt(0)
	v_max_f32_e32 v143, v205, v205
	v_med3_f32 v140, v140, s5, v191
	v_med3_f32 v143, v143, s5, v191
	v_cvt_pk_fp8_f32 v195, v140, v143 op_sel:[0,0,1]
	ds_read2_b32 v[196:197], v181 offset1:32
	ds_read2_b32 v[198:199], v181 offset0:64 offset1:96
	ds_read2_b32 v[200:201], v181 offset0:128 offset1:160
	ds_read2_b32 v[202:203], v181 offset0:192 offset1:224
	ds_read_b32 v140, v182
	ds_read_b32 v143, v183
	ds_read_b32 v204, v184
	ds_read_b32 v205, v185
	ds_read_b32 v206, v186
	ds_read_b32 v207, v187
	ds_read_b32 v208, v188
	ds_read_b32 v209, v189
	s_waitcnt lgkmcnt(11)
	v_max_f32_e32 v196, v196, v196
	v_med3_f32 v210, v196, s5, v191
	v_max_f32_e32 v196, v197, v197
	v_med3_f32 v197, v196, s5, v191
	v_mov_b32_e32 v196, 0
	v_cvt_pk_fp8_f32 v196, v210, v197
	s_waitcnt lgkmcnt(10)
	v_max_f32_e32 v197, v198, v198
	v_max_f32_e32 v198, v199, v199
	v_med3_f32 v197, v197, s5, v191
	v_med3_f32 v198, v198, s5, v191
	v_cvt_pk_fp8_f32 v196, v197, v198 op_sel:[0,0,1]
	s_waitcnt lgkmcnt(9)
	v_max_f32_e32 v197, v200, v200
	v_med3_f32 v198, v197, s5, v191
	v_max_f32_e32 v197, v201, v201
	v_med3_f32 v199, v197, s5, v191
	v_mov_b32_e32 v197, 0
	v_cvt_pk_fp8_f32 v197, v198, v199
	s_waitcnt lgkmcnt(8)
	v_max_f32_e32 v198, v202, v202
	v_max_f32_e32 v199, v203, v203
	v_med3_f32 v198, v198, s5, v191
	v_med3_f32 v199, v199, s5, v191
	s_waitcnt lgkmcnt(7)
	v_max_f32_e32 v140, v140, v140
	s_waitcnt lgkmcnt(6)
	v_max_f32_e32 v143, v143, v143
	v_cvt_pk_fp8_f32 v197, v198, v199 op_sel:[0,0,1]
	v_med3_f32 v140, v140, s5, v191
	v_med3_f32 v143, v143, s5, v191
	v_mov_b32_e32 v198, 0
	v_cvt_pk_fp8_f32 v198, v140, v143
	s_waitcnt lgkmcnt(5)
	v_max_f32_e32 v140, v204, v204
	s_waitcnt lgkmcnt(4)
	v_max_f32_e32 v143, v205, v205
	v_med3_f32 v140, v140, s5, v191
	v_med3_f32 v143, v143, s5, v191
	v_cvt_pk_fp8_f32 v198, v140, v143 op_sel:[0,0,1]
	s_waitcnt lgkmcnt(3)
	v_max_f32_e32 v140, v206, v206
	s_waitcnt lgkmcnt(2)
	v_max_f32_e32 v143, v207, v207
	v_med3_f32 v140, v140, s5, v191
	v_med3_f32 v143, v143, s5, v191
	v_mov_b32_e32 v199, 0
	v_cvt_pk_fp8_f32 v199, v140, v143
	s_waitcnt lgkmcnt(1)
	v_max_f32_e32 v140, v208, v208
	s_waitcnt lgkmcnt(0)
	v_max_f32_e32 v143, v209, v209
	v_med3_f32 v140, v140, s5, v191
	v_med3_f32 v143, v143, s5, v191
	v_cvt_pk_fp8_f32 v199, v140, v143 op_sel:[0,0,1]
	v_lshl_add_u64 v[200:201], v[144:145], 0, v[136:137]
	v_lshl_add_u64 v[144:145], v[144:145], 0, v[138:139]
	global_store_dwordx4 v[200:201], v[192:195], off nt
	global_store_dwordx4 v[144:145], v[196:199], off nt
	s_waitcnt lgkmcnt(0)
	s_cbranch_vccnz .LBB0_373
	s_add_i32 s24, s24, 2
	s_mul_i32 s0, s24, 0x240
	s_add_i32 s0, s0, s23
	s_cmp_lt_i32 s0, 0xb09d
	s_cselect_b64 s[10:11], -1, 0
	s_cmp_gt_i32 s0, 0xb09c
	s_cbranch_scc1 .LBB0_395
	s_mul_hi_i32 s6, s0, 0x2aaaaaab
	s_lshr_b32 s7, s6, 31
	s_ashr_i32 s6, s6, 9
	s_add_i32 s6, s6, s7
	s_mul_i32 s7, s6, 0xc00
	s_sub_i32 s25, s0, s7
	s_cmpk_gt_i32 s25, 0x7ff
	s_mov_b64 s[54:55], -1
	s_cbranch_scc0 .LBB0_388
	s_ashr_i32 s7, s6, 31
	s_lshl_b64 s[16:17], s[6:7], 22
	s_lshl_b64 s[12:13], s[6:7], 24
	s_add_u32 s7, s42, s12
	s_addc_u32 s14, s43, s13
	s_lshl_b32 s0, s25, 1
	s_and_b32 s0, s0, 0x7fffff80
	s_addk_i32 s0, 0xf000
	s_lshl_b64 s[12:13], s[0:1], 13
	s_add_u32 s7, s7, s12
	s_addc_u32 s15, s14, s13
	s_lshl_b32 s12, s25, 5
	s_and_b32 s12, s12, 0x7e0
	s_lshl_b32 s14, s12, 2
	s_add_u32 s14, s7, s14
	s_addc_u32 s15, s15, 0
	s_add_u32 s18, s2, s16
	s_mov_b32 s13, s1
	s_addc_u32 s19, s3, s17
	s_mov_b64 s[54:55], 0
	s_mov_b64 s[16:17], s[0:1]

; #define GAS __attribute__((address_space(1)))
; #define LAS __attribute__((address_space(3)))
; __device__ __forceinline__ void p8_issue(const TItem8& t, f32x4 (&v)[16], int lane) {
;     const GAS f32x4* src = (const GAS f32x4*)((const GAS float*)t.src + (size_t)(lane >> 3) * t.N + 4 * (lane & 7));
; #pragma unroll
;     for (int i = 0; i < 16; ++i) v[i] = __builtin_nontemporal_load(src + (size_t)(2 * i) * t.N);
; }
; __device__ __forceinline__ void p8_finish(const TItem8& t, const f32x4 (&v)[16], LAS float* scr, int lane) {
; #pragma unroll
;     for (int i = 0; i < 16; ++i) *(LAS f32x4*)(scr + (8 * i + (lane >> 3)) * 32 + (((lane & 7) ^ (i & 7)) << 2)) = v[i] * W8_SCALE;
.LBB0_394:
	s_lshl_b64 s[6:7], s[12:13], 11
	s_add_u32 s0, s18, s6
	v_mul_u32_u24_e32 v2, s54, v1
	s_addc_u32 s7, s19, s7
	v_lshlrev_b32_e32 v140, 2, v2
	s_add_u32 s6, s0, s16
	v_lshl_add_u64 v[2:3], s[14:15], 0, v[140:141]
	v_mov_b32_e32 v143, v141
	s_addc_u32 s7, s7, s17
	v_lshl_add_u64 v[2:3], v[2:3], 0, v[142:143]
	s_lshl_b32 s0, s54, 5
	v_lshl_add_u64 v[10:11], v[2:3], 0, s[0:1]
	global_load_dwordx4 v[2:5], v[2:3], off nt
	s_nop 0
	global_load_dwordx4 v[6:9], v[10:11], off nt
	v_lshl_add_u64 v[10:11], v[10:11], 0, s[0:1]
	v_lshl_add_u64 v[18:19], v[10:11], 0, s[0:1]
	global_load_dwordx4 v[10:13], v[10:11], off nt
	s_nop 0
	global_load_dwordx4 v[14:17], v[18:19], off nt
	v_lshl_add_u64 v[18:19], v[18:19], 0, s[0:1]
	v_lshl_add_u64 v[26:27], v[18:19], 0, s[0:1]
	global_load_dwordx4 v[18:21], v[18:19], off nt
	s_nop 0
	global_load_dwordx4 v[22:25], v[26:27], off nt
	v_lshl_add_u64 v[26:27], v[26:27], 0, s[0:1]
	v_lshl_add_u64 v[34:35], v[26:27], 0, s[0:1]
	v_lshl_add_u64 v[38:39], v[34:35], 0, s[0:1]
	v_lshl_add_u64 v[42:43], v[38:39], 0, s[0:1]
	v_lshl_add_u64 v[46:47], v[42:43], 0, s[0:1]
	v_lshl_add_u64 v[50:51], v[46:47], 0, s[0:1]
	v_lshl_add_u64 v[54:55], v[50:51], 0, s[0:1]
	v_lshl_add_u64 v[58:59], v[54:55], 0, s[0:1]
	v_lshl_add_u64 v[62:63], v[58:59], 0, s[0:1]
	global_load_dwordx4 v[26:29], v[26:27], off nt
	s_nop 0
	global_load_dwordx4 v[30:33], v[34:35], off nt
	s_nop 0
	global_load_dwordx4 v[34:37], v[38:39], off nt
	s_nop 0
	global_load_dwordx4 v[38:41], v[42:43], off nt
	s_nop 0
	global_load_dwordx4 v[42:45], v[46:47], off nt
	s_nop 0
	global_load_dwordx4 v[46:49], v[50:51], off nt
	s_nop 0
	global_load_dwordx4 v[50:53], v[54:55], off nt
	s_nop 0
	global_load_dwordx4 v[54:57], v[58:59], off nt
	s_nop 0
	global_load_dwordx4 v[58:61], v[62:63], off nt
	v_lshl_add_u64 v[62:63], v[62:63], 0, s[0:1]
	global_load_dwordx4 v[62:65], v[62:63], off nt
	s_waitcnt vmcnt(35)
	v_pk_mul_f32 v[194:195], v[68:69], s[4:5] op_sel_hi:[1,0]
	v_pk_mul_f32 v[192:193], v[66:67], s[4:5] op_sel_hi:[1,0]
	ds_write_b128 v146, v[192:195]
	s_waitcnt vmcnt(34)
	v_pk_mul_f32 v[194:195], v[72:73], s[4:5] op_sel_hi:[1,0]
	v_pk_mul_f32 v[192:193], v[70:71], s[4:5] op_sel_hi:[1,0]
	ds_write_b128 v147, v[192:195] offset:1024
	s_waitcnt vmcnt(33)
	v_pk_mul_f32 v[194:195], v[76:77], s[4:5] op_sel_hi:[1,0]
	v_pk_mul_f32 v[192:193], v[74:75], s[4:5] op_sel_hi:[1,0]
	ds_write_b128 v148, v[192:195] offset:2048
	s_waitcnt vmcnt(32)
	v_pk_mul_f32 v[194:195], v[80:81], s[4:5] op_sel_hi:[1,0]
	v_pk_mul_f32 v[192:193], v[78:79], s[4:5] op_sel_hi:[1,0]
	ds_write_b128 v149, v[192:195] offset:3072
	s_waitcnt vmcnt(31)
	v_pk_mul_f32 v[194:195], v[84:85], s[4:5] op_sel_hi:[1,0]
	v_pk_mul_f32 v[192:193], v[82:83], s[4:5] op_sel_hi:[1,0]
	ds_write_b128 v150, v[192:195] offset:4096
	s_waitcnt vmcnt(30)
	v_pk_mul_f32 v[194:195], v[88:89], s[4:5] op_sel_hi:[1,0]
	v_pk_mul_f32 v[192:193], v[86:87], s[4:5] op_sel_hi:[1,0]
	ds_write_b128 v151, v[192:195] offset:5120
	s_waitcnt vmcnt(29)
	v_pk_mul_f32 v[194:195], v[92:93], s[4:5] op_sel_hi:[1,0]
	v_pk_mul_f32 v[192:193], v[90:91], s[4:5] op_sel_hi:[1,0]
	ds_write_b128 v152, v[192:195] offset:6144
	s_waitcnt vmcnt(28)
	v_pk_mul_f32 v[194:195], v[96:97], s[4:5] op_sel_hi:[1,0]
	v_pk_mul_f32 v[192:193], v[94:95], s[4:5] op_sel_hi:[1,0]
	ds_write_b128 v153, v[192:195] offset:7168
	s_waitcnt vmcnt(27)
	v_pk_mul_f32 v[194:195], v[100:101], s[4:5] op_sel_hi:[1,0]
	v_pk_mul_f32 v[192:193], v[98:99], s[4:5] op_sel_hi:[1,0]
	ds_write_b128 v146, v[192:195] offset:8192
	s_waitcnt vmcnt(26)
	v_pk_mul_f32 v[194:195], v[104:105], s[4:5] op_sel_hi:[1,0]
	v_pk_mul_f32 v[192:193], v[102:103], s[4:5] op_sel_hi:[1,0]
	ds_write_b128 v147, v[192:195] offset:9216
	s_waitcnt vmcnt(25)
	v_pk_mul_f32 v[194:195], v[108:109], s[4:5] op_sel_hi:[1,0]
	v_pk_mul_f32 v[192:193], v[106:107], s[4:5] op_sel_hi:[1,0]
	ds_write_b128 v148, v[192:195] offset:10240
	s_waitcnt vmcnt(24)
	v_pk_mul_f32 v[194:195], v[112:113], s[4:5] op_sel_hi:[1,0]
	v_pk_mul_f32 v[192:193], v[110:111], s[4:5] op_sel_hi:[1,0]
	ds_write_b128 v149, v[192:195] offset:11264
	s_waitcnt vmcnt(23)
	v_pk_mul_f32 v[194:195], v[116:117], s[4:5] op_sel_hi:[1,0]
	v_pk_mul_f32 v[192:193], v[114:115], s[4:5] op_sel_hi:[1,0]
	ds_write_b128 v150, v[192:195] offset:12288
	s_waitcnt vmcnt(22)
	v_pk_mul_f32 v[194:195], v[120:121], s[4:5] op_sel_hi:[1,0]
	v_pk_mul_f32 v[192:193], v[118:119], s[4:5] op_sel_hi:[1,0]
	ds_write_b128 v151, v[192:195] offset:13312
	s_waitcnt vmcnt(21)
	v_pk_mul_f32 v[194:195], v[124:125], s[4:5] op_sel_hi:[1,0]
	v_pk_mul_f32 v[192:193], v[122:123], s[4:5] op_sel_hi:[1,0]
	ds_write_b128 v152, v[192:195] offset:14336
	s_waitcnt vmcnt(20)
	v_pk_mul_f32 v[194:195], v[128:129], s[4:5] op_sel_hi:[1,0]
	v_pk_mul_f32 v[192:193], v[126:127], s[4:5] op_sel_hi:[1,0]
	ds_write_b128 v153, v[192:195] offset:15360
	s_branch .Lcv2_9_384
; #define GAS __attribute__((address_space(1)))
; #define LAS __attribute__((address_space(3)))
; #define LDS_WAIT() asm volatile("s_waitcnt lgkmcnt(0)" ::: "memory")
; __device__ __forceinline__ void p8_finish(const TItem8& t, const f32x4 (&v)[16], LAS float* scr, int lane) {
;     ...
;     for (int i = 0; i < 16; ++i) *(LAS f32x4*)(scr + (8 * i + (lane >> 3)) * 32 + (((lane & 7) ^ (i & 7)) << 2)) = v[i] * W8_SCALE;
;     LDS_WAIT(); asm volatile("" ::: "memory");
;     const int c = lane & 7;
; #pragma unroll
;     for (int j = 0; j < 4; ++j) { const int n = (lane >> 3) + 8 * j; float x[16];
; #pragma unroll
;         for (int i = 0; i < 16; ++i) { const int k = 16 * c + i; x[i] = scr[k * 32 + ((((n >> 2) ^ ((k >> 3) & 7)) << 2) | (n & 3))]; }
;         int w[4];
; #pragma unroll
;         for (int g = 0; g < 4; ++g) { int q = 0; q = __builtin_amdgcn_cvt_pk_fp8_f32(fminf(fmaxf(x[4 * g], -448.f), 448.f), fminf(fmaxf(x[4 * g + 1], -448.f), 448.f), q, false);
;             q = __builtin_amdgcn_cvt_pk_fp8_f32(fminf(fmaxf(x[4 * g + 2], -448.f), 448.f), fminf(fmaxf(x[4 * g + 3], -448.f), 448.f), q, true); w[g] = q; }
;         v4u o; o.x = (unsigned)w[0]; o.y = (unsigned)w[1]; o.z = (unsigned)w[2]; o.w = (unsigned)w[3];
;         __builtin_nontemporal_store(o, (GAS v4u*)(t.dst + (size_t)n * t.Kd + 16 * c)); }
.LBB0_395:
	s_waitcnt vmcnt(19)
	v_pk_mul_f32 v[194:195], v[68:69], s[4:5] op_sel_hi:[1,0]
	v_pk_mul_f32 v[192:193], v[66:67], s[4:5] op_sel_hi:[1,0]
	ds_write_b128 v146, v[192:195]
	s_waitcnt vmcnt(18)
	v_pk_mul_f32 v[194:195], v[72:73], s[4:5] op_sel_hi:[1,0]
	v_pk_mul_f32 v[192:193], v[70:71], s[4:5] op_sel_hi:[1,0]
	ds_write_b128 v147, v[192:195] offset:1024
	s_waitcnt vmcnt(17)
	v_pk_mul_f32 v[194:195], v[76:77], s[4:5] op_sel_hi:[1,0]
	v_pk_mul_f32 v[192:193], v[74:75], s[4:5] op_sel_hi:[1,0]
	ds_write_b128 v148, v[192:195] offset:2048
	s_waitcnt vmcnt(16)
	v_pk_mul_f32 v[194:195], v[80:81], s[4:5] op_sel_hi:[1,0]
	v_pk_mul_f32 v[192:193], v[78:79], s[4:5] op_sel_hi:[1,0]
	ds_write_b128 v149, v[192:195] offset:3072
	s_waitcnt vmcnt(15)
	v_pk_mul_f32 v[194:195], v[84:85], s[4:5] op_sel_hi:[1,0]
	v_pk_mul_f32 v[192:193], v[82:83], s[4:5] op_sel_hi:[1,0]
	ds_write_b128 v150, v[192:195] offset:4096
	s_waitcnt vmcnt(14)
	v_pk_mul_f32 v[194:195], v[88:89], s[4:5] op_sel_hi:[1,0]
	v_pk_mul_f32 v[192:193], v[86:87], s[4:5] op_sel_hi:[1,0]
	ds_write_b128 v151, v[192:195] offset:5120
	s_waitcnt vmcnt(13)
	v_pk_mul_f32 v[194:195], v[92:93], s[4:5] op_sel_hi:[1,0]
	v_pk_mul_f32 v[192:193], v[90:91], s[4:5] op_sel_hi:[1,0]
	ds_write_b128 v152, v[192:195] offset:6144
	s_waitcnt vmcnt(12)
	v_pk_mul_f32 v[194:195], v[96:97], s[4:5] op_sel_hi:[1,0]
	v_pk_mul_f32 v[192:193], v[94:95], s[4:5] op_sel_hi:[1,0]
	ds_write_b128 v153, v[192:195] offset:7168
	s_waitcnt vmcnt(11)
	v_pk_mul_f32 v[194:195], v[100:101], s[4:5] op_sel_hi:[1,0]
	v_pk_mul_f32 v[192:193], v[98:99], s[4:5] op_sel_hi:[1,0]
	ds_write_b128 v146, v[192:195] offset:8192
	s_waitcnt vmcnt(10)
	v_pk_mul_f32 v[194:195], v[104:105], s[4:5] op_sel_hi:[1,0]
	v_pk_mul_f32 v[192:193], v[102:103], s[4:5] op_sel_hi:[1,0]
	ds_write_b128 v147, v[192:195] offset:9216
	s_waitcnt vmcnt(9)
	v_pk_mul_f32 v[194:195], v[108:109], s[4:5] op_sel_hi:[1,0]
	v_pk_mul_f32 v[192:193], v[106:107], s[4:5] op_sel_hi:[1,0]
	ds_write_b128 v148, v[192:195] offset:10240
	s_waitcnt vmcnt(8)
	v_pk_mul_f32 v[194:195], v[112:113], s[4:5] op_sel_hi:[1,0]
	v_pk_mul_f32 v[192:193], v[110:111], s[4:5] op_sel_hi:[1,0]
	ds_write_b128 v149, v[192:195] offset:11264
	s_waitcnt vmcnt(7)
	v_pk_mul_f32 v[194:195], v[116:117], s[4:5] op_sel_hi:[1,0]
	v_pk_mul_f32 v[192:193], v[114:115], s[4:5] op_sel_hi:[1,0]
	ds_write_b128 v150, v[192:195] offset:12288
	s_waitcnt vmcnt(6)
	v_pk_mul_f32 v[194:195], v[120:121], s[4:5] op_sel_hi:[1,0]
	v_pk_mul_f32 v[192:193], v[118:119], s[4:5] op_sel_hi:[1,0]
	ds_write_b128 v151, v[192:195] offset:13312
	s_waitcnt vmcnt(5)
	v_pk_mul_f32 v[194:195], v[124:125], s[4:5] op_sel_hi:[1,0]
	v_pk_mul_f32 v[192:193], v[122:123], s[4:5] op_sel_hi:[1,0]
	ds_write_b128 v152, v[192:195] offset:14336
	s_waitcnt vmcnt(4)
	v_pk_mul_f32 v[194:195], v[128:129], s[4:5] op_sel_hi:[1,0]
	v_pk_mul_f32 v[192:193], v[126:127], s[4:5] op_sel_hi:[1,0]
	ds_write_b128 v153, v[192:195] offset:15360
.Lcv2_9_384:
	s_waitcnt lgkmcnt(0)
	ds_read2_b32 v[192:193], v154 offset1:32
	ds_read2_b32 v[194:195], v154 offset0:64 offset1:96
	ds_read2_b32 v[196:197], v154 offset0:128 offset1:160
	ds_read2_b32 v[198:199], v154 offset0:192 offset1:224
	ds_read_b32 v140, v155
	ds_read_b32 v143, v156
	ds_read_b32 v200, v157
	ds_read_b32 v201, v158
	ds_read_b32 v202, v159
	ds_read_b32 v203, v160
	ds_read_b32 v204, v161
	ds_read_b32 v205, v162
	s_waitcnt lgkmcnt(11)
	v_max_f32_e32 v192, v192, v192
	v_med3_f32 v206, v192, s5, v191
	v_max_f32_e32 v192, v193, v193
	v_med3_f32 v193, v192, s5, v191
	v_mov_b32_e32 v192, v141
	v_cvt_pk_fp8_f32 v192, v206, v193
	s_waitcnt lgkmcnt(10)
	v_max_f32_e32 v193, v194, v194
	v_max_f32_e32 v194, v195, v195
	v_med3_f32 v193, v193, s5, v191
	v_med3_f32 v194, v194, s5, v191
	v_cvt_pk_fp8_f32 v192, v193, v194 op_sel:[0,0,1]
	s_waitcnt lgkmcnt(9)
	v_max_f32_e32 v193, v196, v196
	v_med3_f32 v194, v193, s5, v191
	v_max_f32_e32 v193, v197, v197
	v_med3_f32 v195, v193, s5, v191
	v_mov_b32_e32 v193, v141
	v_cvt_pk_fp8_f32 v193, v194, v195
	s_waitcnt lgkmcnt(8)
	v_max_f32_e32 v194, v198, v198
	v_max_f32_e32 v195, v199, v199
	v_med3_f32 v194, v194, s5, v191
	v_med3_f32 v195, v195, s5, v191
	s_waitcnt lgkmcnt(7)
	v_max_f32_e32 v140, v140, v140
	s_waitcnt lgkmcnt(6)
	v_max_f32_e32 v143, v143, v143
	v_cvt_pk_fp8_f32 v193, v194, v195 op_sel:[0,0,1]
	v_med3_f32 v140, v140, s5, v191
	v_med3_f32 v143, v143, s5, v191
	v_mov_b32_e32 v194, v141
	v_cvt_pk_fp8_f32 v194, v140, v143
	s_waitcnt lgkmcnt(5)
	v_max_f32_e32 v140, v200, v200
	s_waitcnt lgkmcnt(4)
	v_max_f32_e32 v143, v201, v201
	v_med3_f32 v140, v140, s5, v191
	v_med3_f32 v143, v143, s5, v191
	v_cvt_pk_fp8_f32 v194, v140, v143 op_sel:[0,0,1]
	s_waitcnt lgkmcnt(3)
	v_max_f32_e32 v140, v202, v202
	s_waitcnt lgkmcnt(2)
	v_max_f32_e32 v143, v203, v203
	v_med3_f32 v140, v140, s5, v191
	v_med3_f32 v143, v143, s5, v191
	v_mov_b32_e32 v195, v141
	v_cvt_pk_fp8_f32 v195, v140, v143
	s_waitcnt lgkmcnt(1)
	v_max_f32_e32 v140, v204, v204
	s_waitcnt lgkmcnt(0)
	v_max_f32_e32 v143, v205, v205
	v_med3_f32 v140, v140, s5, v191
	v_med3_f32 v143, v143, s5, v191
	v_cvt_pk_fp8_f32 v195, v140, v143 op_sel:[0,0,1]
	ds_read2_b32 v[196:197], v163 offset1:32
	ds_read2_b32 v[198:199], v163 offset0:64 offset1:96
	ds_read2_b32 v[200:201], v163 offset0:128 offset1:160
	ds_read2_b32 v[202:203], v163 offset0:192 offset1:224
	ds_read_b32 v140, v164
	ds_read_b32 v143, v165
	ds_read_b32 v204, v166
	ds_read_b32 v205, v167
	ds_read_b32 v206, v168
	ds_read_b32 v207, v169
	ds_read_b32 v208, v170
	ds_read_b32 v209, v171
	s_waitcnt lgkmcnt(11)
; #define GAS __attribute__((address_space(1)))
; __device__ __forceinline__ void p8_finish(const TItem8& t, const f32x4 (&v)[16], LAS float* scr, int lane) {
;     ...
;     for (int j = 0; j < 4; ++j) { const int n = (lane >> 3) + 8 * j; float x[16];
; #pragma unroll
;         for (int i = 0; i < 16; ++i) { const int k = 16 * c + i; x[i] = scr[k * 32 + ((((n >> 2) ^ ((k >> 3) & 7)) << 2) | (n & 3))]; }
;         int w[4];
; #pragma unroll
;         for (int g = 0; g < 4; ++g) { int q = 0; q = __builtin_amdgcn_cvt_pk_fp8_f32(fminf(fmaxf(x[4 * g], -448.f), 448.f), fminf(fmaxf(x[4 * g + 1], -448.f), 448.f), q, false);
;             q = __builtin_amdgcn_cvt_pk_fp8_f32(fminf(fmaxf(x[4 * g + 2], -448.f), 448.f), fminf(fmaxf(x[4 * g + 3], -448.f), 448.f), q, true); w[g] = q; }
;         v4u o; o.x = (unsigned)w[0]; o.y = (unsigned)w[1]; o.z = (unsigned)w[2]; o.w = (unsigned)w[3];
;         __builtin_nontemporal_store(o, (GAS v4u*)(t.dst + (size_t)n * t.Kd + 16 * c)); }
	v_max_f32_e32 v196, v196, v196
	v_med3_f32 v210, v196, s5, v191
	v_max_f32_e32 v196, v197, v197
	v_med3_f32 v197, v196, s5, v191
	v_mov_b32_e32 v196, v141
	v_cvt_pk_fp8_f32 v196, v210, v197
	s_waitcnt lgkmcnt(10)
	v_max_f32_e32 v197, v198, v198
	v_max_f32_e32 v198, v199, v199
	v_med3_f32 v197, v197, s5, v191
	v_med3_f32 v198, v198, s5, v191
	v_cvt_pk_fp8_f32 v196, v197, v198 op_sel:[0,0,1]
	s_waitcnt lgkmcnt(9)
	v_max_f32_e32 v197, v200, v200
	v_med3_f32 v198, v197, s5, v191
	v_max_f32_e32 v197, v201, v201
	v_med3_f32 v199, v197, s5, v191
	v_mov_b32_e32 v197, v141
	v_cvt_pk_fp8_f32 v197, v198, v199
	s_waitcnt lgkmcnt(8)
	v_max_f32_e32 v198, v202, v202
	v_max_f32_e32 v199, v203, v203
	v_med3_f32 v198, v198, s5, v191
	v_med3_f32 v199, v199, s5, v191
	s_waitcnt lgkmcnt(7)
	v_max_f32_e32 v140, v140, v140
	s_waitcnt lgkmcnt(6)
	v_max_f32_e32 v143, v143, v143
	v_cvt_pk_fp8_f32 v197, v198, v199 op_sel:[0,0,1]
	v_med3_f32 v140, v140, s5, v191
	v_med3_f32 v143, v143, s5, v191
	v_mov_b32_e32 v198, v141
	v_cvt_pk_fp8_f32 v198, v140, v143
	s_waitcnt lgkmcnt(5)
	v_max_f32_e32 v140, v204, v204
	s_waitcnt lgkmcnt(4)
	v_max_f32_e32 v143, v205, v205
	v_med3_f32 v140, v140, s5, v191
	v_med3_f32 v143, v143, s5, v191
	v_cvt_pk_fp8_f32 v198, v140, v143 op_sel:[0,0,1]
	s_waitcnt lgkmcnt(3)
	v_max_f32_e32 v140, v206, v206
	s_waitcnt lgkmcnt(2)
	v_max_f32_e32 v143, v207, v207
	v_med3_f32 v140, v140, s5, v191
	v_med3_f32 v143, v143, s5, v191
	v_mov_b32_e32 v199, v141
	v_cvt_pk_fp8_f32 v199, v140, v143
	s_waitcnt lgkmcnt(1)
	v_max_f32_e32 v140, v208, v208
	s_waitcnt lgkmcnt(0)
	v_max_f32_e32 v143, v209, v209
	v_med3_f32 v140, v140, s5, v191
	v_med3_f32 v143, v143, s5, v191
	v_cvt_pk_fp8_f32 v199, v140, v143 op_sel:[0,0,1]
	v_lshl_add_u64 v[144:145], s[8:9], 0, v[130:131]
	v_lshl_add_u64 v[200:201], v[144:145], 0, v[132:133]
	global_store_dwordx4 v[200:201], v[192:195], off nt
	s_nop 1
	v_lshl_add_u64 v[192:193], v[144:145], 0, v[134:135]
	global_store_dwordx4 v[192:193], v[196:199], off nt
	ds_read2_b32 v[192:193], v172 offset1:32
	ds_read2_b32 v[194:195], v172 offset0:64 offset1:96
	ds_read2_b32 v[196:197], v172 offset0:128 offset1:160
	ds_read2_b32 v[198:199], v172 offset0:192 offset1:224
	ds_read_b32 v140, v173
	ds_read_b32 v143, v174
	ds_read_b32 v200, v175
	ds_read_b32 v201, v176
	ds_read_b32 v202, v177
	ds_read_b32 v203, v178
	ds_read_b32 v204, v179
	ds_read_b32 v205, v180
	s_waitcnt lgkmcnt(11)
	v_max_f32_e32 v192, v192, v192
	v_med3_f32 v206, v192, s5, v191
	v_max_f32_e32 v192, v193, v193
	v_med3_f32 v193, v192, s5, v191
	v_mov_b32_e32 v192, v141
	v_cvt_pk_fp8_f32 v192, v206, v193
	s_waitcnt lgkmcnt(10)
	v_max_f32_e32 v193, v194, v194
	v_max_f32_e32 v194, v195, v195
	v_med3_f32 v193, v193, s5, v191
	v_med3_f32 v194, v194, s5, v191
	v_cvt_pk_fp8_f32 v192, v193, v194 op_sel:[0,0,1]
	s_waitcnt lgkmcnt(9)
	v_max_f32_e32 v193, v196, v196
	v_med3_f32 v194, v193, s5, v191
	v_max_f32_e32 v193, v197, v197
	v_med3_f32 v195, v193, s5, v191
	v_mov_b32_e32 v193, v141
	v_cvt_pk_fp8_f32 v193, v194, v195
	s_waitcnt lgkmcnt(8)
	v_max_f32_e32 v194, v198, v198
	v_max_f32_e32 v195, v199, v199
	v_med3_f32 v194, v194, s5, v191
	v_med3_f32 v195, v195, s5, v191
	s_waitcnt lgkmcnt(7)
	v_max_f32_e32 v140, v140, v140
	s_waitcnt lgkmcnt(6)
	v_max_f32_e32 v143, v143, v143
	v_cvt_pk_fp8_f32 v193, v194, v195 op_sel:[0,0,1]
	v_med3_f32 v140, v140, s5, v191
	v_med3_f32 v143, v143, s5, v191
	v_mov_b32_e32 v194, v141
	v_cvt_pk_fp8_f32 v194, v140, v143
	s_waitcnt lgkmcnt(5)
	v_max_f32_e32 v140, v200, v200
	s_waitcnt lgkmcnt(4)
	v_max_f32_e32 v143, v201, v201
	v_med3_f32 v140, v140, s5, v191
	v_med3_f32 v143, v143, s5, v191
	v_cvt_pk_fp8_f32 v194, v140, v143 op_sel:[0,0,1]
	s_waitcnt lgkmcnt(3)
	v_max_f32_e32 v140, v202, v202
	s_waitcnt lgkmcnt(2)
	v_max_f32_e32 v143, v203, v203
	v_med3_f32 v140, v140, s5, v191
	v_med3_f32 v143, v143, s5, v191
	v_mov_b32_e32 v195, v141
	v_cvt_pk_fp8_f32 v195, v140, v143
	s_waitcnt lgkmcnt(1)
	v_max_f32_e32 v140, v204, v204
	s_waitcnt lgkmcnt(0)
	v_max_f32_e32 v143, v205, v205
	v_med3_f32 v140, v140, s5, v191
	v_med3_f32 v143, v143, s5, v191
	v_cvt_pk_fp8_f32 v195, v140, v143 op_sel:[0,0,1]
	ds_read2_b32 v[196:197], v181 offset1:32
	ds_read2_b32 v[198:199], v181 offset0:64 offset1:96
	ds_read2_b32 v[200:201], v181 offset0:128 offset1:160
	ds_read2_b32 v[202:203], v181 offset0:192 offset1:224
	ds_read_b32 v140, v182
	ds_read_b32 v143, v183
	ds_read_b32 v204, v184
	ds_read_b32 v205, v185
	ds_read_b32 v206, v186
	ds_read_b32 v207, v187
	ds_read_b32 v208, v188
	ds_read_b32 v209, v189
	s_waitcnt lgkmcnt(11)
	v_max_f32_e32 v196, v196, v196
	v_med3_f32 v210, v196, s5, v191
	v_max_f32_e32 v196, v197, v197
	v_med3_f32 v197, v196, s5, v191
	v_mov_b32_e32 v196, v141
	v_cvt_pk_fp8_f32 v196, v210, v197
	s_waitcnt lgkmcnt(10)
	v_max_f32_e32 v197, v198, v198
	v_max_f32_e32 v198, v199, v199
	v_med3_f32 v197, v197, s5, v191
	v_med3_f32 v198, v198, s5, v191
	v_cvt_pk_fp8_f32 v196, v197, v198 op_sel:[0,0,1]
	s_waitcnt lgkmcnt(9)
	v_max_f32_e32 v197, v200, v200
	v_med3_f32 v198, v197, s5, v191
	v_max_f32_e32 v197, v201, v201
	v_med3_f32 v199, v197, s5, v191
	v_mov_b32_e32 v197, v141
	v_cvt_pk_fp8_f32 v197, v198, v199
	s_waitcnt lgkmcnt(8)
	v_max_f32_e32 v198, v202, v202
	v_max_f32_e32 v199, v203, v203
	v_med3_f32 v198, v198, s5, v191
	v_med3_f32 v199, v199, s5, v191
	s_waitcnt lgkmcnt(7)
	v_max_f32_e32 v140, v140, v140
	s_waitcnt lgkmcnt(6)
	v_max_f32_e32 v143, v143, v143
	v_cvt_pk_fp8_f32 v197, v198, v199 op_sel:[0,0,1]
	v_med3_f32 v140, v140, s5, v191
	v_med3_f32 v143, v143, s5, v191
	v_mov_b32_e32 v198, v141
	v_cvt_pk_fp8_f32 v198, v140, v143
	s_waitcnt lgkmcnt(5)
	v_max_f32_e32 v140, v204, v204
	s_waitcnt lgkmcnt(4)
	v_max_f32_e32 v143, v205, v205
	v_med3_f32 v140, v140, s5, v191
	v_med3_f32 v143, v143, s5, v191
	v_cvt_pk_fp8_f32 v198, v140, v143 op_sel:[0,0,1]
	s_waitcnt lgkmcnt(3)
	v_max_f32_e32 v140, v206, v206
	s_waitcnt lgkmcnt(2)
	v_max_f32_e32 v143, v207, v207
	v_med3_f32 v140, v140, s5, v191
	v_med3_f32 v143, v143, s5, v191
	v_mov_b32_e32 v199, v141
	v_cvt_pk_fp8_f32 v199, v140, v143
	s_waitcnt lgkmcnt(1)
	v_max_f32_e32 v140, v208, v208
	s_waitcnt lgkmcnt(0)
	v_max_f32_e32 v143, v209, v209
	v_med3_f32 v140, v140, s5, v191
	v_med3_f32 v143, v143, s5, v191
	v_cvt_pk_fp8_f32 v199, v140, v143 op_sel:[0,0,1]
	v_lshl_add_u64 v[200:201], v[144:145], 0, v[136:137]
	v_lshl_add_u64 v[144:145], v[144:145], 0, v[138:139]
	global_store_dwordx4 v[200:201], v[192:195], off nt
	global_store_dwordx4 v[144:145], v[196:199], off nt
	s_waitcnt lgkmcnt(0)
	s_xor_b64 s[10:11], s[10:11], -1
	s_and_b64 vcc, exec, s[10:11]
	s_cbranch_vccz .LBB0_374

; #define GAS __attribute__((address_space(1)))
; __device__ __forceinline__ void p8_finish(const TItem8& t, const f32x4 (&v)[16], LAS float* scr, int lane) {
;     ...
;     for (int j = 0; j < 4; ++j) { const int n = (lane >> 3) + 8 * j; float x[16];
; #pragma unroll
;         for (int i = 0; i < 16; ++i) { const int k = 16 * c + i; x[i] = scr[k * 32 + ((((n >> 2) ^ ((k >> 3) & 7)) << 2) | (n & 3))]; }
;         int w[4];
; #pragma unroll
;         for (int g = 0; g < 4; ++g) { int q = 0; q = __builtin_amdgcn_cvt_pk_fp8_f32(fminf(fmaxf(x[4 * g], -448.f), 448.f), fminf(fmaxf(x[4 * g + 1], -448.f), 448.f), q, false);
;             q = __builtin_amdgcn_cvt_pk_fp8_f32(fminf(fmaxf(x[4 * g + 2], -448.f), 448.f), fminf(fmaxf(x[4 * g + 3], -448.f), 448.f), q, true); w[g] = q; }
;         v4u o; o.x = (unsigned)w[0]; o.y = (unsigned)w[1]; o.z = (unsigned)w[2]; o.w = (unsigned)w[3];
;         __builtin_nontemporal_store(o, (GAS v4u*)(t.dst + (size_t)n * t.Kd + 16 * c)); }
.Lcv1_8_414:
	s_waitcnt lgkmcnt(0)
	ds_read2_b32 v[192:193], v154 offset1:32
	ds_read2_b32 v[194:195], v154 offset0:64 offset1:96
	ds_read2_b32 v[196:197], v154 offset0:128 offset1:160
	ds_read2_b32 v[198:199], v154 offset0:192 offset1:224
	ds_read_b32 v140, v155
	ds_read_b32 v143, v156
	ds_read_b32 v191, v157
	ds_read_b32 v200, v158
	ds_read_b32 v201, v159
	ds_read_b32 v202, v160
	ds_read_b32 v203, v161
	ds_read_b32 v204, v162
	s_waitcnt lgkmcnt(11)
	v_max_f32_e32 v192, v192, v192
	v_med3_f32 v205, v192, s5, v190
	v_max_f32_e32 v192, v193, v193
	v_med3_f32 v193, v192, s5, v190
	v_mov_b32_e32 v192, 0
	v_cvt_pk_fp8_f32 v192, v205, v193
	s_waitcnt lgkmcnt(10)
	v_max_f32_e32 v193, v194, v194
	v_max_f32_e32 v194, v195, v195
	v_med3_f32 v193, v193, s5, v190
	v_med3_f32 v194, v194, s5, v190
	v_cvt_pk_fp8_f32 v192, v193, v194 op_sel:[0,0,1]
	s_waitcnt lgkmcnt(9)
	v_max_f32_e32 v193, v196, v196
	v_med3_f32 v194, v193, s5, v190
	v_max_f32_e32 v193, v197, v197
	v_med3_f32 v195, v193, s5, v190
	v_mov_b32_e32 v193, 0
	v_cvt_pk_fp8_f32 v193, v194, v195
	s_waitcnt lgkmcnt(8)
	v_max_f32_e32 v194, v198, v198
	v_max_f32_e32 v195, v199, v199
	v_med3_f32 v194, v194, s5, v190
	v_med3_f32 v195, v195, s5, v190
	s_waitcnt lgkmcnt(7)
	v_max_f32_e32 v140, v140, v140
	s_waitcnt lgkmcnt(6)
	v_max_f32_e32 v143, v143, v143
	v_cvt_pk_fp8_f32 v193, v194, v195 op_sel:[0,0,1]
	v_med3_f32 v140, v140, s5, v190
	v_med3_f32 v143, v143, s5, v190
	v_mov_b32_e32 v194, 0
	v_cvt_pk_fp8_f32 v194, v140, v143
	s_waitcnt lgkmcnt(5)
	v_max_f32_e32 v140, v191, v191
	s_waitcnt lgkmcnt(4)
	v_max_f32_e32 v143, v200, v200
	v_med3_f32 v140, v140, s5, v190
	v_med3_f32 v143, v143, s5, v190
	v_cvt_pk_fp8_f32 v194, v140, v143 op_sel:[0,0,1]
	s_waitcnt lgkmcnt(3)
	v_max_f32_e32 v140, v201, v201
	s_waitcnt lgkmcnt(2)
	v_max_f32_e32 v143, v202, v202
	v_med3_f32 v140, v140, s5, v190
	v_med3_f32 v143, v143, s5, v190
	v_mov_b32_e32 v195, 0
	v_cvt_pk_fp8_f32 v195, v140, v143
	s_waitcnt lgkmcnt(1)
	v_max_f32_e32 v140, v203, v203
	s_waitcnt lgkmcnt(0)
	v_max_f32_e32 v143, v204, v204
	v_med3_f32 v140, v140, s5, v190
	v_med3_f32 v143, v143, s5, v190
	v_cvt_pk_fp8_f32 v195, v140, v143 op_sel:[0,0,1]
	ds_read2_b32 v[196:197], v163 offset1:32
	ds_read2_b32 v[198:199], v163 offset0:64 offset1:96
	ds_read2_b32 v[200:201], v163 offset0:128 offset1:160
	ds_read2_b32 v[202:203], v163 offset0:192 offset1:224
	ds_read_b32 v140, v164
	ds_read_b32 v143, v165
	ds_read_b32 v191, v166
	ds_read_b32 v204, v167
	ds_read_b32 v205, v168
	ds_read_b32 v206, v169
	ds_read_b32 v207, v170
	ds_read_b32 v208, v171
	s_waitcnt lgkmcnt(11)
	v_max_f32_e32 v196, v196, v196
	v_med3_f32 v209, v196, s5, v190
	v_max_f32_e32 v196, v197, v197
	v_med3_f32 v197, v196, s5, v190
	v_mov_b32_e32 v196, 0
	v_cvt_pk_fp8_f32 v196, v209, v197
	s_waitcnt lgkmcnt(10)
	v_max_f32_e32 v197, v198, v198
	v_max_f32_e32 v198, v199, v199
	v_med3_f32 v197, v197, s5, v190
	v_med3_f32 v198, v198, s5, v190
	v_cvt_pk_fp8_f32 v196, v197, v198 op_sel:[0,0,1]
	s_waitcnt lgkmcnt(9)
	v_max_f32_e32 v197, v200, v200
	v_med3_f32 v198, v197, s5, v190
	v_max_f32_e32 v197, v201, v201
	v_med3_f32 v199, v197, s5, v190
	v_mov_b32_e32 v197, 0
	v_cvt_pk_fp8_f32 v197, v198, v199
	s_waitcnt lgkmcnt(8)
	v_max_f32_e32 v198, v202, v202
	v_max_f32_e32 v199, v203, v203
	v_med3_f32 v198, v198, s5, v190
	v_med3_f32 v199, v199, s5, v190
	s_waitcnt lgkmcnt(7)
	v_max_f32_e32 v140, v140, v140
	s_waitcnt lgkmcnt(6)
	v_max_f32_e32 v143, v143, v143
	v_cvt_pk_fp8_f32 v197, v198, v199 op_sel:[0,0,1]
	v_med3_f32 v140, v140, s5, v190
	v_med3_f32 v143, v143, s5, v190
	v_mov_b32_e32 v198, 0
	v_cvt_pk_fp8_f32 v198, v140, v143
	s_waitcnt lgkmcnt(5)
	v_max_f32_e32 v140, v191, v191
	s_waitcnt lgkmcnt(4)
	v_max_f32_e32 v143, v204, v204
	v_med3_f32 v140, v140, s5, v190
	v_med3_f32 v143, v143, s5, v190
	v_cvt_pk_fp8_f32 v198, v140, v143 op_sel:[0,0,1]
	s_waitcnt lgkmcnt(3)
	v_max_f32_e32 v140, v205, v205
	s_waitcnt lgkmcnt(2)
	v_max_f32_e32 v143, v206, v206
	v_med3_f32 v140, v140, s5, v190
	v_med3_f32 v143, v143, s5, v190
	v_mov_b32_e32 v199, 0
	v_cvt_pk_fp8_f32 v199, v140, v143
	s_waitcnt lgkmcnt(1)
	v_max_f32_e32 v140, v207, v207
	s_waitcnt lgkmcnt(0)
	v_max_f32_e32 v143, v208, v208
	v_med3_f32 v140, v140, s5, v190
	v_med3_f32 v143, v143, s5, v190
	v_cvt_pk_fp8_f32 v199, v140, v143 op_sel:[0,0,1]
	v_lshl_add_u64 v[144:145], s[6:7], 0, v[130:131]
	v_lshl_add_u64 v[200:201], v[144:145], 0, v[132:133]
	global_store_dwordx4 v[200:201], v[192:195], off nt
	s_andn2_b64 vcc, exec, s[10:11]
	s_mov_b64 s[10:11], 0
	v_lshl_add_u64 v[192:193], v[144:145], 0, v[134:135]
	global_store_dwordx4 v[192:193], v[196:199], off nt
	ds_read2_b32 v[192:193], v172 offset1:32
	ds_read2_b32 v[194:195], v172 offset0:64 offset1:96
	ds_read2_b32 v[196:197], v172 offset0:128 offset1:160
	ds_read2_b32 v[198:199], v172 offset0:192 offset1:224
	ds_read_b32 v140, v173
	ds_read_b32 v143, v174
	ds_read_b32 v191, v175
	ds_read_b32 v200, v176
	ds_read_b32 v201, v177
	ds_read_b32 v202, v178
	ds_read_b32 v203, v179
	ds_read_b32 v204, v180
	s_waitcnt lgkmcnt(11)
; #define GAS __attribute__((address_space(1)))
; __device__ __forceinline__ TItem8 p8_decode(const Args& args, unsigned char* ws, int it) {
;     TItem8 t;
;     if (it >= P8_N) { const int j = it - P8_N; it = (P8_E0 + j / P8_DN1) * (P8_GU1 + P8_DN1) + P8_GU1 + j % P8_DN1; }
;     else if (it >= P8_E0 * (P8_GU1 + P8_DN1)) { const int r = it - P8_E0 * (P8_GU1 + P8_DN1); it = (P8_E0 + r / P8_GU1) * (P8_GU1 + P8_DN1) + r % P8_GU1; }
;     const int e = it / (P8_GU1 + P8_DN1), q = it % (P8_GU1 + P8_DN1);
;     if (q < P8_GU1) { const int kb = q / 128, nb = q % 128, n0 = nb * 32;
;         const int dr = (n0 < DE) ? (256 * (n0 / 128) + (n0 % 128)) : (256 * ((n0 - DE) / 128) + 128 + ((n0 - DE) % 128));
;         t.src = args.in[25] + (size_t)e * D * 2 * DE + (size_t)(kb * 128) * (2 * DE) + n0; t.N = 2 * DE; t.dst = ws + WS_WGU + (size_t)e * 2 * DE * D + (size_t)dr * D + kb * 128; t.Kd = D; }
; __device__ __forceinline__ void p8_finish(const TItem8& t, const f32x4 (&v)[16], LAS float* scr, int lane) {
;     ...
;     for (int j = 0; j < 4; ++j) { const int n = (lane >> 3) + 8 * j; float x[16];
; #pragma unroll
;         for (int i = 0; i < 16; ++i) { const int k = 16 * c + i; x[i] = scr[k * 32 + ((((n >> 2) ^ ((k >> 3) & 7)) << 2) | (n & 3))]; }
;         int w[4];
; #pragma unroll
;         for (int g = 0; g < 4; ++g) { int q = 0; q = __builtin_amdgcn_cvt_pk_fp8_f32(fminf(fmaxf(x[4 * g], -448.f), 448.f), fminf(fmaxf(x[4 * g + 1], -448.f), 448.f), q, false);
;             q = __builtin_amdgcn_cvt_pk_fp8_f32(fminf(fmaxf(x[4 * g + 2], -448.f), 448.f), fminf(fmaxf(x[4 * g + 3], -448.f), 448.f), q, true); w[g] = q; }
;         v4u o; o.x = (unsigned)w[0]; o.y = (unsigned)w[1]; o.z = (unsigned)w[2]; o.w = (unsigned)w[3];
;         __builtin_nontemporal_store(o, (GAS v4u*)(t.dst + (size_t)n * t.Kd + 16 * c)); }
	v_max_f32_e32 v192, v192, v192
	v_med3_f32 v205, v192, s5, v190
	v_max_f32_e32 v192, v193, v193
	v_med3_f32 v193, v192, s5, v190
	v_mov_b32_e32 v192, 0
	v_cvt_pk_fp8_f32 v192, v205, v193
	s_waitcnt lgkmcnt(10)
	v_max_f32_e32 v193, v194, v194
	v_max_f32_e32 v194, v195, v195
	v_med3_f32 v193, v193, s5, v190
	v_med3_f32 v194, v194, s5, v190
	v_cvt_pk_fp8_f32 v192, v193, v194 op_sel:[0,0,1]
	s_waitcnt lgkmcnt(9)
	v_max_f32_e32 v193, v196, v196
	v_med3_f32 v194, v193, s5, v190
	v_max_f32_e32 v193, v197, v197
	v_med3_f32 v195, v193, s5, v190
	v_mov_b32_e32 v193, 0
	v_cvt_pk_fp8_f32 v193, v194, v195
	s_waitcnt lgkmcnt(8)
	v_max_f32_e32 v194, v198, v198
	v_max_f32_e32 v195, v199, v199
	v_med3_f32 v194, v194, s5, v190
	v_med3_f32 v195, v195, s5, v190
	s_waitcnt lgkmcnt(7)
	v_max_f32_e32 v140, v140, v140
	s_waitcnt lgkmcnt(6)
	v_max_f32_e32 v143, v143, v143
	v_cvt_pk_fp8_f32 v193, v194, v195 op_sel:[0,0,1]
	v_med3_f32 v140, v140, s5, v190
	v_med3_f32 v143, v143, s5, v190
	v_mov_b32_e32 v194, 0
	v_cvt_pk_fp8_f32 v194, v140, v143
	s_waitcnt lgkmcnt(5)
	v_max_f32_e32 v140, v191, v191
	s_waitcnt lgkmcnt(4)
	v_max_f32_e32 v143, v200, v200
	v_med3_f32 v140, v140, s5, v190
	v_med3_f32 v143, v143, s5, v190
	v_cvt_pk_fp8_f32 v194, v140, v143 op_sel:[0,0,1]
	s_waitcnt lgkmcnt(3)
	v_max_f32_e32 v140, v201, v201
	s_waitcnt lgkmcnt(2)
	v_max_f32_e32 v143, v202, v202
	v_med3_f32 v140, v140, s5, v190
	v_med3_f32 v143, v143, s5, v190
	v_mov_b32_e32 v195, 0
	v_cvt_pk_fp8_f32 v195, v140, v143
	s_waitcnt lgkmcnt(1)
	v_max_f32_e32 v140, v203, v203
	s_waitcnt lgkmcnt(0)
	v_max_f32_e32 v143, v204, v204
	v_med3_f32 v140, v140, s5, v190
	v_med3_f32 v143, v143, s5, v190
	v_cvt_pk_fp8_f32 v195, v140, v143 op_sel:[0,0,1]
	ds_read2_b32 v[196:197], v181 offset1:32
	ds_read2_b32 v[198:199], v181 offset0:64 offset1:96
	ds_read2_b32 v[200:201], v181 offset0:128 offset1:160
	ds_read2_b32 v[202:203], v181 offset0:192 offset1:224
	ds_read_b32 v140, v182
	ds_read_b32 v143, v183
	ds_read_b32 v191, v184
	ds_read_b32 v204, v185
	ds_read_b32 v205, v186
	ds_read_b32 v206, v187
	ds_read_b32 v207, v188
	ds_read_b32 v208, v189
	s_waitcnt lgkmcnt(11)
	v_max_f32_e32 v196, v196, v196
	v_med3_f32 v209, v196, s5, v190
	v_max_f32_e32 v196, v197, v197
	v_med3_f32 v197, v196, s5, v190
	v_mov_b32_e32 v196, 0
	v_cvt_pk_fp8_f32 v196, v209, v197
	s_waitcnt lgkmcnt(10)
	v_max_f32_e32 v197, v198, v198
	v_max_f32_e32 v198, v199, v199
	v_med3_f32 v197, v197, s5, v190
	v_med3_f32 v198, v198, s5, v190
	v_cvt_pk_fp8_f32 v196, v197, v198 op_sel:[0,0,1]
	s_waitcnt lgkmcnt(9)
	v_max_f32_e32 v197, v200, v200
	v_med3_f32 v198, v197, s5, v190
	v_max_f32_e32 v197, v201, v201
	v_med3_f32 v199, v197, s5, v190
	v_mov_b32_e32 v197, 0
	v_cvt_pk_fp8_f32 v197, v198, v199
	s_waitcnt lgkmcnt(8)
	v_max_f32_e32 v198, v202, v202
	v_max_f32_e32 v199, v203, v203
	v_med3_f32 v198, v198, s5, v190
	v_med3_f32 v199, v199, s5, v190
	s_waitcnt lgkmcnt(7)
	v_max_f32_e32 v140, v140, v140
	s_waitcnt lgkmcnt(6)
	v_max_f32_e32 v143, v143, v143
	v_cvt_pk_fp8_f32 v197, v198, v199 op_sel:[0,0,1]
	v_med3_f32 v140, v140, s5, v190
	v_med3_f32 v143, v143, s5, v190
	v_mov_b32_e32 v198, 0
	v_cvt_pk_fp8_f32 v198, v140, v143
	s_waitcnt lgkmcnt(5)
	v_max_f32_e32 v140, v191, v191
	s_waitcnt lgkmcnt(4)
	v_max_f32_e32 v143, v204, v204
	v_med3_f32 v140, v140, s5, v190
	v_med3_f32 v143, v143, s5, v190
	v_cvt_pk_fp8_f32 v198, v140, v143 op_sel:[0,0,1]
	s_waitcnt lgkmcnt(3)
	v_max_f32_e32 v140, v205, v205
	s_waitcnt lgkmcnt(2)
	v_max_f32_e32 v143, v206, v206
	v_med3_f32 v140, v140, s5, v190
	v_med3_f32 v143, v143, s5, v190
	v_mov_b32_e32 v199, 0
	v_cvt_pk_fp8_f32 v199, v140, v143
	s_waitcnt lgkmcnt(1)
	v_max_f32_e32 v140, v207, v207
	s_waitcnt lgkmcnt(0)
	v_max_f32_e32 v143, v208, v208
	v_med3_f32 v140, v140, s5, v190
	v_med3_f32 v143, v143, s5, v190
	v_cvt_pk_fp8_f32 v199, v140, v143 op_sel:[0,0,1]
	v_lshl_add_u64 v[200:201], v[144:145], 0, v[136:137]
	v_lshl_add_u64 v[144:145], v[144:145], 0, v[138:139]
	global_store_dwordx4 v[200:201], v[192:195], off nt
	global_store_dwordx4 v[144:145], v[196:199], off nt
	s_waitcnt lgkmcnt(0)
	s_cbranch_vccnz .LBB0_403
	s_add_i32 s23, s23, 2
	s_mul_i32 s0, s23, 0xc0
	s_add_i32 s0, s0, s22
	s_cmpk_lt_i32 s0, 0x6acd
	s_cselect_b64 s[10:11], -1, 0
	s_cmpk_gt_i32 s0, 0x6acc
	s_cbranch_scc1 .LBB0_425
	s_mul_hi_i32 s6, s0, 0x2aaaaaab
	s_lshr_b32 s7, s6, 31
	s_ashr_i32 s6, s6, 9
	s_add_i32 s6, s6, s7
	s_mul_i32 s7, s6, 0xc00
	s_sub_i32 s24, s0, s7
	s_cmpk_gt_i32 s24, 0x7ff
	s_mov_b64 s[54:55], -1
	s_cbranch_scc0 .LBB0_418
	s_ashr_i32 s7, s6, 31
	s_lshl_b64 s[16:17], s[6:7], 22
	s_lshl_b64 s[12:13], s[6:7], 24
	s_add_u32 s7, s42, s12
	s_addc_u32 s14, s43, s13
	s_lshl_b32 s0, s24, 1
	s_and_b32 s0, s0, 0x7fffff80
	s_addk_i32 s0, 0xf000
	s_lshl_b64 s[12:13], s[0:1], 13
	s_add_u32 s7, s7, s12
	s_addc_u32 s15, s14, s13
	s_lshl_b32 s12, s24, 5
	s_and_b32 s12, s12, 0x7e0
	s_lshl_b32 s14, s12, 2
	s_add_u32 s14, s7, s14
	s_addc_u32 s15, s15, 0
	s_add_u32 s18, s2, s16
	s_mov_b32 s13, s1
	s_addc_u32 s19, s3, s17
	s_mov_b64 s[54:55], 0
	s_mov_b64 s[16:17], s[0:1]

; #define GAS __attribute__((address_space(1)))
; __device__ __forceinline__ void p8_finish(const TItem8& t, const f32x4 (&v)[16], LAS float* scr, int lane) {
;     ...
;     for (int j = 0; j < 4; ++j) { const int n = (lane >> 3) + 8 * j; float x[16];
; #pragma unroll
;         for (int i = 0; i < 16; ++i) { const int k = 16 * c + i; x[i] = scr[k * 32 + ((((n >> 2) ^ ((k >> 3) & 7)) << 2) | (n & 3))]; }
;         int w[4];
; #pragma unroll
;         for (int g = 0; g < 4; ++g) { int q = 0; q = __builtin_amdgcn_cvt_pk_fp8_f32(fminf(fmaxf(x[4 * g], -448.f), 448.f), fminf(fmaxf(x[4 * g + 1], -448.f), 448.f), q, false);
;             q = __builtin_amdgcn_cvt_pk_fp8_f32(fminf(fmaxf(x[4 * g + 2], -448.f), 448.f), fminf(fmaxf(x[4 * g + 3], -448.f), 448.f), q, true); w[g] = q; }
;         v4u o; o.x = (unsigned)w[0]; o.y = (unsigned)w[1]; o.z = (unsigned)w[2]; o.w = (unsigned)w[3];
;         __builtin_nontemporal_store(o, (GAS v4u*)(t.dst + (size_t)n * t.Kd + 16 * c)); }
.Lcv2_8_414:
	s_waitcnt lgkmcnt(0)
	ds_read2_b32 v[192:193], v154 offset1:32
	ds_read2_b32 v[194:195], v154 offset0:64 offset1:96
	ds_read2_b32 v[196:197], v154 offset0:128 offset1:160
	ds_read2_b32 v[198:199], v154 offset0:192 offset1:224
	ds_read_b32 v140, v155
	ds_read_b32 v143, v156
	ds_read_b32 v191, v157
	ds_read_b32 v200, v158
	ds_read_b32 v201, v159
	ds_read_b32 v202, v160
	ds_read_b32 v203, v161
	ds_read_b32 v204, v162
	s_waitcnt lgkmcnt(11)
	v_max_f32_e32 v192, v192, v192
	v_med3_f32 v205, v192, s5, v190
	v_max_f32_e32 v192, v193, v193
	v_med3_f32 v193, v192, s5, v190
	v_mov_b32_e32 v192, v141
	v_cvt_pk_fp8_f32 v192, v205, v193
	s_waitcnt lgkmcnt(10)
	v_max_f32_e32 v193, v194, v194
	v_max_f32_e32 v194, v195, v195
	v_med3_f32 v193, v193, s5, v190
	v_med3_f32 v194, v194, s5, v190
	v_cvt_pk_fp8_f32 v192, v193, v194 op_sel:[0,0,1]
	s_waitcnt lgkmcnt(9)
	v_max_f32_e32 v193, v196, v196
	v_med3_f32 v194, v193, s5, v190
	v_max_f32_e32 v193, v197, v197
	v_med3_f32 v195, v193, s5, v190
	v_mov_b32_e32 v193, v141
	v_cvt_pk_fp8_f32 v193, v194, v195
	s_waitcnt lgkmcnt(8)
	v_max_f32_e32 v194, v198, v198
	v_max_f32_e32 v195, v199, v199
	v_med3_f32 v194, v194, s5, v190
	v_med3_f32 v195, v195, s5, v190
	s_waitcnt lgkmcnt(7)
	v_max_f32_e32 v140, v140, v140
	s_waitcnt lgkmcnt(6)
	v_max_f32_e32 v143, v143, v143
	v_cvt_pk_fp8_f32 v193, v194, v195 op_sel:[0,0,1]
	v_med3_f32 v140, v140, s5, v190
	v_med3_f32 v143, v143, s5, v190
	v_mov_b32_e32 v194, v141
	v_cvt_pk_fp8_f32 v194, v140, v143
	s_waitcnt lgkmcnt(5)
	v_max_f32_e32 v140, v191, v191
	s_waitcnt lgkmcnt(4)
	v_max_f32_e32 v143, v200, v200
	v_med3_f32 v140, v140, s5, v190
	v_med3_f32 v143, v143, s5, v190
	v_cvt_pk_fp8_f32 v194, v140, v143 op_sel:[0,0,1]
	s_waitcnt lgkmcnt(3)
	v_max_f32_e32 v140, v201, v201
	s_waitcnt lgkmcnt(2)
	v_max_f32_e32 v143, v202, v202
	v_med3_f32 v140, v140, s5, v190
	v_med3_f32 v143, v143, s5, v190
	v_mov_b32_e32 v195, v141
	v_cvt_pk_fp8_f32 v195, v140, v143
	s_waitcnt lgkmcnt(1)
	v_max_f32_e32 v140, v203, v203
	s_waitcnt lgkmcnt(0)
	v_max_f32_e32 v143, v204, v204
	v_med3_f32 v140, v140, s5, v190
	v_med3_f32 v143, v143, s5, v190
	v_cvt_pk_fp8_f32 v195, v140, v143 op_sel:[0,0,1]
	ds_read2_b32 v[196:197], v163 offset1:32
	ds_read2_b32 v[198:199], v163 offset0:64 offset1:96
	ds_read2_b32 v[200:201], v163 offset0:128 offset1:160
	ds_read2_b32 v[202:203], v163 offset0:192 offset1:224
	ds_read_b32 v140, v164
	ds_read_b32 v143, v165
	ds_read_b32 v191, v166
	ds_read_b32 v204, v167
	ds_read_b32 v205, v168
	ds_read_b32 v206, v169
	ds_read_b32 v207, v170
	ds_read_b32 v208, v171
	s_waitcnt lgkmcnt(11)
	v_max_f32_e32 v196, v196, v196
	v_med3_f32 v209, v196, s5, v190
	v_max_f32_e32 v196, v197, v197
	v_med3_f32 v197, v196, s5, v190
	v_mov_b32_e32 v196, v141
	v_cvt_pk_fp8_f32 v196, v209, v197
	s_waitcnt lgkmcnt(10)
	v_max_f32_e32 v197, v198, v198
	v_max_f32_e32 v198, v199, v199
	v_med3_f32 v197, v197, s5, v190
	v_med3_f32 v198, v198, s5, v190
	v_cvt_pk_fp8_f32 v196, v197, v198 op_sel:[0,0,1]
	s_waitcnt lgkmcnt(9)
	v_max_f32_e32 v197, v200, v200
	v_med3_f32 v198, v197, s5, v190
	v_max_f32_e32 v197, v201, v201
	v_med3_f32 v199, v197, s5, v190
	v_mov_b32_e32 v197, v141
	v_cvt_pk_fp8_f32 v197, v198, v199
	s_waitcnt lgkmcnt(8)
	v_max_f32_e32 v198, v202, v202
	v_max_f32_e32 v199, v203, v203
	v_med3_f32 v198, v198, s5, v190
	v_med3_f32 v199, v199, s5, v190
	s_waitcnt lgkmcnt(7)
	v_max_f32_e32 v140, v140, v140
	s_waitcnt lgkmcnt(6)
	v_max_f32_e32 v143, v143, v143
	v_cvt_pk_fp8_f32 v197, v198, v199 op_sel:[0,0,1]
	v_med3_f32 v140, v140, s5, v190
	v_med3_f32 v143, v143, s5, v190
	v_mov_b32_e32 v198, v141
	v_cvt_pk_fp8_f32 v198, v140, v143
	s_waitcnt lgkmcnt(5)
	v_max_f32_e32 v140, v191, v191
	s_waitcnt lgkmcnt(4)
	v_max_f32_e32 v143, v204, v204
	v_med3_f32 v140, v140, s5, v190
	v_med3_f32 v143, v143, s5, v190
	v_cvt_pk_fp8_f32 v198, v140, v143 op_sel:[0,0,1]
	s_waitcnt lgkmcnt(3)
	v_max_f32_e32 v140, v205, v205
	s_waitcnt lgkmcnt(2)
	v_max_f32_e32 v143, v206, v206
	v_med3_f32 v140, v140, s5, v190
	v_med3_f32 v143, v143, s5, v190
	v_mov_b32_e32 v199, v141
	v_cvt_pk_fp8_f32 v199, v140, v143
	s_waitcnt lgkmcnt(1)
	v_max_f32_e32 v140, v207, v207
	s_waitcnt lgkmcnt(0)
	v_max_f32_e32 v143, v208, v208
	v_med3_f32 v140, v140, s5, v190
	v_med3_f32 v143, v143, s5, v190
	v_cvt_pk_fp8_f32 v199, v140, v143 op_sel:[0,0,1]
	v_lshl_add_u64 v[144:145], s[8:9], 0, v[130:131]
	v_lshl_add_u64 v[200:201], v[144:145], 0, v[132:133]
	global_store_dwordx4 v[200:201], v[192:195], off nt
	s_nop 1
	v_lshl_add_u64 v[192:193], v[144:145], 0, v[134:135]
	global_store_dwordx4 v[192:193], v[196:199], off nt
	ds_read2_b32 v[192:193], v172 offset1:32
	ds_read2_b32 v[194:195], v172 offset0:64 offset1:96
	ds_read2_b32 v[196:197], v172 offset0:128 offset1:160
	ds_read2_b32 v[198:199], v172 offset0:192 offset1:224
	ds_read_b32 v140, v173
	ds_read_b32 v143, v174
	ds_read_b32 v191, v175
	ds_read_b32 v200, v176
	ds_read_b32 v201, v177
	ds_read_b32 v202, v178
	ds_read_b32 v203, v179
	ds_read_b32 v204, v180
	s_waitcnt lgkmcnt(11)
; #define GAS __attribute__((address_space(1)))
; __device__ __forceinline__ void p8_finish(const TItem8& t, const f32x4 (&v)[16], LAS float* scr, int lane) {
;     ...
;     for (int j = 0; j < 4; ++j) { const int n = (lane >> 3) + 8 * j; float x[16];
; #pragma unroll
;         for (int i = 0; i < 16; ++i) { const int k = 16 * c + i; x[i] = scr[k * 32 + ((((n >> 2) ^ ((k >> 3) & 7)) << 2) | (n & 3))]; }
;         int w[4];
; #pragma unroll
;         for (int g = 0; g < 4; ++g) { int q = 0; q = __builtin_amdgcn_cvt_pk_fp8_f32(fminf(fmaxf(x[4 * g], -448.f), 448.f), fminf(fmaxf(x[4 * g + 1], -448.f), 448.f), q, false);
;             q = __builtin_amdgcn_cvt_pk_fp8_f32(fminf(fmaxf(x[4 * g + 2], -448.f), 448.f), fminf(fmaxf(x[4 * g + 3], -448.f), 448.f), q, true); w[g] = q; }
;         v4u o; o.x = (unsigned)w[0]; o.y = (unsigned)w[1]; o.z = (unsigned)w[2]; o.w = (unsigned)w[3];
;         __builtin_nontemporal_store(o, (GAS v4u*)(t.dst + (size_t)n * t.Kd + 16 * c)); }
	v_max_f32_e32 v192, v192, v192
	v_med3_f32 v205, v192, s5, v190
	v_max_f32_e32 v192, v193, v193
	v_med3_f32 v193, v192, s5, v190
	v_mov_b32_e32 v192, v141
	v_cvt_pk_fp8_f32 v192, v205, v193
	s_waitcnt lgkmcnt(10)
	v_max_f32_e32 v193, v194, v194
	v_max_f32_e32 v194, v195, v195
	v_med3_f32 v193, v193, s5, v190
	v_med3_f32 v194, v194, s5, v190
	v_cvt_pk_fp8_f32 v192, v193, v194 op_sel:[0,0,1]
	s_waitcnt lgkmcnt(9)
	v_max_f32_e32 v193, v196, v196
	v_med3_f32 v194, v193, s5, v190
	v_max_f32_e32 v193, v197, v197
	v_med3_f32 v195, v193, s5, v190
	v_mov_b32_e32 v193, v141
	v_cvt_pk_fp8_f32 v193, v194, v195
	s_waitcnt lgkmcnt(8)
	v_max_f32_e32 v194, v198, v198
	v_max_f32_e32 v195, v199, v199
	v_med3_f32 v194, v194, s5, v190
	v_med3_f32 v195, v195, s5, v190
	s_waitcnt lgkmcnt(7)
	v_max_f32_e32 v140, v140, v140
	s_waitcnt lgkmcnt(6)
	v_max_f32_e32 v143, v143, v143
	v_cvt_pk_fp8_f32 v193, v194, v195 op_sel:[0,0,1]
	v_med3_f32 v140, v140, s5, v190
	v_med3_f32 v143, v143, s5, v190
	v_mov_b32_e32 v194, v141
	v_cvt_pk_fp8_f32 v194, v140, v143
	s_waitcnt lgkmcnt(5)
	v_max_f32_e32 v140, v191, v191
	s_waitcnt lgkmcnt(4)
	v_max_f32_e32 v143, v200, v200
	v_med3_f32 v140, v140, s5, v190
	v_med3_f32 v143, v143, s5, v190
	v_cvt_pk_fp8_f32 v194, v140, v143 op_sel:[0,0,1]
	s_waitcnt lgkmcnt(3)
	v_max_f32_e32 v140, v201, v201
	s_waitcnt lgkmcnt(2)
	v_max_f32_e32 v143, v202, v202
	v_med3_f32 v140, v140, s5, v190
	v_med3_f32 v143, v143, s5, v190
	v_mov_b32_e32 v195, v141
	v_cvt_pk_fp8_f32 v195, v140, v143
	s_waitcnt lgkmcnt(1)
	v_max_f32_e32 v140, v203, v203
	s_waitcnt lgkmcnt(0)
	v_max_f32_e32 v143, v204, v204
	v_med3_f32 v140, v140, s5, v190
	v_med3_f32 v143, v143, s5, v190
	v_cvt_pk_fp8_f32 v195, v140, v143 op_sel:[0,0,1]
	ds_read2_b32 v[196:197], v181 offset1:32
	ds_read2_b32 v[198:199], v181 offset0:64 offset1:96
	ds_read2_b32 v[200:201], v181 offset0:128 offset1:160
	ds_read2_b32 v[202:203], v181 offset0:192 offset1:224
	ds_read_b32 v140, v182
	ds_read_b32 v143, v183
	ds_read_b32 v191, v184
	ds_read_b32 v204, v185
	ds_read_b32 v205, v186
	ds_read_b32 v206, v187
	ds_read_b32 v207, v188
	ds_read_b32 v208, v189
	s_waitcnt lgkmcnt(11)
	v_max_f32_e32 v196, v196, v196
	v_med3_f32 v209, v196, s5, v190
	v_max_f32_e32 v196, v197, v197
	v_med3_f32 v197, v196, s5, v190
	v_mov_b32_e32 v196, v141
	v_cvt_pk_fp8_f32 v196, v209, v197
	s_waitcnt lgkmcnt(10)
	v_max_f32_e32 v197, v198, v198
	v_max_f32_e32 v198, v199, v199
	v_med3_f32 v197, v197, s5, v190
	v_med3_f32 v198, v198, s5, v190
	v_cvt_pk_fp8_f32 v196, v197, v198 op_sel:[0,0,1]
	s_waitcnt lgkmcnt(9)
	v_max_f32_e32 v197, v200, v200
	v_med3_f32 v198, v197, s5, v190
	v_max_f32_e32 v197, v201, v201
	v_med3_f32 v199, v197, s5, v190
	v_mov_b32_e32 v197, v141
	v_cvt_pk_fp8_f32 v197, v198, v199
	s_waitcnt lgkmcnt(8)
	v_max_f32_e32 v198, v202, v202
	v_max_f32_e32 v199, v203, v203
	v_med3_f32 v198, v198, s5, v190
	v_med3_f32 v199, v199, s5, v190
	s_waitcnt lgkmcnt(7)
	v_max_f32_e32 v140, v140, v140
	s_waitcnt lgkmcnt(6)
	v_max_f32_e32 v143, v143, v143
	v_cvt_pk_fp8_f32 v197, v198, v199 op_sel:[0,0,1]
	v_med3_f32 v140, v140, s5, v190
	v_med3_f32 v143, v143, s5, v190
	v_mov_b32_e32 v198, v141
	v_cvt_pk_fp8_f32 v198, v140, v143
	s_waitcnt lgkmcnt(5)
	v_max_f32_e32 v140, v191, v191
	s_waitcnt lgkmcnt(4)
	v_max_f32_e32 v143, v204, v204
	v_med3_f32 v140, v140, s5, v190
	v_med3_f32 v143, v143, s5, v190
	v_cvt_pk_fp8_f32 v198, v140, v143 op_sel:[0,0,1]
	s_waitcnt lgkmcnt(3)
	v_max_f32_e32 v140, v205, v205
	s_waitcnt lgkmcnt(2)
	v_max_f32_e32 v143, v206, v206
	v_med3_f32 v140, v140, s5, v190
	v_med3_f32 v143, v143, s5, v190
	v_mov_b32_e32 v199, v141
	v_cvt_pk_fp8_f32 v199, v140, v143
	s_waitcnt lgkmcnt(1)
	v_max_f32_e32 v140, v207, v207
	s_waitcnt lgkmcnt(0)
	v_max_f32_e32 v143, v208, v208
	v_med3_f32 v140, v140, s5, v190
	v_med3_f32 v143, v143, s5, v190
	v_cvt_pk_fp8_f32 v199, v140, v143 op_sel:[0,0,1]
	v_lshl_add_u64 v[200:201], v[144:145], 0, v[136:137]
	v_lshl_add_u64 v[144:145], v[144:145], 0, v[138:139]
	global_store_dwordx4 v[200:201], v[192:195], off nt
	global_store_dwordx4 v[144:145], v[196:199], off nt
	s_waitcnt lgkmcnt(0)
	s_xor_b64 s[10:11], s[10:11], -1
	s_and_b64 vcc, exec, s[10:11]
	s_cbranch_vccz .LBB0_404

; #define GAS __attribute__((address_space(1)))
; #define LAS __attribute__((address_space(3)))
; __device__ __forceinline__ void p8_issue(const TItem8& t, f32x4 (&v)[16], int lane) {
;     const GAS f32x4* src = (const GAS f32x4*)((const GAS float*)t.src + (size_t)(lane >> 3) * t.N + 4 * (lane & 7));
; #pragma unroll
;     for (int i = 0; i < 16; ++i) v[i] = __builtin_nontemporal_load(src + (size_t)(2 * i) * t.N);
; }
; __device__ __forceinline__ void p8_finish(const TItem8& t, const f32x4 (&v)[16], LAS float* scr, int lane) {
; #pragma unroll
;     for (int i = 0; i < 16; ++i) *(LAS f32x4*)(scr + (8 * i + (lane >> 3)) * 32 + (((lane & 7) ^ (i & 7)) << 2)) = v[i] * W8_SCALE;
.LBB0_730:
	s_lshl_b64 s[12:13], s[86:87], 11
	s_add_u32 s0, s92, s12
	v_mul_u32_u24_e32 v66, s94, v225
	s_addc_u32 s12, s93, s13
	v_lshlrev_b32_e32 v142, 2, v66
	s_add_u32 s82, s0, s90
	v_lshl_add_u64 v[66:67], s[88:89], 0, v[142:143]
	v_mov_b32_e32 v145, v143
	s_addc_u32 s83, s12, s91
	v_lshl_add_u64 v[66:67], v[66:67], 0, v[144:145]
	s_lshl_b32 s0, s94, 5
	s_waitcnt vmcnt(32)
	v_lshl_add_u64 v[74:75], v[66:67], 0, s[0:1]
	global_load_dwordx4 v[66:69], v[66:67], off nt
	s_nop 0
	global_load_dwordx4 v[70:73], v[74:75], off nt
	v_lshl_add_u64 v[74:75], v[74:75], 0, s[0:1]
	s_waitcnt vmcnt(26)
	v_lshl_add_u64 v[82:83], v[74:75], 0, s[0:1]
	global_load_dwordx4 v[74:77], v[74:75], off nt
	s_nop 0
	global_load_dwordx4 v[78:81], v[82:83], off nt
	v_lshl_add_u64 v[82:83], v[82:83], 0, s[0:1]
	v_lshl_add_u64 v[90:91], v[82:83], 0, s[0:1]
	global_load_dwordx4 v[82:85], v[82:83], off nt
	s_nop 0
	global_load_dwordx4 v[86:89], v[90:91], off nt
	v_lshl_add_u64 v[90:91], v[90:91], 0, s[0:1]
	v_lshl_add_u64 v[98:99], v[90:91], 0, s[0:1]
	v_lshl_add_u64 v[102:103], v[98:99], 0, s[0:1]
	v_lshl_add_u64 v[106:107], v[102:103], 0, s[0:1]
	v_lshl_add_u64 v[110:111], v[106:107], 0, s[0:1]
	v_lshl_add_u64 v[114:115], v[110:111], 0, s[0:1]
	v_lshl_add_u64 v[118:119], v[114:115], 0, s[0:1]
	v_lshl_add_u64 v[122:123], v[118:119], 0, s[0:1]
	v_lshl_add_u64 v[126:127], v[122:123], 0, s[0:1]
	global_load_dwordx4 v[90:93], v[90:91], off nt
	s_nop 0
	global_load_dwordx4 v[94:97], v[98:99], off nt
	s_nop 0
	global_load_dwordx4 v[98:101], v[102:103], off nt
	s_nop 0
	global_load_dwordx4 v[102:105], v[106:107], off nt
	s_nop 0
	global_load_dwordx4 v[106:109], v[110:111], off nt
	s_nop 0
	global_load_dwordx4 v[110:113], v[114:115], off nt
	s_nop 0
	global_load_dwordx4 v[114:117], v[118:119], off nt
	s_nop 0
	global_load_dwordx4 v[118:121], v[122:123], off nt
	s_nop 0
	global_load_dwordx4 v[122:125], v[126:127], off nt
	v_lshl_add_u64 v[126:127], v[126:127], 0, s[0:1]
	global_load_dwordx4 v[126:129], v[126:127], off nt
	s_waitcnt vmcnt(31)
	v_pk_mul_f32 v[200:201], v[4:5], s[74:75] op_sel_hi:[1,0]
	v_pk_mul_f32 v[198:199], v[2:3], s[74:75] op_sel_hi:[1,0]
	ds_write_b128 v148, v[198:201]
	s_waitcnt vmcnt(30)
	v_pk_mul_f32 v[200:201], v[8:9], s[74:75] op_sel_hi:[1,0]
	v_pk_mul_f32 v[198:199], v[6:7], s[74:75] op_sel_hi:[1,0]
	ds_write_b128 v149, v[198:201] offset:1024
	s_waitcnt vmcnt(29)
	v_pk_mul_f32 v[200:201], v[12:13], s[74:75] op_sel_hi:[1,0]
	v_pk_mul_f32 v[198:199], v[10:11], s[74:75] op_sel_hi:[1,0]
	ds_write_b128 v150, v[198:201] offset:2048
	s_waitcnt vmcnt(28)
	v_pk_mul_f32 v[200:201], v[16:17], s[74:75] op_sel_hi:[1,0]
	v_pk_mul_f32 v[198:199], v[14:15], s[74:75] op_sel_hi:[1,0]
	ds_write_b128 v151, v[198:201] offset:3072
	s_waitcnt vmcnt(27)
	v_pk_mul_f32 v[200:201], v[20:21], s[74:75] op_sel_hi:[1,0]
	v_pk_mul_f32 v[198:199], v[18:19], s[74:75] op_sel_hi:[1,0]
	ds_write_b128 v152, v[198:201] offset:4096
	s_waitcnt vmcnt(26)
	v_pk_mul_f32 v[200:201], v[24:25], s[74:75] op_sel_hi:[1,0]
	v_pk_mul_f32 v[198:199], v[22:23], s[74:75] op_sel_hi:[1,0]
	ds_write_b128 v153, v[198:201] offset:5120
	s_waitcnt vmcnt(25)
	v_pk_mul_f32 v[200:201], v[28:29], s[74:75] op_sel_hi:[1,0]
	v_pk_mul_f32 v[198:199], v[26:27], s[74:75] op_sel_hi:[1,0]
	ds_write_b128 v154, v[198:201] offset:6144
	s_waitcnt vmcnt(24)
	v_pk_mul_f32 v[200:201], v[32:33], s[74:75] op_sel_hi:[1,0]
	v_pk_mul_f32 v[198:199], v[30:31], s[74:75] op_sel_hi:[1,0]
	ds_write_b128 v155, v[198:201] offset:7168
	s_waitcnt vmcnt(23)
	v_pk_mul_f32 v[200:201], v[36:37], s[74:75] op_sel_hi:[1,0]
	v_pk_mul_f32 v[198:199], v[34:35], s[74:75] op_sel_hi:[1,0]
	ds_write_b128 v148, v[198:201] offset:8192
	s_waitcnt vmcnt(22)
	v_pk_mul_f32 v[200:201], v[40:41], s[74:75] op_sel_hi:[1,0]
	v_pk_mul_f32 v[198:199], v[38:39], s[74:75] op_sel_hi:[1,0]
	ds_write_b128 v149, v[198:201] offset:9216
	s_waitcnt vmcnt(21)
	v_pk_mul_f32 v[200:201], v[44:45], s[74:75] op_sel_hi:[1,0]
	v_pk_mul_f32 v[198:199], v[42:43], s[74:75] op_sel_hi:[1,0]
	ds_write_b128 v150, v[198:201] offset:10240
	s_waitcnt vmcnt(20)
	v_pk_mul_f32 v[200:201], v[48:49], s[74:75] op_sel_hi:[1,0]
	v_pk_mul_f32 v[198:199], v[46:47], s[74:75] op_sel_hi:[1,0]
	ds_write_b128 v151, v[198:201] offset:11264
	s_waitcnt vmcnt(19)
	v_pk_mul_f32 v[200:201], v[52:53], s[74:75] op_sel_hi:[1,0]
	v_pk_mul_f32 v[198:199], v[50:51], s[74:75] op_sel_hi:[1,0]
	ds_write_b128 v152, v[198:201] offset:12288
	s_waitcnt vmcnt(18)
	v_pk_mul_f32 v[200:201], v[56:57], s[74:75] op_sel_hi:[1,0]
	v_pk_mul_f32 v[198:199], v[54:55], s[74:75] op_sel_hi:[1,0]
	ds_write_b128 v153, v[198:201] offset:13312
	s_waitcnt vmcnt(17)
	v_pk_mul_f32 v[200:201], v[60:61], s[74:75] op_sel_hi:[1,0]
	v_pk_mul_f32 v[198:199], v[58:59], s[74:75] op_sel_hi:[1,0]
	ds_write_b128 v154, v[198:201] offset:14336
	s_waitcnt vmcnt(16)
	v_pk_mul_f32 v[200:201], v[64:65], s[74:75] op_sel_hi:[1,0]
	v_pk_mul_f32 v[198:199], v[62:63], s[74:75] op_sel_hi:[1,0]
	ds_write_b128 v155, v[198:201] offset:15360
	s_branch .Lcv1_7_731

; #define GAS __attribute__((address_space(1)))
; __device__ __forceinline__ void p8_finish(const TItem8& t, const f32x4 (&v)[16], LAS float* scr, int lane) {
;     ...
;     for (int j = 0; j < 4; ++j) { const int n = (lane >> 3) + 8 * j; float x[16];
; #pragma unroll
;         for (int i = 0; i < 16; ++i) { const int k = 16 * c + i; x[i] = scr[k * 32 + ((((n >> 2) ^ ((k >> 3) & 7)) << 2) | (n & 3))]; }
;         int w[4];
; #pragma unroll
;         for (int g = 0; g < 4; ++g) { int q = 0; q = __builtin_amdgcn_cvt_pk_fp8_f32(fminf(fmaxf(x[4 * g], -448.f), 448.f), fminf(fmaxf(x[4 * g + 1], -448.f), 448.f), q, false);
;             q = __builtin_amdgcn_cvt_pk_fp8_f32(fminf(fmaxf(x[4 * g + 2], -448.f), 448.f), fminf(fmaxf(x[4 * g + 3], -448.f), 448.f), q, true); w[g] = q; }
;         v4u o; o.x = (unsigned)w[0]; o.y = (unsigned)w[1]; o.z = (unsigned)w[2]; o.w = (unsigned)w[3];
;         __builtin_nontemporal_store(o, (GAS v4u*)(t.dst + (size_t)n * t.Kd + 16 * c)); }
.Lcv1_7_731:
	s_waitcnt lgkmcnt(0)
	ds_read2_b32 v[198:199], v156 offset1:32
	ds_read2_b32 v[200:201], v156 offset0:64 offset1:96
	ds_read2_b32 v[202:203], v156 offset0:128 offset1:160
	ds_read2_b32 v[204:205], v156 offset0:192 offset1:224
	ds_read_b32 v142, v157
	ds_read_b32 v145, v158
	ds_read_b32 v206, v159
	ds_read_b32 v207, v160
	ds_read_b32 v208, v161
	ds_read_b32 v209, v162
	ds_read_b32 v210, v163
	ds_read_b32 v211, v164
	s_waitcnt lgkmcnt(11)
	v_max_f32_e32 v198, v198, v198
	v_med3_f32 v212, v198, s7, v1
	v_max_f32_e32 v198, v199, v199
	v_med3_f32 v199, v198, s7, v1
	v_mov_b32_e32 v198, 0
	v_cvt_pk_fp8_f32 v198, v212, v199
	s_waitcnt lgkmcnt(10)
	v_max_f32_e32 v199, v200, v200
	v_max_f32_e32 v200, v201, v201
	v_med3_f32 v199, v199, s7, v1
	v_med3_f32 v200, v200, s7, v1
	v_cvt_pk_fp8_f32 v198, v199, v200 op_sel:[0,0,1]
	s_waitcnt lgkmcnt(9)
	v_max_f32_e32 v199, v202, v202
	v_med3_f32 v200, v199, s7, v1
	v_max_f32_e32 v199, v203, v203
	v_med3_f32 v201, v199, s7, v1
	v_mov_b32_e32 v199, 0
	v_cvt_pk_fp8_f32 v199, v200, v201
	s_waitcnt lgkmcnt(8)
	v_max_f32_e32 v200, v204, v204
	v_max_f32_e32 v201, v205, v205
	v_med3_f32 v200, v200, s7, v1
	v_med3_f32 v201, v201, s7, v1
	s_waitcnt lgkmcnt(7)
	v_max_f32_e32 v142, v142, v142
	s_waitcnt lgkmcnt(6)
	v_max_f32_e32 v145, v145, v145
	v_cvt_pk_fp8_f32 v199, v200, v201 op_sel:[0,0,1]
	v_med3_f32 v142, v142, s7, v1
	v_med3_f32 v145, v145, s7, v1
	v_mov_b32_e32 v200, 0
	v_cvt_pk_fp8_f32 v200, v142, v145
	s_waitcnt lgkmcnt(5)
	v_max_f32_e32 v142, v206, v206
	s_waitcnt lgkmcnt(4)
	v_max_f32_e32 v145, v207, v207
	v_med3_f32 v142, v142, s7, v1
	v_med3_f32 v145, v145, s7, v1
	v_cvt_pk_fp8_f32 v200, v142, v145 op_sel:[0,0,1]
	s_waitcnt lgkmcnt(3)
	v_max_f32_e32 v142, v208, v208
	s_waitcnt lgkmcnt(2)
	v_max_f32_e32 v145, v209, v209
	v_med3_f32 v142, v142, s7, v1
	v_med3_f32 v145, v145, s7, v1
	v_mov_b32_e32 v201, 0
	v_cvt_pk_fp8_f32 v201, v142, v145
	s_waitcnt lgkmcnt(1)
	v_max_f32_e32 v142, v210, v210
	s_waitcnt lgkmcnt(0)
	v_max_f32_e32 v145, v211, v211
	v_med3_f32 v142, v142, s7, v1
	v_med3_f32 v145, v145, s7, v1
	v_cvt_pk_fp8_f32 v201, v142, v145 op_sel:[0,0,1]
	ds_read2_b32 v[202:203], v165 offset1:32
	ds_read2_b32 v[204:205], v165 offset0:64 offset1:96
	ds_read2_b32 v[206:207], v165 offset0:128 offset1:160
	ds_read2_b32 v[208:209], v165 offset0:192 offset1:224
	ds_read_b32 v142, v166
	ds_read_b32 v145, v167
	ds_read_b32 v210, v168
	ds_read_b32 v211, v169
	ds_read_b32 v212, v170
	ds_read_b32 v213, v171
	ds_read_b32 v214, v172
	ds_read_b32 v215, v173
	s_waitcnt lgkmcnt(11)
	v_max_f32_e32 v202, v202, v202
	v_med3_f32 v216, v202, s7, v1
	v_max_f32_e32 v202, v203, v203
	v_med3_f32 v203, v202, s7, v1
	v_mov_b32_e32 v202, 0
	v_cvt_pk_fp8_f32 v202, v216, v203
	s_waitcnt lgkmcnt(10)
	v_max_f32_e32 v203, v204, v204
	v_max_f32_e32 v204, v205, v205
	v_med3_f32 v203, v203, s7, v1
	v_med3_f32 v204, v204, s7, v1
	v_cvt_pk_fp8_f32 v202, v203, v204 op_sel:[0,0,1]
	s_waitcnt lgkmcnt(9)
	v_max_f32_e32 v203, v206, v206
	v_med3_f32 v204, v203, s7, v1
	v_max_f32_e32 v203, v207, v207
	v_med3_f32 v205, v203, s7, v1
	v_mov_b32_e32 v203, 0
	v_cvt_pk_fp8_f32 v203, v204, v205
	s_waitcnt lgkmcnt(8)
	v_max_f32_e32 v204, v208, v208
	v_max_f32_e32 v205, v209, v209
	v_med3_f32 v204, v204, s7, v1
	v_med3_f32 v205, v205, s7, v1
	s_waitcnt lgkmcnt(7)
	v_max_f32_e32 v142, v142, v142
	s_waitcnt lgkmcnt(6)
	v_max_f32_e32 v145, v145, v145
	v_cvt_pk_fp8_f32 v203, v204, v205 op_sel:[0,0,1]
	v_med3_f32 v142, v142, s7, v1
	v_med3_f32 v145, v145, s7, v1
	v_mov_b32_e32 v204, 0
	v_cvt_pk_fp8_f32 v204, v142, v145
	s_waitcnt lgkmcnt(5)
	v_max_f32_e32 v142, v210, v210
	s_waitcnt lgkmcnt(4)
	v_max_f32_e32 v145, v211, v211
	v_med3_f32 v142, v142, s7, v1
	v_med3_f32 v145, v145, s7, v1
	v_cvt_pk_fp8_f32 v204, v142, v145 op_sel:[0,0,1]
	s_waitcnt lgkmcnt(3)
	v_max_f32_e32 v142, v212, v212
	s_waitcnt lgkmcnt(2)
	v_max_f32_e32 v145, v213, v213
	v_med3_f32 v142, v142, s7, v1
	v_med3_f32 v145, v145, s7, v1
	v_mov_b32_e32 v205, 0
	v_cvt_pk_fp8_f32 v205, v142, v145
	s_waitcnt lgkmcnt(1)
	v_max_f32_e32 v142, v214, v214
	s_waitcnt lgkmcnt(0)
	v_max_f32_e32 v145, v215, v215
	v_med3_f32 v142, v142, s7, v1
	v_med3_f32 v145, v145, s7, v1
	v_cvt_pk_fp8_f32 v205, v142, v145 op_sel:[0,0,1]
	v_lshl_add_u64 v[146:147], s[80:81], 0, v[130:131]
	v_lshl_add_u64 v[206:207], v[146:147], 0, v[132:133]
	global_store_dwordx4 v[206:207], v[198:201], off nt
	s_andn2_b64 vcc, exec, s[84:85]
	s_mov_b64 s[84:85], 0
	v_lshl_add_u64 v[198:199], v[146:147], 0, v[134:135]
	global_store_dwordx4 v[198:199], v[202:205], off nt
	ds_read2_b32 v[198:199], v174 offset1:32
	ds_read2_b32 v[200:201], v174 offset0:64 offset1:96
	ds_read2_b32 v[202:203], v174 offset0:128 offset1:160
	ds_read2_b32 v[204:205], v174 offset0:192 offset1:224
	ds_read_b32 v142, v175
	ds_read_b32 v145, v176
	ds_read_b32 v206, v177
	ds_read_b32 v207, v178
	ds_read_b32 v208, v179
	ds_read_b32 v209, v180
	ds_read_b32 v210, v181
	ds_read_b32 v211, v182
	s_waitcnt lgkmcnt(11)
; #define GAS __attribute__((address_space(1)))
; __device__ __forceinline__ TItem8 p8_decode(const Args& args, unsigned char* ws, int it) {
;     TItem8 t;
;     if (it >= P8_N) { const int j = it - P8_N; it = (P8_E0 + j / P8_DN1) * (P8_GU1 + P8_DN1) + P8_GU1 + j % P8_DN1; }
;     else if (it >= P8_E0 * (P8_GU1 + P8_DN1)) { const int r = it - P8_E0 * (P8_GU1 + P8_DN1); it = (P8_E0 + r / P8_GU1) * (P8_GU1 + P8_DN1) + r % P8_GU1; }
;     const int e = it / (P8_GU1 + P8_DN1), q = it % (P8_GU1 + P8_DN1);
;     if (q < P8_GU1) { const int kb = q / 128, nb = q % 128, n0 = nb * 32;
;         const int dr = (n0 < DE) ? (256 * (n0 / 128) + (n0 % 128)) : (256 * ((n0 - DE) / 128) + 128 + ((n0 - DE) % 128));
;         t.src = args.in[25] + (size_t)e * D * 2 * DE + (size_t)(kb * 128) * (2 * DE) + n0; t.N = 2 * DE; t.dst = ws + WS_WGU + (size_t)e * 2 * DE * D + (size_t)dr * D + kb * 128; t.Kd = D; }
; __device__ __forceinline__ void p8_finish(const TItem8& t, const f32x4 (&v)[16], LAS float* scr, int lane) {
;     ...
;     for (int j = 0; j < 4; ++j) { const int n = (lane >> 3) + 8 * j; float x[16];
; #pragma unroll
;         for (int i = 0; i < 16; ++i) { const int k = 16 * c + i; x[i] = scr[k * 32 + ((((n >> 2) ^ ((k >> 3) & 7)) << 2) | (n & 3))]; }
;         int w[4];
; #pragma unroll
;         for (int g = 0; g < 4; ++g) { int q = 0; q = __builtin_amdgcn_cvt_pk_fp8_f32(fminf(fmaxf(x[4 * g], -448.f), 448.f), fminf(fmaxf(x[4 * g + 1], -448.f), 448.f), q, false);
;             q = __builtin_amdgcn_cvt_pk_fp8_f32(fminf(fmaxf(x[4 * g + 2], -448.f), 448.f), fminf(fmaxf(x[4 * g + 3], -448.f), 448.f), q, true); w[g] = q; }
;         v4u o; o.x = (unsigned)w[0]; o.y = (unsigned)w[1]; o.z = (unsigned)w[2]; o.w = (unsigned)w[3];
;         __builtin_nontemporal_store(o, (GAS v4u*)(t.dst + (size_t)n * t.Kd + 16 * c)); }
	v_max_f32_e32 v198, v198, v198
	v_med3_f32 v212, v198, s7, v1
	v_max_f32_e32 v198, v199, v199
	v_med3_f32 v199, v198, s7, v1
	v_mov_b32_e32 v198, 0
	v_cvt_pk_fp8_f32 v198, v212, v199
	s_waitcnt lgkmcnt(10)
	v_max_f32_e32 v199, v200, v200
	v_max_f32_e32 v200, v201, v201
	v_med3_f32 v199, v199, s7, v1
	v_med3_f32 v200, v200, s7, v1
	v_cvt_pk_fp8_f32 v198, v199, v200 op_sel:[0,0,1]
	s_waitcnt lgkmcnt(9)
	v_max_f32_e32 v199, v202, v202
	v_med3_f32 v200, v199, s7, v1
	v_max_f32_e32 v199, v203, v203
	v_med3_f32 v201, v199, s7, v1
	v_mov_b32_e32 v199, 0
	v_cvt_pk_fp8_f32 v199, v200, v201
	s_waitcnt lgkmcnt(8)
	v_max_f32_e32 v200, v204, v204
	v_max_f32_e32 v201, v205, v205
	v_med3_f32 v200, v200, s7, v1
	v_med3_f32 v201, v201, s7, v1
	s_waitcnt lgkmcnt(7)
	v_max_f32_e32 v142, v142, v142
	s_waitcnt lgkmcnt(6)
	v_max_f32_e32 v145, v145, v145
	v_cvt_pk_fp8_f32 v199, v200, v201 op_sel:[0,0,1]
	v_med3_f32 v142, v142, s7, v1
	v_med3_f32 v145, v145, s7, v1
	v_mov_b32_e32 v200, 0
	v_cvt_pk_fp8_f32 v200, v142, v145
	s_waitcnt lgkmcnt(5)
	v_max_f32_e32 v142, v206, v206
	s_waitcnt lgkmcnt(4)
	v_max_f32_e32 v145, v207, v207
	v_med3_f32 v142, v142, s7, v1
	v_med3_f32 v145, v145, s7, v1
	v_cvt_pk_fp8_f32 v200, v142, v145 op_sel:[0,0,1]
	s_waitcnt lgkmcnt(3)
	v_max_f32_e32 v142, v208, v208
	s_waitcnt lgkmcnt(2)
	v_max_f32_e32 v145, v209, v209
	v_med3_f32 v142, v142, s7, v1
	v_med3_f32 v145, v145, s7, v1
	v_mov_b32_e32 v201, 0
	v_cvt_pk_fp8_f32 v201, v142, v145
	s_waitcnt lgkmcnt(1)
	v_max_f32_e32 v142, v210, v210
	s_waitcnt lgkmcnt(0)
	v_max_f32_e32 v145, v211, v211
	v_med3_f32 v142, v142, s7, v1
	v_med3_f32 v145, v145, s7, v1
	v_cvt_pk_fp8_f32 v201, v142, v145 op_sel:[0,0,1]
	ds_read2_b32 v[202:203], v183 offset1:32
	ds_read2_b32 v[204:205], v183 offset0:64 offset1:96
	ds_read2_b32 v[206:207], v183 offset0:128 offset1:160
	ds_read2_b32 v[208:209], v183 offset0:192 offset1:224
	ds_read_b32 v142, v184
	ds_read_b32 v145, v185
	ds_read_b32 v210, v186
	ds_read_b32 v211, v187
	ds_read_b32 v212, v188
	ds_read_b32 v213, v189
	ds_read_b32 v214, v190
	ds_read_b32 v215, v191
	s_waitcnt lgkmcnt(11)
	v_max_f32_e32 v202, v202, v202
	v_med3_f32 v216, v202, s7, v1
	v_max_f32_e32 v202, v203, v203
	v_med3_f32 v203, v202, s7, v1
	v_mov_b32_e32 v202, 0
	v_cvt_pk_fp8_f32 v202, v216, v203
	s_waitcnt lgkmcnt(10)
	v_max_f32_e32 v203, v204, v204
	v_max_f32_e32 v204, v205, v205
	v_med3_f32 v203, v203, s7, v1
	v_med3_f32 v204, v204, s7, v1
	v_cvt_pk_fp8_f32 v202, v203, v204 op_sel:[0,0,1]
	s_waitcnt lgkmcnt(9)
	v_max_f32_e32 v203, v206, v206
	v_med3_f32 v204, v203, s7, v1
	v_max_f32_e32 v203, v207, v207
	v_med3_f32 v205, v203, s7, v1
	v_mov_b32_e32 v203, 0
	v_cvt_pk_fp8_f32 v203, v204, v205
	s_waitcnt lgkmcnt(8)
	v_max_f32_e32 v204, v208, v208
	v_max_f32_e32 v205, v209, v209
	v_med3_f32 v204, v204, s7, v1
	v_med3_f32 v205, v205, s7, v1
	s_waitcnt lgkmcnt(7)
	v_max_f32_e32 v142, v142, v142
	s_waitcnt lgkmcnt(6)
	v_max_f32_e32 v145, v145, v145
	v_cvt_pk_fp8_f32 v203, v204, v205 op_sel:[0,0,1]
	v_med3_f32 v142, v142, s7, v1
	v_med3_f32 v145, v145, s7, v1
	v_mov_b32_e32 v204, 0
	v_cvt_pk_fp8_f32 v204, v142, v145
	s_waitcnt lgkmcnt(5)
	v_max_f32_e32 v142, v210, v210
	s_waitcnt lgkmcnt(4)
	v_max_f32_e32 v145, v211, v211
	v_med3_f32 v142, v142, s7, v1
	v_med3_f32 v145, v145, s7, v1
	v_cvt_pk_fp8_f32 v204, v142, v145 op_sel:[0,0,1]
	s_waitcnt lgkmcnt(3)
	v_max_f32_e32 v142, v212, v212
	s_waitcnt lgkmcnt(2)
	v_max_f32_e32 v145, v213, v213
	v_med3_f32 v142, v142, s7, v1
	v_med3_f32 v145, v145, s7, v1
	v_mov_b32_e32 v205, 0
	v_cvt_pk_fp8_f32 v205, v142, v145
	s_waitcnt lgkmcnt(1)
	v_max_f32_e32 v142, v214, v214
	s_waitcnt lgkmcnt(0)
	v_max_f32_e32 v145, v215, v215
	v_med3_f32 v142, v142, s7, v1
	v_med3_f32 v145, v145, s7, v1
	v_cvt_pk_fp8_f32 v205, v142, v145 op_sel:[0,0,1]
	v_lshl_add_u64 v[206:207], v[146:147], 0, v[136:137]
	v_lshl_add_u64 v[146:147], v[146:147], 0, v[138:139]
	global_store_dwordx4 v[206:207], v[198:201], off nt
	global_store_dwordx4 v[146:147], v[202:205], off nt
	s_waitcnt lgkmcnt(0)
	s_cbranch_vccnz .LBB0_720
	s_add_i32 s10, s10, 2
	s_mul_i32 s0, s10, s4
	s_add_i32 s0, s0, s5
	s_cmp_lt_i32 s0, 0xaae1
	s_cselect_b64 s[84:85], -1, 0
	s_cmp_gt_i32 s0, 0xaae0
	s_cbranch_scc1 .LBB0_742
	s_mul_hi_i32 s11, s0, 0x2aaaaaab
	s_lshr_b32 s12, s11, 31
	s_ashr_i32 s11, s11, 9
	s_add_i32 s80, s11, s12
	s_mul_i32 s11, s80, 0xc00
	s_sub_i32 s11, s0, s11
	s_cmpk_gt_i32 s11, 0x7ff
	s_mov_b64 s[94:95], -1
	s_cbranch_scc0 .LBB0_735
	s_ashr_i32 s81, s80, 31
	s_lshl_b64 s[12:13], s[80:81], 22
	s_lshl_b64 s[14:15], s[80:81], 24
	s_add_u32 s16, s42, s14
	s_addc_u32 s17, s43, s15
	s_lshl_b32 s0, s11, 1
	s_and_b32 s0, s0, 0x7fffff80
	s_addk_i32 s0, 0xf000
	s_lshl_b64 s[14:15], s[0:1], 13
	s_add_u32 s14, s16, s14
	s_addc_u32 s15, s17, s15
	s_lshl_b32 s16, s11, 5
	s_and_b32 s86, s16, 0x7e0
	s_lshl_b32 s16, s86, 2
	s_add_u32 s88, s14, s16
	s_addc_u32 s89, s15, 0
	v_readlane_b32 s2, v254, 46
	s_add_u32 s92, s2, s12
	v_readlane_b32 s2, v254, 47
	s_mov_b32 s87, s1
	s_addc_u32 s93, s2, s13
	v_readlane_b32 s2, v254, 59
	s_mov_b64 s[94:95], 0
	s_mov_b64 s[90:91], s[0:1]

; #define GAS __attribute__((address_space(1)))
; #define LAS __attribute__((address_space(3)))
; __device__ __forceinline__ void p8_issue(const TItem8& t, f32x4 (&v)[16], int lane) {
;     const GAS f32x4* src = (const GAS f32x4*)((const GAS float*)t.src + (size_t)(lane >> 3) * t.N + 4 * (lane & 7));
; #pragma unroll
;     for (int i = 0; i < 16; ++i) v[i] = __builtin_nontemporal_load(src + (size_t)(2 * i) * t.N);
; }
; __device__ __forceinline__ void p8_finish(const TItem8& t, const f32x4 (&v)[16], LAS float* scr, int lane) {
; #pragma unroll
;     for (int i = 0; i < 16; ++i) *(LAS f32x4*)(scr + (8 * i + (lane >> 3)) * 32 + (((lane & 7) ^ (i & 7)) << 2)) = v[i] * W8_SCALE;
.LBB0_741:
	s_lshl_b64 s[12:13], s[86:87], 11
	s_add_u32 s0, s92, s12
	v_mul_u32_u24_e32 v2, s94, v225
	s_addc_u32 s11, s93, s13
	v_lshlrev_b32_e32 v142, 2, v2
	s_add_u32 s80, s0, s90
	v_lshl_add_u64 v[2:3], s[88:89], 0, v[142:143]
	v_mov_b32_e32 v145, v143
	s_addc_u32 s81, s11, s91
	v_lshl_add_u64 v[2:3], v[2:3], 0, v[144:145]
	s_lshl_b32 s0, s94, 5
	v_lshl_add_u64 v[10:11], v[2:3], 0, s[0:1]
	global_load_dwordx4 v[2:5], v[2:3], off nt
	s_nop 0
	global_load_dwordx4 v[6:9], v[10:11], off nt
	v_lshl_add_u64 v[10:11], v[10:11], 0, s[0:1]
	v_lshl_add_u64 v[18:19], v[10:11], 0, s[0:1]
	global_load_dwordx4 v[10:13], v[10:11], off nt
	s_nop 0
	global_load_dwordx4 v[14:17], v[18:19], off nt
	v_lshl_add_u64 v[18:19], v[18:19], 0, s[0:1]
	v_lshl_add_u64 v[26:27], v[18:19], 0, s[0:1]
	global_load_dwordx4 v[18:21], v[18:19], off nt
	s_nop 0
	global_load_dwordx4 v[22:25], v[26:27], off nt
	v_lshl_add_u64 v[26:27], v[26:27], 0, s[0:1]
	v_lshl_add_u64 v[34:35], v[26:27], 0, s[0:1]
	v_lshl_add_u64 v[38:39], v[34:35], 0, s[0:1]
	v_lshl_add_u64 v[42:43], v[38:39], 0, s[0:1]
	v_lshl_add_u64 v[46:47], v[42:43], 0, s[0:1]
	v_lshl_add_u64 v[50:51], v[46:47], 0, s[0:1]
	v_lshl_add_u64 v[54:55], v[50:51], 0, s[0:1]
	v_lshl_add_u64 v[58:59], v[54:55], 0, s[0:1]
	v_lshl_add_u64 v[62:63], v[58:59], 0, s[0:1]
	global_load_dwordx4 v[26:29], v[26:27], off nt
	s_nop 0
	global_load_dwordx4 v[30:33], v[34:35], off nt
	s_nop 0
	global_load_dwordx4 v[34:37], v[38:39], off nt
	s_nop 0
	global_load_dwordx4 v[38:41], v[42:43], off nt
	s_nop 0
	global_load_dwordx4 v[42:45], v[46:47], off nt
	s_nop 0
	global_load_dwordx4 v[46:49], v[50:51], off nt
	s_nop 0
	global_load_dwordx4 v[50:53], v[54:55], off nt
	s_nop 0
	global_load_dwordx4 v[54:57], v[58:59], off nt
	s_nop 0
	global_load_dwordx4 v[58:61], v[62:63], off nt
	v_lshl_add_u64 v[62:63], v[62:63], 0, s[0:1]
	global_load_dwordx4 v[62:65], v[62:63], off nt
	s_waitcnt vmcnt(35)
	v_pk_mul_f32 v[200:201], v[68:69], s[74:75] op_sel_hi:[1,0]
	v_pk_mul_f32 v[198:199], v[66:67], s[74:75] op_sel_hi:[1,0]
	ds_write_b128 v148, v[198:201]
	s_waitcnt vmcnt(34)
	v_pk_mul_f32 v[200:201], v[72:73], s[74:75] op_sel_hi:[1,0]
	v_pk_mul_f32 v[198:199], v[70:71], s[74:75] op_sel_hi:[1,0]
	ds_write_b128 v149, v[198:201] offset:1024
	s_waitcnt vmcnt(33)
	v_pk_mul_f32 v[200:201], v[76:77], s[74:75] op_sel_hi:[1,0]
	v_pk_mul_f32 v[198:199], v[74:75], s[74:75] op_sel_hi:[1,0]
	ds_write_b128 v150, v[198:201] offset:2048
	s_waitcnt vmcnt(32)
	v_pk_mul_f32 v[200:201], v[80:81], s[74:75] op_sel_hi:[1,0]
	v_pk_mul_f32 v[198:199], v[78:79], s[74:75] op_sel_hi:[1,0]
	ds_write_b128 v151, v[198:201] offset:3072
	s_waitcnt vmcnt(31)
	v_pk_mul_f32 v[200:201], v[84:85], s[74:75] op_sel_hi:[1,0]
	v_pk_mul_f32 v[198:199], v[82:83], s[74:75] op_sel_hi:[1,0]
	ds_write_b128 v152, v[198:201] offset:4096
	s_waitcnt vmcnt(30)
	v_pk_mul_f32 v[200:201], v[88:89], s[74:75] op_sel_hi:[1,0]
	v_pk_mul_f32 v[198:199], v[86:87], s[74:75] op_sel_hi:[1,0]
	ds_write_b128 v153, v[198:201] offset:5120
	s_waitcnt vmcnt(29)
	v_pk_mul_f32 v[200:201], v[92:93], s[74:75] op_sel_hi:[1,0]
	v_pk_mul_f32 v[198:199], v[90:91], s[74:75] op_sel_hi:[1,0]
	ds_write_b128 v154, v[198:201] offset:6144
	s_waitcnt vmcnt(28)
	v_pk_mul_f32 v[200:201], v[96:97], s[74:75] op_sel_hi:[1,0]
	v_pk_mul_f32 v[198:199], v[94:95], s[74:75] op_sel_hi:[1,0]
	ds_write_b128 v155, v[198:201] offset:7168
	s_waitcnt vmcnt(27)
	v_pk_mul_f32 v[200:201], v[100:101], s[74:75] op_sel_hi:[1,0]
	v_pk_mul_f32 v[198:199], v[98:99], s[74:75] op_sel_hi:[1,0]
	ds_write_b128 v148, v[198:201] offset:8192
	s_waitcnt vmcnt(26)
	v_pk_mul_f32 v[200:201], v[104:105], s[74:75] op_sel_hi:[1,0]
	v_pk_mul_f32 v[198:199], v[102:103], s[74:75] op_sel_hi:[1,0]
	ds_write_b128 v149, v[198:201] offset:9216
	s_waitcnt vmcnt(25)
	v_pk_mul_f32 v[200:201], v[108:109], s[74:75] op_sel_hi:[1,0]
	v_pk_mul_f32 v[198:199], v[106:107], s[74:75] op_sel_hi:[1,0]
	ds_write_b128 v150, v[198:201] offset:10240
	s_waitcnt vmcnt(24)
	v_pk_mul_f32 v[200:201], v[112:113], s[74:75] op_sel_hi:[1,0]
	v_pk_mul_f32 v[198:199], v[110:111], s[74:75] op_sel_hi:[1,0]
	ds_write_b128 v151, v[198:201] offset:11264
	s_waitcnt vmcnt(23)
	v_pk_mul_f32 v[200:201], v[116:117], s[74:75] op_sel_hi:[1,0]
	v_pk_mul_f32 v[198:199], v[114:115], s[74:75] op_sel_hi:[1,0]
	ds_write_b128 v152, v[198:201] offset:12288
	s_waitcnt vmcnt(22)
	v_pk_mul_f32 v[200:201], v[120:121], s[74:75] op_sel_hi:[1,0]
	v_pk_mul_f32 v[198:199], v[118:119], s[74:75] op_sel_hi:[1,0]
	ds_write_b128 v153, v[198:201] offset:13312
	s_waitcnt vmcnt(21)
	v_pk_mul_f32 v[200:201], v[124:125], s[74:75] op_sel_hi:[1,0]
	v_pk_mul_f32 v[198:199], v[122:123], s[74:75] op_sel_hi:[1,0]
	ds_write_b128 v154, v[198:201] offset:14336
	s_waitcnt vmcnt(20)
	v_pk_mul_f32 v[200:201], v[128:129], s[74:75] op_sel_hi:[1,0]
	v_pk_mul_f32 v[198:199], v[126:127], s[74:75] op_sel_hi:[1,0]
	ds_write_b128 v155, v[198:201] offset:15360
	s_branch .Lcv2_7_731
; #define GAS __attribute__((address_space(1)))
; #define LAS __attribute__((address_space(3)))
; #define LDS_WAIT() asm volatile("s_waitcnt lgkmcnt(0)" ::: "memory")
; __device__ __forceinline__ void p8_finish(const TItem8& t, const f32x4 (&v)[16], LAS float* scr, int lane) {
;     ...
;     for (int i = 0; i < 16; ++i) *(LAS f32x4*)(scr + (8 * i + (lane >> 3)) * 32 + (((lane & 7) ^ (i & 7)) << 2)) = v[i] * W8_SCALE;
;     LDS_WAIT(); asm volatile("" ::: "memory");
;     const int c = lane & 7;
; #pragma unroll
;     for (int j = 0; j < 4; ++j) { const int n = (lane >> 3) + 8 * j; float x[16];
; #pragma unroll
;         for (int i = 0; i < 16; ++i) { const int k = 16 * c + i; x[i] = scr[k * 32 + ((((n >> 2) ^ ((k >> 3) & 7)) << 2) | (n & 3))]; }
;         int w[4];
; #pragma unroll
;         for (int g = 0; g < 4; ++g) { int q = 0; q = __builtin_amdgcn_cvt_pk_fp8_f32(fminf(fmaxf(x[4 * g], -448.f), 448.f), fminf(fmaxf(x[4 * g + 1], -448.f), 448.f), q, false);
;             q = __builtin_amdgcn_cvt_pk_fp8_f32(fminf(fmaxf(x[4 * g + 2], -448.f), 448.f), fminf(fmaxf(x[4 * g + 3], -448.f), 448.f), q, true); w[g] = q; }
;         v4u o; o.x = (unsigned)w[0]; o.y = (unsigned)w[1]; o.z = (unsigned)w[2]; o.w = (unsigned)w[3];
;         __builtin_nontemporal_store(o, (GAS v4u*)(t.dst + (size_t)n * t.Kd + 16 * c)); }
.LBB0_742:
	s_waitcnt vmcnt(19)
	v_pk_mul_f32 v[200:201], v[68:69], s[74:75] op_sel_hi:[1,0]
	v_pk_mul_f32 v[198:199], v[66:67], s[74:75] op_sel_hi:[1,0]
	ds_write_b128 v148, v[198:201]
	s_waitcnt vmcnt(18)
	v_pk_mul_f32 v[200:201], v[72:73], s[74:75] op_sel_hi:[1,0]
	v_pk_mul_f32 v[198:199], v[70:71], s[74:75] op_sel_hi:[1,0]
	ds_write_b128 v149, v[198:201] offset:1024
	s_waitcnt vmcnt(17)
	v_pk_mul_f32 v[200:201], v[76:77], s[74:75] op_sel_hi:[1,0]
	v_pk_mul_f32 v[198:199], v[74:75], s[74:75] op_sel_hi:[1,0]
	ds_write_b128 v150, v[198:201] offset:2048
	s_waitcnt vmcnt(16)
	v_pk_mul_f32 v[200:201], v[80:81], s[74:75] op_sel_hi:[1,0]
	v_pk_mul_f32 v[198:199], v[78:79], s[74:75] op_sel_hi:[1,0]
	ds_write_b128 v151, v[198:201] offset:3072
	s_waitcnt vmcnt(15)
	v_pk_mul_f32 v[200:201], v[84:85], s[74:75] op_sel_hi:[1,0]
	v_pk_mul_f32 v[198:199], v[82:83], s[74:75] op_sel_hi:[1,0]
	ds_write_b128 v152, v[198:201] offset:4096
	s_waitcnt vmcnt(14)
	v_pk_mul_f32 v[200:201], v[88:89], s[74:75] op_sel_hi:[1,0]
	v_pk_mul_f32 v[198:199], v[86:87], s[74:75] op_sel_hi:[1,0]
	ds_write_b128 v153, v[198:201] offset:5120
	s_waitcnt vmcnt(13)
	v_pk_mul_f32 v[200:201], v[92:93], s[74:75] op_sel_hi:[1,0]
	v_pk_mul_f32 v[198:199], v[90:91], s[74:75] op_sel_hi:[1,0]
	ds_write_b128 v154, v[198:201] offset:6144
	s_waitcnt vmcnt(12)
	v_pk_mul_f32 v[200:201], v[96:97], s[74:75] op_sel_hi:[1,0]
	v_pk_mul_f32 v[198:199], v[94:95], s[74:75] op_sel_hi:[1,0]
	ds_write_b128 v155, v[198:201] offset:7168
	s_waitcnt vmcnt(11)
	v_pk_mul_f32 v[200:201], v[100:101], s[74:75] op_sel_hi:[1,0]
	v_pk_mul_f32 v[198:199], v[98:99], s[74:75] op_sel_hi:[1,0]
	ds_write_b128 v148, v[198:201] offset:8192
	s_waitcnt vmcnt(10)
	v_pk_mul_f32 v[200:201], v[104:105], s[74:75] op_sel_hi:[1,0]
	v_pk_mul_f32 v[198:199], v[102:103], s[74:75] op_sel_hi:[1,0]
	ds_write_b128 v149, v[198:201] offset:9216
	s_waitcnt vmcnt(9)
	v_pk_mul_f32 v[200:201], v[108:109], s[74:75] op_sel_hi:[1,0]
	v_pk_mul_f32 v[198:199], v[106:107], s[74:75] op_sel_hi:[1,0]
	ds_write_b128 v150, v[198:201] offset:10240
	s_waitcnt vmcnt(8)
	v_pk_mul_f32 v[200:201], v[112:113], s[74:75] op_sel_hi:[1,0]
	v_pk_mul_f32 v[198:199], v[110:111], s[74:75] op_sel_hi:[1,0]
	ds_write_b128 v151, v[198:201] offset:11264
	s_waitcnt vmcnt(7)
	v_pk_mul_f32 v[200:201], v[116:117], s[74:75] op_sel_hi:[1,0]
	v_pk_mul_f32 v[198:199], v[114:115], s[74:75] op_sel_hi:[1,0]
	ds_write_b128 v152, v[198:201] offset:12288
	s_waitcnt vmcnt(6)
	v_pk_mul_f32 v[200:201], v[120:121], s[74:75] op_sel_hi:[1,0]
	v_pk_mul_f32 v[198:199], v[118:119], s[74:75] op_sel_hi:[1,0]
	ds_write_b128 v153, v[198:201] offset:13312
	s_waitcnt vmcnt(5)
	v_pk_mul_f32 v[200:201], v[124:125], s[74:75] op_sel_hi:[1,0]
	v_pk_mul_f32 v[198:199], v[122:123], s[74:75] op_sel_hi:[1,0]
	ds_write_b128 v154, v[198:201] offset:14336
	s_waitcnt vmcnt(4)
	v_pk_mul_f32 v[200:201], v[128:129], s[74:75] op_sel_hi:[1,0]
	v_pk_mul_f32 v[198:199], v[126:127], s[74:75] op_sel_hi:[1,0]
	ds_write_b128 v155, v[198:201] offset:15360
.Lcv2_7_731:
	s_waitcnt lgkmcnt(0)
	ds_read2_b32 v[198:199], v156 offset1:32
	ds_read2_b32 v[200:201], v156 offset0:64 offset1:96
	ds_read2_b32 v[202:203], v156 offset0:128 offset1:160
	ds_read2_b32 v[204:205], v156 offset0:192 offset1:224
	ds_read_b32 v142, v157
	ds_read_b32 v145, v158
	ds_read_b32 v206, v159
	ds_read_b32 v207, v160
	ds_read_b32 v208, v161
	ds_read_b32 v209, v162
	ds_read_b32 v210, v163
	ds_read_b32 v211, v164
	s_waitcnt lgkmcnt(11)
	v_max_f32_e32 v198, v198, v198
	v_med3_f32 v212, v198, s7, v1
	v_max_f32_e32 v198, v199, v199
	v_med3_f32 v199, v198, s7, v1
	v_mov_b32_e32 v198, v143
	v_cvt_pk_fp8_f32 v198, v212, v199
	s_waitcnt lgkmcnt(10)
	v_max_f32_e32 v199, v200, v200
	v_max_f32_e32 v200, v201, v201
	v_med3_f32 v199, v199, s7, v1
	v_med3_f32 v200, v200, s7, v1
	v_cvt_pk_fp8_f32 v198, v199, v200 op_sel:[0,0,1]
	s_waitcnt lgkmcnt(9)
	v_max_f32_e32 v199, v202, v202
	v_med3_f32 v200, v199, s7, v1
	v_max_f32_e32 v199, v203, v203
	v_med3_f32 v201, v199, s7, v1
	v_mov_b32_e32 v199, v143
	v_cvt_pk_fp8_f32 v199, v200, v201
	s_waitcnt lgkmcnt(8)
	v_max_f32_e32 v200, v204, v204
	v_max_f32_e32 v201, v205, v205
	v_med3_f32 v200, v200, s7, v1
	v_med3_f32 v201, v201, s7, v1
	s_waitcnt lgkmcnt(7)
	v_max_f32_e32 v142, v142, v142
	s_waitcnt lgkmcnt(6)
	v_max_f32_e32 v145, v145, v145
	v_cvt_pk_fp8_f32 v199, v200, v201 op_sel:[0,0,1]
	v_med3_f32 v142, v142, s7, v1
	v_med3_f32 v145, v145, s7, v1
	v_mov_b32_e32 v200, v143
	v_cvt_pk_fp8_f32 v200, v142, v145
	s_waitcnt lgkmcnt(5)
	v_max_f32_e32 v142, v206, v206
	s_waitcnt lgkmcnt(4)
	v_max_f32_e32 v145, v207, v207
	v_med3_f32 v142, v142, s7, v1
	v_med3_f32 v145, v145, s7, v1
	v_cvt_pk_fp8_f32 v200, v142, v145 op_sel:[0,0,1]
	s_waitcnt lgkmcnt(3)
	v_max_f32_e32 v142, v208, v208
	s_waitcnt lgkmcnt(2)
	v_max_f32_e32 v145, v209, v209
	v_med3_f32 v142, v142, s7, v1
	v_med3_f32 v145, v145, s7, v1
	v_mov_b32_e32 v201, v143
	v_cvt_pk_fp8_f32 v201, v142, v145
	s_waitcnt lgkmcnt(1)
	v_max_f32_e32 v142, v210, v210
	s_waitcnt lgkmcnt(0)
	v_max_f32_e32 v145, v211, v211
	v_med3_f32 v142, v142, s7, v1
	v_med3_f32 v145, v145, s7, v1
	v_cvt_pk_fp8_f32 v201, v142, v145 op_sel:[0,0,1]
	v_lshl_add_u64 v[146:147], s[82:83], 0, v[130:131]
	v_lshl_add_u64 v[202:203], v[146:147], 0, v[132:133]
	global_store_dwordx4 v[202:203], v[198:201], off nt
	ds_read2_b32 v[198:199], v165 offset1:32
	ds_read2_b32 v[200:201], v165 offset0:64 offset1:96
	ds_read2_b32 v[202:203], v165 offset0:128 offset1:160
	ds_read2_b32 v[204:205], v165 offset0:192 offset1:224
	ds_read_b32 v142, v166
	ds_read_b32 v145, v167
	ds_read_b32 v206, v168
	ds_read_b32 v207, v169
	ds_read_b32 v208, v170
	ds_read_b32 v209, v171
	ds_read_b32 v210, v172
	ds_read_b32 v211, v173
	s_waitcnt lgkmcnt(11)
; #define GAS __attribute__((address_space(1)))
; __device__ __forceinline__ void p8_finish(const TItem8& t, const f32x4 (&v)[16], LAS float* scr, int lane) {
;     ...
;     for (int j = 0; j < 4; ++j) { const int n = (lane >> 3) + 8 * j; float x[16];
; #pragma unroll
;         for (int i = 0; i < 16; ++i) { const int k = 16 * c + i; x[i] = scr[k * 32 + ((((n >> 2) ^ ((k >> 3) & 7)) << 2) | (n & 3))]; }
;         int w[4];
; #pragma unroll
;         for (int g = 0; g < 4; ++g) { int q = 0; q = __builtin_amdgcn_cvt_pk_fp8_f32(fminf(fmaxf(x[4 * g], -448.f), 448.f), fminf(fmaxf(x[4 * g + 1], -448.f), 448.f), q, false);
;             q = __builtin_amdgcn_cvt_pk_fp8_f32(fminf(fmaxf(x[4 * g + 2], -448.f), 448.f), fminf(fmaxf(x[4 * g + 3], -448.f), 448.f), q, true); w[g] = q; }
;         v4u o; o.x = (unsigned)w[0]; o.y = (unsigned)w[1]; o.z = (unsigned)w[2]; o.w = (unsigned)w[3];
;         __builtin_nontemporal_store(o, (GAS v4u*)(t.dst + (size_t)n * t.Kd + 16 * c)); }
	v_max_f32_e32 v198, v198, v198
	v_med3_f32 v212, v198, s7, v1
	v_max_f32_e32 v198, v199, v199
	v_med3_f32 v199, v198, s7, v1
	v_mov_b32_e32 v198, v143
	v_cvt_pk_fp8_f32 v198, v212, v199
	s_waitcnt lgkmcnt(10)
	v_max_f32_e32 v199, v200, v200
	v_max_f32_e32 v200, v201, v201
	v_med3_f32 v199, v199, s7, v1
	v_med3_f32 v200, v200, s7, v1
	v_cvt_pk_fp8_f32 v198, v199, v200 op_sel:[0,0,1]
	s_waitcnt lgkmcnt(9)
	v_max_f32_e32 v199, v202, v202
	v_med3_f32 v200, v199, s7, v1
	v_max_f32_e32 v199, v203, v203
	v_med3_f32 v201, v199, s7, v1
	v_mov_b32_e32 v199, v143
	v_cvt_pk_fp8_f32 v199, v200, v201
	s_waitcnt lgkmcnt(8)
	v_max_f32_e32 v200, v204, v204
	v_max_f32_e32 v201, v205, v205
	v_med3_f32 v200, v200, s7, v1
	v_med3_f32 v201, v201, s7, v1
	s_waitcnt lgkmcnt(7)
	v_max_f32_e32 v142, v142, v142
	s_waitcnt lgkmcnt(6)
	v_max_f32_e32 v145, v145, v145
	v_cvt_pk_fp8_f32 v199, v200, v201 op_sel:[0,0,1]
	v_med3_f32 v142, v142, s7, v1
	v_med3_f32 v145, v145, s7, v1
	v_mov_b32_e32 v200, v143
	v_cvt_pk_fp8_f32 v200, v142, v145
	s_waitcnt lgkmcnt(5)
	v_max_f32_e32 v142, v206, v206
	s_waitcnt lgkmcnt(4)
	v_max_f32_e32 v145, v207, v207
	v_med3_f32 v142, v142, s7, v1
	v_med3_f32 v145, v145, s7, v1
	v_cvt_pk_fp8_f32 v200, v142, v145 op_sel:[0,0,1]
	s_waitcnt lgkmcnt(3)
	v_max_f32_e32 v142, v208, v208
	s_waitcnt lgkmcnt(2)
	v_max_f32_e32 v145, v209, v209
	v_med3_f32 v142, v142, s7, v1
	v_med3_f32 v145, v145, s7, v1
	v_mov_b32_e32 v201, v143
	v_cvt_pk_fp8_f32 v201, v142, v145
	s_waitcnt lgkmcnt(1)
	v_max_f32_e32 v142, v210, v210
	s_waitcnt lgkmcnt(0)
	v_max_f32_e32 v145, v211, v211
	v_med3_f32 v142, v142, s7, v1
	v_med3_f32 v145, v145, s7, v1
	v_cvt_pk_fp8_f32 v201, v142, v145 op_sel:[0,0,1]
	v_lshl_add_u64 v[202:203], v[146:147], 0, v[134:135]
	global_store_dwordx4 v[202:203], v[198:201], off nt
	ds_read2_b32 v[198:199], v174 offset1:32
	ds_read2_b32 v[200:201], v174 offset0:64 offset1:96
	ds_read2_b32 v[202:203], v174 offset0:128 offset1:160
	ds_read2_b32 v[204:205], v174 offset0:192 offset1:224
	ds_read_b32 v142, v175
	ds_read_b32 v145, v176
	ds_read_b32 v206, v177
	ds_read_b32 v207, v178
	ds_read_b32 v208, v179
	ds_read_b32 v209, v180
	ds_read_b32 v210, v181
	ds_read_b32 v211, v182
	s_waitcnt lgkmcnt(11)
	v_max_f32_e32 v198, v198, v198
	v_med3_f32 v212, v198, s7, v1
	v_max_f32_e32 v198, v199, v199
	v_med3_f32 v199, v198, s7, v1
	v_mov_b32_e32 v198, v143
	v_cvt_pk_fp8_f32 v198, v212, v199
	s_waitcnt lgkmcnt(10)
	v_max_f32_e32 v199, v200, v200
	v_max_f32_e32 v200, v201, v201
	v_med3_f32 v199, v199, s7, v1
	v_med3_f32 v200, v200, s7, v1
	v_cvt_pk_fp8_f32 v198, v199, v200 op_sel:[0,0,1]
	s_waitcnt lgkmcnt(9)
	v_max_f32_e32 v199, v202, v202
	v_med3_f32 v200, v199, s7, v1
	v_max_f32_e32 v199, v203, v203
	v_med3_f32 v201, v199, s7, v1
	v_mov_b32_e32 v199, v143
	v_cvt_pk_fp8_f32 v199, v200, v201
	s_waitcnt lgkmcnt(8)
	v_max_f32_e32 v200, v204, v204
	v_max_f32_e32 v201, v205, v205
	v_med3_f32 v200, v200, s7, v1
	v_med3_f32 v201, v201, s7, v1
	s_waitcnt lgkmcnt(7)
	v_max_f32_e32 v142, v142, v142
	s_waitcnt lgkmcnt(6)
	v_max_f32_e32 v145, v145, v145
	v_cvt_pk_fp8_f32 v199, v200, v201 op_sel:[0,0,1]
	v_med3_f32 v142, v142, s7, v1
	v_med3_f32 v145, v145, s7, v1
	v_mov_b32_e32 v200, v143
	v_cvt_pk_fp8_f32 v200, v142, v145
	s_waitcnt lgkmcnt(5)
	v_max_f32_e32 v142, v206, v206
	s_waitcnt lgkmcnt(4)
	v_max_f32_e32 v145, v207, v207
	v_med3_f32 v142, v142, s7, v1
	v_med3_f32 v145, v145, s7, v1
	v_cvt_pk_fp8_f32 v200, v142, v145 op_sel:[0,0,1]
	s_waitcnt lgkmcnt(3)
	v_max_f32_e32 v142, v208, v208
	s_waitcnt lgkmcnt(2)
	v_max_f32_e32 v145, v209, v209
	v_med3_f32 v142, v142, s7, v1
	v_med3_f32 v145, v145, s7, v1
	v_mov_b32_e32 v201, v143
	v_cvt_pk_fp8_f32 v201, v142, v145
	s_waitcnt lgkmcnt(1)
	v_max_f32_e32 v142, v210, v210
	s_waitcnt lgkmcnt(0)
	v_max_f32_e32 v145, v211, v211
	v_med3_f32 v142, v142, s7, v1
	v_med3_f32 v145, v145, s7, v1
	v_cvt_pk_fp8_f32 v201, v142, v145 op_sel:[0,0,1]
	v_lshl_add_u64 v[202:203], v[146:147], 0, v[136:137]
	v_lshl_add_u64 v[146:147], v[146:147], 0, v[138:139]
	global_store_dwordx4 v[202:203], v[198:201], off nt
	ds_read2_b32 v[198:199], v183 offset1:32
	ds_read2_b32 v[200:201], v183 offset0:64 offset1:96
	ds_read2_b32 v[202:203], v183 offset0:128 offset1:160
	ds_read2_b32 v[204:205], v183 offset0:192 offset1:224
	ds_read_b32 v142, v184
	ds_read_b32 v145, v185
	ds_read_b32 v206, v186
	ds_read_b32 v207, v187
	ds_read_b32 v208, v188
	ds_read_b32 v209, v189
	ds_read_b32 v210, v190
	ds_read_b32 v211, v191
	s_waitcnt lgkmcnt(11)
	v_max_f32_e32 v198, v198, v198
	v_med3_f32 v212, v198, s7, v1
	v_max_f32_e32 v198, v199, v199
	v_med3_f32 v199, v198, s7, v1
	v_mov_b32_e32 v198, v143
	v_cvt_pk_fp8_f32 v198, v212, v199
	s_waitcnt lgkmcnt(10)
	v_max_f32_e32 v199, v200, v200
	v_max_f32_e32 v200, v201, v201
	v_med3_f32 v199, v199, s7, v1
	v_med3_f32 v200, v200, s7, v1
	v_cvt_pk_fp8_f32 v198, v199, v200 op_sel:[0,0,1]
	s_waitcnt lgkmcnt(9)
	v_max_f32_e32 v199, v202, v202
	v_med3_f32 v200, v199, s7, v1
	v_max_f32_e32 v199, v203, v203
	v_med3_f32 v201, v199, s7, v1
	v_mov_b32_e32 v199, v143
	v_cvt_pk_fp8_f32 v199, v200, v201
	s_waitcnt lgkmcnt(8)
	v_max_f32_e32 v200, v204, v204
	v_max_f32_e32 v201, v205, v205
	v_med3_f32 v200, v200, s7, v1
	v_med3_f32 v201, v201, s7, v1
	s_waitcnt lgkmcnt(7)
	v_max_f32_e32 v142, v142, v142
	s_waitcnt lgkmcnt(6)
	v_max_f32_e32 v145, v145, v145
	v_cvt_pk_fp8_f32 v199, v200, v201 op_sel:[0,0,1]
	v_med3_f32 v142, v142, s7, v1
	v_med3_f32 v145, v145, s7, v1
	v_mov_b32_e32 v200, v143
	v_cvt_pk_fp8_f32 v200, v142, v145
	s_waitcnt lgkmcnt(5)
	v_max_f32_e32 v142, v206, v206
	s_waitcnt lgkmcnt(4)
	v_max_f32_e32 v145, v207, v207
	v_med3_f32 v142, v142, s7, v1
	v_med3_f32 v145, v145, s7, v1
	v_cvt_pk_fp8_f32 v200, v142, v145 op_sel:[0,0,1]
	s_waitcnt lgkmcnt(3)
	v_max_f32_e32 v142, v208, v208
	s_waitcnt lgkmcnt(2)
	v_max_f32_e32 v145, v209, v209
	v_med3_f32 v142, v142, s7, v1
	v_med3_f32 v145, v145, s7, v1
	v_mov_b32_e32 v201, v143
	v_cvt_pk_fp8_f32 v201, v142, v145
	s_waitcnt lgkmcnt(1)
	v_max_f32_e32 v142, v210, v210
	s_waitcnt lgkmcnt(0)
	v_max_f32_e32 v145, v211, v211
	v_med3_f32 v142, v142, s7, v1
	v_med3_f32 v145, v145, s7, v1
	v_cvt_pk_fp8_f32 v201, v142, v145 op_sel:[0,0,1]
	global_store_dwordx4 v[146:147], v[198:201], off nt
	s_waitcnt lgkmcnt(0)
	s_xor_b64 s[84:85], s[84:85], -1
	s_andn2_b64 vcc, exec, s[84:85]
	s_cbranch_vccnz .LBB0_721

; #define GAS __attribute__((address_space(1)))
; #define LAS __attribute__((address_space(3)))
; __device__ __forceinline__ void p8_issue(const TItem8& t, f32x4 (&v)[16], int lane) {
;     const GAS f32x4* src = (const GAS f32x4*)((const GAS float*)t.src + (size_t)(lane >> 3) * t.N + 4 * (lane & 7));
; #pragma unroll
;     for (int i = 0; i < 16; ++i) v[i] = __builtin_nontemporal_load(src + (size_t)(2 * i) * t.N);
; }
; __device__ __forceinline__ void p8_finish(const TItem8& t, const f32x4 (&v)[16], LAS float* scr, int lane) {
; #pragma unroll
;     for (int i = 0; i < 16; ++i) *(LAS f32x4*)(scr + (8 * i + (lane >> 3)) * 32 + (((lane & 7) ^ (i & 7)) << 2)) = v[i] * W8_SCALE;
.LBB0_766:
	s_lshl_b64 s[12:13], s[86:87], 11
	s_add_u32 s0, s92, s12
	v_mul_u32_u24_e32 v66, s94, v225
	s_addc_u32 s11, s93, s13
	v_lshlrev_b32_e32 v142, 2, v66
	s_add_u32 s82, s0, s90
	v_lshl_add_u64 v[66:67], s[88:89], 0, v[142:143]
	v_mov_b32_e32 v145, v143
	s_addc_u32 s83, s11, s91
	v_lshl_add_u64 v[66:67], v[66:67], 0, v[144:145]
	s_lshl_b32 s0, s94, 5
	v_lshl_add_u64 v[74:75], v[66:67], 0, s[0:1]
	global_load_dwordx4 v[66:69], v[66:67], off nt
	s_nop 0
	global_load_dwordx4 v[70:73], v[74:75], off nt
	v_lshl_add_u64 v[74:75], v[74:75], 0, s[0:1]
	v_lshl_add_u64 v[82:83], v[74:75], 0, s[0:1]
	global_load_dwordx4 v[74:77], v[74:75], off nt
	s_nop 0
	global_load_dwordx4 v[78:81], v[82:83], off nt
	v_lshl_add_u64 v[82:83], v[82:83], 0, s[0:1]
	v_lshl_add_u64 v[90:91], v[82:83], 0, s[0:1]
	global_load_dwordx4 v[82:85], v[82:83], off nt
	s_nop 0
	global_load_dwordx4 v[86:89], v[90:91], off nt
	v_lshl_add_u64 v[90:91], v[90:91], 0, s[0:1]
	v_lshl_add_u64 v[98:99], v[90:91], 0, s[0:1]
	v_lshl_add_u64 v[102:103], v[98:99], 0, s[0:1]
	v_lshl_add_u64 v[106:107], v[102:103], 0, s[0:1]
	v_lshl_add_u64 v[110:111], v[106:107], 0, s[0:1]
	v_lshl_add_u64 v[114:115], v[110:111], 0, s[0:1]
	v_lshl_add_u64 v[118:119], v[114:115], 0, s[0:1]
	v_lshl_add_u64 v[122:123], v[118:119], 0, s[0:1]
	v_lshl_add_u64 v[126:127], v[122:123], 0, s[0:1]
	global_load_dwordx4 v[90:93], v[90:91], off nt
	s_nop 0
	global_load_dwordx4 v[94:97], v[98:99], off nt
	s_nop 0
	global_load_dwordx4 v[98:101], v[102:103], off nt
	s_nop 0
	global_load_dwordx4 v[102:105], v[106:107], off nt
	s_nop 0
	global_load_dwordx4 v[106:109], v[110:111], off nt
	s_nop 0
	global_load_dwordx4 v[110:113], v[114:115], off nt
	s_nop 0
	global_load_dwordx4 v[114:117], v[118:119], off nt
	s_nop 0
	global_load_dwordx4 v[118:121], v[122:123], off nt
	s_nop 0
	global_load_dwordx4 v[122:125], v[126:127], off nt
	v_lshl_add_u64 v[126:127], v[126:127], 0, s[0:1]
	global_load_dwordx4 v[126:129], v[126:127], off nt
	s_waitcnt vmcnt(31)
	v_pk_mul_f32 v[200:201], v[4:5], s[74:75] op_sel_hi:[1,0]
	v_pk_mul_f32 v[198:199], v[2:3], s[74:75] op_sel_hi:[1,0]
	ds_write_b128 v148, v[198:201]
	s_waitcnt vmcnt(30)
	v_pk_mul_f32 v[200:201], v[8:9], s[74:75] op_sel_hi:[1,0]
	v_pk_mul_f32 v[198:199], v[6:7], s[74:75] op_sel_hi:[1,0]
	ds_write_b128 v149, v[198:201] offset:1024
	s_waitcnt vmcnt(29)
	v_pk_mul_f32 v[200:201], v[12:13], s[74:75] op_sel_hi:[1,0]
	v_pk_mul_f32 v[198:199], v[10:11], s[74:75] op_sel_hi:[1,0]
	ds_write_b128 v150, v[198:201] offset:2048
	s_waitcnt vmcnt(28)
	v_pk_mul_f32 v[200:201], v[16:17], s[74:75] op_sel_hi:[1,0]
	v_pk_mul_f32 v[198:199], v[14:15], s[74:75] op_sel_hi:[1,0]
	ds_write_b128 v151, v[198:201] offset:3072
	s_waitcnt vmcnt(27)
	v_pk_mul_f32 v[200:201], v[20:21], s[74:75] op_sel_hi:[1,0]
	v_pk_mul_f32 v[198:199], v[18:19], s[74:75] op_sel_hi:[1,0]
	ds_write_b128 v152, v[198:201] offset:4096
	s_waitcnt vmcnt(26)
	v_pk_mul_f32 v[200:201], v[24:25], s[74:75] op_sel_hi:[1,0]
	v_pk_mul_f32 v[198:199], v[22:23], s[74:75] op_sel_hi:[1,0]
	ds_write_b128 v153, v[198:201] offset:5120
	s_waitcnt vmcnt(25)
	v_pk_mul_f32 v[200:201], v[28:29], s[74:75] op_sel_hi:[1,0]
	v_pk_mul_f32 v[198:199], v[26:27], s[74:75] op_sel_hi:[1,0]
	ds_write_b128 v154, v[198:201] offset:6144
	s_waitcnt vmcnt(24)
	v_pk_mul_f32 v[200:201], v[32:33], s[74:75] op_sel_hi:[1,0]
	v_pk_mul_f32 v[198:199], v[30:31], s[74:75] op_sel_hi:[1,0]
	ds_write_b128 v155, v[198:201] offset:7168
	s_waitcnt vmcnt(23)
	v_pk_mul_f32 v[200:201], v[36:37], s[74:75] op_sel_hi:[1,0]
	v_pk_mul_f32 v[198:199], v[34:35], s[74:75] op_sel_hi:[1,0]
	ds_write_b128 v148, v[198:201] offset:8192
	s_waitcnt vmcnt(22)
	v_pk_mul_f32 v[200:201], v[40:41], s[74:75] op_sel_hi:[1,0]
	v_pk_mul_f32 v[198:199], v[38:39], s[74:75] op_sel_hi:[1,0]
	ds_write_b128 v149, v[198:201] offset:9216
	s_waitcnt vmcnt(21)
	v_pk_mul_f32 v[200:201], v[44:45], s[74:75] op_sel_hi:[1,0]
	v_pk_mul_f32 v[198:199], v[42:43], s[74:75] op_sel_hi:[1,0]
	ds_write_b128 v150, v[198:201] offset:10240
	s_waitcnt vmcnt(20)
	v_pk_mul_f32 v[200:201], v[48:49], s[74:75] op_sel_hi:[1,0]
	v_pk_mul_f32 v[198:199], v[46:47], s[74:75] op_sel_hi:[1,0]
	ds_write_b128 v151, v[198:201] offset:11264
	s_waitcnt vmcnt(19)
	v_pk_mul_f32 v[200:201], v[52:53], s[74:75] op_sel_hi:[1,0]
	v_pk_mul_f32 v[198:199], v[50:51], s[74:75] op_sel_hi:[1,0]
	ds_write_b128 v152, v[198:201] offset:12288
	s_waitcnt vmcnt(18)
	v_pk_mul_f32 v[200:201], v[56:57], s[74:75] op_sel_hi:[1,0]
	v_pk_mul_f32 v[198:199], v[54:55], s[74:75] op_sel_hi:[1,0]
	ds_write_b128 v153, v[198:201] offset:13312
	s_waitcnt vmcnt(17)
	v_pk_mul_f32 v[200:201], v[60:61], s[74:75] op_sel_hi:[1,0]
	v_pk_mul_f32 v[198:199], v[58:59], s[74:75] op_sel_hi:[1,0]
	ds_write_b128 v154, v[198:201] offset:14336
	s_waitcnt vmcnt(16)
	v_pk_mul_f32 v[200:201], v[64:65], s[74:75] op_sel_hi:[1,0]
	v_pk_mul_f32 v[198:199], v[62:63], s[74:75] op_sel_hi:[1,0]
	ds_write_b128 v155, v[198:201] offset:15360
	s_branch .Lcv1_6_767

; #define GAS __attribute__((address_space(1)))
; __device__ __forceinline__ void p8_finish(const TItem8& t, const f32x4 (&v)[16], LAS float* scr, int lane) {
;     ...
;     for (int j = 0; j < 4; ++j) { const int n = (lane >> 3) + 8 * j; float x[16];
; #pragma unroll
;         for (int i = 0; i < 16; ++i) { const int k = 16 * c + i; x[i] = scr[k * 32 + ((((n >> 2) ^ ((k >> 3) & 7)) << 2) | (n & 3))]; }
;         int w[4];
; #pragma unroll
;         for (int g = 0; g < 4; ++g) { int q = 0; q = __builtin_amdgcn_cvt_pk_fp8_f32(fminf(fmaxf(x[4 * g], -448.f), 448.f), fminf(fmaxf(x[4 * g + 1], -448.f), 448.f), q, false);
;             q = __builtin_amdgcn_cvt_pk_fp8_f32(fminf(fmaxf(x[4 * g + 2], -448.f), 448.f), fminf(fmaxf(x[4 * g + 3], -448.f), 448.f), q, true); w[g] = q; }
;         v4u o; o.x = (unsigned)w[0]; o.y = (unsigned)w[1]; o.z = (unsigned)w[2]; o.w = (unsigned)w[3];
;         __builtin_nontemporal_store(o, (GAS v4u*)(t.dst + (size_t)n * t.Kd + 16 * c)); }
.Lcv1_6_767:
	s_waitcnt lgkmcnt(0)
	ds_read2_b32 v[198:199], v156 offset1:32
	ds_read2_b32 v[200:201], v156 offset0:64 offset1:96
	ds_read2_b32 v[202:203], v156 offset0:128 offset1:160
	ds_read2_b32 v[204:205], v156 offset0:192 offset1:224
	ds_read_b32 v142, v157
	ds_read_b32 v145, v158
	ds_read_b32 v206, v159
	ds_read_b32 v207, v160
	ds_read_b32 v208, v161
	ds_read_b32 v209, v162
	ds_read_b32 v210, v163
	ds_read_b32 v211, v164
	s_waitcnt lgkmcnt(11)
	v_max_f32_e32 v198, v198, v198
	v_med3_f32 v212, v198, s6, v1
	v_max_f32_e32 v198, v199, v199
	v_med3_f32 v199, v198, s6, v1
	v_mov_b32_e32 v198, 0
	v_cvt_pk_fp8_f32 v198, v212, v199
	s_waitcnt lgkmcnt(10)
	v_max_f32_e32 v199, v200, v200
	v_max_f32_e32 v200, v201, v201
	v_med3_f32 v199, v199, s6, v1
	v_med3_f32 v200, v200, s6, v1
	v_cvt_pk_fp8_f32 v198, v199, v200 op_sel:[0,0,1]
	s_waitcnt lgkmcnt(9)
	v_max_f32_e32 v199, v202, v202
	v_med3_f32 v200, v199, s6, v1
	v_max_f32_e32 v199, v203, v203
	v_med3_f32 v201, v199, s6, v1
	v_mov_b32_e32 v199, 0
	v_cvt_pk_fp8_f32 v199, v200, v201
	s_waitcnt lgkmcnt(8)
	v_max_f32_e32 v200, v204, v204
	v_max_f32_e32 v201, v205, v205
	v_med3_f32 v200, v200, s6, v1
	v_med3_f32 v201, v201, s6, v1
	s_waitcnt lgkmcnt(7)
	v_max_f32_e32 v142, v142, v142
	s_waitcnt lgkmcnt(6)
	v_max_f32_e32 v145, v145, v145
	v_cvt_pk_fp8_f32 v199, v200, v201 op_sel:[0,0,1]
	v_med3_f32 v142, v142, s6, v1
	v_med3_f32 v145, v145, s6, v1
	v_mov_b32_e32 v200, 0
	v_cvt_pk_fp8_f32 v200, v142, v145
	s_waitcnt lgkmcnt(5)
	v_max_f32_e32 v142, v206, v206
	s_waitcnt lgkmcnt(4)
	v_max_f32_e32 v145, v207, v207
	v_med3_f32 v142, v142, s6, v1
	v_med3_f32 v145, v145, s6, v1
	v_cvt_pk_fp8_f32 v200, v142, v145 op_sel:[0,0,1]
	s_waitcnt lgkmcnt(3)
	v_max_f32_e32 v142, v208, v208
	s_waitcnt lgkmcnt(2)
	v_max_f32_e32 v145, v209, v209
	v_med3_f32 v142, v142, s6, v1
	v_med3_f32 v145, v145, s6, v1
	v_mov_b32_e32 v201, 0
	v_cvt_pk_fp8_f32 v201, v142, v145
	s_waitcnt lgkmcnt(1)
	v_max_f32_e32 v142, v210, v210
	s_waitcnt lgkmcnt(0)
	v_max_f32_e32 v145, v211, v211
	v_med3_f32 v142, v142, s6, v1
	v_med3_f32 v145, v145, s6, v1
	v_cvt_pk_fp8_f32 v201, v142, v145 op_sel:[0,0,1]
	ds_read2_b32 v[202:203], v165 offset1:32
	ds_read2_b32 v[204:205], v165 offset0:64 offset1:96
	ds_read2_b32 v[206:207], v165 offset0:128 offset1:160
	ds_read2_b32 v[208:209], v165 offset0:192 offset1:224
	ds_read_b32 v142, v166
	ds_read_b32 v145, v167
	ds_read_b32 v210, v168
	ds_read_b32 v211, v169
	ds_read_b32 v212, v170
	ds_read_b32 v213, v171
	ds_read_b32 v214, v172
	ds_read_b32 v215, v173
	s_waitcnt lgkmcnt(11)
	v_max_f32_e32 v202, v202, v202
	v_med3_f32 v216, v202, s6, v1
	v_max_f32_e32 v202, v203, v203
	v_med3_f32 v203, v202, s6, v1
	v_mov_b32_e32 v202, 0
	v_cvt_pk_fp8_f32 v202, v216, v203
	s_waitcnt lgkmcnt(10)
	v_max_f32_e32 v203, v204, v204
	v_max_f32_e32 v204, v205, v205
	v_med3_f32 v203, v203, s6, v1
	v_med3_f32 v204, v204, s6, v1
	v_cvt_pk_fp8_f32 v202, v203, v204 op_sel:[0,0,1]
	s_waitcnt lgkmcnt(9)
	v_max_f32_e32 v203, v206, v206
	v_med3_f32 v204, v203, s6, v1
	v_max_f32_e32 v203, v207, v207
	v_med3_f32 v205, v203, s6, v1
	v_mov_b32_e32 v203, 0
	v_cvt_pk_fp8_f32 v203, v204, v205
	s_waitcnt lgkmcnt(8)
	v_max_f32_e32 v204, v208, v208
	v_max_f32_e32 v205, v209, v209
	v_med3_f32 v204, v204, s6, v1
	v_med3_f32 v205, v205, s6, v1
	s_waitcnt lgkmcnt(7)
	v_max_f32_e32 v142, v142, v142
	s_waitcnt lgkmcnt(6)
	v_max_f32_e32 v145, v145, v145
	v_cvt_pk_fp8_f32 v203, v204, v205 op_sel:[0,0,1]
	v_med3_f32 v142, v142, s6, v1
	v_med3_f32 v145, v145, s6, v1
	v_mov_b32_e32 v204, 0
	v_cvt_pk_fp8_f32 v204, v142, v145
	s_waitcnt lgkmcnt(5)
	v_max_f32_e32 v142, v210, v210
	s_waitcnt lgkmcnt(4)
	v_max_f32_e32 v145, v211, v211
	v_med3_f32 v142, v142, s6, v1
	v_med3_f32 v145, v145, s6, v1
	v_cvt_pk_fp8_f32 v204, v142, v145 op_sel:[0,0,1]
	s_waitcnt lgkmcnt(3)
	v_max_f32_e32 v142, v212, v212
	s_waitcnt lgkmcnt(2)
	v_max_f32_e32 v145, v213, v213
	v_med3_f32 v142, v142, s6, v1
	v_med3_f32 v145, v145, s6, v1
	v_mov_b32_e32 v205, 0
	v_cvt_pk_fp8_f32 v205, v142, v145
	s_waitcnt lgkmcnt(1)
	v_max_f32_e32 v142, v214, v214
	s_waitcnt lgkmcnt(0)
	v_max_f32_e32 v145, v215, v215
	v_med3_f32 v142, v142, s6, v1
	v_med3_f32 v145, v145, s6, v1
	v_cvt_pk_fp8_f32 v205, v142, v145 op_sel:[0,0,1]
	v_lshl_add_u64 v[146:147], s[80:81], 0, v[130:131]
	v_lshl_add_u64 v[206:207], v[146:147], 0, v[132:133]
	global_store_dwordx4 v[206:207], v[198:201], off nt
	s_andn2_b64 vcc, exec, s[84:85]
	s_mov_b64 s[84:85], 0
	v_lshl_add_u64 v[198:199], v[146:147], 0, v[134:135]
	global_store_dwordx4 v[198:199], v[202:205], off nt
	ds_read2_b32 v[198:199], v174 offset1:32
	ds_read2_b32 v[200:201], v174 offset0:64 offset1:96
	ds_read2_b32 v[202:203], v174 offset0:128 offset1:160
	ds_read2_b32 v[204:205], v174 offset0:192 offset1:224
	ds_read_b32 v142, v175
	ds_read_b32 v145, v176
	ds_read_b32 v206, v177
	ds_read_b32 v207, v178
	ds_read_b32 v208, v179
	ds_read_b32 v209, v180
	ds_read_b32 v210, v181
	ds_read_b32 v211, v182
	s_waitcnt lgkmcnt(11)
; #define GAS __attribute__((address_space(1)))
; __device__ __forceinline__ TItem8 p8_decode(const Args& args, unsigned char* ws, int it) {
;     ...
;     if (it >= P8_N) { const int j = it - P8_N; it = (P8_E0 + j / P8_DN1) * (P8_GU1 + P8_DN1) + P8_GU1 + j % P8_DN1; }
;     else if (it >= P8_E0 * (P8_GU1 + P8_DN1)) { const int r = it - P8_E0 * (P8_GU1 + P8_DN1); it = (P8_E0 + r / P8_GU1) * (P8_GU1 + P8_DN1) + r % P8_GU1; }
;     const int e = it / (P8_GU1 + P8_DN1), q = it % (P8_GU1 + P8_DN1);
;     if (q < P8_GU1) { const int kb = q / 128, nb = q % 128, n0 = nb * 32;
;         const int dr = (n0 < DE) ? (256 * (n0 / 128) + (n0 % 128)) : (256 * ((n0 - DE) / 128) + 128 + ((n0 - DE) % 128));
;         t.src = args.in[25] + (size_t)e * D * 2 * DE + (size_t)(kb * 128) * (2 * DE) + n0; t.N = 2 * DE; t.dst = ws + WS_WGU + (size_t)e * 2 * DE * D + (size_t)dr * D + kb * 128; t.Kd = D; }
; __device__ __forceinline__ void p8_finish(const TItem8& t, const f32x4 (&v)[16], LAS float* scr, int lane) {
;     ...
;     for (int j = 0; j < 4; ++j) { const int n = (lane >> 3) + 8 * j; float x[16];
; #pragma unroll
;         for (int i = 0; i < 16; ++i) { const int k = 16 * c + i; x[i] = scr[k * 32 + ((((n >> 2) ^ ((k >> 3) & 7)) << 2) | (n & 3))]; }
;         int w[4];
; #pragma unroll
;         for (int g = 0; g < 4; ++g) { int q = 0; q = __builtin_amdgcn_cvt_pk_fp8_f32(fminf(fmaxf(x[4 * g], -448.f), 448.f), fminf(fmaxf(x[4 * g + 1], -448.f), 448.f), q, false);
;             q = __builtin_amdgcn_cvt_pk_fp8_f32(fminf(fmaxf(x[4 * g + 2], -448.f), 448.f), fminf(fmaxf(x[4 * g + 3], -448.f), 448.f), q, true); w[g] = q; }
;         v4u o; o.x = (unsigned)w[0]; o.y = (unsigned)w[1]; o.z = (unsigned)w[2]; o.w = (unsigned)w[3];
;         __builtin_nontemporal_store(o, (GAS v4u*)(t.dst + (size_t)n * t.Kd + 16 * c)); }
	v_max_f32_e32 v198, v198, v198
	v_med3_f32 v212, v198, s6, v1
	v_max_f32_e32 v198, v199, v199
	v_med3_f32 v199, v198, s6, v1
	v_mov_b32_e32 v198, 0
	v_cvt_pk_fp8_f32 v198, v212, v199
	s_waitcnt lgkmcnt(10)
	v_max_f32_e32 v199, v200, v200
	v_max_f32_e32 v200, v201, v201
	v_med3_f32 v199, v199, s6, v1
	v_med3_f32 v200, v200, s6, v1
	v_cvt_pk_fp8_f32 v198, v199, v200 op_sel:[0,0,1]
	s_waitcnt lgkmcnt(9)
	v_max_f32_e32 v199, v202, v202
	v_med3_f32 v200, v199, s6, v1
	v_max_f32_e32 v199, v203, v203
	v_med3_f32 v201, v199, s6, v1
	v_mov_b32_e32 v199, 0
	v_cvt_pk_fp8_f32 v199, v200, v201
	s_waitcnt lgkmcnt(8)
	v_max_f32_e32 v200, v204, v204
	v_max_f32_e32 v201, v205, v205
	v_med3_f32 v200, v200, s6, v1
	v_med3_f32 v201, v201, s6, v1
	s_waitcnt lgkmcnt(7)
	v_max_f32_e32 v142, v142, v142
	s_waitcnt lgkmcnt(6)
	v_max_f32_e32 v145, v145, v145
	v_cvt_pk_fp8_f32 v199, v200, v201 op_sel:[0,0,1]
	v_med3_f32 v142, v142, s6, v1
	v_med3_f32 v145, v145, s6, v1
	v_mov_b32_e32 v200, 0
	v_cvt_pk_fp8_f32 v200, v142, v145
	s_waitcnt lgkmcnt(5)
	v_max_f32_e32 v142, v206, v206
	s_waitcnt lgkmcnt(4)
	v_max_f32_e32 v145, v207, v207
	v_med3_f32 v142, v142, s6, v1
	v_med3_f32 v145, v145, s6, v1
	v_cvt_pk_fp8_f32 v200, v142, v145 op_sel:[0,0,1]
	s_waitcnt lgkmcnt(3)
	v_max_f32_e32 v142, v208, v208
	s_waitcnt lgkmcnt(2)
	v_max_f32_e32 v145, v209, v209
	v_med3_f32 v142, v142, s6, v1
	v_med3_f32 v145, v145, s6, v1
	v_mov_b32_e32 v201, 0
	v_cvt_pk_fp8_f32 v201, v142, v145
	s_waitcnt lgkmcnt(1)
	v_max_f32_e32 v142, v210, v210
	s_waitcnt lgkmcnt(0)
	v_max_f32_e32 v145, v211, v211
	v_med3_f32 v142, v142, s6, v1
	v_med3_f32 v145, v145, s6, v1
	v_cvt_pk_fp8_f32 v201, v142, v145 op_sel:[0,0,1]
	ds_read2_b32 v[202:203], v183 offset1:32
	ds_read2_b32 v[204:205], v183 offset0:64 offset1:96
	ds_read2_b32 v[206:207], v183 offset0:128 offset1:160
	ds_read2_b32 v[208:209], v183 offset0:192 offset1:224
	ds_read_b32 v142, v184
	ds_read_b32 v145, v185
	ds_read_b32 v210, v186
	ds_read_b32 v211, v187
	ds_read_b32 v212, v188
	ds_read_b32 v213, v189
	ds_read_b32 v214, v190
	ds_read_b32 v215, v191
	s_waitcnt lgkmcnt(11)
	v_max_f32_e32 v202, v202, v202
	v_med3_f32 v216, v202, s6, v1
	v_max_f32_e32 v202, v203, v203
	v_med3_f32 v203, v202, s6, v1
	v_mov_b32_e32 v202, 0
	v_cvt_pk_fp8_f32 v202, v216, v203
	s_waitcnt lgkmcnt(10)
	v_max_f32_e32 v203, v204, v204
	v_max_f32_e32 v204, v205, v205
	v_med3_f32 v203, v203, s6, v1
	v_med3_f32 v204, v204, s6, v1
	v_cvt_pk_fp8_f32 v202, v203, v204 op_sel:[0,0,1]
	s_waitcnt lgkmcnt(9)
	v_max_f32_e32 v203, v206, v206
	v_med3_f32 v204, v203, s6, v1
	v_max_f32_e32 v203, v207, v207
	v_med3_f32 v205, v203, s6, v1
	v_mov_b32_e32 v203, 0
	v_cvt_pk_fp8_f32 v203, v204, v205
	s_waitcnt lgkmcnt(8)
	v_max_f32_e32 v204, v208, v208
	v_max_f32_e32 v205, v209, v209
	v_med3_f32 v204, v204, s6, v1
	v_med3_f32 v205, v205, s6, v1
	s_waitcnt lgkmcnt(7)
	v_max_f32_e32 v142, v142, v142
	s_waitcnt lgkmcnt(6)
	v_max_f32_e32 v145, v145, v145
	v_cvt_pk_fp8_f32 v203, v204, v205 op_sel:[0,0,1]
	v_med3_f32 v142, v142, s6, v1
	v_med3_f32 v145, v145, s6, v1
	v_mov_b32_e32 v204, 0
	v_cvt_pk_fp8_f32 v204, v142, v145
	s_waitcnt lgkmcnt(5)
	v_max_f32_e32 v142, v210, v210
	s_waitcnt lgkmcnt(4)
	v_max_f32_e32 v145, v211, v211
	v_med3_f32 v142, v142, s6, v1
	v_med3_f32 v145, v145, s6, v1
	v_cvt_pk_fp8_f32 v204, v142, v145 op_sel:[0,0,1]
	s_waitcnt lgkmcnt(3)
	v_max_f32_e32 v142, v212, v212
	s_waitcnt lgkmcnt(2)
	v_max_f32_e32 v145, v213, v213
	v_med3_f32 v142, v142, s6, v1
	v_med3_f32 v145, v145, s6, v1
	v_mov_b32_e32 v205, 0
	v_cvt_pk_fp8_f32 v205, v142, v145
	s_waitcnt lgkmcnt(1)
	v_max_f32_e32 v142, v214, v214
	s_waitcnt lgkmcnt(0)
	v_max_f32_e32 v145, v215, v215
	v_med3_f32 v142, v142, s6, v1
	v_med3_f32 v145, v145, s6, v1
	v_cvt_pk_fp8_f32 v205, v142, v145 op_sel:[0,0,1]
	v_lshl_add_u64 v[206:207], v[146:147], 0, v[136:137]
	v_lshl_add_u64 v[146:147], v[146:147], 0, v[138:139]
	global_store_dwordx4 v[206:207], v[198:201], off nt
	global_store_dwordx4 v[146:147], v[202:205], off nt
	s_waitcnt lgkmcnt(0)
	s_cbranch_vccnz .LBB0_754
	s_add_i32 s7, s7, 2
	s_mul_i32 s0, s7, s4
	s_add_i32 s0, s0, s5
	s_cmp_lt_i32 s0, 0x16400
	s_cselect_b64 s[84:85], -1, 0
	s_cmp_gt_i32 s0, 0x163ff
	s_cbranch_scc1 .LBB0_780
	s_cmp_lt_i32 s0, 0x12c00
	s_cbranch_scc1 .LBB0_771
	s_add_i32 s0, s0, 0xfffed400
	s_lshr_b32 s10, s0, 11
	s_mulk_i32 s10, 0xc00
	s_and_b32 s0, s0, 0x7ff
	s_add_i32 s0, s0, s10
	s_add_i32 s0, s0, 0x12c00

; #define GAS __attribute__((address_space(1)))
; #define LAS __attribute__((address_space(3)))
; __device__ __forceinline__ void p8_issue(const TItem8& t, f32x4 (&v)[16], int lane) {
;     const GAS f32x4* src = (const GAS f32x4*)((const GAS float*)t.src + (size_t)(lane >> 3) * t.N + 4 * (lane & 7));
; #pragma unroll
;     for (int i = 0; i < 16; ++i) v[i] = __builtin_nontemporal_load(src + (size_t)(2 * i) * t.N);
; }
; __device__ __forceinline__ void p8_finish(const TItem8& t, const f32x4 (&v)[16], LAS float* scr, int lane) {
; #pragma unroll
;     for (int i = 0; i < 16; ++i) *(LAS f32x4*)(scr + (8 * i + (lane >> 3)) * 32 + (((lane & 7) ^ (i & 7)) << 2)) = v[i] * W8_SCALE;
.LBB0_779:
	s_lshl_b64 s[10:11], s[86:87], 11
	s_add_u32 s0, s92, s10
	v_mul_u32_u24_e32 v2, s94, v225
	s_addc_u32 s10, s93, s11
	v_lshlrev_b32_e32 v142, 2, v2
	s_add_u32 s80, s0, s90
	v_lshl_add_u64 v[2:3], s[88:89], 0, v[142:143]
	v_mov_b32_e32 v145, v143
	s_addc_u32 s81, s10, s91
	v_lshl_add_u64 v[2:3], v[2:3], 0, v[144:145]
	s_lshl_b32 s0, s94, 5
	v_lshl_add_u64 v[10:11], v[2:3], 0, s[0:1]
	global_load_dwordx4 v[2:5], v[2:3], off nt
	s_nop 0
	global_load_dwordx4 v[6:9], v[10:11], off nt
	v_lshl_add_u64 v[10:11], v[10:11], 0, s[0:1]
	v_lshl_add_u64 v[18:19], v[10:11], 0, s[0:1]
	global_load_dwordx4 v[10:13], v[10:11], off nt
	s_nop 0
	global_load_dwordx4 v[14:17], v[18:19], off nt
	v_lshl_add_u64 v[18:19], v[18:19], 0, s[0:1]
	v_lshl_add_u64 v[26:27], v[18:19], 0, s[0:1]
	global_load_dwordx4 v[18:21], v[18:19], off nt
	s_nop 0
	global_load_dwordx4 v[22:25], v[26:27], off nt
	v_lshl_add_u64 v[26:27], v[26:27], 0, s[0:1]
	v_lshl_add_u64 v[34:35], v[26:27], 0, s[0:1]
	v_lshl_add_u64 v[38:39], v[34:35], 0, s[0:1]
	v_lshl_add_u64 v[42:43], v[38:39], 0, s[0:1]
	v_lshl_add_u64 v[46:47], v[42:43], 0, s[0:1]
	v_lshl_add_u64 v[50:51], v[46:47], 0, s[0:1]
	v_lshl_add_u64 v[54:55], v[50:51], 0, s[0:1]
	v_lshl_add_u64 v[58:59], v[54:55], 0, s[0:1]
	v_lshl_add_u64 v[62:63], v[58:59], 0, s[0:1]
	global_load_dwordx4 v[26:29], v[26:27], off nt
	s_nop 0
	global_load_dwordx4 v[30:33], v[34:35], off nt
	s_nop 0
	global_load_dwordx4 v[34:37], v[38:39], off nt
	s_nop 0
	global_load_dwordx4 v[38:41], v[42:43], off nt
	s_nop 0
	global_load_dwordx4 v[42:45], v[46:47], off nt
	s_nop 0
	global_load_dwordx4 v[46:49], v[50:51], off nt
	s_nop 0
	global_load_dwordx4 v[50:53], v[54:55], off nt
	s_nop 0
	global_load_dwordx4 v[54:57], v[58:59], off nt
	s_nop 0
	global_load_dwordx4 v[58:61], v[62:63], off nt
	v_lshl_add_u64 v[62:63], v[62:63], 0, s[0:1]
	global_load_dwordx4 v[62:65], v[62:63], off nt
	s_waitcnt vmcnt(35)
	v_pk_mul_f32 v[200:201], v[68:69], s[74:75] op_sel_hi:[1,0]
	v_pk_mul_f32 v[198:199], v[66:67], s[74:75] op_sel_hi:[1,0]
	ds_write_b128 v148, v[198:201]
	s_waitcnt vmcnt(34)
	v_pk_mul_f32 v[200:201], v[72:73], s[74:75] op_sel_hi:[1,0]
	v_pk_mul_f32 v[198:199], v[70:71], s[74:75] op_sel_hi:[1,0]
	ds_write_b128 v149, v[198:201] offset:1024
	s_waitcnt vmcnt(33)
	v_pk_mul_f32 v[200:201], v[76:77], s[74:75] op_sel_hi:[1,0]
	v_pk_mul_f32 v[198:199], v[74:75], s[74:75] op_sel_hi:[1,0]
	ds_write_b128 v150, v[198:201] offset:2048
	s_waitcnt vmcnt(32)
	v_pk_mul_f32 v[200:201], v[80:81], s[74:75] op_sel_hi:[1,0]
	v_pk_mul_f32 v[198:199], v[78:79], s[74:75] op_sel_hi:[1,0]
	ds_write_b128 v151, v[198:201] offset:3072
	s_waitcnt vmcnt(31)
	v_pk_mul_f32 v[200:201], v[84:85], s[74:75] op_sel_hi:[1,0]
	v_pk_mul_f32 v[198:199], v[82:83], s[74:75] op_sel_hi:[1,0]
	ds_write_b128 v152, v[198:201] offset:4096
	s_waitcnt vmcnt(30)
	v_pk_mul_f32 v[200:201], v[88:89], s[74:75] op_sel_hi:[1,0]
	v_pk_mul_f32 v[198:199], v[86:87], s[74:75] op_sel_hi:[1,0]
	ds_write_b128 v153, v[198:201] offset:5120
	s_waitcnt vmcnt(29)
	v_pk_mul_f32 v[200:201], v[92:93], s[74:75] op_sel_hi:[1,0]
	v_pk_mul_f32 v[198:199], v[90:91], s[74:75] op_sel_hi:[1,0]
	ds_write_b128 v154, v[198:201] offset:6144
	s_waitcnt vmcnt(28)
	v_pk_mul_f32 v[200:201], v[96:97], s[74:75] op_sel_hi:[1,0]
	v_pk_mul_f32 v[198:199], v[94:95], s[74:75] op_sel_hi:[1,0]
	ds_write_b128 v155, v[198:201] offset:7168
	s_waitcnt vmcnt(27)
	v_pk_mul_f32 v[200:201], v[100:101], s[74:75] op_sel_hi:[1,0]
	v_pk_mul_f32 v[198:199], v[98:99], s[74:75] op_sel_hi:[1,0]
	ds_write_b128 v148, v[198:201] offset:8192
	s_waitcnt vmcnt(26)
	v_pk_mul_f32 v[200:201], v[104:105], s[74:75] op_sel_hi:[1,0]
	v_pk_mul_f32 v[198:199], v[102:103], s[74:75] op_sel_hi:[1,0]
	ds_write_b128 v149, v[198:201] offset:9216
	s_waitcnt vmcnt(25)
	v_pk_mul_f32 v[200:201], v[108:109], s[74:75] op_sel_hi:[1,0]
	v_pk_mul_f32 v[198:199], v[106:107], s[74:75] op_sel_hi:[1,0]
	ds_write_b128 v150, v[198:201] offset:10240
	s_waitcnt vmcnt(24)
	v_pk_mul_f32 v[200:201], v[112:113], s[74:75] op_sel_hi:[1,0]
	v_pk_mul_f32 v[198:199], v[110:111], s[74:75] op_sel_hi:[1,0]
	ds_write_b128 v151, v[198:201] offset:11264
	s_waitcnt vmcnt(23)
	v_pk_mul_f32 v[200:201], v[116:117], s[74:75] op_sel_hi:[1,0]
	v_pk_mul_f32 v[198:199], v[114:115], s[74:75] op_sel_hi:[1,0]
	ds_write_b128 v152, v[198:201] offset:12288
	s_waitcnt vmcnt(22)
	v_pk_mul_f32 v[200:201], v[120:121], s[74:75] op_sel_hi:[1,0]
	v_pk_mul_f32 v[198:199], v[118:119], s[74:75] op_sel_hi:[1,0]
	ds_write_b128 v153, v[198:201] offset:13312
	s_waitcnt vmcnt(21)
	v_pk_mul_f32 v[200:201], v[124:125], s[74:75] op_sel_hi:[1,0]
	v_pk_mul_f32 v[198:199], v[122:123], s[74:75] op_sel_hi:[1,0]
	ds_write_b128 v154, v[198:201] offset:14336
	s_waitcnt vmcnt(20)
	v_pk_mul_f32 v[200:201], v[128:129], s[74:75] op_sel_hi:[1,0]
	v_pk_mul_f32 v[198:199], v[126:127], s[74:75] op_sel_hi:[1,0]
	ds_write_b128 v155, v[198:201] offset:15360
	s_branch .Lcv2_6_767

; #define GAS __attribute__((address_space(1)))
; __device__ __forceinline__ void p8_finish(const TItem8& t, const f32x4 (&v)[16], LAS float* scr, int lane) {
;     ...
;     const int c = lane & 7;
; #pragma unroll
;     for (int j = 0; j < 4; ++j) { const int n = (lane >> 3) + 8 * j; float x[16];
; #pragma unroll
;         for (int i = 0; i < 16; ++i) { const int k = 16 * c + i; x[i] = scr[k * 32 + ((((n >> 2) ^ ((k >> 3) & 7)) << 2) | (n & 3))]; }
;         int w[4];
; #pragma unroll
;         for (int g = 0; g < 4; ++g) { int q = 0; q = __builtin_amdgcn_cvt_pk_fp8_f32(fminf(fmaxf(x[4 * g], -448.f), 448.f), fminf(fmaxf(x[4 * g + 1], -448.f), 448.f), q, false);
;             q = __builtin_amdgcn_cvt_pk_fp8_f32(fminf(fmaxf(x[4 * g + 2], -448.f), 448.f), fminf(fmaxf(x[4 * g + 3], -448.f), 448.f), q, true); w[g] = q; }
;         v4u o; o.x = (unsigned)w[0]; o.y = (unsigned)w[1]; o.z = (unsigned)w[2]; o.w = (unsigned)w[3];
;         __builtin_nontemporal_store(o, (GAS v4u*)(t.dst + (size_t)n * t.Kd + 16 * c)); }
.Lcv2_6_767:
	s_waitcnt lgkmcnt(0)
	ds_read2_b32 v[198:199], v156 offset1:32
	ds_read2_b32 v[200:201], v156 offset0:64 offset1:96
	ds_read2_b32 v[202:203], v156 offset0:128 offset1:160
	ds_read2_b32 v[204:205], v156 offset0:192 offset1:224
	ds_read_b32 v142, v157
	ds_read_b32 v145, v158
	ds_read_b32 v206, v159
	ds_read_b32 v207, v160
	ds_read_b32 v208, v161
	ds_read_b32 v209, v162
	ds_read_b32 v210, v163
	ds_read_b32 v211, v164
	s_waitcnt lgkmcnt(11)
	v_max_f32_e32 v198, v198, v198
	v_med3_f32 v212, v198, s6, v1
	v_max_f32_e32 v198, v199, v199
	v_med3_f32 v199, v198, s6, v1
	v_mov_b32_e32 v198, v143
	v_cvt_pk_fp8_f32 v198, v212, v199
	s_waitcnt lgkmcnt(10)
	v_max_f32_e32 v199, v200, v200
	v_max_f32_e32 v200, v201, v201
	v_med3_f32 v199, v199, s6, v1
	v_med3_f32 v200, v200, s6, v1
	v_cvt_pk_fp8_f32 v198, v199, v200 op_sel:[0,0,1]
	s_waitcnt lgkmcnt(9)
	v_max_f32_e32 v199, v202, v202
	v_med3_f32 v200, v199, s6, v1
	v_max_f32_e32 v199, v203, v203
	v_med3_f32 v201, v199, s6, v1
	v_mov_b32_e32 v199, v143
	v_cvt_pk_fp8_f32 v199, v200, v201
	s_waitcnt lgkmcnt(8)
	v_max_f32_e32 v200, v204, v204
	v_max_f32_e32 v201, v205, v205
	v_med3_f32 v200, v200, s6, v1
	v_med3_f32 v201, v201, s6, v1
	s_waitcnt lgkmcnt(7)
	v_max_f32_e32 v142, v142, v142
	s_waitcnt lgkmcnt(6)
	v_max_f32_e32 v145, v145, v145
	v_cvt_pk_fp8_f32 v199, v200, v201 op_sel:[0,0,1]
	v_med3_f32 v142, v142, s6, v1
	v_med3_f32 v145, v145, s6, v1
	v_mov_b32_e32 v200, v143
	v_cvt_pk_fp8_f32 v200, v142, v145
	s_waitcnt lgkmcnt(5)
	v_max_f32_e32 v142, v206, v206
	s_waitcnt lgkmcnt(4)
	v_max_f32_e32 v145, v207, v207
	v_med3_f32 v142, v142, s6, v1
	v_med3_f32 v145, v145, s6, v1
	v_cvt_pk_fp8_f32 v200, v142, v145 op_sel:[0,0,1]
	s_waitcnt lgkmcnt(3)
	v_max_f32_e32 v142, v208, v208
	s_waitcnt lgkmcnt(2)
	v_max_f32_e32 v145, v209, v209
	v_med3_f32 v142, v142, s6, v1
	v_med3_f32 v145, v145, s6, v1
	v_mov_b32_e32 v201, v143
	v_cvt_pk_fp8_f32 v201, v142, v145
	s_waitcnt lgkmcnt(1)
	v_max_f32_e32 v142, v210, v210
	s_waitcnt lgkmcnt(0)
	v_max_f32_e32 v145, v211, v211
	v_med3_f32 v142, v142, s6, v1
	v_med3_f32 v145, v145, s6, v1
	v_cvt_pk_fp8_f32 v201, v142, v145 op_sel:[0,0,1]
	v_lshl_add_u64 v[146:147], s[82:83], 0, v[130:131]
	v_lshl_add_u64 v[202:203], v[146:147], 0, v[132:133]
	global_store_dwordx4 v[202:203], v[198:201], off nt
	ds_read2_b32 v[198:199], v165 offset1:32
	ds_read2_b32 v[200:201], v165 offset0:64 offset1:96
	ds_read2_b32 v[202:203], v165 offset0:128 offset1:160
	ds_read2_b32 v[204:205], v165 offset0:192 offset1:224
	ds_read_b32 v142, v166
	ds_read_b32 v145, v167
	ds_read_b32 v206, v168
	ds_read_b32 v207, v169
	ds_read_b32 v208, v170
	ds_read_b32 v209, v171
	ds_read_b32 v210, v172
	ds_read_b32 v211, v173
	s_waitcnt lgkmcnt(11)
	v_max_f32_e32 v198, v198, v198
	v_med3_f32 v212, v198, s6, v1
	v_max_f32_e32 v198, v199, v199
	v_med3_f32 v199, v198, s6, v1
	v_mov_b32_e32 v198, v143
	v_cvt_pk_fp8_f32 v198, v212, v199
	s_waitcnt lgkmcnt(10)
	v_max_f32_e32 v199, v200, v200
	v_max_f32_e32 v200, v201, v201
	v_med3_f32 v199, v199, s6, v1
	v_med3_f32 v200, v200, s6, v1
	v_cvt_pk_fp8_f32 v198, v199, v200 op_sel:[0,0,1]
	s_waitcnt lgkmcnt(9)
	v_max_f32_e32 v199, v202, v202
	v_med3_f32 v200, v199, s6, v1
	v_max_f32_e32 v199, v203, v203
	v_med3_f32 v201, v199, s6, v1
	v_mov_b32_e32 v199, v143
	v_cvt_pk_fp8_f32 v199, v200, v201
	s_waitcnt lgkmcnt(8)
	v_max_f32_e32 v200, v204, v204
	v_max_f32_e32 v201, v205, v205
	v_med3_f32 v200, v200, s6, v1
	v_med3_f32 v201, v201, s6, v1
	s_waitcnt lgkmcnt(7)
	v_max_f32_e32 v142, v142, v142
	s_waitcnt lgkmcnt(6)
	v_max_f32_e32 v145, v145, v145
	v_cvt_pk_fp8_f32 v199, v200, v201 op_sel:[0,0,1]
	v_med3_f32 v142, v142, s6, v1
	v_med3_f32 v145, v145, s6, v1
	v_mov_b32_e32 v200, v143
	v_cvt_pk_fp8_f32 v200, v142, v145
	s_waitcnt lgkmcnt(5)
	v_max_f32_e32 v142, v206, v206
	s_waitcnt lgkmcnt(4)
	v_max_f32_e32 v145, v207, v207
	v_med3_f32 v142, v142, s6, v1
	v_med3_f32 v145, v145, s6, v1
	v_cvt_pk_fp8_f32 v200, v142, v145 op_sel:[0,0,1]
	s_waitcnt lgkmcnt(3)
	v_max_f32_e32 v142, v208, v208
	s_waitcnt lgkmcnt(2)
	v_max_f32_e32 v145, v209, v209
	v_med3_f32 v142, v142, s6, v1
	v_med3_f32 v145, v145, s6, v1
	v_mov_b32_e32 v201, v143
	v_cvt_pk_fp8_f32 v201, v142, v145
	s_waitcnt lgkmcnt(1)
	v_max_f32_e32 v142, v210, v210
	s_waitcnt lgkmcnt(0)
; #define GAS __attribute__((address_space(1)))
; __device__ __forceinline__ void p8_finish(const TItem8& t, const f32x4 (&v)[16], LAS float* scr, int lane) {
;     ...
;     const int c = lane & 7;
; #pragma unroll
;     for (int j = 0; j < 4; ++j) { const int n = (lane >> 3) + 8 * j; float x[16];
; #pragma unroll
;         for (int i = 0; i < 16; ++i) { const int k = 16 * c + i; x[i] = scr[k * 32 + ((((n >> 2) ^ ((k >> 3) & 7)) << 2) | (n & 3))]; }
;         int w[4];
; #pragma unroll
;         for (int g = 0; g < 4; ++g) { int q = 0; q = __builtin_amdgcn_cvt_pk_fp8_f32(fminf(fmaxf(x[4 * g], -448.f), 448.f), fminf(fmaxf(x[4 * g + 1], -448.f), 448.f), q, false);
;             q = __builtin_amdgcn_cvt_pk_fp8_f32(fminf(fmaxf(x[4 * g + 2], -448.f), 448.f), fminf(fmaxf(x[4 * g + 3], -448.f), 448.f), q, true); w[g] = q; }
;         v4u o; o.x = (unsigned)w[0]; o.y = (unsigned)w[1]; o.z = (unsigned)w[2]; o.w = (unsigned)w[3];
;         __builtin_nontemporal_store(o, (GAS v4u*)(t.dst + (size_t)n * t.Kd + 16 * c)); }
	v_max_f32_e32 v145, v211, v211
	v_med3_f32 v142, v142, s6, v1
	v_med3_f32 v145, v145, s6, v1
	v_cvt_pk_fp8_f32 v201, v142, v145 op_sel:[0,0,1]
	v_lshl_add_u64 v[202:203], v[146:147], 0, v[134:135]
	global_store_dwordx4 v[202:203], v[198:201], off nt
	ds_read2_b32 v[198:199], v174 offset1:32
	ds_read2_b32 v[200:201], v174 offset0:64 offset1:96
	ds_read2_b32 v[202:203], v174 offset0:128 offset1:160
	ds_read2_b32 v[204:205], v174 offset0:192 offset1:224
	ds_read_b32 v142, v175
	ds_read_b32 v145, v176
	ds_read_b32 v206, v177
	ds_read_b32 v207, v178
	ds_read_b32 v208, v179
	ds_read_b32 v209, v180
	ds_read_b32 v210, v181
	ds_read_b32 v211, v182
	s_waitcnt lgkmcnt(11)
	v_max_f32_e32 v198, v198, v198
	v_med3_f32 v212, v198, s6, v1
	v_max_f32_e32 v198, v199, v199
	v_med3_f32 v199, v198, s6, v1
	v_mov_b32_e32 v198, v143
	v_cvt_pk_fp8_f32 v198, v212, v199
	s_waitcnt lgkmcnt(10)
	v_max_f32_e32 v199, v200, v200
	v_max_f32_e32 v200, v201, v201
	v_med3_f32 v199, v199, s6, v1
	v_med3_f32 v200, v200, s6, v1
	v_cvt_pk_fp8_f32 v198, v199, v200 op_sel:[0,0,1]
	s_waitcnt lgkmcnt(9)
	v_max_f32_e32 v199, v202, v202
	v_med3_f32 v200, v199, s6, v1
	v_max_f32_e32 v199, v203, v203
	v_med3_f32 v201, v199, s6, v1
	v_mov_b32_e32 v199, v143
	v_cvt_pk_fp8_f32 v199, v200, v201
	s_waitcnt lgkmcnt(8)
	v_max_f32_e32 v200, v204, v204
	v_max_f32_e32 v201, v205, v205
	v_med3_f32 v200, v200, s6, v1
	v_med3_f32 v201, v201, s6, v1
	s_waitcnt lgkmcnt(7)
	v_max_f32_e32 v142, v142, v142
	s_waitcnt lgkmcnt(6)
	v_max_f32_e32 v145, v145, v145
	v_cvt_pk_fp8_f32 v199, v200, v201 op_sel:[0,0,1]
	v_med3_f32 v142, v142, s6, v1
	v_med3_f32 v145, v145, s6, v1
	v_mov_b32_e32 v200, v143
	v_cvt_pk_fp8_f32 v200, v142, v145
	s_waitcnt lgkmcnt(5)
	v_max_f32_e32 v142, v206, v206
	s_waitcnt lgkmcnt(4)
	v_max_f32_e32 v145, v207, v207
	v_med3_f32 v142, v142, s6, v1
	v_med3_f32 v145, v145, s6, v1
	v_cvt_pk_fp8_f32 v200, v142, v145 op_sel:[0,0,1]
	s_waitcnt lgkmcnt(3)
	v_max_f32_e32 v142, v208, v208
	s_waitcnt lgkmcnt(2)
	v_max_f32_e32 v145, v209, v209
	v_med3_f32 v142, v142, s6, v1
	v_med3_f32 v145, v145, s6, v1
	v_mov_b32_e32 v201, v143
	v_cvt_pk_fp8_f32 v201, v142, v145
	s_waitcnt lgkmcnt(1)
	v_max_f32_e32 v142, v210, v210
	s_waitcnt lgkmcnt(0)
	v_max_f32_e32 v145, v211, v211
	v_med3_f32 v142, v142, s6, v1
	v_med3_f32 v145, v145, s6, v1
	v_cvt_pk_fp8_f32 v201, v142, v145 op_sel:[0,0,1]
	v_lshl_add_u64 v[202:203], v[146:147], 0, v[136:137]
	v_lshl_add_u64 v[146:147], v[146:147], 0, v[138:139]
	global_store_dwordx4 v[202:203], v[198:201], off nt
	ds_read2_b32 v[198:199], v183 offset1:32
	ds_read2_b32 v[200:201], v183 offset0:64 offset1:96
	ds_read2_b32 v[202:203], v183 offset0:128 offset1:160
	ds_read2_b32 v[204:205], v183 offset0:192 offset1:224
	ds_read_b32 v142, v184
	ds_read_b32 v145, v185
	ds_read_b32 v206, v186
	ds_read_b32 v207, v187
	ds_read_b32 v208, v188
	ds_read_b32 v209, v189
	ds_read_b32 v210, v190
	ds_read_b32 v211, v191
	s_waitcnt lgkmcnt(11)
	v_max_f32_e32 v198, v198, v198
	v_med3_f32 v212, v198, s6, v1
	v_max_f32_e32 v198, v199, v199
	v_med3_f32 v199, v198, s6, v1
	v_mov_b32_e32 v198, v143
	v_cvt_pk_fp8_f32 v198, v212, v199
	s_waitcnt lgkmcnt(10)
	v_max_f32_e32 v199, v200, v200
	v_max_f32_e32 v200, v201, v201
	v_med3_f32 v199, v199, s6, v1
	v_med3_f32 v200, v200, s6, v1
	v_cvt_pk_fp8_f32 v198, v199, v200 op_sel:[0,0,1]
	s_waitcnt lgkmcnt(9)
	v_max_f32_e32 v199, v202, v202
	v_med3_f32 v200, v199, s6, v1
	v_max_f32_e32 v199, v203, v203
	v_med3_f32 v201, v199, s6, v1
	v_mov_b32_e32 v199, v143
	v_cvt_pk_fp8_f32 v199, v200, v201
	s_waitcnt lgkmcnt(8)
	v_max_f32_e32 v200, v204, v204
	v_max_f32_e32 v201, v205, v205
	v_med3_f32 v200, v200, s6, v1
	v_med3_f32 v201, v201, s6, v1
	s_waitcnt lgkmcnt(7)
	v_max_f32_e32 v142, v142, v142
	s_waitcnt lgkmcnt(6)
	v_max_f32_e32 v145, v145, v145
	v_cvt_pk_fp8_f32 v199, v200, v201 op_sel:[0,0,1]
	v_med3_f32 v142, v142, s6, v1
	v_med3_f32 v145, v145, s6, v1
	v_mov_b32_e32 v200, v143
	v_cvt_pk_fp8_f32 v200, v142, v145
	s_waitcnt lgkmcnt(5)
	v_max_f32_e32 v142, v206, v206
	s_waitcnt lgkmcnt(4)
	v_max_f32_e32 v145, v207, v207
	v_med3_f32 v142, v142, s6, v1
	v_med3_f32 v145, v145, s6, v1
	v_cvt_pk_fp8_f32 v200, v142, v145 op_sel:[0,0,1]
	s_waitcnt lgkmcnt(3)
	v_max_f32_e32 v142, v208, v208
	s_waitcnt lgkmcnt(2)
	v_max_f32_e32 v145, v209, v209
	v_med3_f32 v142, v142, s6, v1
	v_med3_f32 v145, v145, s6, v1
	v_mov_b32_e32 v201, v143
	v_cvt_pk_fp8_f32 v201, v142, v145
	s_waitcnt lgkmcnt(1)
	v_max_f32_e32 v142, v210, v210
	s_waitcnt lgkmcnt(0)
	v_max_f32_e32 v145, v211, v211
	v_med3_f32 v142, v142, s6, v1
	v_med3_f32 v145, v145, s6, v1
	v_cvt_pk_fp8_f32 v201, v142, v145 op_sel:[0,0,1]
	global_store_dwordx4 v[146:147], v[198:201], off nt
	s_waitcnt lgkmcnt(0)
	s_xor_b64 s[84:85], s[84:85], -1
	s_and_b64 vcc, exec, s[84:85]
	s_cbranch_vccz .LBB0_755

; #define GAS __attribute__((address_space(1)))
; #define LAS __attribute__((address_space(3)))
; __device__ __forceinline__ void p8_issue(const TItem8& t, f32x4 (&v)[16], int lane) {
;     const GAS f32x4* src = (const GAS f32x4*)((const GAS float*)t.src + (size_t)(lane >> 3) * t.N + 4 * (lane & 7));
; #pragma unroll
;     for (int i = 0; i < 16; ++i) v[i] = __builtin_nontemporal_load(src + (size_t)(2 * i) * t.N);
; }
; __device__ __forceinline__ void p8_finish(const TItem8& t, const f32x4 (&v)[16], LAS float* scr, int lane) {
; #pragma unroll
;     for (int i = 0; i < 16; ++i) *(LAS f32x4*)(scr + (8 * i + (lane >> 3)) * 32 + (((lane & 7) ^ (i & 7)) << 2)) = v[i] * W8_SCALE;
.LBB0_809:
	s_lshl_b64 s[10:11], s[86:87], 11
	s_add_u32 s0, s92, s10
	v_mul_u32_u24_e32 v66, s94, v225
	s_addc_u32 s10, s93, s11
	v_lshlrev_b32_e32 v142, 2, v66
	s_add_u32 s82, s0, s90
	v_lshl_add_u64 v[66:67], s[88:89], 0, v[142:143]
	v_mov_b32_e32 v145, v143
	s_addc_u32 s83, s10, s91
	v_lshl_add_u64 v[66:67], v[66:67], 0, v[144:145]
	s_lshl_b32 s0, s94, 5
	v_lshl_add_u64 v[74:75], v[66:67], 0, s[0:1]
	global_load_dwordx4 v[66:69], v[66:67], off nt
	s_nop 0
	global_load_dwordx4 v[70:73], v[74:75], off nt
	v_lshl_add_u64 v[74:75], v[74:75], 0, s[0:1]
	v_lshl_add_u64 v[82:83], v[74:75], 0, s[0:1]
	global_load_dwordx4 v[74:77], v[74:75], off nt
	s_nop 0
	global_load_dwordx4 v[78:81], v[82:83], off nt
	v_lshl_add_u64 v[82:83], v[82:83], 0, s[0:1]
	v_lshl_add_u64 v[90:91], v[82:83], 0, s[0:1]
	global_load_dwordx4 v[82:85], v[82:83], off nt
	s_nop 0
	global_load_dwordx4 v[86:89], v[90:91], off nt
	v_lshl_add_u64 v[90:91], v[90:91], 0, s[0:1]
	v_lshl_add_u64 v[98:99], v[90:91], 0, s[0:1]
	v_lshl_add_u64 v[102:103], v[98:99], 0, s[0:1]
	v_lshl_add_u64 v[106:107], v[102:103], 0, s[0:1]
	v_lshl_add_u64 v[110:111], v[106:107], 0, s[0:1]
	v_lshl_add_u64 v[114:115], v[110:111], 0, s[0:1]
	v_lshl_add_u64 v[118:119], v[114:115], 0, s[0:1]
	v_lshl_add_u64 v[122:123], v[118:119], 0, s[0:1]
	v_lshl_add_u64 v[126:127], v[122:123], 0, s[0:1]
	global_load_dwordx4 v[90:93], v[90:91], off nt
	s_nop 0
	global_load_dwordx4 v[94:97], v[98:99], off nt
	s_nop 0
	global_load_dwordx4 v[98:101], v[102:103], off nt
	s_nop 0
	global_load_dwordx4 v[102:105], v[106:107], off nt
	s_nop 0
	global_load_dwordx4 v[106:109], v[110:111], off nt
	s_nop 0
	global_load_dwordx4 v[110:113], v[114:115], off nt
	s_nop 0
	global_load_dwordx4 v[114:117], v[118:119], off nt
	s_nop 0
	global_load_dwordx4 v[118:121], v[122:123], off nt
	s_nop 0
	global_load_dwordx4 v[122:125], v[126:127], off nt
	v_lshl_add_u64 v[126:127], v[126:127], 0, s[0:1]
	global_load_dwordx4 v[126:129], v[126:127], off nt
	s_waitcnt vmcnt(31)
	v_pk_mul_f32 v[200:201], v[4:5], s[74:75] op_sel_hi:[1,0]
	v_pk_mul_f32 v[198:199], v[2:3], s[74:75] op_sel_hi:[1,0]
	ds_write_b128 v148, v[198:201]
	s_waitcnt vmcnt(30)
	v_pk_mul_f32 v[200:201], v[8:9], s[74:75] op_sel_hi:[1,0]
	v_pk_mul_f32 v[198:199], v[6:7], s[74:75] op_sel_hi:[1,0]
	ds_write_b128 v149, v[198:201] offset:1024
	s_waitcnt vmcnt(29)
	v_pk_mul_f32 v[200:201], v[12:13], s[74:75] op_sel_hi:[1,0]
	v_pk_mul_f32 v[198:199], v[10:11], s[74:75] op_sel_hi:[1,0]
	ds_write_b128 v150, v[198:201] offset:2048
	s_waitcnt vmcnt(28)
	v_pk_mul_f32 v[200:201], v[16:17], s[74:75] op_sel_hi:[1,0]
	v_pk_mul_f32 v[198:199], v[14:15], s[74:75] op_sel_hi:[1,0]
	ds_write_b128 v151, v[198:201] offset:3072
	s_waitcnt vmcnt(27)
	v_pk_mul_f32 v[200:201], v[20:21], s[74:75] op_sel_hi:[1,0]
	v_pk_mul_f32 v[198:199], v[18:19], s[74:75] op_sel_hi:[1,0]
	ds_write_b128 v152, v[198:201] offset:4096
	s_waitcnt vmcnt(26)
	v_pk_mul_f32 v[200:201], v[24:25], s[74:75] op_sel_hi:[1,0]
	v_pk_mul_f32 v[198:199], v[22:23], s[74:75] op_sel_hi:[1,0]
	ds_write_b128 v153, v[198:201] offset:5120
	s_waitcnt vmcnt(25)
	v_pk_mul_f32 v[200:201], v[28:29], s[74:75] op_sel_hi:[1,0]
	v_pk_mul_f32 v[198:199], v[26:27], s[74:75] op_sel_hi:[1,0]
	ds_write_b128 v154, v[198:201] offset:6144
	s_waitcnt vmcnt(24)
	v_pk_mul_f32 v[200:201], v[32:33], s[74:75] op_sel_hi:[1,0]
	v_pk_mul_f32 v[198:199], v[30:31], s[74:75] op_sel_hi:[1,0]
	ds_write_b128 v155, v[198:201] offset:7168
	s_waitcnt vmcnt(23)
	v_pk_mul_f32 v[200:201], v[36:37], s[74:75] op_sel_hi:[1,0]
	v_pk_mul_f32 v[198:199], v[34:35], s[74:75] op_sel_hi:[1,0]
	ds_write_b128 v148, v[198:201] offset:8192
	s_waitcnt vmcnt(22)
	v_pk_mul_f32 v[200:201], v[40:41], s[74:75] op_sel_hi:[1,0]
	v_pk_mul_f32 v[198:199], v[38:39], s[74:75] op_sel_hi:[1,0]
	ds_write_b128 v149, v[198:201] offset:9216
	s_waitcnt vmcnt(21)
	v_pk_mul_f32 v[200:201], v[44:45], s[74:75] op_sel_hi:[1,0]
	v_pk_mul_f32 v[198:199], v[42:43], s[74:75] op_sel_hi:[1,0]
	ds_write_b128 v150, v[198:201] offset:10240
	s_waitcnt vmcnt(20)
	v_pk_mul_f32 v[200:201], v[48:49], s[74:75] op_sel_hi:[1,0]
	v_pk_mul_f32 v[198:199], v[46:47], s[74:75] op_sel_hi:[1,0]
	ds_write_b128 v151, v[198:201] offset:11264
	s_waitcnt vmcnt(19)
	v_pk_mul_f32 v[200:201], v[52:53], s[74:75] op_sel_hi:[1,0]
	v_pk_mul_f32 v[198:199], v[50:51], s[74:75] op_sel_hi:[1,0]
	ds_write_b128 v152, v[198:201] offset:12288
	s_waitcnt vmcnt(18)
	v_pk_mul_f32 v[200:201], v[56:57], s[74:75] op_sel_hi:[1,0]
	v_pk_mul_f32 v[198:199], v[54:55], s[74:75] op_sel_hi:[1,0]
	ds_write_b128 v153, v[198:201] offset:13312
	s_waitcnt vmcnt(17)
	v_pk_mul_f32 v[200:201], v[60:61], s[74:75] op_sel_hi:[1,0]
	v_pk_mul_f32 v[198:199], v[58:59], s[74:75] op_sel_hi:[1,0]
	ds_write_b128 v154, v[198:201] offset:14336
	s_waitcnt vmcnt(16)
	v_pk_mul_f32 v[200:201], v[64:65], s[74:75] op_sel_hi:[1,0]
	v_pk_mul_f32 v[198:199], v[62:63], s[74:75] op_sel_hi:[1,0]
	ds_write_b128 v155, v[198:201] offset:15360
	s_branch .Lcv1_5_810

; #define GAS __attribute__((address_space(1)))
; __device__ __forceinline__ void p8_finish(const TItem8& t, const f32x4 (&v)[16], LAS float* scr, int lane) {
;     ...
;     const int c = lane & 7;
; #pragma unroll
;     for (int j = 0; j < 4; ++j) { const int n = (lane >> 3) + 8 * j; float x[16];
; #pragma unroll
;         for (int i = 0; i < 16; ++i) { const int k = 16 * c + i; x[i] = scr[k * 32 + ((((n >> 2) ^ ((k >> 3) & 7)) << 2) | (n & 3))]; }
;         int w[4];
; #pragma unroll
;         for (int g = 0; g < 4; ++g) { int q = 0; q = __builtin_amdgcn_cvt_pk_fp8_f32(fminf(fmaxf(x[4 * g], -448.f), 448.f), fminf(fmaxf(x[4 * g + 1], -448.f), 448.f), q, false);
;             q = __builtin_amdgcn_cvt_pk_fp8_f32(fminf(fmaxf(x[4 * g + 2], -448.f), 448.f), fminf(fmaxf(x[4 * g + 3], -448.f), 448.f), q, true); w[g] = q; }
;         v4u o; o.x = (unsigned)w[0]; o.y = (unsigned)w[1]; o.z = (unsigned)w[2]; o.w = (unsigned)w[3];
;         __builtin_nontemporal_store(o, (GAS v4u*)(t.dst + (size_t)n * t.Kd + 16 * c)); }
.Lcv1_5_810:
	s_waitcnt lgkmcnt(0)
	ds_read2_b32 v[198:199], v156 offset1:32
	ds_read2_b32 v[200:201], v156 offset0:64 offset1:96
	ds_read2_b32 v[202:203], v156 offset0:128 offset1:160
	ds_read2_b32 v[204:205], v156 offset0:192 offset1:224
	ds_read_b32 v142, v157
	ds_read_b32 v145, v158
	ds_read_b32 v206, v159
	ds_read_b32 v207, v160
	ds_read_b32 v208, v161
	ds_read_b32 v209, v162
	ds_read_b32 v210, v163
	ds_read_b32 v211, v164
	s_waitcnt lgkmcnt(11)
	v_max_f32_e32 v198, v198, v198
	v_med3_f32 v212, v198, s5, v1
	v_max_f32_e32 v198, v199, v199
	v_med3_f32 v199, v198, s5, v1
	v_mov_b32_e32 v198, 0
	v_cvt_pk_fp8_f32 v198, v212, v199
	s_waitcnt lgkmcnt(10)
	v_max_f32_e32 v199, v200, v200
	v_max_f32_e32 v200, v201, v201
	v_med3_f32 v199, v199, s5, v1
	v_med3_f32 v200, v200, s5, v1
	v_cvt_pk_fp8_f32 v198, v199, v200 op_sel:[0,0,1]
	s_waitcnt lgkmcnt(9)
	v_max_f32_e32 v199, v202, v202
	v_med3_f32 v200, v199, s5, v1
	v_max_f32_e32 v199, v203, v203
	v_med3_f32 v201, v199, s5, v1
	v_mov_b32_e32 v199, 0
	v_cvt_pk_fp8_f32 v199, v200, v201
	s_waitcnt lgkmcnt(8)
	v_max_f32_e32 v200, v204, v204
	v_max_f32_e32 v201, v205, v205
	v_med3_f32 v200, v200, s5, v1
	v_med3_f32 v201, v201, s5, v1
	s_waitcnt lgkmcnt(7)
	v_max_f32_e32 v142, v142, v142
	s_waitcnt lgkmcnt(6)
	v_max_f32_e32 v145, v145, v145
	v_cvt_pk_fp8_f32 v199, v200, v201 op_sel:[0,0,1]
	v_med3_f32 v142, v142, s5, v1
	v_med3_f32 v145, v145, s5, v1
	v_mov_b32_e32 v200, 0
	v_cvt_pk_fp8_f32 v200, v142, v145
	s_waitcnt lgkmcnt(5)
	v_max_f32_e32 v142, v206, v206
	s_waitcnt lgkmcnt(4)
	v_max_f32_e32 v145, v207, v207
	v_med3_f32 v142, v142, s5, v1
	v_med3_f32 v145, v145, s5, v1
	v_cvt_pk_fp8_f32 v200, v142, v145 op_sel:[0,0,1]
	s_waitcnt lgkmcnt(3)
	v_max_f32_e32 v142, v208, v208
	s_waitcnt lgkmcnt(2)
	v_max_f32_e32 v145, v209, v209
	v_med3_f32 v142, v142, s5, v1
	v_med3_f32 v145, v145, s5, v1
	v_mov_b32_e32 v201, 0
	v_cvt_pk_fp8_f32 v201, v142, v145
	s_waitcnt lgkmcnt(1)
	v_max_f32_e32 v142, v210, v210
	s_waitcnt lgkmcnt(0)
	v_max_f32_e32 v145, v211, v211
	v_med3_f32 v142, v142, s5, v1
	v_med3_f32 v145, v145, s5, v1
	v_cvt_pk_fp8_f32 v201, v142, v145 op_sel:[0,0,1]
	ds_read2_b32 v[202:203], v165 offset1:32
	ds_read2_b32 v[204:205], v165 offset0:64 offset1:96
	ds_read2_b32 v[206:207], v165 offset0:128 offset1:160
	ds_read2_b32 v[208:209], v165 offset0:192 offset1:224
	ds_read_b32 v142, v166
	ds_read_b32 v145, v167
	ds_read_b32 v210, v168
	ds_read_b32 v211, v169
	ds_read_b32 v212, v170
	ds_read_b32 v213, v171
	ds_read_b32 v214, v172
	ds_read_b32 v215, v173
	s_waitcnt lgkmcnt(11)
	v_max_f32_e32 v202, v202, v202
	v_med3_f32 v216, v202, s5, v1
	v_max_f32_e32 v202, v203, v203
	v_med3_f32 v203, v202, s5, v1
	v_mov_b32_e32 v202, 0
	v_cvt_pk_fp8_f32 v202, v216, v203
	s_waitcnt lgkmcnt(10)
	v_max_f32_e32 v203, v204, v204
	v_max_f32_e32 v204, v205, v205
	v_med3_f32 v203, v203, s5, v1
	v_med3_f32 v204, v204, s5, v1
	v_cvt_pk_fp8_f32 v202, v203, v204 op_sel:[0,0,1]
	s_waitcnt lgkmcnt(9)
	v_max_f32_e32 v203, v206, v206
	v_med3_f32 v204, v203, s5, v1
	v_max_f32_e32 v203, v207, v207
	v_med3_f32 v205, v203, s5, v1
	v_mov_b32_e32 v203, 0
	v_cvt_pk_fp8_f32 v203, v204, v205
	s_waitcnt lgkmcnt(8)
	v_max_f32_e32 v204, v208, v208
	v_max_f32_e32 v205, v209, v209
	v_med3_f32 v204, v204, s5, v1
	v_med3_f32 v205, v205, s5, v1
	s_waitcnt lgkmcnt(7)
	v_max_f32_e32 v142, v142, v142
	s_waitcnt lgkmcnt(6)
	v_max_f32_e32 v145, v145, v145
	v_cvt_pk_fp8_f32 v203, v204, v205 op_sel:[0,0,1]
	v_med3_f32 v142, v142, s5, v1
	v_med3_f32 v145, v145, s5, v1
	v_mov_b32_e32 v204, 0
	v_cvt_pk_fp8_f32 v204, v142, v145
	s_waitcnt lgkmcnt(5)
	v_max_f32_e32 v142, v210, v210
	s_waitcnt lgkmcnt(4)
	v_max_f32_e32 v145, v211, v211
	v_med3_f32 v142, v142, s5, v1
	v_med3_f32 v145, v145, s5, v1
	v_cvt_pk_fp8_f32 v204, v142, v145 op_sel:[0,0,1]
	s_waitcnt lgkmcnt(3)
	v_max_f32_e32 v142, v212, v212
	s_waitcnt lgkmcnt(2)
	v_max_f32_e32 v145, v213, v213
	v_med3_f32 v142, v142, s5, v1
	v_med3_f32 v145, v145, s5, v1
	v_mov_b32_e32 v205, 0
	v_cvt_pk_fp8_f32 v205, v142, v145
	s_waitcnt lgkmcnt(1)
	v_max_f32_e32 v142, v214, v214
	s_waitcnt lgkmcnt(0)
	v_max_f32_e32 v145, v215, v215
	v_med3_f32 v142, v142, s5, v1
	v_med3_f32 v145, v145, s5, v1
	v_cvt_pk_fp8_f32 v205, v142, v145 op_sel:[0,0,1]
	v_lshl_add_u64 v[146:147], s[80:81], 0, v[130:131]
	v_lshl_add_u64 v[206:207], v[146:147], 0, v[132:133]
	global_store_dwordx4 v[206:207], v[198:201], off nt
	s_andn2_b64 vcc, exec, s[84:85]
	s_mov_b64 s[84:85], 0
	v_lshl_add_u64 v[198:199], v[146:147], 0, v[134:135]
	global_store_dwordx4 v[198:199], v[202:205], off nt
	ds_read2_b32 v[198:199], v174 offset1:32
	ds_read2_b32 v[200:201], v174 offset0:64 offset1:96
	ds_read2_b32 v[202:203], v174 offset0:128 offset1:160
	ds_read2_b32 v[204:205], v174 offset0:192 offset1:224
	ds_read_b32 v142, v175
	ds_read_b32 v145, v176
	ds_read_b32 v206, v177
	ds_read_b32 v207, v178
	ds_read_b32 v208, v179
	ds_read_b32 v209, v180
	ds_read_b32 v210, v181
	ds_read_b32 v211, v182
	s_waitcnt lgkmcnt(11)
; #define GAS __attribute__((address_space(1)))
; __device__ __forceinline__ TItem8 p8_decode(const Args& args, unsigned char* ws, int it) {
;     TItem8 t;
;     if (it >= P8_N) { const int j = it - P8_N; it = (P8_E0 + j / P8_DN1) * (P8_GU1 + P8_DN1) + P8_GU1 + j % P8_DN1; }
;     else if (it >= P8_E0 * (P8_GU1 + P8_DN1)) { const int r = it - P8_E0 * (P8_GU1 + P8_DN1); it = (P8_E0 + r / P8_GU1) * (P8_GU1 + P8_DN1) + r % P8_GU1; }
;     const int e = it / (P8_GU1 + P8_DN1), q = it % (P8_GU1 + P8_DN1);
; __device__ __forceinline__ void p8_finish(const TItem8& t, const f32x4 (&v)[16], LAS float* scr, int lane) {
;     ...
;     const int c = lane & 7;
; #pragma unroll
;     for (int j = 0; j < 4; ++j) { const int n = (lane >> 3) + 8 * j; float x[16];
; #pragma unroll
;         for (int i = 0; i < 16; ++i) { const int k = 16 * c + i; x[i] = scr[k * 32 + ((((n >> 2) ^ ((k >> 3) & 7)) << 2) | (n & 3))]; }
;         int w[4];
; #pragma unroll
;         for (int g = 0; g < 4; ++g) { int q = 0; q = __builtin_amdgcn_cvt_pk_fp8_f32(fminf(fmaxf(x[4 * g], -448.f), 448.f), fminf(fmaxf(x[4 * g + 1], -448.f), 448.f), q, false);
;             q = __builtin_amdgcn_cvt_pk_fp8_f32(fminf(fmaxf(x[4 * g + 2], -448.f), 448.f), fminf(fmaxf(x[4 * g + 3], -448.f), 448.f), q, true); w[g] = q; }
;         v4u o; o.x = (unsigned)w[0]; o.y = (unsigned)w[1]; o.z = (unsigned)w[2]; o.w = (unsigned)w[3];
;         __builtin_nontemporal_store(o, (GAS v4u*)(t.dst + (size_t)n * t.Kd + 16 * c)); }
	v_max_f32_e32 v198, v198, v198
	v_med3_f32 v212, v198, s5, v1
	v_max_f32_e32 v198, v199, v199
	v_med3_f32 v199, v198, s5, v1
	v_mov_b32_e32 v198, 0
	v_cvt_pk_fp8_f32 v198, v212, v199
	s_waitcnt lgkmcnt(10)
	v_max_f32_e32 v199, v200, v200
	v_max_f32_e32 v200, v201, v201
	v_med3_f32 v199, v199, s5, v1
	v_med3_f32 v200, v200, s5, v1
	v_cvt_pk_fp8_f32 v198, v199, v200 op_sel:[0,0,1]
	s_waitcnt lgkmcnt(9)
	v_max_f32_e32 v199, v202, v202
	v_med3_f32 v200, v199, s5, v1
	v_max_f32_e32 v199, v203, v203
	v_med3_f32 v201, v199, s5, v1
	v_mov_b32_e32 v199, 0
	v_cvt_pk_fp8_f32 v199, v200, v201
	s_waitcnt lgkmcnt(8)
	v_max_f32_e32 v200, v204, v204
	v_max_f32_e32 v201, v205, v205
	v_med3_f32 v200, v200, s5, v1
	v_med3_f32 v201, v201, s5, v1
	s_waitcnt lgkmcnt(7)
	v_max_f32_e32 v142, v142, v142
	s_waitcnt lgkmcnt(6)
	v_max_f32_e32 v145, v145, v145
	v_cvt_pk_fp8_f32 v199, v200, v201 op_sel:[0,0,1]
	v_med3_f32 v142, v142, s5, v1
	v_med3_f32 v145, v145, s5, v1
	v_mov_b32_e32 v200, 0
	v_cvt_pk_fp8_f32 v200, v142, v145
	s_waitcnt lgkmcnt(5)
	v_max_f32_e32 v142, v206, v206
	s_waitcnt lgkmcnt(4)
	v_max_f32_e32 v145, v207, v207
	v_med3_f32 v142, v142, s5, v1
	v_med3_f32 v145, v145, s5, v1
	v_cvt_pk_fp8_f32 v200, v142, v145 op_sel:[0,0,1]
	s_waitcnt lgkmcnt(3)
	v_max_f32_e32 v142, v208, v208
	s_waitcnt lgkmcnt(2)
	v_max_f32_e32 v145, v209, v209
	v_med3_f32 v142, v142, s5, v1
	v_med3_f32 v145, v145, s5, v1
	v_mov_b32_e32 v201, 0
	v_cvt_pk_fp8_f32 v201, v142, v145
	s_waitcnt lgkmcnt(1)
	v_max_f32_e32 v142, v210, v210
	s_waitcnt lgkmcnt(0)
	v_max_f32_e32 v145, v211, v211
	v_med3_f32 v142, v142, s5, v1
	v_med3_f32 v145, v145, s5, v1
	v_cvt_pk_fp8_f32 v201, v142, v145 op_sel:[0,0,1]
	ds_read2_b32 v[202:203], v183 offset1:32
	ds_read2_b32 v[204:205], v183 offset0:64 offset1:96
	ds_read2_b32 v[206:207], v183 offset0:128 offset1:160
	ds_read2_b32 v[208:209], v183 offset0:192 offset1:224
	ds_read_b32 v142, v184
	ds_read_b32 v145, v185
	ds_read_b32 v210, v186
	ds_read_b32 v211, v187
	ds_read_b32 v212, v188
	ds_read_b32 v213, v189
	ds_read_b32 v214, v190
	ds_read_b32 v215, v191
	s_waitcnt lgkmcnt(11)
	v_max_f32_e32 v202, v202, v202
	v_med3_f32 v216, v202, s5, v1
	v_max_f32_e32 v202, v203, v203
	v_med3_f32 v203, v202, s5, v1
	v_mov_b32_e32 v202, 0
	v_cvt_pk_fp8_f32 v202, v216, v203
	s_waitcnt lgkmcnt(10)
	v_max_f32_e32 v203, v204, v204
	v_max_f32_e32 v204, v205, v205
	v_med3_f32 v203, v203, s5, v1
	v_med3_f32 v204, v204, s5, v1
	v_cvt_pk_fp8_f32 v202, v203, v204 op_sel:[0,0,1]
	s_waitcnt lgkmcnt(9)
	v_max_f32_e32 v203, v206, v206
	v_med3_f32 v204, v203, s5, v1
	v_max_f32_e32 v203, v207, v207
	v_med3_f32 v205, v203, s5, v1
	v_mov_b32_e32 v203, 0
	v_cvt_pk_fp8_f32 v203, v204, v205
	s_waitcnt lgkmcnt(8)
	v_max_f32_e32 v204, v208, v208
	v_max_f32_e32 v205, v209, v209
	v_med3_f32 v204, v204, s5, v1
	v_med3_f32 v205, v205, s5, v1
	s_waitcnt lgkmcnt(7)
	v_max_f32_e32 v142, v142, v142
	s_waitcnt lgkmcnt(6)
	v_max_f32_e32 v145, v145, v145
	v_cvt_pk_fp8_f32 v203, v204, v205 op_sel:[0,0,1]
	v_med3_f32 v142, v142, s5, v1
	v_med3_f32 v145, v145, s5, v1
	v_mov_b32_e32 v204, 0
	v_cvt_pk_fp8_f32 v204, v142, v145
	s_waitcnt lgkmcnt(5)
	v_max_f32_e32 v142, v210, v210
	s_waitcnt lgkmcnt(4)
	v_max_f32_e32 v145, v211, v211
	v_med3_f32 v142, v142, s5, v1
	v_med3_f32 v145, v145, s5, v1
	v_cvt_pk_fp8_f32 v204, v142, v145 op_sel:[0,0,1]
	s_waitcnt lgkmcnt(3)
	v_max_f32_e32 v142, v212, v212
	s_waitcnt lgkmcnt(2)
	v_max_f32_e32 v145, v213, v213
	v_med3_f32 v142, v142, s5, v1
	v_med3_f32 v145, v145, s5, v1
	v_mov_b32_e32 v205, 0
	v_cvt_pk_fp8_f32 v205, v142, v145
	s_waitcnt lgkmcnt(1)
	v_max_f32_e32 v142, v214, v214
	s_waitcnt lgkmcnt(0)
	v_max_f32_e32 v145, v215, v215
	v_med3_f32 v142, v142, s5, v1
	v_med3_f32 v145, v145, s5, v1
	v_cvt_pk_fp8_f32 v205, v142, v145 op_sel:[0,0,1]
	v_lshl_add_u64 v[206:207], v[146:147], 0, v[136:137]
	v_lshl_add_u64 v[146:147], v[146:147], 0, v[138:139]
	global_store_dwordx4 v[206:207], v[198:201], off nt
	global_store_dwordx4 v[146:147], v[202:205], off nt
	s_waitcnt lgkmcnt(0)
	s_cbranch_vccnz .LBB0_797
	s_add_i32 s6, s6, 2
	s_lshl_b32 s0, s6, 9
	s_add_i32 s0, s0, s4
	s_cmp_lt_i32 s0, 0x16400
	s_cselect_b64 s[84:85], -1, 0
	s_cmp_gt_i32 s0, 0x163ff
	s_cbranch_scc1 .LBB0_823
	s_cmp_lt_i32 s0, 0x12c00
	s_cbranch_scc1 .LBB0_814
	s_add_i32 s0, s0, 0xfffed400
	s_lshr_b32 s7, s0, 11
	s_mulk_i32 s7, 0xc00
	s_and_b32 s0, s0, 0x7ff
	s_add_i32 s0, s0, s7
	s_add_i32 s0, s0, 0x12c00

; #define GAS __attribute__((address_space(1)))
; #define LAS __attribute__((address_space(3)))
; __device__ __forceinline__ void p8_issue(const TItem8& t, f32x4 (&v)[16], int lane) {
;     const GAS f32x4* src = (const GAS f32x4*)((const GAS float*)t.src + (size_t)(lane >> 3) * t.N + 4 * (lane & 7));
; #pragma unroll
;     for (int i = 0; i < 16; ++i) v[i] = __builtin_nontemporal_load(src + (size_t)(2 * i) * t.N);
; }
; __device__ __forceinline__ void p8_finish(const TItem8& t, const f32x4 (&v)[16], LAS float* scr, int lane) {
; #pragma unroll
;     for (int i = 0; i < 16; ++i) *(LAS f32x4*)(scr + (8 * i + (lane >> 3)) * 32 + (((lane & 7) ^ (i & 7)) << 2)) = v[i] * W8_SCALE;
.LBB0_822:
	s_lshl_b64 s[10:11], s[86:87], 11
	s_add_u32 s0, s92, s10
	v_mul_u32_u24_e32 v2, s94, v225
	s_addc_u32 s7, s93, s11
	v_lshlrev_b32_e32 v142, 2, v2
	s_add_u32 s80, s0, s90
	v_lshl_add_u64 v[2:3], s[88:89], 0, v[142:143]
	v_mov_b32_e32 v145, v143
	s_addc_u32 s81, s7, s91
	v_lshl_add_u64 v[2:3], v[2:3], 0, v[144:145]
	s_lshl_b32 s0, s94, 5
	v_lshl_add_u64 v[10:11], v[2:3], 0, s[0:1]
	global_load_dwordx4 v[2:5], v[2:3], off nt
	s_nop 0
	global_load_dwordx4 v[6:9], v[10:11], off nt
	v_lshl_add_u64 v[10:11], v[10:11], 0, s[0:1]
	v_lshl_add_u64 v[18:19], v[10:11], 0, s[0:1]
	global_load_dwordx4 v[10:13], v[10:11], off nt
	s_nop 0
	global_load_dwordx4 v[14:17], v[18:19], off nt
	v_lshl_add_u64 v[18:19], v[18:19], 0, s[0:1]
	v_lshl_add_u64 v[26:27], v[18:19], 0, s[0:1]
	global_load_dwordx4 v[18:21], v[18:19], off nt
	s_nop 0
	global_load_dwordx4 v[22:25], v[26:27], off nt
	v_lshl_add_u64 v[26:27], v[26:27], 0, s[0:1]
	v_lshl_add_u64 v[34:35], v[26:27], 0, s[0:1]
	v_lshl_add_u64 v[38:39], v[34:35], 0, s[0:1]
	v_lshl_add_u64 v[42:43], v[38:39], 0, s[0:1]
	v_lshl_add_u64 v[46:47], v[42:43], 0, s[0:1]
	v_lshl_add_u64 v[50:51], v[46:47], 0, s[0:1]
	v_lshl_add_u64 v[54:55], v[50:51], 0, s[0:1]
	v_lshl_add_u64 v[58:59], v[54:55], 0, s[0:1]
	v_lshl_add_u64 v[62:63], v[58:59], 0, s[0:1]
	global_load_dwordx4 v[26:29], v[26:27], off nt
	s_nop 0
	global_load_dwordx4 v[30:33], v[34:35], off nt
	s_nop 0
	global_load_dwordx4 v[34:37], v[38:39], off nt
	s_nop 0
	global_load_dwordx4 v[38:41], v[42:43], off nt
	s_nop 0
	global_load_dwordx4 v[42:45], v[46:47], off nt
	s_nop 0
	global_load_dwordx4 v[46:49], v[50:51], off nt
	s_nop 0
	global_load_dwordx4 v[50:53], v[54:55], off nt
	s_nop 0
	global_load_dwordx4 v[54:57], v[58:59], off nt
	s_nop 0
	global_load_dwordx4 v[58:61], v[62:63], off nt
	v_lshl_add_u64 v[62:63], v[62:63], 0, s[0:1]
	global_load_dwordx4 v[62:65], v[62:63], off nt
	s_waitcnt vmcnt(35)
	v_pk_mul_f32 v[200:201], v[68:69], s[74:75] op_sel_hi:[1,0]
	v_pk_mul_f32 v[198:199], v[66:67], s[74:75] op_sel_hi:[1,0]
	ds_write_b128 v148, v[198:201]
	s_waitcnt vmcnt(34)
	v_pk_mul_f32 v[200:201], v[72:73], s[74:75] op_sel_hi:[1,0]
	v_pk_mul_f32 v[198:199], v[70:71], s[74:75] op_sel_hi:[1,0]
	ds_write_b128 v149, v[198:201] offset:1024
	s_waitcnt vmcnt(33)
	v_pk_mul_f32 v[200:201], v[76:77], s[74:75] op_sel_hi:[1,0]
	v_pk_mul_f32 v[198:199], v[74:75], s[74:75] op_sel_hi:[1,0]
	ds_write_b128 v150, v[198:201] offset:2048
	s_waitcnt vmcnt(32)
	v_pk_mul_f32 v[200:201], v[80:81], s[74:75] op_sel_hi:[1,0]
	v_pk_mul_f32 v[198:199], v[78:79], s[74:75] op_sel_hi:[1,0]
	ds_write_b128 v151, v[198:201] offset:3072
	s_waitcnt vmcnt(31)
	v_pk_mul_f32 v[200:201], v[84:85], s[74:75] op_sel_hi:[1,0]
	v_pk_mul_f32 v[198:199], v[82:83], s[74:75] op_sel_hi:[1,0]
	ds_write_b128 v152, v[198:201] offset:4096
	s_waitcnt vmcnt(30)
	v_pk_mul_f32 v[200:201], v[88:89], s[74:75] op_sel_hi:[1,0]
	v_pk_mul_f32 v[198:199], v[86:87], s[74:75] op_sel_hi:[1,0]
	ds_write_b128 v153, v[198:201] offset:5120
	s_waitcnt vmcnt(29)
	v_pk_mul_f32 v[200:201], v[92:93], s[74:75] op_sel_hi:[1,0]
	v_pk_mul_f32 v[198:199], v[90:91], s[74:75] op_sel_hi:[1,0]
	ds_write_b128 v154, v[198:201] offset:6144
	s_waitcnt vmcnt(28)
	v_pk_mul_f32 v[200:201], v[96:97], s[74:75] op_sel_hi:[1,0]
	v_pk_mul_f32 v[198:199], v[94:95], s[74:75] op_sel_hi:[1,0]
	ds_write_b128 v155, v[198:201] offset:7168
	s_waitcnt vmcnt(27)
	v_pk_mul_f32 v[200:201], v[100:101], s[74:75] op_sel_hi:[1,0]
	v_pk_mul_f32 v[198:199], v[98:99], s[74:75] op_sel_hi:[1,0]
	ds_write_b128 v148, v[198:201] offset:8192
	s_waitcnt vmcnt(26)
	v_pk_mul_f32 v[200:201], v[104:105], s[74:75] op_sel_hi:[1,0]
	v_pk_mul_f32 v[198:199], v[102:103], s[74:75] op_sel_hi:[1,0]
	ds_write_b128 v149, v[198:201] offset:9216
	s_waitcnt vmcnt(25)
	v_pk_mul_f32 v[200:201], v[108:109], s[74:75] op_sel_hi:[1,0]
	v_pk_mul_f32 v[198:199], v[106:107], s[74:75] op_sel_hi:[1,0]
	ds_write_b128 v150, v[198:201] offset:10240
	s_waitcnt vmcnt(24)
	v_pk_mul_f32 v[200:201], v[112:113], s[74:75] op_sel_hi:[1,0]
	v_pk_mul_f32 v[198:199], v[110:111], s[74:75] op_sel_hi:[1,0]
	ds_write_b128 v151, v[198:201] offset:11264
	s_waitcnt vmcnt(23)
	v_pk_mul_f32 v[200:201], v[116:117], s[74:75] op_sel_hi:[1,0]
	v_pk_mul_f32 v[198:199], v[114:115], s[74:75] op_sel_hi:[1,0]
	ds_write_b128 v152, v[198:201] offset:12288
	s_waitcnt vmcnt(22)
	v_pk_mul_f32 v[200:201], v[120:121], s[74:75] op_sel_hi:[1,0]
	v_pk_mul_f32 v[198:199], v[118:119], s[74:75] op_sel_hi:[1,0]
	ds_write_b128 v153, v[198:201] offset:13312
	s_waitcnt vmcnt(21)
	v_pk_mul_f32 v[200:201], v[124:125], s[74:75] op_sel_hi:[1,0]
	v_pk_mul_f32 v[198:199], v[122:123], s[74:75] op_sel_hi:[1,0]
	ds_write_b128 v154, v[198:201] offset:14336
	s_waitcnt vmcnt(20)
	v_pk_mul_f32 v[200:201], v[128:129], s[74:75] op_sel_hi:[1,0]
	v_pk_mul_f32 v[198:199], v[126:127], s[74:75] op_sel_hi:[1,0]
	ds_write_b128 v155, v[198:201] offset:15360
	s_branch .Lcv2_5_810

; #define GAS __attribute__((address_space(1)))
; __device__ __forceinline__ void p8_finish(const TItem8& t, const f32x4 (&v)[16], LAS float* scr, int lane) {
;     ...
;     const int c = lane & 7;
; #pragma unroll
;     for (int j = 0; j < 4; ++j) { const int n = (lane >> 3) + 8 * j; float x[16];
; #pragma unroll
;         for (int i = 0; i < 16; ++i) { const int k = 16 * c + i; x[i] = scr[k * 32 + ((((n >> 2) ^ ((k >> 3) & 7)) << 2) | (n & 3))]; }
;         int w[4];
; #pragma unroll
;         for (int g = 0; g < 4; ++g) { int q = 0; q = __builtin_amdgcn_cvt_pk_fp8_f32(fminf(fmaxf(x[4 * g], -448.f), 448.f), fminf(fmaxf(x[4 * g + 1], -448.f), 448.f), q, false);
;             q = __builtin_amdgcn_cvt_pk_fp8_f32(fminf(fmaxf(x[4 * g + 2], -448.f), 448.f), fminf(fmaxf(x[4 * g + 3], -448.f), 448.f), q, true); w[g] = q; }
;         v4u o; o.x = (unsigned)w[0]; o.y = (unsigned)w[1]; o.z = (unsigned)w[2]; o.w = (unsigned)w[3];
;         __builtin_nontemporal_store(o, (GAS v4u*)(t.dst + (size_t)n * t.Kd + 16 * c)); }
.Lcv2_5_810:
	s_waitcnt lgkmcnt(0)
	ds_read2_b32 v[198:199], v156 offset1:32
	ds_read2_b32 v[200:201], v156 offset0:64 offset1:96
	ds_read2_b32 v[202:203], v156 offset0:128 offset1:160
	ds_read2_b32 v[204:205], v156 offset0:192 offset1:224
	ds_read_b32 v142, v157
	ds_read_b32 v145, v158
	ds_read_b32 v206, v159
	ds_read_b32 v207, v160
	ds_read_b32 v208, v161
	ds_read_b32 v209, v162
	ds_read_b32 v210, v163
	ds_read_b32 v211, v164
	s_waitcnt lgkmcnt(11)
	v_max_f32_e32 v198, v198, v198
	v_med3_f32 v212, v198, s5, v1
	v_max_f32_e32 v198, v199, v199
	v_med3_f32 v199, v198, s5, v1
	v_mov_b32_e32 v198, v143
	v_cvt_pk_fp8_f32 v198, v212, v199
	s_waitcnt lgkmcnt(10)
	v_max_f32_e32 v199, v200, v200
	v_max_f32_e32 v200, v201, v201
	v_med3_f32 v199, v199, s5, v1
	v_med3_f32 v200, v200, s5, v1
	v_cvt_pk_fp8_f32 v198, v199, v200 op_sel:[0,0,1]
	s_waitcnt lgkmcnt(9)
	v_max_f32_e32 v199, v202, v202
	v_med3_f32 v200, v199, s5, v1
	v_max_f32_e32 v199, v203, v203
	v_med3_f32 v201, v199, s5, v1
	v_mov_b32_e32 v199, v143
	v_cvt_pk_fp8_f32 v199, v200, v201
	s_waitcnt lgkmcnt(8)
	v_max_f32_e32 v200, v204, v204
	v_max_f32_e32 v201, v205, v205
	v_med3_f32 v200, v200, s5, v1
	v_med3_f32 v201, v201, s5, v1
	s_waitcnt lgkmcnt(7)
	v_max_f32_e32 v142, v142, v142
	s_waitcnt lgkmcnt(6)
	v_max_f32_e32 v145, v145, v145
	v_cvt_pk_fp8_f32 v199, v200, v201 op_sel:[0,0,1]
	v_med3_f32 v142, v142, s5, v1
	v_med3_f32 v145, v145, s5, v1
	v_mov_b32_e32 v200, v143
	v_cvt_pk_fp8_f32 v200, v142, v145
	s_waitcnt lgkmcnt(5)
	v_max_f32_e32 v142, v206, v206
	s_waitcnt lgkmcnt(4)
	v_max_f32_e32 v145, v207, v207
	v_med3_f32 v142, v142, s5, v1
	v_med3_f32 v145, v145, s5, v1
	v_cvt_pk_fp8_f32 v200, v142, v145 op_sel:[0,0,1]
	s_waitcnt lgkmcnt(3)
	v_max_f32_e32 v142, v208, v208
	s_waitcnt lgkmcnt(2)
	v_max_f32_e32 v145, v209, v209
	v_med3_f32 v142, v142, s5, v1
	v_med3_f32 v145, v145, s5, v1
	v_mov_b32_e32 v201, v143
	v_cvt_pk_fp8_f32 v201, v142, v145
	s_waitcnt lgkmcnt(1)
	v_max_f32_e32 v142, v210, v210
	s_waitcnt lgkmcnt(0)
	v_max_f32_e32 v145, v211, v211
	v_med3_f32 v142, v142, s5, v1
	v_med3_f32 v145, v145, s5, v1
	v_cvt_pk_fp8_f32 v201, v142, v145 op_sel:[0,0,1]
	v_lshl_add_u64 v[146:147], s[82:83], 0, v[130:131]
	v_lshl_add_u64 v[202:203], v[146:147], 0, v[132:133]
	global_store_dwordx4 v[202:203], v[198:201], off nt
	ds_read2_b32 v[198:199], v165 offset1:32
	ds_read2_b32 v[200:201], v165 offset0:64 offset1:96
	ds_read2_b32 v[202:203], v165 offset0:128 offset1:160
	ds_read2_b32 v[204:205], v165 offset0:192 offset1:224
	ds_read_b32 v142, v166
	ds_read_b32 v145, v167
	ds_read_b32 v206, v168
	ds_read_b32 v207, v169
	ds_read_b32 v208, v170
	ds_read_b32 v209, v171
	ds_read_b32 v210, v172
	ds_read_b32 v211, v173
	s_waitcnt lgkmcnt(11)
	v_max_f32_e32 v198, v198, v198
	v_med3_f32 v212, v198, s5, v1
	v_max_f32_e32 v198, v199, v199
	v_med3_f32 v199, v198, s5, v1
	v_mov_b32_e32 v198, v143
	v_cvt_pk_fp8_f32 v198, v212, v199
	s_waitcnt lgkmcnt(10)
	v_max_f32_e32 v199, v200, v200
	v_max_f32_e32 v200, v201, v201
	v_med3_f32 v199, v199, s5, v1
	v_med3_f32 v200, v200, s5, v1
	v_cvt_pk_fp8_f32 v198, v199, v200 op_sel:[0,0,1]
	s_waitcnt lgkmcnt(9)
	v_max_f32_e32 v199, v202, v202
	v_med3_f32 v200, v199, s5, v1
	v_max_f32_e32 v199, v203, v203
	v_med3_f32 v201, v199, s5, v1
	v_mov_b32_e32 v199, v143
	v_cvt_pk_fp8_f32 v199, v200, v201
	s_waitcnt lgkmcnt(8)
	v_max_f32_e32 v200, v204, v204
	v_max_f32_e32 v201, v205, v205
	v_med3_f32 v200, v200, s5, v1
	v_med3_f32 v201, v201, s5, v1
	s_waitcnt lgkmcnt(7)
	v_max_f32_e32 v142, v142, v142
	s_waitcnt lgkmcnt(6)
	v_max_f32_e32 v145, v145, v145
	v_cvt_pk_fp8_f32 v199, v200, v201 op_sel:[0,0,1]
	v_med3_f32 v142, v142, s5, v1
	v_med3_f32 v145, v145, s5, v1
	v_mov_b32_e32 v200, v143
	v_cvt_pk_fp8_f32 v200, v142, v145
	s_waitcnt lgkmcnt(5)
	v_max_f32_e32 v142, v206, v206
	s_waitcnt lgkmcnt(4)
	v_max_f32_e32 v145, v207, v207
	v_med3_f32 v142, v142, s5, v1
	v_med3_f32 v145, v145, s5, v1
	v_cvt_pk_fp8_f32 v200, v142, v145 op_sel:[0,0,1]
	s_waitcnt lgkmcnt(3)
	v_max_f32_e32 v142, v208, v208
	s_waitcnt lgkmcnt(2)
	v_max_f32_e32 v145, v209, v209
	v_med3_f32 v142, v142, s5, v1
	v_med3_f32 v145, v145, s5, v1
	v_mov_b32_e32 v201, v143
	v_cvt_pk_fp8_f32 v201, v142, v145
	s_waitcnt lgkmcnt(1)
	v_max_f32_e32 v142, v210, v210
	s_waitcnt lgkmcnt(0)
; #define GAS __attribute__((address_space(1)))
; __device__ __forceinline__ void p8_finish(const TItem8& t, const f32x4 (&v)[16], LAS float* scr, int lane) {
;     ...
;     const int c = lane & 7;
; #pragma unroll
;     for (int j = 0; j < 4; ++j) { const int n = (lane >> 3) + 8 * j; float x[16];
; #pragma unroll
;         for (int i = 0; i < 16; ++i) { const int k = 16 * c + i; x[i] = scr[k * 32 + ((((n >> 2) ^ ((k >> 3) & 7)) << 2) | (n & 3))]; }
;         int w[4];
; #pragma unroll
;         for (int g = 0; g < 4; ++g) { int q = 0; q = __builtin_amdgcn_cvt_pk_fp8_f32(fminf(fmaxf(x[4 * g], -448.f), 448.f), fminf(fmaxf(x[4 * g + 1], -448.f), 448.f), q, false);
;             q = __builtin_amdgcn_cvt_pk_fp8_f32(fminf(fmaxf(x[4 * g + 2], -448.f), 448.f), fminf(fmaxf(x[4 * g + 3], -448.f), 448.f), q, true); w[g] = q; }
;         v4u o; o.x = (unsigned)w[0]; o.y = (unsigned)w[1]; o.z = (unsigned)w[2]; o.w = (unsigned)w[3];
;         __builtin_nontemporal_store(o, (GAS v4u*)(t.dst + (size_t)n * t.Kd + 16 * c)); }
	v_max_f32_e32 v145, v211, v211
	v_med3_f32 v142, v142, s5, v1
	v_med3_f32 v145, v145, s5, v1
	v_cvt_pk_fp8_f32 v201, v142, v145 op_sel:[0,0,1]
	v_lshl_add_u64 v[202:203], v[146:147], 0, v[134:135]
	global_store_dwordx4 v[202:203], v[198:201], off nt
	ds_read2_b32 v[198:199], v174 offset1:32
	ds_read2_b32 v[200:201], v174 offset0:64 offset1:96
	ds_read2_b32 v[202:203], v174 offset0:128 offset1:160
	ds_read2_b32 v[204:205], v174 offset0:192 offset1:224
	ds_read_b32 v142, v175
	ds_read_b32 v145, v176
	ds_read_b32 v206, v177
	ds_read_b32 v207, v178
	ds_read_b32 v208, v179
	ds_read_b32 v209, v180
	ds_read_b32 v210, v181
	ds_read_b32 v211, v182
	s_waitcnt lgkmcnt(11)
	v_max_f32_e32 v198, v198, v198
	v_med3_f32 v212, v198, s5, v1
	v_max_f32_e32 v198, v199, v199
	v_med3_f32 v199, v198, s5, v1
	v_mov_b32_e32 v198, v143
	v_cvt_pk_fp8_f32 v198, v212, v199
	s_waitcnt lgkmcnt(10)
	v_max_f32_e32 v199, v200, v200
	v_max_f32_e32 v200, v201, v201
	v_med3_f32 v199, v199, s5, v1
	v_med3_f32 v200, v200, s5, v1
	v_cvt_pk_fp8_f32 v198, v199, v200 op_sel:[0,0,1]
	s_waitcnt lgkmcnt(9)
	v_max_f32_e32 v199, v202, v202
	v_med3_f32 v200, v199, s5, v1
	v_max_f32_e32 v199, v203, v203
	v_med3_f32 v201, v199, s5, v1
	v_mov_b32_e32 v199, v143
	v_cvt_pk_fp8_f32 v199, v200, v201
	s_waitcnt lgkmcnt(8)
	v_max_f32_e32 v200, v204, v204
	v_max_f32_e32 v201, v205, v205
	v_med3_f32 v200, v200, s5, v1
	v_med3_f32 v201, v201, s5, v1
	s_waitcnt lgkmcnt(7)
	v_max_f32_e32 v142, v142, v142
	s_waitcnt lgkmcnt(6)
	v_max_f32_e32 v145, v145, v145
	v_cvt_pk_fp8_f32 v199, v200, v201 op_sel:[0,0,1]
	v_med3_f32 v142, v142, s5, v1
	v_med3_f32 v145, v145, s5, v1
	v_mov_b32_e32 v200, v143
	v_cvt_pk_fp8_f32 v200, v142, v145
	s_waitcnt lgkmcnt(5)
	v_max_f32_e32 v142, v206, v206
	s_waitcnt lgkmcnt(4)
	v_max_f32_e32 v145, v207, v207
	v_med3_f32 v142, v142, s5, v1
	v_med3_f32 v145, v145, s5, v1
	v_cvt_pk_fp8_f32 v200, v142, v145 op_sel:[0,0,1]
	s_waitcnt lgkmcnt(3)
	v_max_f32_e32 v142, v208, v208
	s_waitcnt lgkmcnt(2)
	v_max_f32_e32 v145, v209, v209
	v_med3_f32 v142, v142, s5, v1
	v_med3_f32 v145, v145, s5, v1
	v_mov_b32_e32 v201, v143
	v_cvt_pk_fp8_f32 v201, v142, v145
	s_waitcnt lgkmcnt(1)
	v_max_f32_e32 v142, v210, v210
	s_waitcnt lgkmcnt(0)
	v_max_f32_e32 v145, v211, v211
	v_med3_f32 v142, v142, s5, v1
	v_med3_f32 v145, v145, s5, v1
	v_cvt_pk_fp8_f32 v201, v142, v145 op_sel:[0,0,1]
	v_lshl_add_u64 v[202:203], v[146:147], 0, v[136:137]
	v_lshl_add_u64 v[146:147], v[146:147], 0, v[138:139]
	global_store_dwordx4 v[202:203], v[198:201], off nt
	ds_read2_b32 v[198:199], v183 offset1:32
	ds_read2_b32 v[200:201], v183 offset0:64 offset1:96
	ds_read2_b32 v[202:203], v183 offset0:128 offset1:160
	ds_read2_b32 v[204:205], v183 offset0:192 offset1:224
	ds_read_b32 v142, v184
	ds_read_b32 v145, v185
	ds_read_b32 v206, v186
	ds_read_b32 v207, v187
	ds_read_b32 v208, v188
	ds_read_b32 v209, v189
	ds_read_b32 v210, v190
	ds_read_b32 v211, v191
	s_waitcnt lgkmcnt(11)
	v_max_f32_e32 v198, v198, v198
	v_med3_f32 v212, v198, s5, v1
	v_max_f32_e32 v198, v199, v199
	v_med3_f32 v199, v198, s5, v1
	v_mov_b32_e32 v198, v143
	v_cvt_pk_fp8_f32 v198, v212, v199
	s_waitcnt lgkmcnt(10)
	v_max_f32_e32 v199, v200, v200
	v_max_f32_e32 v200, v201, v201
	v_med3_f32 v199, v199, s5, v1
	v_med3_f32 v200, v200, s5, v1
	v_cvt_pk_fp8_f32 v198, v199, v200 op_sel:[0,0,1]
	s_waitcnt lgkmcnt(9)
	v_max_f32_e32 v199, v202, v202
	v_med3_f32 v200, v199, s5, v1
	v_max_f32_e32 v199, v203, v203
	v_med3_f32 v201, v199, s5, v1
	v_mov_b32_e32 v199, v143
	v_cvt_pk_fp8_f32 v199, v200, v201
	s_waitcnt lgkmcnt(8)
	v_max_f32_e32 v200, v204, v204
	v_max_f32_e32 v201, v205, v205
	v_med3_f32 v200, v200, s5, v1
	v_med3_f32 v201, v201, s5, v1
	s_waitcnt lgkmcnt(7)
	v_max_f32_e32 v142, v142, v142
	s_waitcnt lgkmcnt(6)
	v_max_f32_e32 v145, v145, v145
	v_cvt_pk_fp8_f32 v199, v200, v201 op_sel:[0,0,1]
	v_med3_f32 v142, v142, s5, v1
	v_med3_f32 v145, v145, s5, v1
	v_mov_b32_e32 v200, v143
	v_cvt_pk_fp8_f32 v200, v142, v145
	s_waitcnt lgkmcnt(5)
	v_max_f32_e32 v142, v206, v206
	s_waitcnt lgkmcnt(4)
	v_max_f32_e32 v145, v207, v207
	v_med3_f32 v142, v142, s5, v1
	v_med3_f32 v145, v145, s5, v1
	v_cvt_pk_fp8_f32 v200, v142, v145 op_sel:[0,0,1]
	s_waitcnt lgkmcnt(3)
	v_max_f32_e32 v142, v208, v208
	s_waitcnt lgkmcnt(2)
	v_max_f32_e32 v145, v209, v209
	v_med3_f32 v142, v142, s5, v1
	v_med3_f32 v145, v145, s5, v1
	v_mov_b32_e32 v201, v143
	v_cvt_pk_fp8_f32 v201, v142, v145
	s_waitcnt lgkmcnt(1)
	v_max_f32_e32 v142, v210, v210
	s_waitcnt lgkmcnt(0)
	v_max_f32_e32 v145, v211, v211
	v_med3_f32 v142, v142, s5, v1
	v_med3_f32 v145, v145, s5, v1
	v_cvt_pk_fp8_f32 v201, v142, v145 op_sel:[0,0,1]
	global_store_dwordx4 v[146:147], v[198:201], off nt
	s_waitcnt lgkmcnt(0)
	s_xor_b64 s[84:85], s[84:85], -1
	s_and_b64 vcc, exec, s[84:85]
	s_cbranch_vccz .LBB0_798

; #define GAS __attribute__((address_space(1)))
; #define LAS __attribute__((address_space(3)))
; __device__ __forceinline__ void p8_issue(const TItem8& t, f32x4 (&v)[16], int lane) {
;     const GAS f32x4* src = (const GAS f32x4*)((const GAS float*)t.src + (size_t)(lane >> 3) * t.N + 4 * (lane & 7));
; #pragma unroll
;     for (int i = 0; i < 16; ++i) v[i] = __builtin_nontemporal_load(src + (size_t)(2 * i) * t.N);
; }
; __device__ __forceinline__ void p8_finish(const TItem8& t, const f32x4 (&v)[16], LAS float* scr, int lane) {
; #pragma unroll
;     for (int i = 0; i < 16; ++i) *(LAS f32x4*)(scr + (8 * i + (lane >> 3)) * 32 + (((lane & 7) ^ (i & 7)) << 2)) = v[i] * W8_SCALE;
.LBB0_853:
	s_lshl_b64 s[10:11], s[84:85], 11
	s_add_u32 s0, s90, s10
	v_mul_u32_u24_e32 v66, s92, v225
	s_addc_u32 s10, s91, s11
	v_lshlrev_b32_e32 v140, 2, v66
	s_add_u32 s80, s0, s88
	v_lshl_add_u64 v[66:67], s[86:87], 0, v[140:141]
	v_mov_b32_e32 v143, v141
	s_addc_u32 s81, s10, s89
	v_lshl_add_u64 v[66:67], v[66:67], 0, v[142:143]
	s_lshl_b32 s0, s92, 5
	v_lshl_add_u64 v[74:75], v[66:67], 0, s[0:1]
	global_load_dwordx4 v[66:69], v[66:67], off nt
	s_nop 0
	global_load_dwordx4 v[70:73], v[74:75], off nt
	v_lshl_add_u64 v[74:75], v[74:75], 0, s[0:1]
	v_lshl_add_u64 v[82:83], v[74:75], 0, s[0:1]
	global_load_dwordx4 v[74:77], v[74:75], off nt
	s_nop 0
	global_load_dwordx4 v[78:81], v[82:83], off nt
	v_lshl_add_u64 v[82:83], v[82:83], 0, s[0:1]
	v_lshl_add_u64 v[90:91], v[82:83], 0, s[0:1]
	global_load_dwordx4 v[82:85], v[82:83], off nt
	s_nop 0
	global_load_dwordx4 v[86:89], v[90:91], off nt
	v_lshl_add_u64 v[90:91], v[90:91], 0, s[0:1]
	v_lshl_add_u64 v[98:99], v[90:91], 0, s[0:1]
	v_lshl_add_u64 v[102:103], v[98:99], 0, s[0:1]
	v_lshl_add_u64 v[106:107], v[102:103], 0, s[0:1]
	v_lshl_add_u64 v[110:111], v[106:107], 0, s[0:1]
	v_lshl_add_u64 v[114:115], v[110:111], 0, s[0:1]
	v_lshl_add_u64 v[118:119], v[114:115], 0, s[0:1]
	v_lshl_add_u64 v[122:123], v[118:119], 0, s[0:1]
	v_lshl_add_u64 v[126:127], v[122:123], 0, s[0:1]
	global_load_dwordx4 v[90:93], v[90:91], off nt
	s_nop 0
	global_load_dwordx4 v[94:97], v[98:99], off nt
	s_nop 0
	global_load_dwordx4 v[98:101], v[102:103], off nt
	s_nop 0
	global_load_dwordx4 v[102:105], v[106:107], off nt
	s_nop 0
	global_load_dwordx4 v[106:109], v[110:111], off nt
	s_nop 0
	global_load_dwordx4 v[110:113], v[114:115], off nt
	s_nop 0
	global_load_dwordx4 v[114:117], v[118:119], off nt
	s_nop 0
	global_load_dwordx4 v[118:121], v[122:123], off nt
	s_nop 0
	global_load_dwordx4 v[122:125], v[126:127], off nt
	v_lshl_add_u64 v[126:127], v[126:127], 0, s[0:1]
	global_load_dwordx4 v[126:129], v[126:127], off nt
	s_waitcnt vmcnt(31)
	v_pk_mul_f32 v[146:147], v[4:5], s[72:73] op_sel_hi:[1,0]
	v_pk_mul_f32 v[144:145], v[2:3], s[72:73] op_sel_hi:[1,0]
	ds_write_b128 v148, v[144:147]
	s_waitcnt vmcnt(30)
	v_pk_mul_f32 v[146:147], v[8:9], s[72:73] op_sel_hi:[1,0]
	v_pk_mul_f32 v[144:145], v[6:7], s[72:73] op_sel_hi:[1,0]
	ds_write_b128 v149, v[144:147] offset:1024
	s_waitcnt vmcnt(29)
	v_pk_mul_f32 v[146:147], v[12:13], s[72:73] op_sel_hi:[1,0]
	v_pk_mul_f32 v[144:145], v[10:11], s[72:73] op_sel_hi:[1,0]
	ds_write_b128 v150, v[144:147] offset:2048
	s_waitcnt vmcnt(28)
	v_pk_mul_f32 v[146:147], v[16:17], s[72:73] op_sel_hi:[1,0]
	v_pk_mul_f32 v[144:145], v[14:15], s[72:73] op_sel_hi:[1,0]
	ds_write_b128 v151, v[144:147] offset:3072
	s_waitcnt vmcnt(27)
	v_pk_mul_f32 v[146:147], v[20:21], s[72:73] op_sel_hi:[1,0]
	v_pk_mul_f32 v[144:145], v[18:19], s[72:73] op_sel_hi:[1,0]
	ds_write_b128 v152, v[144:147] offset:4096
	s_waitcnt vmcnt(26)
	v_pk_mul_f32 v[146:147], v[24:25], s[72:73] op_sel_hi:[1,0]
	v_pk_mul_f32 v[144:145], v[22:23], s[72:73] op_sel_hi:[1,0]
	ds_write_b128 v153, v[144:147] offset:5120
	s_waitcnt vmcnt(25)
	v_pk_mul_f32 v[146:147], v[28:29], s[72:73] op_sel_hi:[1,0]
	v_pk_mul_f32 v[144:145], v[26:27], s[72:73] op_sel_hi:[1,0]
	ds_write_b128 v154, v[144:147] offset:6144
	s_waitcnt vmcnt(24)
	v_pk_mul_f32 v[146:147], v[32:33], s[72:73] op_sel_hi:[1,0]
	v_pk_mul_f32 v[144:145], v[30:31], s[72:73] op_sel_hi:[1,0]
	ds_write_b128 v155, v[144:147] offset:7168
	s_waitcnt vmcnt(23)
	v_pk_mul_f32 v[146:147], v[36:37], s[72:73] op_sel_hi:[1,0]
	v_pk_mul_f32 v[144:145], v[34:35], s[72:73] op_sel_hi:[1,0]
	ds_write_b128 v148, v[144:147] offset:8192
	s_waitcnt vmcnt(22)
	v_pk_mul_f32 v[146:147], v[40:41], s[72:73] op_sel_hi:[1,0]
	v_pk_mul_f32 v[144:145], v[38:39], s[72:73] op_sel_hi:[1,0]
	ds_write_b128 v149, v[144:147] offset:9216
	s_waitcnt vmcnt(21)
	v_pk_mul_f32 v[146:147], v[44:45], s[72:73] op_sel_hi:[1,0]
	v_pk_mul_f32 v[144:145], v[42:43], s[72:73] op_sel_hi:[1,0]
	ds_write_b128 v150, v[144:147] offset:10240
	s_waitcnt vmcnt(20)
	v_pk_mul_f32 v[146:147], v[48:49], s[72:73] op_sel_hi:[1,0]
	v_pk_mul_f32 v[144:145], v[46:47], s[72:73] op_sel_hi:[1,0]
	ds_write_b128 v151, v[144:147] offset:11264
	s_waitcnt vmcnt(19)
	v_pk_mul_f32 v[146:147], v[52:53], s[72:73] op_sel_hi:[1,0]
	v_pk_mul_f32 v[144:145], v[50:51], s[72:73] op_sel_hi:[1,0]
	ds_write_b128 v152, v[144:147] offset:12288
	s_waitcnt vmcnt(18)
	v_pk_mul_f32 v[146:147], v[56:57], s[72:73] op_sel_hi:[1,0]
	v_pk_mul_f32 v[144:145], v[54:55], s[72:73] op_sel_hi:[1,0]
	ds_write_b128 v153, v[144:147] offset:13312
	s_waitcnt vmcnt(17)
	v_pk_mul_f32 v[146:147], v[60:61], s[72:73] op_sel_hi:[1,0]
	v_pk_mul_f32 v[144:145], v[58:59], s[72:73] op_sel_hi:[1,0]
	ds_write_b128 v154, v[144:147] offset:14336
	s_waitcnt vmcnt(16)
	v_pk_mul_f32 v[146:147], v[64:65], s[72:73] op_sel_hi:[1,0]
	v_pk_mul_f32 v[144:145], v[62:63], s[72:73] op_sel_hi:[1,0]
	ds_write_b128 v155, v[144:147] offset:15360
	s_branch .Lcv1_4_854

; #define GAS __attribute__((address_space(1)))
; __device__ __forceinline__ void p8_finish(const TItem8& t, const f32x4 (&v)[16], LAS float* scr, int lane) {
;     ...
;     const int c = lane & 7;
; #pragma unroll
;     for (int j = 0; j < 4; ++j) { const int n = (lane >> 3) + 8 * j; float x[16];
; #pragma unroll
;         for (int i = 0; i < 16; ++i) { const int k = 16 * c + i; x[i] = scr[k * 32 + ((((n >> 2) ^ ((k >> 3) & 7)) << 2) | (n & 3))]; }
;         int w[4];
; #pragma unroll
;         for (int g = 0; g < 4; ++g) { int q = 0; q = __builtin_amdgcn_cvt_pk_fp8_f32(fminf(fmaxf(x[4 * g], -448.f), 448.f), fminf(fmaxf(x[4 * g + 1], -448.f), 448.f), q, false);
;             q = __builtin_amdgcn_cvt_pk_fp8_f32(fminf(fmaxf(x[4 * g + 2], -448.f), 448.f), fminf(fmaxf(x[4 * g + 3], -448.f), 448.f), q, true); w[g] = q; }
;         v4u o; o.x = (unsigned)w[0]; o.y = (unsigned)w[1]; o.z = (unsigned)w[2]; o.w = (unsigned)w[3];
;         __builtin_nontemporal_store(o, (GAS v4u*)(t.dst + (size_t)n * t.Kd + 16 * c)); }
.Lcv1_4_854:
	s_waitcnt lgkmcnt(0)
	ds_read2_b32 v[146:147], v156 offset1:32
	ds_read2_b32 v[198:199], v156 offset0:64 offset1:96
	ds_read2_b32 v[200:201], v156 offset0:128 offset1:160
	ds_read2_b32 v[202:203], v156 offset0:192 offset1:224
	ds_read_b32 v140, v157
	ds_read_b32 v143, v158
	ds_read_b32 v193, v159
	ds_read_b32 v195, v160
	ds_read_b32 v204, v161
	ds_read_b32 v205, v162
	ds_read_b32 v206, v163
	ds_read_b32 v207, v164
	s_waitcnt lgkmcnt(11)
	v_max_f32_e32 v146, v146, v146
	v_max_f32_e32 v147, v147, v147
	v_med3_f32 v146, v146, s5, v1
	v_med3_f32 v147, v147, s5, v1
	v_mov_b32_e32 v196, 0
	s_waitcnt lgkmcnt(7)
	v_max_f32_e32 v140, v140, v140
	s_waitcnt lgkmcnt(6)
	v_max_f32_e32 v143, v143, v143
	v_cvt_pk_fp8_f32 v196, v146, v147
	v_max_f32_e32 v146, v198, v198
	v_med3_f32 v140, v140, s5, v1
	v_med3_f32 v143, v143, s5, v1
	v_mov_b32_e32 v198, 0
	v_cvt_pk_fp8_f32 v198, v140, v143
	v_max_f32_e32 v147, v199, v199
	s_waitcnt lgkmcnt(5)
	v_max_f32_e32 v140, v193, v193
	s_waitcnt lgkmcnt(4)
	v_max_f32_e32 v143, v195, v195
	v_med3_f32 v146, v146, s5, v1
	v_med3_f32 v147, v147, s5, v1
	v_med3_f32 v140, v140, s5, v1
	v_med3_f32 v143, v143, s5, v1
	v_cvt_pk_fp8_f32 v196, v146, v147 op_sel:[0,0,1]
	v_max_f32_e32 v146, v200, v200
	v_max_f32_e32 v147, v201, v201
	v_cvt_pk_fp8_f32 v198, v140, v143 op_sel:[0,0,1]
	s_waitcnt lgkmcnt(3)
	v_max_f32_e32 v140, v204, v204
	s_waitcnt lgkmcnt(2)
	v_max_f32_e32 v143, v205, v205
	v_med3_f32 v146, v146, s5, v1
	v_med3_f32 v147, v147, s5, v1
	v_mov_b32_e32 v197, 0
	v_med3_f32 v140, v140, s5, v1
	v_med3_f32 v143, v143, s5, v1
	v_mov_b32_e32 v199, 0
	v_cvt_pk_fp8_f32 v197, v146, v147
	v_cvt_pk_fp8_f32 v199, v140, v143
	v_max_f32_e32 v146, v202, v202
	v_max_f32_e32 v147, v203, v203
	s_waitcnt lgkmcnt(1)
	v_max_f32_e32 v140, v206, v206
	s_waitcnt lgkmcnt(0)
	v_max_f32_e32 v143, v207, v207
	v_med3_f32 v146, v146, s5, v1
	v_med3_f32 v147, v147, s5, v1
	v_med3_f32 v140, v140, s5, v1
	v_med3_f32 v143, v143, s5, v1
	v_cvt_pk_fp8_f32 v197, v146, v147 op_sel:[0,0,1]
	v_cvt_pk_fp8_f32 v199, v140, v143 op_sel:[0,0,1]
	ds_read2_b32 v[146:147], v165 offset1:32
	ds_read2_b32 v[202:203], v165 offset0:64 offset1:96
	ds_read2_b32 v[204:205], v165 offset0:128 offset1:160
	ds_read2_b32 v[206:207], v165 offset0:192 offset1:224
	ds_read_b32 v140, v166
	ds_read_b32 v143, v167
	ds_read_b32 v193, v168
	ds_read_b32 v195, v169
	ds_read_b32 v208, v170
	ds_read_b32 v209, v171
	ds_read_b32 v210, v172
	ds_read_b32 v211, v173
	s_waitcnt lgkmcnt(11)
	v_max_f32_e32 v146, v146, v146
	v_max_f32_e32 v147, v147, v147
	v_med3_f32 v146, v146, s5, v1
	v_med3_f32 v147, v147, s5, v1
	v_mov_b32_e32 v200, 0
	s_waitcnt lgkmcnt(7)
	v_max_f32_e32 v140, v140, v140
	s_waitcnt lgkmcnt(6)
	v_max_f32_e32 v143, v143, v143
	v_cvt_pk_fp8_f32 v200, v146, v147
	v_max_f32_e32 v146, v202, v202
	v_med3_f32 v140, v140, s5, v1
	v_med3_f32 v143, v143, s5, v1
	v_mov_b32_e32 v202, 0
	v_cvt_pk_fp8_f32 v202, v140, v143
	v_max_f32_e32 v147, v203, v203
	s_waitcnt lgkmcnt(5)
	v_max_f32_e32 v140, v193, v193
	s_waitcnt lgkmcnt(4)
	v_max_f32_e32 v143, v195, v195
	v_med3_f32 v146, v146, s5, v1
	v_med3_f32 v147, v147, s5, v1
	v_med3_f32 v140, v140, s5, v1
	v_med3_f32 v143, v143, s5, v1
	v_cvt_pk_fp8_f32 v200, v146, v147 op_sel:[0,0,1]
	v_max_f32_e32 v146, v204, v204
	v_max_f32_e32 v147, v205, v205
	v_cvt_pk_fp8_f32 v202, v140, v143 op_sel:[0,0,1]
	s_waitcnt lgkmcnt(3)
	v_max_f32_e32 v140, v208, v208
	s_waitcnt lgkmcnt(2)
	v_max_f32_e32 v143, v209, v209
	v_med3_f32 v146, v146, s5, v1
	v_med3_f32 v147, v147, s5, v1
	v_mov_b32_e32 v201, 0
	v_med3_f32 v140, v140, s5, v1
	v_med3_f32 v143, v143, s5, v1
	v_mov_b32_e32 v203, 0
	v_cvt_pk_fp8_f32 v201, v146, v147
	v_cvt_pk_fp8_f32 v203, v140, v143
	v_max_f32_e32 v146, v206, v206
	v_max_f32_e32 v147, v207, v207
	s_waitcnt lgkmcnt(1)
	v_max_f32_e32 v140, v210, v210
	s_waitcnt lgkmcnt(0)
	v_max_f32_e32 v143, v211, v211
	v_med3_f32 v146, v146, s5, v1
	v_med3_f32 v147, v147, s5, v1
	v_med3_f32 v140, v140, s5, v1
	v_med3_f32 v143, v143, s5, v1
	v_cvt_pk_fp8_f32 v201, v146, v147 op_sel:[0,0,1]
	v_cvt_pk_fp8_f32 v203, v140, v143 op_sel:[0,0,1]
	v_lshl_add_u64 v[144:145], s[74:75], 0, v[130:131]
	v_lshl_add_u64 v[146:147], v[144:145], 0, v[132:133]
	global_store_dwordx4 v[146:147], v[196:199], off nt
	v_lshl_add_u64 v[146:147], v[144:145], 0, v[134:135]
	global_store_dwordx4 v[146:147], v[200:203], off nt
	ds_read2_b32 v[146:147], v174 offset1:32
	ds_read2_b32 v[198:199], v174 offset0:64 offset1:96
	ds_read2_b32 v[200:201], v174 offset0:128 offset1:160
	ds_read2_b32 v[202:203], v174 offset0:192 offset1:224
	ds_read_b32 v140, v175
	ds_read_b32 v143, v176
	ds_read_b32 v193, v177
	ds_read_b32 v195, v178
	ds_read_b32 v204, v179
	ds_read_b32 v205, v180
	ds_read_b32 v206, v181
	ds_read_b32 v207, v182
	s_waitcnt lgkmcnt(11)
	v_max_f32_e32 v146, v146, v146
	v_max_f32_e32 v147, v147, v147
	v_med3_f32 v146, v146, s5, v1
	v_med3_f32 v147, v147, s5, v1
	v_mov_b32_e32 v196, 0
	s_waitcnt lgkmcnt(7)
; #define GAS __attribute__((address_space(1)))
; __device__ __forceinline__ TItem8 p8_decode(const Args& args, unsigned char* ws, int it) {
;     TItem8 t;
;     if (it >= P8_N) { const int j = it - P8_N; it = (P8_E0 + j / P8_DN1) * (P8_GU1 + P8_DN1) + P8_GU1 + j % P8_DN1; }
;     else if (it >= P8_E0 * (P8_GU1 + P8_DN1)) { const int r = it - P8_E0 * (P8_GU1 + P8_DN1); it = (P8_E0 + r / P8_GU1) * (P8_GU1 + P8_DN1) + r % P8_GU1; }
;     const int e = it / (P8_GU1 + P8_DN1), q = it % (P8_GU1 + P8_DN1);
;     if (q < P8_GU1) { const int kb = q / 128, nb = q % 128, n0 = nb * 32;
;         const int dr = (n0 < DE) ? (256 * (n0 / 128) + (n0 % 128)) : (256 * ((n0 - DE) / 128) + 128 + ((n0 - DE) % 128));
;         t.src = args.in[25] + (size_t)e * D * 2 * DE + (size_t)(kb * 128) * (2 * DE) + n0; t.N = 2 * DE; t.dst = ws + WS_WGU + (size_t)e * 2 * DE * D + (size_t)dr * D + kb * 128; t.Kd = D; }
;     else { const int q2 = q - P8_GU1, kb = q2 / 64, nb = q2 % 64;
;         t.src = args.in[27] + (size_t)e * DE * D + (size_t)(kb * 128) * D + nb * 32; t.N = D; t.dst = ws + WS_WDN + (size_t)e * D * DE + (size_t)(nb * 32) * DE + kb * 128; t.Kd = DE; }
; __device__ __forceinline__ void p8_finish(const TItem8& t, const f32x4 (&v)[16], LAS float* scr, int lane) {
;     ...
;     const int c = lane & 7;
; #pragma unroll
;     for (int j = 0; j < 4; ++j) { const int n = (lane >> 3) + 8 * j; float x[16];
; #pragma unroll
;         for (int i = 0; i < 16; ++i) { const int k = 16 * c + i; x[i] = scr[k * 32 + ((((n >> 2) ^ ((k >> 3) & 7)) << 2) | (n & 3))]; }
;         int w[4];
; #pragma unroll
;         for (int g = 0; g < 4; ++g) { int q = 0; q = __builtin_amdgcn_cvt_pk_fp8_f32(fminf(fmaxf(x[4 * g], -448.f), 448.f), fminf(fmaxf(x[4 * g + 1], -448.f), 448.f), q, false);
;             q = __builtin_amdgcn_cvt_pk_fp8_f32(fminf(fmaxf(x[4 * g + 2], -448.f), 448.f), fminf(fmaxf(x[4 * g + 3], -448.f), 448.f), q, true); w[g] = q; }
;         v4u o; o.x = (unsigned)w[0]; o.y = (unsigned)w[1]; o.z = (unsigned)w[2]; o.w = (unsigned)w[3];
;         __builtin_nontemporal_store(o, (GAS v4u*)(t.dst + (size_t)n * t.Kd + 16 * c)); }
	v_max_f32_e32 v140, v140, v140
	s_waitcnt lgkmcnt(6)
	v_max_f32_e32 v143, v143, v143
	v_cvt_pk_fp8_f32 v196, v146, v147
	v_max_f32_e32 v146, v198, v198
	v_med3_f32 v140, v140, s5, v1
	v_med3_f32 v143, v143, s5, v1
	v_mov_b32_e32 v198, 0
	v_cvt_pk_fp8_f32 v198, v140, v143
	v_max_f32_e32 v147, v199, v199
	s_waitcnt lgkmcnt(5)
	v_max_f32_e32 v140, v193, v193
	s_waitcnt lgkmcnt(4)
	v_max_f32_e32 v143, v195, v195
	v_med3_f32 v146, v146, s5, v1
	v_med3_f32 v147, v147, s5, v1
	v_med3_f32 v140, v140, s5, v1
	v_med3_f32 v143, v143, s5, v1
	v_cvt_pk_fp8_f32 v196, v146, v147 op_sel:[0,0,1]
	v_max_f32_e32 v146, v200, v200
	v_max_f32_e32 v147, v201, v201
	v_cvt_pk_fp8_f32 v198, v140, v143 op_sel:[0,0,1]
	s_waitcnt lgkmcnt(3)
	v_max_f32_e32 v140, v204, v204
	s_waitcnt lgkmcnt(2)
	v_max_f32_e32 v143, v205, v205
	v_med3_f32 v146, v146, s5, v1
	v_med3_f32 v147, v147, s5, v1
	v_mov_b32_e32 v197, 0
	v_med3_f32 v140, v140, s5, v1
	v_med3_f32 v143, v143, s5, v1
	v_mov_b32_e32 v199, 0
	v_cvt_pk_fp8_f32 v197, v146, v147
	v_cvt_pk_fp8_f32 v199, v140, v143
	v_max_f32_e32 v146, v202, v202
	v_max_f32_e32 v147, v203, v203
	s_waitcnt lgkmcnt(1)
	v_max_f32_e32 v140, v206, v206
	s_waitcnt lgkmcnt(0)
	v_max_f32_e32 v143, v207, v207
	v_med3_f32 v146, v146, s5, v1
	v_med3_f32 v147, v147, s5, v1
	v_med3_f32 v140, v140, s5, v1
	v_med3_f32 v143, v143, s5, v1
	v_cvt_pk_fp8_f32 v197, v146, v147 op_sel:[0,0,1]
	v_cvt_pk_fp8_f32 v199, v140, v143 op_sel:[0,0,1]
	ds_read2_b32 v[146:147], v183 offset1:32
	ds_read2_b32 v[202:203], v183 offset0:64 offset1:96
	ds_read2_b32 v[204:205], v183 offset0:128 offset1:160
	ds_read2_b32 v[206:207], v183 offset0:192 offset1:224
	ds_read_b32 v140, v184
	ds_read_b32 v143, v185
	ds_read_b32 v193, v186
	ds_read_b32 v195, v187
	ds_read_b32 v208, v188
	ds_read_b32 v209, v189
	ds_read_b32 v210, v190
	ds_read_b32 v211, v191
	s_waitcnt lgkmcnt(11)
	v_max_f32_e32 v146, v146, v146
	v_max_f32_e32 v147, v147, v147
	v_med3_f32 v146, v146, s5, v1
	v_med3_f32 v147, v147, s5, v1
	v_mov_b32_e32 v200, 0
	s_waitcnt lgkmcnt(7)
	v_max_f32_e32 v140, v140, v140
	s_waitcnt lgkmcnt(6)
	v_max_f32_e32 v143, v143, v143
	v_cvt_pk_fp8_f32 v200, v146, v147
	v_max_f32_e32 v146, v202, v202
	v_med3_f32 v140, v140, s5, v1
	v_med3_f32 v143, v143, s5, v1
	v_mov_b32_e32 v202, 0
	v_cvt_pk_fp8_f32 v202, v140, v143
	v_max_f32_e32 v147, v203, v203
	s_waitcnt lgkmcnt(5)
	v_max_f32_e32 v140, v193, v193
	s_waitcnt lgkmcnt(4)
	v_max_f32_e32 v143, v195, v195
	v_med3_f32 v146, v146, s5, v1
	v_med3_f32 v147, v147, s5, v1
	v_med3_f32 v140, v140, s5, v1
	v_med3_f32 v143, v143, s5, v1
	v_cvt_pk_fp8_f32 v200, v146, v147 op_sel:[0,0,1]
	v_max_f32_e32 v146, v204, v204
	v_max_f32_e32 v147, v205, v205
	v_cvt_pk_fp8_f32 v202, v140, v143 op_sel:[0,0,1]
	s_waitcnt lgkmcnt(3)
	v_max_f32_e32 v140, v208, v208
	s_waitcnt lgkmcnt(2)
	v_max_f32_e32 v143, v209, v209
	v_med3_f32 v146, v146, s5, v1
	v_med3_f32 v147, v147, s5, v1
	v_mov_b32_e32 v201, 0
	v_med3_f32 v140, v140, s5, v1
	v_med3_f32 v143, v143, s5, v1
	v_mov_b32_e32 v203, 0
	v_cvt_pk_fp8_f32 v201, v146, v147
	v_cvt_pk_fp8_f32 v203, v140, v143
	v_max_f32_e32 v146, v206, v206
	v_max_f32_e32 v147, v207, v207
	s_waitcnt lgkmcnt(1)
	v_max_f32_e32 v140, v210, v210
	s_waitcnt lgkmcnt(0)
	v_max_f32_e32 v143, v211, v211
	v_med3_f32 v146, v146, s5, v1
	v_med3_f32 v147, v147, s5, v1
	v_med3_f32 v140, v140, s5, v1
	v_med3_f32 v143, v143, s5, v1
	v_cvt_pk_fp8_f32 v201, v146, v147 op_sel:[0,0,1]
	v_cvt_pk_fp8_f32 v203, v140, v143 op_sel:[0,0,1]
	v_lshl_add_u64 v[146:147], v[144:145], 0, v[136:137]
	v_lshl_add_u64 v[144:145], v[144:145], 0, v[138:139]
	global_store_dwordx4 v[146:147], v[196:199], off nt
	global_store_dwordx4 v[144:145], v[200:203], off nt
	s_waitcnt lgkmcnt(0)
	s_andn2_b64 vcc, exec, s[82:83]
	s_mov_b64 s[82:83], 0
	s_cbranch_vccnz .LBB0_843
	s_add_i32 s6, s6, 2
	s_lshl_b32 s0, s6, 9
	s_add_i32 s0, s0, s4
	s_cmp_lt_i32 s0, 0x9b41
	s_cselect_b64 s[82:83], -1, 0
	s_cmp_gt_i32 s0, 0x9b40
	s_cbranch_scc1 .LBB0_865
	s_mul_hi_i32 s7, s0, 0x2aaaaaab
	s_lshr_b32 s10, s7, 31
	s_ashr_i32 s7, s7, 9
	s_add_i32 s74, s7, s10
	s_mul_i32 s7, s74, 0xc00
	s_sub_i32 s7, s0, s7
	s_cmpk_gt_i32 s7, 0x7ff
	s_mov_b64 s[92:93], -1
	s_cbranch_scc0 .LBB0_858
	s_ashr_i32 s75, s74, 31
	s_lshl_b64 s[10:11], s[74:75], 22
	s_lshl_b64 s[12:13], s[74:75], 24
	s_add_u32 s14, s42, s12
	s_addc_u32 s15, s43, s13
	s_lshl_b32 s0, s7, 1
	s_and_b32 s0, s0, 0x7fffff80
	s_addk_i32 s0, 0xf000
	s_lshl_b64 s[12:13], s[0:1], 13
	s_add_u32 s12, s14, s12
	s_addc_u32 s13, s15, s13
	s_lshl_b32 s14, s7, 5
	s_and_b32 s84, s14, 0x7e0
	s_lshl_b32 s14, s84, 2
	s_add_u32 s86, s12, s14
	s_addc_u32 s87, s13, 0
	v_readlane_b32 s2, v254, 46
	s_add_u32 s90, s2, s10
	v_readlane_b32 s2, v254, 47
	s_mov_b32 s85, s1
	s_addc_u32 s91, s2, s11
	v_readlane_b32 s2, v254, 59
	s_mov_b64 s[92:93], 0
	s_mov_b64 s[88:89], s[0:1]

; #define GAS __attribute__((address_space(1)))
; #define LAS __attribute__((address_space(3)))
; __device__ __forceinline__ void p8_issue(const TItem8& t, f32x4 (&v)[16], int lane) {
;     const GAS f32x4* src = (const GAS f32x4*)((const GAS float*)t.src + (size_t)(lane >> 3) * t.N + 4 * (lane & 7));
; #pragma unroll
;     for (int i = 0; i < 16; ++i) v[i] = __builtin_nontemporal_load(src + (size_t)(2 * i) * t.N);
; }
; __device__ __forceinline__ void p8_finish(const TItem8& t, const f32x4 (&v)[16], LAS float* scr, int lane) {
; #pragma unroll
;     for (int i = 0; i < 16; ++i) *(LAS f32x4*)(scr + (8 * i + (lane >> 3)) * 32 + (((lane & 7) ^ (i & 7)) << 2)) = v[i] * W8_SCALE;
.LBB0_864:
	s_lshl_b64 s[10:11], s[84:85], 11
	s_add_u32 s0, s90, s10
	v_mul_u32_u24_e32 v2, s92, v225
	s_addc_u32 s7, s91, s11
	v_lshlrev_b32_e32 v140, 2, v2
	s_add_u32 s74, s0, s88
	v_lshl_add_u64 v[2:3], s[86:87], 0, v[140:141]
	v_mov_b32_e32 v143, v141
	s_addc_u32 s75, s7, s89
	v_lshl_add_u64 v[2:3], v[2:3], 0, v[142:143]
	s_lshl_b32 s0, s92, 5
	v_lshl_add_u64 v[10:11], v[2:3], 0, s[0:1]
	global_load_dwordx4 v[2:5], v[2:3], off nt
	s_nop 0
	global_load_dwordx4 v[6:9], v[10:11], off nt
	v_lshl_add_u64 v[10:11], v[10:11], 0, s[0:1]
	v_lshl_add_u64 v[18:19], v[10:11], 0, s[0:1]
	global_load_dwordx4 v[10:13], v[10:11], off nt
	s_nop 0
	global_load_dwordx4 v[14:17], v[18:19], off nt
	v_lshl_add_u64 v[18:19], v[18:19], 0, s[0:1]
	v_lshl_add_u64 v[26:27], v[18:19], 0, s[0:1]
	global_load_dwordx4 v[18:21], v[18:19], off nt
	s_nop 0
	global_load_dwordx4 v[22:25], v[26:27], off nt
	v_lshl_add_u64 v[26:27], v[26:27], 0, s[0:1]
	v_lshl_add_u64 v[34:35], v[26:27], 0, s[0:1]
	v_lshl_add_u64 v[38:39], v[34:35], 0, s[0:1]
	v_lshl_add_u64 v[42:43], v[38:39], 0, s[0:1]
	v_lshl_add_u64 v[46:47], v[42:43], 0, s[0:1]
	v_lshl_add_u64 v[50:51], v[46:47], 0, s[0:1]
	v_lshl_add_u64 v[54:55], v[50:51], 0, s[0:1]
	v_lshl_add_u64 v[58:59], v[54:55], 0, s[0:1]
	v_lshl_add_u64 v[62:63], v[58:59], 0, s[0:1]
	global_load_dwordx4 v[26:29], v[26:27], off nt
	s_nop 0
	global_load_dwordx4 v[30:33], v[34:35], off nt
	s_nop 0
	global_load_dwordx4 v[34:37], v[38:39], off nt
	s_nop 0
	global_load_dwordx4 v[38:41], v[42:43], off nt
	s_nop 0
	global_load_dwordx4 v[42:45], v[46:47], off nt
	s_nop 0
	global_load_dwordx4 v[46:49], v[50:51], off nt
	s_nop 0
	global_load_dwordx4 v[50:53], v[54:55], off nt
	s_nop 0
	global_load_dwordx4 v[54:57], v[58:59], off nt
	s_nop 0
	global_load_dwordx4 v[58:61], v[62:63], off nt
	v_lshl_add_u64 v[62:63], v[62:63], 0, s[0:1]
	global_load_dwordx4 v[62:65], v[62:63], off nt
	s_waitcnt vmcnt(35)
	v_pk_mul_f32 v[146:147], v[68:69], s[72:73] op_sel_hi:[1,0]
	v_pk_mul_f32 v[144:145], v[66:67], s[72:73] op_sel_hi:[1,0]
	ds_write_b128 v148, v[144:147]
	s_waitcnt vmcnt(34)
	v_pk_mul_f32 v[146:147], v[72:73], s[72:73] op_sel_hi:[1,0]
	v_pk_mul_f32 v[144:145], v[70:71], s[72:73] op_sel_hi:[1,0]
	ds_write_b128 v149, v[144:147] offset:1024
	s_waitcnt vmcnt(33)
	v_pk_mul_f32 v[146:147], v[76:77], s[72:73] op_sel_hi:[1,0]
	v_pk_mul_f32 v[144:145], v[74:75], s[72:73] op_sel_hi:[1,0]
	ds_write_b128 v150, v[144:147] offset:2048
	s_waitcnt vmcnt(32)
	v_pk_mul_f32 v[146:147], v[80:81], s[72:73] op_sel_hi:[1,0]
	v_pk_mul_f32 v[144:145], v[78:79], s[72:73] op_sel_hi:[1,0]
	ds_write_b128 v151, v[144:147] offset:3072
	s_waitcnt vmcnt(31)
	v_pk_mul_f32 v[146:147], v[84:85], s[72:73] op_sel_hi:[1,0]
	v_pk_mul_f32 v[144:145], v[82:83], s[72:73] op_sel_hi:[1,0]
	ds_write_b128 v152, v[144:147] offset:4096
	s_waitcnt vmcnt(30)
	v_pk_mul_f32 v[146:147], v[88:89], s[72:73] op_sel_hi:[1,0]
	v_pk_mul_f32 v[144:145], v[86:87], s[72:73] op_sel_hi:[1,0]
	ds_write_b128 v153, v[144:147] offset:5120
	s_waitcnt vmcnt(29)
	v_pk_mul_f32 v[146:147], v[92:93], s[72:73] op_sel_hi:[1,0]
	v_pk_mul_f32 v[144:145], v[90:91], s[72:73] op_sel_hi:[1,0]
	ds_write_b128 v154, v[144:147] offset:6144
	s_waitcnt vmcnt(28)
	v_pk_mul_f32 v[146:147], v[96:97], s[72:73] op_sel_hi:[1,0]
	v_pk_mul_f32 v[144:145], v[94:95], s[72:73] op_sel_hi:[1,0]
	ds_write_b128 v155, v[144:147] offset:7168
	s_waitcnt vmcnt(27)
	v_pk_mul_f32 v[146:147], v[100:101], s[72:73] op_sel_hi:[1,0]
	v_pk_mul_f32 v[144:145], v[98:99], s[72:73] op_sel_hi:[1,0]
	ds_write_b128 v148, v[144:147] offset:8192
	s_waitcnt vmcnt(26)
	v_pk_mul_f32 v[146:147], v[104:105], s[72:73] op_sel_hi:[1,0]
	v_pk_mul_f32 v[144:145], v[102:103], s[72:73] op_sel_hi:[1,0]
	ds_write_b128 v149, v[144:147] offset:9216
	s_waitcnt vmcnt(25)
	v_pk_mul_f32 v[146:147], v[108:109], s[72:73] op_sel_hi:[1,0]
	v_pk_mul_f32 v[144:145], v[106:107], s[72:73] op_sel_hi:[1,0]
	ds_write_b128 v150, v[144:147] offset:10240
	s_waitcnt vmcnt(24)
	v_pk_mul_f32 v[146:147], v[112:113], s[72:73] op_sel_hi:[1,0]
	v_pk_mul_f32 v[144:145], v[110:111], s[72:73] op_sel_hi:[1,0]
	ds_write_b128 v151, v[144:147] offset:11264
	s_waitcnt vmcnt(23)
	v_pk_mul_f32 v[146:147], v[116:117], s[72:73] op_sel_hi:[1,0]
	v_pk_mul_f32 v[144:145], v[114:115], s[72:73] op_sel_hi:[1,0]
	ds_write_b128 v152, v[144:147] offset:12288
	s_waitcnt vmcnt(22)
	v_pk_mul_f32 v[146:147], v[120:121], s[72:73] op_sel_hi:[1,0]
	v_pk_mul_f32 v[144:145], v[118:119], s[72:73] op_sel_hi:[1,0]
	ds_write_b128 v153, v[144:147] offset:13312
	s_waitcnt vmcnt(21)
	v_pk_mul_f32 v[146:147], v[124:125], s[72:73] op_sel_hi:[1,0]
	v_pk_mul_f32 v[144:145], v[122:123], s[72:73] op_sel_hi:[1,0]
	ds_write_b128 v154, v[144:147] offset:14336
	s_waitcnt vmcnt(20)
	v_pk_mul_f32 v[146:147], v[128:129], s[72:73] op_sel_hi:[1,0]
	v_pk_mul_f32 v[144:145], v[126:127], s[72:73] op_sel_hi:[1,0]
	ds_write_b128 v155, v[144:147] offset:15360
	s_branch .Lcv2_4_854
; #define GAS __attribute__((address_space(1)))
; #define LAS __attribute__((address_space(3)))
; __device__ __forceinline__ void p8_finish(const TItem8& t, const f32x4 (&v)[16], LAS float* scr, int lane) {
;     ...
;     for (int i = 0; i < 16; ++i) *(LAS f32x4*)(scr + (8 * i + (lane >> 3)) * 32 + (((lane & 7) ^ (i & 7)) << 2)) = v[i] * W8_SCALE;
;     ...
;     const int c = lane & 7;
; #pragma unroll
;     for (int j = 0; j < 4; ++j) { const int n = (lane >> 3) + 8 * j; float x[16];
; #pragma unroll
;         for (int i = 0; i < 16; ++i) { const int k = 16 * c + i; x[i] = scr[k * 32 + ((((n >> 2) ^ ((k >> 3) & 7)) << 2) | (n & 3))]; }
;         int w[4];
; #pragma unroll
;         for (int g = 0; g < 4; ++g) { int q = 0; q = __builtin_amdgcn_cvt_pk_fp8_f32(fminf(fmaxf(x[4 * g], -448.f), 448.f), fminf(fmaxf(x[4 * g + 1], -448.f), 448.f), q, false);
;             q = __builtin_amdgcn_cvt_pk_fp8_f32(fminf(fmaxf(x[4 * g + 2], -448.f), 448.f), fminf(fmaxf(x[4 * g + 3], -448.f), 448.f), q, true); w[g] = q; }
;         v4u o; o.x = (unsigned)w[0]; o.y = (unsigned)w[1]; o.z = (unsigned)w[2]; o.w = (unsigned)w[3];
;         __builtin_nontemporal_store(o, (GAS v4u*)(t.dst + (size_t)n * t.Kd + 16 * c)); }
.LBB0_865:
	s_waitcnt vmcnt(19)
	v_pk_mul_f32 v[146:147], v[68:69], s[72:73] op_sel_hi:[1,0]
	v_pk_mul_f32 v[144:145], v[66:67], s[72:73] op_sel_hi:[1,0]
	ds_write_b128 v148, v[144:147]
	s_waitcnt vmcnt(18)
	v_pk_mul_f32 v[146:147], v[72:73], s[72:73] op_sel_hi:[1,0]
	v_pk_mul_f32 v[144:145], v[70:71], s[72:73] op_sel_hi:[1,0]
	ds_write_b128 v149, v[144:147] offset:1024
	s_waitcnt vmcnt(17)
	v_pk_mul_f32 v[146:147], v[76:77], s[72:73] op_sel_hi:[1,0]
	v_pk_mul_f32 v[144:145], v[74:75], s[72:73] op_sel_hi:[1,0]
	ds_write_b128 v150, v[144:147] offset:2048
	s_waitcnt vmcnt(16)
	v_pk_mul_f32 v[146:147], v[80:81], s[72:73] op_sel_hi:[1,0]
	v_pk_mul_f32 v[144:145], v[78:79], s[72:73] op_sel_hi:[1,0]
	ds_write_b128 v151, v[144:147] offset:3072
	s_waitcnt vmcnt(15)
	v_pk_mul_f32 v[146:147], v[84:85], s[72:73] op_sel_hi:[1,0]
	v_pk_mul_f32 v[144:145], v[82:83], s[72:73] op_sel_hi:[1,0]
	ds_write_b128 v152, v[144:147] offset:4096
	s_waitcnt vmcnt(14)
	v_pk_mul_f32 v[146:147], v[88:89], s[72:73] op_sel_hi:[1,0]
	v_pk_mul_f32 v[144:145], v[86:87], s[72:73] op_sel_hi:[1,0]
	ds_write_b128 v153, v[144:147] offset:5120
	s_waitcnt vmcnt(13)
	v_pk_mul_f32 v[146:147], v[92:93], s[72:73] op_sel_hi:[1,0]
	v_pk_mul_f32 v[144:145], v[90:91], s[72:73] op_sel_hi:[1,0]
	ds_write_b128 v154, v[144:147] offset:6144
	s_waitcnt vmcnt(12)
	v_pk_mul_f32 v[146:147], v[96:97], s[72:73] op_sel_hi:[1,0]
	v_pk_mul_f32 v[144:145], v[94:95], s[72:73] op_sel_hi:[1,0]
	ds_write_b128 v155, v[144:147] offset:7168
	s_waitcnt vmcnt(11)
	v_pk_mul_f32 v[146:147], v[100:101], s[72:73] op_sel_hi:[1,0]
	v_pk_mul_f32 v[144:145], v[98:99], s[72:73] op_sel_hi:[1,0]
	ds_write_b128 v148, v[144:147] offset:8192
	s_waitcnt vmcnt(10)
	v_pk_mul_f32 v[146:147], v[104:105], s[72:73] op_sel_hi:[1,0]
	v_pk_mul_f32 v[144:145], v[102:103], s[72:73] op_sel_hi:[1,0]
	ds_write_b128 v149, v[144:147] offset:9216
	s_waitcnt vmcnt(9)
	v_pk_mul_f32 v[146:147], v[108:109], s[72:73] op_sel_hi:[1,0]
	v_pk_mul_f32 v[144:145], v[106:107], s[72:73] op_sel_hi:[1,0]
	ds_write_b128 v150, v[144:147] offset:10240
	s_waitcnt vmcnt(8)
	v_pk_mul_f32 v[146:147], v[112:113], s[72:73] op_sel_hi:[1,0]
	v_pk_mul_f32 v[144:145], v[110:111], s[72:73] op_sel_hi:[1,0]
	ds_write_b128 v151, v[144:147] offset:11264
	s_waitcnt vmcnt(7)
	v_pk_mul_f32 v[146:147], v[116:117], s[72:73] op_sel_hi:[1,0]
	v_pk_mul_f32 v[144:145], v[114:115], s[72:73] op_sel_hi:[1,0]
	ds_write_b128 v152, v[144:147] offset:12288
	s_waitcnt vmcnt(6)
	v_pk_mul_f32 v[146:147], v[120:121], s[72:73] op_sel_hi:[1,0]
	v_pk_mul_f32 v[144:145], v[118:119], s[72:73] op_sel_hi:[1,0]
	ds_write_b128 v153, v[144:147] offset:13312
	s_waitcnt vmcnt(5)
	v_pk_mul_f32 v[146:147], v[124:125], s[72:73] op_sel_hi:[1,0]
	v_pk_mul_f32 v[144:145], v[122:123], s[72:73] op_sel_hi:[1,0]
	ds_write_b128 v154, v[144:147] offset:14336
	s_waitcnt vmcnt(4)
	v_pk_mul_f32 v[146:147], v[128:129], s[72:73] op_sel_hi:[1,0]
	v_pk_mul_f32 v[144:145], v[126:127], s[72:73] op_sel_hi:[1,0]
	ds_write_b128 v155, v[144:147] offset:15360
.Lcv2_4_854:
	s_waitcnt lgkmcnt(0)
	ds_read2_b32 v[146:147], v156 offset1:32
	ds_read2_b32 v[198:199], v156 offset0:64 offset1:96
	ds_read2_b32 v[200:201], v156 offset0:128 offset1:160
	ds_read2_b32 v[202:203], v156 offset0:192 offset1:224
	ds_read_b32 v140, v157
	ds_read_b32 v143, v158
	ds_read_b32 v193, v159
	ds_read_b32 v195, v160
	ds_read_b32 v204, v161
	ds_read_b32 v205, v162
	ds_read_b32 v206, v163
	ds_read_b32 v207, v164
	s_waitcnt lgkmcnt(11)
	v_max_f32_e32 v146, v146, v146
	v_max_f32_e32 v147, v147, v147
	v_med3_f32 v146, v146, s5, v1
	v_med3_f32 v147, v147, s5, v1
	v_mov_b32_e32 v196, v141
	s_waitcnt lgkmcnt(7)
	v_max_f32_e32 v140, v140, v140
	s_waitcnt lgkmcnt(6)
	v_max_f32_e32 v143, v143, v143
	v_cvt_pk_fp8_f32 v196, v146, v147
	v_max_f32_e32 v146, v198, v198
	v_med3_f32 v140, v140, s5, v1
	v_med3_f32 v143, v143, s5, v1
	v_mov_b32_e32 v198, v141
	v_cvt_pk_fp8_f32 v198, v140, v143
	v_max_f32_e32 v147, v199, v199
	s_waitcnt lgkmcnt(5)
	v_max_f32_e32 v140, v193, v193
	s_waitcnt lgkmcnt(4)
	v_max_f32_e32 v143, v195, v195
	v_med3_f32 v146, v146, s5, v1
	v_med3_f32 v147, v147, s5, v1
	v_med3_f32 v140, v140, s5, v1
	v_med3_f32 v143, v143, s5, v1
	v_cvt_pk_fp8_f32 v196, v146, v147 op_sel:[0,0,1]
	v_max_f32_e32 v146, v200, v200
	v_max_f32_e32 v147, v201, v201
	v_cvt_pk_fp8_f32 v198, v140, v143 op_sel:[0,0,1]
	s_waitcnt lgkmcnt(3)
	v_max_f32_e32 v140, v204, v204
	s_waitcnt lgkmcnt(2)
	v_max_f32_e32 v143, v205, v205
	v_med3_f32 v146, v146, s5, v1
	v_med3_f32 v147, v147, s5, v1
	v_mov_b32_e32 v197, v141
	v_med3_f32 v140, v140, s5, v1
	v_med3_f32 v143, v143, s5, v1
	v_mov_b32_e32 v199, v141
	v_cvt_pk_fp8_f32 v197, v146, v147
	v_cvt_pk_fp8_f32 v199, v140, v143
	v_max_f32_e32 v146, v202, v202
	v_max_f32_e32 v147, v203, v203
	s_waitcnt lgkmcnt(1)
	v_max_f32_e32 v140, v206, v206
	s_waitcnt lgkmcnt(0)
	v_max_f32_e32 v143, v207, v207
	v_med3_f32 v146, v146, s5, v1
	v_med3_f32 v147, v147, s5, v1
	v_med3_f32 v140, v140, s5, v1
	v_med3_f32 v143, v143, s5, v1
	v_cvt_pk_fp8_f32 v197, v146, v147 op_sel:[0,0,1]
	v_cvt_pk_fp8_f32 v199, v140, v143 op_sel:[0,0,1]
	v_lshl_add_u64 v[144:145], s[80:81], 0, v[130:131]
	v_lshl_add_u64 v[146:147], v[144:145], 0, v[132:133]
	global_store_dwordx4 v[146:147], v[196:199], off nt
	ds_read2_b32 v[146:147], v165 offset1:32
	ds_read2_b32 v[198:199], v165 offset0:64 offset1:96
	ds_read2_b32 v[200:201], v165 offset0:128 offset1:160
	ds_read2_b32 v[202:203], v165 offset0:192 offset1:224
	ds_read_b32 v140, v166
	ds_read_b32 v143, v167
	ds_read_b32 v193, v168
	ds_read_b32 v195, v169
	ds_read_b32 v204, v170
	ds_read_b32 v205, v171
	ds_read_b32 v206, v172
	ds_read_b32 v207, v173
	s_waitcnt lgkmcnt(11)
; #define GAS __attribute__((address_space(1)))
; __device__ __forceinline__ void p8_finish(const TItem8& t, const f32x4 (&v)[16], LAS float* scr, int lane) {
;     ...
;     const int c = lane & 7;
; #pragma unroll
;     for (int j = 0; j < 4; ++j) { const int n = (lane >> 3) + 8 * j; float x[16];
; #pragma unroll
;         for (int i = 0; i < 16; ++i) { const int k = 16 * c + i; x[i] = scr[k * 32 + ((((n >> 2) ^ ((k >> 3) & 7)) << 2) | (n & 3))]; }
;         int w[4];
; #pragma unroll
;         for (int g = 0; g < 4; ++g) { int q = 0; q = __builtin_amdgcn_cvt_pk_fp8_f32(fminf(fmaxf(x[4 * g], -448.f), 448.f), fminf(fmaxf(x[4 * g + 1], -448.f), 448.f), q, false);
;             q = __builtin_amdgcn_cvt_pk_fp8_f32(fminf(fmaxf(x[4 * g + 2], -448.f), 448.f), fminf(fmaxf(x[4 * g + 3], -448.f), 448.f), q, true); w[g] = q; }
;         v4u o; o.x = (unsigned)w[0]; o.y = (unsigned)w[1]; o.z = (unsigned)w[2]; o.w = (unsigned)w[3];
;         __builtin_nontemporal_store(o, (GAS v4u*)(t.dst + (size_t)n * t.Kd + 16 * c)); }
	v_max_f32_e32 v146, v146, v146
	v_max_f32_e32 v147, v147, v147
	v_med3_f32 v146, v146, s5, v1
	v_med3_f32 v147, v147, s5, v1
	v_mov_b32_e32 v196, v141
	s_waitcnt lgkmcnt(7)
	v_max_f32_e32 v140, v140, v140
	s_waitcnt lgkmcnt(6)
	v_max_f32_e32 v143, v143, v143
	v_cvt_pk_fp8_f32 v196, v146, v147
	v_max_f32_e32 v146, v198, v198
	v_med3_f32 v140, v140, s5, v1
	v_med3_f32 v143, v143, s5, v1
	v_mov_b32_e32 v198, v141
	v_cvt_pk_fp8_f32 v198, v140, v143
	v_max_f32_e32 v147, v199, v199
	s_waitcnt lgkmcnt(5)
	v_max_f32_e32 v140, v193, v193
	s_waitcnt lgkmcnt(4)
	v_max_f32_e32 v143, v195, v195
	v_med3_f32 v146, v146, s5, v1
	v_med3_f32 v147, v147, s5, v1
	v_med3_f32 v140, v140, s5, v1
	v_med3_f32 v143, v143, s5, v1
	v_cvt_pk_fp8_f32 v196, v146, v147 op_sel:[0,0,1]
	v_max_f32_e32 v146, v200, v200
	v_max_f32_e32 v147, v201, v201
	v_cvt_pk_fp8_f32 v198, v140, v143 op_sel:[0,0,1]
	s_waitcnt lgkmcnt(3)
	v_max_f32_e32 v140, v204, v204
	s_waitcnt lgkmcnt(2)
	v_max_f32_e32 v143, v205, v205
	v_med3_f32 v146, v146, s5, v1
	v_med3_f32 v147, v147, s5, v1
	v_mov_b32_e32 v197, v141
	v_med3_f32 v140, v140, s5, v1
	v_med3_f32 v143, v143, s5, v1
	v_mov_b32_e32 v199, v141
	v_cvt_pk_fp8_f32 v197, v146, v147
	v_cvt_pk_fp8_f32 v199, v140, v143
	v_max_f32_e32 v146, v202, v202
	v_max_f32_e32 v147, v203, v203
	s_waitcnt lgkmcnt(1)
	v_max_f32_e32 v140, v206, v206
	s_waitcnt lgkmcnt(0)
	v_max_f32_e32 v143, v207, v207
	v_med3_f32 v146, v146, s5, v1
	v_med3_f32 v147, v147, s5, v1
	v_med3_f32 v140, v140, s5, v1
	v_med3_f32 v143, v143, s5, v1
	v_cvt_pk_fp8_f32 v197, v146, v147 op_sel:[0,0,1]
	v_cvt_pk_fp8_f32 v199, v140, v143 op_sel:[0,0,1]
	v_lshl_add_u64 v[146:147], v[144:145], 0, v[134:135]
	global_store_dwordx4 v[146:147], v[196:199], off nt
	ds_read2_b32 v[146:147], v174 offset1:32
	ds_read2_b32 v[198:199], v174 offset0:64 offset1:96
	ds_read2_b32 v[200:201], v174 offset0:128 offset1:160
	ds_read2_b32 v[202:203], v174 offset0:192 offset1:224
	ds_read_b32 v140, v175
	ds_read_b32 v143, v176
	ds_read_b32 v193, v177
	ds_read_b32 v195, v178
	ds_read_b32 v204, v179
	ds_read_b32 v205, v180
	ds_read_b32 v206, v181
	ds_read_b32 v207, v182
	s_waitcnt lgkmcnt(11)
	v_max_f32_e32 v146, v146, v146
	v_max_f32_e32 v147, v147, v147
	v_med3_f32 v146, v146, s5, v1
	v_med3_f32 v147, v147, s5, v1
	v_mov_b32_e32 v196, v141
	s_waitcnt lgkmcnt(7)
	v_max_f32_e32 v140, v140, v140
	s_waitcnt lgkmcnt(6)
	v_max_f32_e32 v143, v143, v143
	v_cvt_pk_fp8_f32 v196, v146, v147
	v_max_f32_e32 v146, v198, v198
	v_med3_f32 v140, v140, s5, v1
	v_med3_f32 v143, v143, s5, v1
	v_mov_b32_e32 v198, v141
	v_cvt_pk_fp8_f32 v198, v140, v143
	v_max_f32_e32 v147, v199, v199
	s_waitcnt lgkmcnt(5)
	v_max_f32_e32 v140, v193, v193
	s_waitcnt lgkmcnt(4)
	v_max_f32_e32 v143, v195, v195
	v_med3_f32 v146, v146, s5, v1
	v_med3_f32 v147, v147, s5, v1
	v_med3_f32 v140, v140, s5, v1
	v_med3_f32 v143, v143, s5, v1
	v_cvt_pk_fp8_f32 v196, v146, v147 op_sel:[0,0,1]
	v_max_f32_e32 v146, v200, v200
	v_max_f32_e32 v147, v201, v201
	v_cvt_pk_fp8_f32 v198, v140, v143 op_sel:[0,0,1]
	s_waitcnt lgkmcnt(3)
	v_max_f32_e32 v140, v204, v204
	s_waitcnt lgkmcnt(2)
	v_max_f32_e32 v143, v205, v205
	v_med3_f32 v146, v146, s5, v1
	v_med3_f32 v147, v147, s5, v1
	v_mov_b32_e32 v197, v141
	v_med3_f32 v140, v140, s5, v1
	v_med3_f32 v143, v143, s5, v1
	v_mov_b32_e32 v199, v141
	v_cvt_pk_fp8_f32 v197, v146, v147
	v_cvt_pk_fp8_f32 v199, v140, v143
	v_max_f32_e32 v146, v202, v202
	v_max_f32_e32 v147, v203, v203
	s_waitcnt lgkmcnt(1)
	v_max_f32_e32 v140, v206, v206
	s_waitcnt lgkmcnt(0)
	v_max_f32_e32 v143, v207, v207
	v_med3_f32 v146, v146, s5, v1
	v_med3_f32 v147, v147, s5, v1
	v_med3_f32 v140, v140, s5, v1
	v_med3_f32 v143, v143, s5, v1
	v_cvt_pk_fp8_f32 v197, v146, v147 op_sel:[0,0,1]
	v_cvt_pk_fp8_f32 v199, v140, v143 op_sel:[0,0,1]
	v_lshl_add_u64 v[146:147], v[144:145], 0, v[136:137]
	v_lshl_add_u64 v[144:145], v[144:145], 0, v[138:139]
	global_store_dwordx4 v[146:147], v[196:199], off nt
	ds_read2_b32 v[146:147], v183 offset1:32
	ds_read2_b32 v[198:199], v183 offset0:64 offset1:96
	ds_read2_b32 v[200:201], v183 offset0:128 offset1:160
	ds_read2_b32 v[202:203], v183 offset0:192 offset1:224
	ds_read_b32 v140, v184
	ds_read_b32 v143, v185
	ds_read_b32 v193, v186
	ds_read_b32 v195, v187
	ds_read_b32 v204, v188
	ds_read_b32 v205, v189
	ds_read_b32 v206, v190
	ds_read_b32 v207, v191
	s_waitcnt lgkmcnt(11)
	v_max_f32_e32 v146, v146, v146
	v_max_f32_e32 v147, v147, v147
	v_med3_f32 v146, v146, s5, v1
	v_med3_f32 v147, v147, s5, v1
	v_mov_b32_e32 v196, v141
	s_waitcnt lgkmcnt(7)
	v_max_f32_e32 v140, v140, v140
	s_waitcnt lgkmcnt(6)
	v_max_f32_e32 v143, v143, v143
	v_cvt_pk_fp8_f32 v196, v146, v147
	v_max_f32_e32 v146, v198, v198
	v_med3_f32 v140, v140, s5, v1
	v_med3_f32 v143, v143, s5, v1
	v_mov_b32_e32 v198, v141
	v_cvt_pk_fp8_f32 v198, v140, v143
	v_max_f32_e32 v147, v199, v199
	s_waitcnt lgkmcnt(5)
	v_max_f32_e32 v140, v193, v193
	s_waitcnt lgkmcnt(4)
	v_max_f32_e32 v143, v195, v195
	v_med3_f32 v146, v146, s5, v1
	v_med3_f32 v147, v147, s5, v1
	v_med3_f32 v140, v140, s5, v1
	v_med3_f32 v143, v143, s5, v1
	v_cvt_pk_fp8_f32 v196, v146, v147 op_sel:[0,0,1]
	v_max_f32_e32 v146, v200, v200
	v_max_f32_e32 v147, v201, v201
	v_cvt_pk_fp8_f32 v198, v140, v143 op_sel:[0,0,1]
	s_waitcnt lgkmcnt(3)
	v_max_f32_e32 v140, v204, v204
	s_waitcnt lgkmcnt(2)
	v_max_f32_e32 v143, v205, v205
	v_med3_f32 v146, v146, s5, v1
	v_med3_f32 v147, v147, s5, v1
	v_mov_b32_e32 v197, v141
	v_med3_f32 v140, v140, s5, v1
	v_med3_f32 v143, v143, s5, v1
	v_mov_b32_e32 v199, v141
	v_cvt_pk_fp8_f32 v197, v146, v147
	v_cvt_pk_fp8_f32 v199, v140, v143
	v_max_f32_e32 v146, v202, v202
	v_max_f32_e32 v147, v203, v203
	s_waitcnt lgkmcnt(1)
	v_max_f32_e32 v140, v206, v206
	s_waitcnt lgkmcnt(0)
	v_max_f32_e32 v143, v207, v207
	v_med3_f32 v146, v146, s5, v1
	v_med3_f32 v147, v147, s5, v1
	v_med3_f32 v140, v140, s5, v1
	v_med3_f32 v143, v143, s5, v1
	v_cvt_pk_fp8_f32 v197, v146, v147 op_sel:[0,0,1]
	v_cvt_pk_fp8_f32 v199, v140, v143 op_sel:[0,0,1]
	global_store_dwordx4 v[144:145], v[196:199], off nt
	s_waitcnt lgkmcnt(0)
	s_xor_b64 s[82:83], s[82:83], -1
	s_and_b64 vcc, exec, s[82:83]
	s_cbranch_vccz .LBB0_844

; #define GAS __attribute__((address_space(1)))
; #define LAS __attribute__((address_space(3)))
; __device__ __forceinline__ void p8_issue(const TItem8& t, f32x4 (&v)[16], int lane) {
;     const GAS f32x4* src = (const GAS f32x4*)((const GAS float*)t.src + (size_t)(lane >> 3) * t.N + 4 * (lane & 7));
; #pragma unroll
;     for (int i = 0; i < 16; ++i) v[i] = __builtin_nontemporal_load(src + (size_t)(2 * i) * t.N);
; }
; __device__ __forceinline__ void p8_finish(const TItem8& t, const f32x4 (&v)[16], LAS float* scr, int lane) {
; #pragma unroll
;     for (int i = 0; i < 16; ++i) *(LAS f32x4*)(scr + (8 * i + (lane >> 3)) * 32 + (((lane & 7) ^ (i & 7)) << 2)) = v[i] * W8_SCALE;
.LBB0_947:
	s_lshl_b64 s[8:9], s[12:13], 11
	s_add_u32 s0, s18, s8
	v_mul_u32_u24_e32 v66, s34, v225
	s_addc_u32 s9, s19, s9
	v_lshlrev_b32_e32 v140, 2, v66
	s_add_u32 s8, s0, s16
	v_lshl_add_u64 v[66:67], s[14:15], 0, v[140:141]
	v_mov_b32_e32 v143, v141
	s_addc_u32 s9, s9, s17
	v_lshl_add_u64 v[66:67], v[66:67], 0, v[142:143]
	s_lshl_b32 s0, s34, 5
	s_waitcnt vmcnt(23)
	v_lshl_add_u64 v[74:75], v[66:67], 0, s[0:1]
	global_load_dwordx4 v[66:69], v[66:67], off nt
	s_nop 0
	global_load_dwordx4 v[70:73], v[74:75], off nt
	v_lshl_add_u64 v[74:75], v[74:75], 0, s[0:1]
	v_lshl_add_u64 v[82:83], v[74:75], 0, s[0:1]
	global_load_dwordx4 v[74:77], v[74:75], off nt
	s_nop 0
	global_load_dwordx4 v[78:81], v[82:83], off nt
	v_lshl_add_u64 v[82:83], v[82:83], 0, s[0:1]
	v_lshl_add_u64 v[90:91], v[82:83], 0, s[0:1]
	global_load_dwordx4 v[82:85], v[82:83], off nt
	s_nop 0
	global_load_dwordx4 v[86:89], v[90:91], off nt
	v_lshl_add_u64 v[90:91], v[90:91], 0, s[0:1]
	v_lshl_add_u64 v[98:99], v[90:91], 0, s[0:1]
	v_lshl_add_u64 v[102:103], v[98:99], 0, s[0:1]
	v_lshl_add_u64 v[106:107], v[102:103], 0, s[0:1]
	v_lshl_add_u64 v[110:111], v[106:107], 0, s[0:1]
	v_lshl_add_u64 v[114:115], v[110:111], 0, s[0:1]
	v_lshl_add_u64 v[118:119], v[114:115], 0, s[0:1]
	v_lshl_add_u64 v[122:123], v[118:119], 0, s[0:1]
	v_lshl_add_u64 v[126:127], v[122:123], 0, s[0:1]
	global_load_dwordx4 v[90:93], v[90:91], off nt
	s_nop 0
	global_load_dwordx4 v[94:97], v[98:99], off nt
	s_nop 0
	global_load_dwordx4 v[98:101], v[102:103], off nt
	s_nop 0
	global_load_dwordx4 v[102:105], v[106:107], off nt
	s_nop 0
	global_load_dwordx4 v[106:109], v[110:111], off nt
	s_nop 0
	global_load_dwordx4 v[110:113], v[114:115], off nt
	s_nop 0
	global_load_dwordx4 v[114:117], v[118:119], off nt
	s_nop 0
	global_load_dwordx4 v[118:121], v[122:123], off nt
	s_nop 0
	global_load_dwordx4 v[122:125], v[126:127], off nt
	v_lshl_add_u64 v[126:127], v[126:127], 0, s[0:1]
	global_load_dwordx4 v[126:129], v[126:127], off nt
	s_waitcnt vmcnt(31)
	v_pk_mul_f32 v[146:147], v[4:5], s[4:5] op_sel_hi:[1,0]
	v_pk_mul_f32 v[144:145], v[2:3], s[4:5] op_sel_hi:[1,0]
	ds_write_b128 v148, v[144:147]
	s_waitcnt vmcnt(30)
	v_pk_mul_f32 v[146:147], v[8:9], s[4:5] op_sel_hi:[1,0]
	v_pk_mul_f32 v[144:145], v[6:7], s[4:5] op_sel_hi:[1,0]
	ds_write_b128 v149, v[144:147] offset:1024
	s_waitcnt vmcnt(29)
	v_pk_mul_f32 v[146:147], v[12:13], s[4:5] op_sel_hi:[1,0]
	v_pk_mul_f32 v[144:145], v[10:11], s[4:5] op_sel_hi:[1,0]
	ds_write_b128 v150, v[144:147] offset:2048
	s_waitcnt vmcnt(28)
	v_pk_mul_f32 v[146:147], v[16:17], s[4:5] op_sel_hi:[1,0]
	v_pk_mul_f32 v[144:145], v[14:15], s[4:5] op_sel_hi:[1,0]
	ds_write_b128 v151, v[144:147] offset:3072
	s_waitcnt vmcnt(27)
	v_pk_mul_f32 v[146:147], v[20:21], s[4:5] op_sel_hi:[1,0]
	v_pk_mul_f32 v[144:145], v[18:19], s[4:5] op_sel_hi:[1,0]
	ds_write_b128 v152, v[144:147] offset:4096
	s_waitcnt vmcnt(26)
	v_pk_mul_f32 v[146:147], v[24:25], s[4:5] op_sel_hi:[1,0]
	v_pk_mul_f32 v[144:145], v[22:23], s[4:5] op_sel_hi:[1,0]
	ds_write_b128 v153, v[144:147] offset:5120
	s_waitcnt vmcnt(25)
	v_pk_mul_f32 v[146:147], v[28:29], s[4:5] op_sel_hi:[1,0]
	v_pk_mul_f32 v[144:145], v[26:27], s[4:5] op_sel_hi:[1,0]
	ds_write_b128 v154, v[144:147] offset:6144
	s_waitcnt vmcnt(24)
	v_pk_mul_f32 v[146:147], v[32:33], s[4:5] op_sel_hi:[1,0]
	v_pk_mul_f32 v[144:145], v[30:31], s[4:5] op_sel_hi:[1,0]
	ds_write_b128 v155, v[144:147] offset:7168
	s_waitcnt vmcnt(23)
	v_pk_mul_f32 v[146:147], v[36:37], s[4:5] op_sel_hi:[1,0]
	v_pk_mul_f32 v[144:145], v[34:35], s[4:5] op_sel_hi:[1,0]
	ds_write_b128 v148, v[144:147] offset:8192
	s_waitcnt vmcnt(22)
	v_pk_mul_f32 v[146:147], v[40:41], s[4:5] op_sel_hi:[1,0]
	v_pk_mul_f32 v[144:145], v[38:39], s[4:5] op_sel_hi:[1,0]
	ds_write_b128 v149, v[144:147] offset:9216
	s_waitcnt vmcnt(21)
	v_pk_mul_f32 v[146:147], v[44:45], s[4:5] op_sel_hi:[1,0]
	v_pk_mul_f32 v[144:145], v[42:43], s[4:5] op_sel_hi:[1,0]
	ds_write_b128 v150, v[144:147] offset:10240
	s_waitcnt vmcnt(20)
	v_pk_mul_f32 v[146:147], v[48:49], s[4:5] op_sel_hi:[1,0]
	v_pk_mul_f32 v[144:145], v[46:47], s[4:5] op_sel_hi:[1,0]
	ds_write_b128 v151, v[144:147] offset:11264
	s_waitcnt vmcnt(19)
	v_pk_mul_f32 v[146:147], v[52:53], s[4:5] op_sel_hi:[1,0]
	v_pk_mul_f32 v[144:145], v[50:51], s[4:5] op_sel_hi:[1,0]
	ds_write_b128 v152, v[144:147] offset:12288
	s_waitcnt vmcnt(18)
	v_pk_mul_f32 v[146:147], v[56:57], s[4:5] op_sel_hi:[1,0]
	v_pk_mul_f32 v[144:145], v[54:55], s[4:5] op_sel_hi:[1,0]
	ds_write_b128 v153, v[144:147] offset:13312
	s_waitcnt vmcnt(17)
	v_pk_mul_f32 v[146:147], v[60:61], s[4:5] op_sel_hi:[1,0]
	v_pk_mul_f32 v[144:145], v[58:59], s[4:5] op_sel_hi:[1,0]
	ds_write_b128 v154, v[144:147] offset:14336
	s_waitcnt vmcnt(16)
	v_pk_mul_f32 v[146:147], v[64:65], s[4:5] op_sel_hi:[1,0]
	v_pk_mul_f32 v[144:145], v[62:63], s[4:5] op_sel_hi:[1,0]
	ds_write_b128 v155, v[144:147] offset:15360
	s_branch .Lcv1_3_948

; #define GAS __attribute__((address_space(1)))
; __device__ __forceinline__ void p8_finish(const TItem8& t, const f32x4 (&v)[16], LAS float* scr, int lane) {
;     ...
;     const int c = lane & 7;
; #pragma unroll
;     for (int j = 0; j < 4; ++j) { const int n = (lane >> 3) + 8 * j; float x[16];
; #pragma unroll
;         for (int i = 0; i < 16; ++i) { const int k = 16 * c + i; x[i] = scr[k * 32 + ((((n >> 2) ^ ((k >> 3) & 7)) << 2) | (n & 3))]; }
;         int w[4];
; #pragma unroll
;         for (int g = 0; g < 4; ++g) { int q = 0; q = __builtin_amdgcn_cvt_pk_fp8_f32(fminf(fmaxf(x[4 * g], -448.f), 448.f), fminf(fmaxf(x[4 * g + 1], -448.f), 448.f), q, false);
;             q = __builtin_amdgcn_cvt_pk_fp8_f32(fminf(fmaxf(x[4 * g + 2], -448.f), 448.f), fminf(fmaxf(x[4 * g + 3], -448.f), 448.f), q, true); w[g] = q; }
;         v4u o; o.x = (unsigned)w[0]; o.y = (unsigned)w[1]; o.z = (unsigned)w[2]; o.w = (unsigned)w[3];
;         __builtin_nontemporal_store(o, (GAS v4u*)(t.dst + (size_t)n * t.Kd + 16 * c)); }
.Lcv1_3_948:
	s_waitcnt lgkmcnt(0)
	ds_read2_b32 v[146:147], v156 offset1:32
	ds_read2_b32 v[192:193], v156 offset0:64 offset1:96
	ds_read2_b32 v[198:199], v156 offset0:128 offset1:160
	ds_read2_b32 v[200:201], v156 offset0:192 offset1:224
	ds_read_b32 v140, v157
	ds_read_b32 v143, v158
	ds_read_b32 v195, v159
	ds_read_b32 v202, v160
	ds_read_b32 v203, v161
	ds_read_b32 v204, v162
	ds_read_b32 v205, v163
	ds_read_b32 v206, v164
	s_waitcnt lgkmcnt(11)
	v_max_f32_e32 v146, v146, v146
	v_max_f32_e32 v147, v147, v147
	v_med3_f32 v146, v146, s3, v1
	v_med3_f32 v147, v147, s3, v1
	v_mov_b32_e32 v196, 0
	v_cvt_pk_fp8_f32 v196, v146, v147
	s_waitcnt lgkmcnt(10)
	v_max_f32_e32 v146, v192, v192
	v_max_f32_e32 v147, v193, v193
	v_med3_f32 v146, v146, s3, v1
	v_med3_f32 v147, v147, s3, v1
	s_waitcnt lgkmcnt(7)
	v_max_f32_e32 v140, v140, v140
	s_waitcnt lgkmcnt(6)
	v_max_f32_e32 v143, v143, v143
	v_cvt_pk_fp8_f32 v196, v146, v147 op_sel:[0,0,1]
	v_max_f32_e32 v146, v198, v198
	v_med3_f32 v140, v140, s3, v1
	v_med3_f32 v143, v143, s3, v1
	v_mov_b32_e32 v198, 0
	v_cvt_pk_fp8_f32 v198, v140, v143
	s_waitcnt lgkmcnt(5)
	v_max_f32_e32 v140, v195, v195
	s_waitcnt lgkmcnt(4)
	v_max_f32_e32 v143, v202, v202
	v_med3_f32 v140, v140, s3, v1
	v_med3_f32 v143, v143, s3, v1
	v_max_f32_e32 v147, v199, v199
	v_cvt_pk_fp8_f32 v198, v140, v143 op_sel:[0,0,1]
	s_waitcnt lgkmcnt(3)
	v_max_f32_e32 v140, v203, v203
	s_waitcnt lgkmcnt(2)
	v_max_f32_e32 v143, v204, v204
	v_med3_f32 v146, v146, s3, v1
	v_med3_f32 v147, v147, s3, v1
	v_mov_b32_e32 v197, 0
	v_med3_f32 v140, v140, s3, v1
	v_med3_f32 v143, v143, s3, v1
	v_mov_b32_e32 v199, 0
	v_cvt_pk_fp8_f32 v197, v146, v147
	v_cvt_pk_fp8_f32 v199, v140, v143
	v_max_f32_e32 v146, v200, v200
	v_max_f32_e32 v147, v201, v201
	s_waitcnt lgkmcnt(1)
	v_max_f32_e32 v140, v205, v205
	s_waitcnt lgkmcnt(0)
	v_max_f32_e32 v143, v206, v206
	v_med3_f32 v146, v146, s3, v1
	v_med3_f32 v147, v147, s3, v1
	v_med3_f32 v140, v140, s3, v1
	v_med3_f32 v143, v143, s3, v1
	v_cvt_pk_fp8_f32 v197, v146, v147 op_sel:[0,0,1]
	v_cvt_pk_fp8_f32 v199, v140, v143 op_sel:[0,0,1]
	ds_read2_b32 v[146:147], v165 offset1:32
	ds_read2_b32 v[192:193], v165 offset0:64 offset1:96
	ds_read2_b32 v[202:203], v165 offset0:128 offset1:160
	ds_read2_b32 v[204:205], v165 offset0:192 offset1:224
	ds_read_b32 v140, v166
	ds_read_b32 v143, v167
	ds_read_b32 v195, v168
	ds_read_b32 v206, v169
	ds_read_b32 v207, v170
	ds_read_b32 v208, v171
	ds_read_b32 v209, v172
	ds_read_b32 v210, v173
	s_waitcnt lgkmcnt(11)
	v_max_f32_e32 v146, v146, v146
	v_max_f32_e32 v147, v147, v147
	v_med3_f32 v146, v146, s3, v1
	v_med3_f32 v147, v147, s3, v1
	v_mov_b32_e32 v200, 0
	v_cvt_pk_fp8_f32 v200, v146, v147
	s_waitcnt lgkmcnt(10)
	v_max_f32_e32 v146, v192, v192
	v_max_f32_e32 v147, v193, v193
	v_med3_f32 v146, v146, s3, v1
	v_med3_f32 v147, v147, s3, v1
	s_waitcnt lgkmcnt(7)
	v_max_f32_e32 v140, v140, v140
	s_waitcnt lgkmcnt(6)
	v_max_f32_e32 v143, v143, v143
	v_cvt_pk_fp8_f32 v200, v146, v147 op_sel:[0,0,1]
	v_max_f32_e32 v146, v202, v202
	v_med3_f32 v140, v140, s3, v1
	v_med3_f32 v143, v143, s3, v1
	v_mov_b32_e32 v202, 0
	v_cvt_pk_fp8_f32 v202, v140, v143
	s_waitcnt lgkmcnt(5)
	v_max_f32_e32 v140, v195, v195
	s_waitcnt lgkmcnt(4)
	v_max_f32_e32 v143, v206, v206
	v_med3_f32 v140, v140, s3, v1
	v_med3_f32 v143, v143, s3, v1
	v_max_f32_e32 v147, v203, v203
	v_cvt_pk_fp8_f32 v202, v140, v143 op_sel:[0,0,1]
	s_waitcnt lgkmcnt(3)
	v_max_f32_e32 v140, v207, v207
	s_waitcnt lgkmcnt(2)
	v_max_f32_e32 v143, v208, v208
	v_med3_f32 v146, v146, s3, v1
	v_med3_f32 v147, v147, s3, v1
	v_mov_b32_e32 v201, 0
	v_med3_f32 v140, v140, s3, v1
	v_med3_f32 v143, v143, s3, v1
	v_mov_b32_e32 v203, 0
	v_cvt_pk_fp8_f32 v201, v146, v147
	v_cvt_pk_fp8_f32 v203, v140, v143
	v_max_f32_e32 v146, v204, v204
	v_max_f32_e32 v147, v205, v205
	s_waitcnt lgkmcnt(1)
	v_max_f32_e32 v140, v209, v209
	s_waitcnt lgkmcnt(0)
	v_max_f32_e32 v143, v210, v210
	v_med3_f32 v146, v146, s3, v1
	v_med3_f32 v147, v147, s3, v1
	v_med3_f32 v140, v140, s3, v1
	v_med3_f32 v143, v143, s3, v1
	v_cvt_pk_fp8_f32 v201, v146, v147 op_sel:[0,0,1]
	v_cvt_pk_fp8_f32 v203, v140, v143 op_sel:[0,0,1]
	v_lshl_add_u64 v[144:145], s[6:7], 0, v[130:131]
	v_lshl_add_u64 v[146:147], v[144:145], 0, v[132:133]
	global_store_dwordx4 v[146:147], v[196:199], off nt
	v_lshl_add_u64 v[146:147], v[144:145], 0, v[134:135]
	global_store_dwordx4 v[146:147], v[200:203], off nt
	ds_read2_b32 v[146:147], v174 offset1:32
	ds_read2_b32 v[192:193], v174 offset0:64 offset1:96
	ds_read2_b32 v[198:199], v174 offset0:128 offset1:160
	ds_read2_b32 v[200:201], v174 offset0:192 offset1:224
	ds_read_b32 v140, v175
	ds_read_b32 v143, v176
	ds_read_b32 v195, v177
	ds_read_b32 v202, v178
	ds_read_b32 v203, v179
	ds_read_b32 v204, v180
	ds_read_b32 v205, v181
	ds_read_b32 v206, v182
	s_waitcnt lgkmcnt(11)
; #define GAS __attribute__((address_space(1)))
; __device__ __forceinline__ TItem8 p8_decode(const Args& args, unsigned char* ws, int it) {
;     TItem8 t;
;     if (it >= P8_N) { const int j = it - P8_N; it = (P8_E0 + j / P8_DN1) * (P8_GU1 + P8_DN1) + P8_GU1 + j % P8_DN1; }
;     else if (it >= P8_E0 * (P8_GU1 + P8_DN1)) { const int r = it - P8_E0 * (P8_GU1 + P8_DN1); it = (P8_E0 + r / P8_GU1) * (P8_GU1 + P8_DN1) + r % P8_GU1; }
;     const int e = it / (P8_GU1 + P8_DN1), q = it % (P8_GU1 + P8_DN1);
;     if (q < P8_GU1) { const int kb = q / 128, nb = q % 128, n0 = nb * 32;
;         const int dr = (n0 < DE) ? (256 * (n0 / 128) + (n0 % 128)) : (256 * ((n0 - DE) / 128) + 128 + ((n0 - DE) % 128));
;         t.src = args.in[25] + (size_t)e * D * 2 * DE + (size_t)(kb * 128) * (2 * DE) + n0; t.N = 2 * DE; t.dst = ws + WS_WGU + (size_t)e * 2 * DE * D + (size_t)dr * D + kb * 128; t.Kd = D; }
;     else { const int q2 = q - P8_GU1, kb = q2 / 64, nb = q2 % 64;
;         t.src = args.in[27] + (size_t)e * DE * D + (size_t)(kb * 128) * D + nb * 32; t.N = D; t.dst = ws + WS_WDN + (size_t)e * D * DE + (size_t)(nb * 32) * DE + kb * 128; t.Kd = DE; }
; __device__ __forceinline__ void p8_finish(const TItem8& t, const f32x4 (&v)[16], LAS float* scr, int lane) {
;     ...
;     const int c = lane & 7;
; #pragma unroll
;     for (int j = 0; j < 4; ++j) { const int n = (lane >> 3) + 8 * j; float x[16];
; #pragma unroll
;         for (int i = 0; i < 16; ++i) { const int k = 16 * c + i; x[i] = scr[k * 32 + ((((n >> 2) ^ ((k >> 3) & 7)) << 2) | (n & 3))]; }
;         int w[4];
; #pragma unroll
;         for (int g = 0; g < 4; ++g) { int q = 0; q = __builtin_amdgcn_cvt_pk_fp8_f32(fminf(fmaxf(x[4 * g], -448.f), 448.f), fminf(fmaxf(x[4 * g + 1], -448.f), 448.f), q, false);
;             q = __builtin_amdgcn_cvt_pk_fp8_f32(fminf(fmaxf(x[4 * g + 2], -448.f), 448.f), fminf(fmaxf(x[4 * g + 3], -448.f), 448.f), q, true); w[g] = q; }
;         v4u o; o.x = (unsigned)w[0]; o.y = (unsigned)w[1]; o.z = (unsigned)w[2]; o.w = (unsigned)w[3];
;         __builtin_nontemporal_store(o, (GAS v4u*)(t.dst + (size_t)n * t.Kd + 16 * c)); }
	v_max_f32_e32 v146, v146, v146
	v_max_f32_e32 v147, v147, v147
	v_med3_f32 v146, v146, s3, v1
	v_med3_f32 v147, v147, s3, v1
	v_mov_b32_e32 v196, 0
	v_cvt_pk_fp8_f32 v196, v146, v147
	s_waitcnt lgkmcnt(10)
	v_max_f32_e32 v146, v192, v192
	v_max_f32_e32 v147, v193, v193
	v_med3_f32 v146, v146, s3, v1
	v_med3_f32 v147, v147, s3, v1
	s_waitcnt lgkmcnt(7)
	v_max_f32_e32 v140, v140, v140
	s_waitcnt lgkmcnt(6)
	v_max_f32_e32 v143, v143, v143
	v_cvt_pk_fp8_f32 v196, v146, v147 op_sel:[0,0,1]
	v_max_f32_e32 v146, v198, v198
	v_med3_f32 v140, v140, s3, v1
	v_med3_f32 v143, v143, s3, v1
	v_mov_b32_e32 v198, 0
	v_cvt_pk_fp8_f32 v198, v140, v143
	s_waitcnt lgkmcnt(5)
	v_max_f32_e32 v140, v195, v195
	s_waitcnt lgkmcnt(4)
	v_max_f32_e32 v143, v202, v202
	v_med3_f32 v140, v140, s3, v1
	v_med3_f32 v143, v143, s3, v1
	v_max_f32_e32 v147, v199, v199
	v_cvt_pk_fp8_f32 v198, v140, v143 op_sel:[0,0,1]
	s_waitcnt lgkmcnt(3)
	v_max_f32_e32 v140, v203, v203
	s_waitcnt lgkmcnt(2)
	v_max_f32_e32 v143, v204, v204
	v_med3_f32 v146, v146, s3, v1
	v_med3_f32 v147, v147, s3, v1
	v_mov_b32_e32 v197, 0
	v_med3_f32 v140, v140, s3, v1
	v_med3_f32 v143, v143, s3, v1
	v_mov_b32_e32 v199, 0
	v_cvt_pk_fp8_f32 v197, v146, v147
	v_cvt_pk_fp8_f32 v199, v140, v143
	v_max_f32_e32 v146, v200, v200
	v_max_f32_e32 v147, v201, v201
	s_waitcnt lgkmcnt(1)
	v_max_f32_e32 v140, v205, v205
	s_waitcnt lgkmcnt(0)
	v_max_f32_e32 v143, v206, v206
	v_med3_f32 v146, v146, s3, v1
	v_med3_f32 v147, v147, s3, v1
	v_med3_f32 v140, v140, s3, v1
	v_med3_f32 v143, v143, s3, v1
	v_cvt_pk_fp8_f32 v197, v146, v147 op_sel:[0,0,1]
	v_cvt_pk_fp8_f32 v199, v140, v143 op_sel:[0,0,1]
	ds_read2_b32 v[146:147], v183 offset1:32
	ds_read2_b32 v[192:193], v183 offset0:64 offset1:96
	ds_read2_b32 v[202:203], v183 offset0:128 offset1:160
	ds_read2_b32 v[204:205], v183 offset0:192 offset1:224
	ds_read_b32 v140, v184
	ds_read_b32 v143, v185
	ds_read_b32 v195, v186
	ds_read_b32 v206, v187
	ds_read_b32 v207, v188
	ds_read_b32 v208, v189
	ds_read_b32 v209, v190
	ds_read_b32 v210, v191
	s_waitcnt lgkmcnt(11)
	v_max_f32_e32 v146, v146, v146
	v_max_f32_e32 v147, v147, v147
	v_med3_f32 v146, v146, s3, v1
	v_med3_f32 v147, v147, s3, v1
	v_mov_b32_e32 v200, 0
	v_cvt_pk_fp8_f32 v200, v146, v147
	s_waitcnt lgkmcnt(10)
	v_max_f32_e32 v146, v192, v192
	v_max_f32_e32 v147, v193, v193
	v_med3_f32 v146, v146, s3, v1
	v_med3_f32 v147, v147, s3, v1
	s_waitcnt lgkmcnt(7)
	v_max_f32_e32 v140, v140, v140
	s_waitcnt lgkmcnt(6)
	v_max_f32_e32 v143, v143, v143
	v_cvt_pk_fp8_f32 v200, v146, v147 op_sel:[0,0,1]
	v_max_f32_e32 v146, v202, v202
	v_med3_f32 v140, v140, s3, v1
	v_med3_f32 v143, v143, s3, v1
	v_mov_b32_e32 v202, 0
	v_cvt_pk_fp8_f32 v202, v140, v143
	s_waitcnt lgkmcnt(5)
	v_max_f32_e32 v140, v195, v195
	s_waitcnt lgkmcnt(4)
	v_max_f32_e32 v143, v206, v206
	v_med3_f32 v140, v140, s3, v1
	v_med3_f32 v143, v143, s3, v1
	v_max_f32_e32 v147, v203, v203
	v_cvt_pk_fp8_f32 v202, v140, v143 op_sel:[0,0,1]
	s_waitcnt lgkmcnt(3)
	v_max_f32_e32 v140, v207, v207
	s_waitcnt lgkmcnt(2)
	v_max_f32_e32 v143, v208, v208
	v_med3_f32 v146, v146, s3, v1
	v_med3_f32 v147, v147, s3, v1
	v_mov_b32_e32 v201, 0
	v_med3_f32 v140, v140, s3, v1
	v_med3_f32 v143, v143, s3, v1
	v_mov_b32_e32 v203, 0
	v_cvt_pk_fp8_f32 v201, v146, v147
	v_cvt_pk_fp8_f32 v203, v140, v143
	v_max_f32_e32 v146, v204, v204
	v_max_f32_e32 v147, v205, v205
	s_waitcnt lgkmcnt(1)
	v_max_f32_e32 v140, v209, v209
	s_waitcnt lgkmcnt(0)
	v_max_f32_e32 v143, v210, v210
	v_med3_f32 v146, v146, s3, v1
	v_med3_f32 v147, v147, s3, v1
	v_med3_f32 v140, v140, s3, v1
	v_med3_f32 v143, v143, s3, v1
	v_cvt_pk_fp8_f32 v201, v146, v147 op_sel:[0,0,1]
	v_cvt_pk_fp8_f32 v203, v140, v143 op_sel:[0,0,1]
	v_lshl_add_u64 v[146:147], v[144:145], 0, v[136:137]
	v_lshl_add_u64 v[144:145], v[144:145], 0, v[138:139]
	global_store_dwordx4 v[146:147], v[196:199], off nt
	global_store_dwordx4 v[144:145], v[200:203], off nt
	s_waitcnt lgkmcnt(0)
	s_andn2_b64 vcc, exec, s[10:11]
	s_mov_b64 s[10:11], 0
	s_cbranch_vccnz .LBB0_937
	s_add_i32 s5, s5, 2
	s_lshl_b32 s0, s5, 10
	s_add_i32 s0, s0, s2
	s_cmpk_lt_i32 s0, 0x6acd
	s_cselect_b64 s[10:11], -1, 0
	s_cmpk_gt_i32 s0, 0x6acc
	s_cbranch_scc1 .LBB0_959
	s_mul_hi_i32 s6, s0, 0x2aaaaaab
	s_lshr_b32 s7, s6, 31
	s_ashr_i32 s6, s6, 9
	s_add_i32 s6, s6, s7
	s_mul_i32 s7, s6, 0xc00
	s_sub_i32 s20, s0, s7
	s_cmpk_gt_i32 s20, 0x7ff
	s_mov_b64 s[34:35], -1
	s_cbranch_scc0 .LBB0_952
	s_ashr_i32 s7, s6, 31
	s_lshl_b64 s[16:17], s[6:7], 22
	s_lshl_b64 s[12:13], s[6:7], 24
	s_add_u32 s7, s42, s12
	s_addc_u32 s14, s43, s13
	s_lshl_b32 s0, s20, 1
	s_and_b32 s0, s0, 0x7fffff80
	s_addk_i32 s0, 0xf000
	s_lshl_b64 s[12:13], s[0:1], 13
	s_add_u32 s7, s7, s12
	s_addc_u32 s15, s14, s13
	s_lshl_b32 s12, s20, 5
	s_and_b32 s12, s12, 0x7e0
	s_lshl_b32 s14, s12, 2
	s_add_u32 s14, s7, s14
	s_addc_u32 s15, s15, 0
	v_readlane_b32 s7, v254, 46
	s_add_u32 s18, s7, s16
	v_readlane_b32 s7, v254, 47
	s_mov_b32 s13, s1
	s_addc_u32 s19, s7, s17
	s_mov_b64 s[34:35], 0
	s_mov_b64 s[16:17], s[0:1]

; #define GAS __attribute__((address_space(1)))
; #define LAS __attribute__((address_space(3)))
; __device__ __forceinline__ void p8_issue(const TItem8& t, f32x4 (&v)[16], int lane) {
;     const GAS f32x4* src = (const GAS f32x4*)((const GAS float*)t.src + (size_t)(lane >> 3) * t.N + 4 * (lane & 7));
; #pragma unroll
;     for (int i = 0; i < 16; ++i) v[i] = __builtin_nontemporal_load(src + (size_t)(2 * i) * t.N);
; }
; __device__ __forceinline__ void p8_finish(const TItem8& t, const f32x4 (&v)[16], LAS float* scr, int lane) {
; #pragma unroll
;     for (int i = 0; i < 16; ++i) *(LAS f32x4*)(scr + (8 * i + (lane >> 3)) * 32 + (((lane & 7) ^ (i & 7)) << 2)) = v[i] * W8_SCALE;
.LBB0_958:
	s_lshl_b64 s[6:7], s[12:13], 11
	s_add_u32 s0, s18, s6
	v_mul_u32_u24_e32 v2, s34, v225
	s_addc_u32 s7, s19, s7
	v_lshlrev_b32_e32 v140, 2, v2
	s_add_u32 s6, s0, s16
	v_lshl_add_u64 v[2:3], s[14:15], 0, v[140:141]
	v_mov_b32_e32 v143, v141
	s_addc_u32 s7, s7, s17
	v_lshl_add_u64 v[2:3], v[2:3], 0, v[142:143]
	s_lshl_b32 s0, s34, 5
	v_lshl_add_u64 v[10:11], v[2:3], 0, s[0:1]
	global_load_dwordx4 v[2:5], v[2:3], off nt
	s_nop 0
	global_load_dwordx4 v[6:9], v[10:11], off nt
	v_lshl_add_u64 v[10:11], v[10:11], 0, s[0:1]
	v_lshl_add_u64 v[18:19], v[10:11], 0, s[0:1]
	global_load_dwordx4 v[10:13], v[10:11], off nt
	s_nop 0
	global_load_dwordx4 v[14:17], v[18:19], off nt
	v_lshl_add_u64 v[18:19], v[18:19], 0, s[0:1]
	v_lshl_add_u64 v[26:27], v[18:19], 0, s[0:1]
	global_load_dwordx4 v[18:21], v[18:19], off nt
	s_nop 0
	global_load_dwordx4 v[22:25], v[26:27], off nt
	v_lshl_add_u64 v[26:27], v[26:27], 0, s[0:1]
	v_lshl_add_u64 v[34:35], v[26:27], 0, s[0:1]
	v_lshl_add_u64 v[38:39], v[34:35], 0, s[0:1]
	v_lshl_add_u64 v[42:43], v[38:39], 0, s[0:1]
	v_lshl_add_u64 v[46:47], v[42:43], 0, s[0:1]
	v_lshl_add_u64 v[50:51], v[46:47], 0, s[0:1]
	v_lshl_add_u64 v[54:55], v[50:51], 0, s[0:1]
	v_lshl_add_u64 v[58:59], v[54:55], 0, s[0:1]
	v_lshl_add_u64 v[62:63], v[58:59], 0, s[0:1]
	global_load_dwordx4 v[26:29], v[26:27], off nt
	s_nop 0
	global_load_dwordx4 v[30:33], v[34:35], off nt
	s_nop 0
	global_load_dwordx4 v[34:37], v[38:39], off nt
	s_nop 0
	global_load_dwordx4 v[38:41], v[42:43], off nt
	s_nop 0
	global_load_dwordx4 v[42:45], v[46:47], off nt
	s_nop 0
	global_load_dwordx4 v[46:49], v[50:51], off nt
	s_nop 0
	global_load_dwordx4 v[50:53], v[54:55], off nt
	s_nop 0
	global_load_dwordx4 v[54:57], v[58:59], off nt
	s_nop 0
	global_load_dwordx4 v[58:61], v[62:63], off nt
	v_lshl_add_u64 v[62:63], v[62:63], 0, s[0:1]
	global_load_dwordx4 v[62:65], v[62:63], off nt
	s_waitcnt vmcnt(35)
	v_pk_mul_f32 v[146:147], v[68:69], s[4:5] op_sel_hi:[1,0]
	v_pk_mul_f32 v[144:145], v[66:67], s[4:5] op_sel_hi:[1,0]
	ds_write_b128 v148, v[144:147]
	s_waitcnt vmcnt(34)
	v_pk_mul_f32 v[146:147], v[72:73], s[4:5] op_sel_hi:[1,0]
	v_pk_mul_f32 v[144:145], v[70:71], s[4:5] op_sel_hi:[1,0]
	ds_write_b128 v149, v[144:147] offset:1024
	s_waitcnt vmcnt(33)
	v_pk_mul_f32 v[146:147], v[76:77], s[4:5] op_sel_hi:[1,0]
	v_pk_mul_f32 v[144:145], v[74:75], s[4:5] op_sel_hi:[1,0]
	ds_write_b128 v150, v[144:147] offset:2048
	s_waitcnt vmcnt(32)
	v_pk_mul_f32 v[146:147], v[80:81], s[4:5] op_sel_hi:[1,0]
	v_pk_mul_f32 v[144:145], v[78:79], s[4:5] op_sel_hi:[1,0]
	ds_write_b128 v151, v[144:147] offset:3072
	s_waitcnt vmcnt(31)
	v_pk_mul_f32 v[146:147], v[84:85], s[4:5] op_sel_hi:[1,0]
	v_pk_mul_f32 v[144:145], v[82:83], s[4:5] op_sel_hi:[1,0]
	ds_write_b128 v152, v[144:147] offset:4096
	s_waitcnt vmcnt(30)
	v_pk_mul_f32 v[146:147], v[88:89], s[4:5] op_sel_hi:[1,0]
	v_pk_mul_f32 v[144:145], v[86:87], s[4:5] op_sel_hi:[1,0]
	ds_write_b128 v153, v[144:147] offset:5120
	s_waitcnt vmcnt(29)
	v_pk_mul_f32 v[146:147], v[92:93], s[4:5] op_sel_hi:[1,0]
	v_pk_mul_f32 v[144:145], v[90:91], s[4:5] op_sel_hi:[1,0]
	ds_write_b128 v154, v[144:147] offset:6144
	s_waitcnt vmcnt(28)
	v_pk_mul_f32 v[146:147], v[96:97], s[4:5] op_sel_hi:[1,0]
	v_pk_mul_f32 v[144:145], v[94:95], s[4:5] op_sel_hi:[1,0]
	ds_write_b128 v155, v[144:147] offset:7168
	s_waitcnt vmcnt(27)
	v_pk_mul_f32 v[146:147], v[100:101], s[4:5] op_sel_hi:[1,0]
	v_pk_mul_f32 v[144:145], v[98:99], s[4:5] op_sel_hi:[1,0]
	ds_write_b128 v148, v[144:147] offset:8192
	s_waitcnt vmcnt(26)
	v_pk_mul_f32 v[146:147], v[104:105], s[4:5] op_sel_hi:[1,0]
	v_pk_mul_f32 v[144:145], v[102:103], s[4:5] op_sel_hi:[1,0]
	ds_write_b128 v149, v[144:147] offset:9216
	s_waitcnt vmcnt(25)
	v_pk_mul_f32 v[146:147], v[108:109], s[4:5] op_sel_hi:[1,0]
	v_pk_mul_f32 v[144:145], v[106:107], s[4:5] op_sel_hi:[1,0]
	ds_write_b128 v150, v[144:147] offset:10240
	s_waitcnt vmcnt(24)
	v_pk_mul_f32 v[146:147], v[112:113], s[4:5] op_sel_hi:[1,0]
	v_pk_mul_f32 v[144:145], v[110:111], s[4:5] op_sel_hi:[1,0]
	ds_write_b128 v151, v[144:147] offset:11264
	s_waitcnt vmcnt(23)
	v_pk_mul_f32 v[146:147], v[116:117], s[4:5] op_sel_hi:[1,0]
	v_pk_mul_f32 v[144:145], v[114:115], s[4:5] op_sel_hi:[1,0]
	ds_write_b128 v152, v[144:147] offset:12288
	s_waitcnt vmcnt(22)
	v_pk_mul_f32 v[146:147], v[120:121], s[4:5] op_sel_hi:[1,0]
	v_pk_mul_f32 v[144:145], v[118:119], s[4:5] op_sel_hi:[1,0]
	ds_write_b128 v153, v[144:147] offset:13312
	s_waitcnt vmcnt(21)
	v_pk_mul_f32 v[146:147], v[124:125], s[4:5] op_sel_hi:[1,0]
	v_pk_mul_f32 v[144:145], v[122:123], s[4:5] op_sel_hi:[1,0]
	ds_write_b128 v154, v[144:147] offset:14336
	s_waitcnt vmcnt(20)
	v_pk_mul_f32 v[146:147], v[128:129], s[4:5] op_sel_hi:[1,0]
	v_pk_mul_f32 v[144:145], v[126:127], s[4:5] op_sel_hi:[1,0]
	ds_write_b128 v155, v[144:147] offset:15360
	s_branch .Lcv2_3_948
; #define GAS __attribute__((address_space(1)))
; #define LAS __attribute__((address_space(3)))
; __device__ __forceinline__ void p8_finish(const TItem8& t, const f32x4 (&v)[16], LAS float* scr, int lane) {
;     ...
;     for (int i = 0; i < 16; ++i) *(LAS f32x4*)(scr + (8 * i + (lane >> 3)) * 32 + (((lane & 7) ^ (i & 7)) << 2)) = v[i] * W8_SCALE;
;     ...
;     const int c = lane & 7;
; #pragma unroll
;     for (int j = 0; j < 4; ++j) { const int n = (lane >> 3) + 8 * j; float x[16];
; #pragma unroll
;         for (int i = 0; i < 16; ++i) { const int k = 16 * c + i; x[i] = scr[k * 32 + ((((n >> 2) ^ ((k >> 3) & 7)) << 2) | (n & 3))]; }
;         int w[4];
; #pragma unroll
;         for (int g = 0; g < 4; ++g) { int q = 0; q = __builtin_amdgcn_cvt_pk_fp8_f32(fminf(fmaxf(x[4 * g], -448.f), 448.f), fminf(fmaxf(x[4 * g + 1], -448.f), 448.f), q, false);
;             q = __builtin_amdgcn_cvt_pk_fp8_f32(fminf(fmaxf(x[4 * g + 2], -448.f), 448.f), fminf(fmaxf(x[4 * g + 3], -448.f), 448.f), q, true); w[g] = q; }
;         v4u o; o.x = (unsigned)w[0]; o.y = (unsigned)w[1]; o.z = (unsigned)w[2]; o.w = (unsigned)w[3];
;         __builtin_nontemporal_store(o, (GAS v4u*)(t.dst + (size_t)n * t.Kd + 16 * c)); }
.LBB0_959:
	s_waitcnt vmcnt(19)
	v_pk_mul_f32 v[146:147], v[68:69], s[4:5] op_sel_hi:[1,0]
	v_pk_mul_f32 v[144:145], v[66:67], s[4:5] op_sel_hi:[1,0]
	ds_write_b128 v148, v[144:147]
	s_waitcnt vmcnt(18)
	v_pk_mul_f32 v[146:147], v[72:73], s[4:5] op_sel_hi:[1,0]
	v_pk_mul_f32 v[144:145], v[70:71], s[4:5] op_sel_hi:[1,0]
	ds_write_b128 v149, v[144:147] offset:1024
	s_waitcnt vmcnt(17)
	v_pk_mul_f32 v[146:147], v[76:77], s[4:5] op_sel_hi:[1,0]
	v_pk_mul_f32 v[144:145], v[74:75], s[4:5] op_sel_hi:[1,0]
	ds_write_b128 v150, v[144:147] offset:2048
	s_waitcnt vmcnt(16)
	v_pk_mul_f32 v[146:147], v[80:81], s[4:5] op_sel_hi:[1,0]
	v_pk_mul_f32 v[144:145], v[78:79], s[4:5] op_sel_hi:[1,0]
	ds_write_b128 v151, v[144:147] offset:3072
	s_waitcnt vmcnt(15)
	v_pk_mul_f32 v[146:147], v[84:85], s[4:5] op_sel_hi:[1,0]
	v_pk_mul_f32 v[144:145], v[82:83], s[4:5] op_sel_hi:[1,0]
	ds_write_b128 v152, v[144:147] offset:4096
	s_waitcnt vmcnt(14)
	v_pk_mul_f32 v[146:147], v[88:89], s[4:5] op_sel_hi:[1,0]
	v_pk_mul_f32 v[144:145], v[86:87], s[4:5] op_sel_hi:[1,0]
	ds_write_b128 v153, v[144:147] offset:5120
	s_waitcnt vmcnt(13)
	v_pk_mul_f32 v[146:147], v[92:93], s[4:5] op_sel_hi:[1,0]
	v_pk_mul_f32 v[144:145], v[90:91], s[4:5] op_sel_hi:[1,0]
	ds_write_b128 v154, v[144:147] offset:6144
	s_waitcnt vmcnt(12)
	v_pk_mul_f32 v[146:147], v[96:97], s[4:5] op_sel_hi:[1,0]
	v_pk_mul_f32 v[144:145], v[94:95], s[4:5] op_sel_hi:[1,0]
	ds_write_b128 v155, v[144:147] offset:7168
	s_waitcnt vmcnt(11)
	v_pk_mul_f32 v[146:147], v[100:101], s[4:5] op_sel_hi:[1,0]
	v_pk_mul_f32 v[144:145], v[98:99], s[4:5] op_sel_hi:[1,0]
	ds_write_b128 v148, v[144:147] offset:8192
	s_waitcnt vmcnt(10)
	v_pk_mul_f32 v[146:147], v[104:105], s[4:5] op_sel_hi:[1,0]
	v_pk_mul_f32 v[144:145], v[102:103], s[4:5] op_sel_hi:[1,0]
	ds_write_b128 v149, v[144:147] offset:9216
	s_waitcnt vmcnt(9)
	v_pk_mul_f32 v[146:147], v[108:109], s[4:5] op_sel_hi:[1,0]
	v_pk_mul_f32 v[144:145], v[106:107], s[4:5] op_sel_hi:[1,0]
	ds_write_b128 v150, v[144:147] offset:10240
	s_waitcnt vmcnt(8)
	v_pk_mul_f32 v[146:147], v[112:113], s[4:5] op_sel_hi:[1,0]
	v_pk_mul_f32 v[144:145], v[110:111], s[4:5] op_sel_hi:[1,0]
	ds_write_b128 v151, v[144:147] offset:11264
	s_waitcnt vmcnt(7)
	v_pk_mul_f32 v[146:147], v[116:117], s[4:5] op_sel_hi:[1,0]
	v_pk_mul_f32 v[144:145], v[114:115], s[4:5] op_sel_hi:[1,0]
	ds_write_b128 v152, v[144:147] offset:12288
	s_waitcnt vmcnt(6)
	v_pk_mul_f32 v[146:147], v[120:121], s[4:5] op_sel_hi:[1,0]
	v_pk_mul_f32 v[144:145], v[118:119], s[4:5] op_sel_hi:[1,0]
	ds_write_b128 v153, v[144:147] offset:13312
	s_waitcnt vmcnt(5)
	v_pk_mul_f32 v[146:147], v[124:125], s[4:5] op_sel_hi:[1,0]
	v_pk_mul_f32 v[144:145], v[122:123], s[4:5] op_sel_hi:[1,0]
	ds_write_b128 v154, v[144:147] offset:14336
	s_waitcnt vmcnt(4)
	v_pk_mul_f32 v[146:147], v[128:129], s[4:5] op_sel_hi:[1,0]
	v_pk_mul_f32 v[144:145], v[126:127], s[4:5] op_sel_hi:[1,0]
	ds_write_b128 v155, v[144:147] offset:15360
.Lcv2_3_948:
	s_waitcnt lgkmcnt(0)
	ds_read2_b32 v[146:147], v156 offset1:32
	ds_read2_b32 v[192:193], v156 offset0:64 offset1:96
	ds_read2_b32 v[198:199], v156 offset0:128 offset1:160
	ds_read2_b32 v[200:201], v156 offset0:192 offset1:224
	ds_read_b32 v140, v157
	ds_read_b32 v143, v158
	ds_read_b32 v195, v159
	ds_read_b32 v202, v160
	ds_read_b32 v203, v161
	ds_read_b32 v204, v162
	ds_read_b32 v205, v163
	ds_read_b32 v206, v164
	s_waitcnt lgkmcnt(11)
	v_max_f32_e32 v146, v146, v146
	v_max_f32_e32 v147, v147, v147
	v_med3_f32 v146, v146, s3, v1
	v_med3_f32 v147, v147, s3, v1
	v_mov_b32_e32 v196, v141
	v_cvt_pk_fp8_f32 v196, v146, v147
	s_waitcnt lgkmcnt(10)
	v_max_f32_e32 v146, v192, v192
	v_max_f32_e32 v147, v193, v193
	v_med3_f32 v146, v146, s3, v1
	v_med3_f32 v147, v147, s3, v1
	s_waitcnt lgkmcnt(7)
	v_max_f32_e32 v140, v140, v140
	s_waitcnt lgkmcnt(6)
	v_max_f32_e32 v143, v143, v143
	v_cvt_pk_fp8_f32 v196, v146, v147 op_sel:[0,0,1]
	v_max_f32_e32 v146, v198, v198
	v_med3_f32 v140, v140, s3, v1
	v_med3_f32 v143, v143, s3, v1
	v_mov_b32_e32 v198, v141
	v_cvt_pk_fp8_f32 v198, v140, v143
	s_waitcnt lgkmcnt(5)
	v_max_f32_e32 v140, v195, v195
	s_waitcnt lgkmcnt(4)
	v_max_f32_e32 v143, v202, v202
	v_med3_f32 v140, v140, s3, v1
	v_med3_f32 v143, v143, s3, v1
	v_max_f32_e32 v147, v199, v199
	v_cvt_pk_fp8_f32 v198, v140, v143 op_sel:[0,0,1]
	s_waitcnt lgkmcnt(3)
	v_max_f32_e32 v140, v203, v203
	s_waitcnt lgkmcnt(2)
	v_max_f32_e32 v143, v204, v204
	v_med3_f32 v146, v146, s3, v1
	v_med3_f32 v147, v147, s3, v1
	v_mov_b32_e32 v197, v141
	v_med3_f32 v140, v140, s3, v1
	v_med3_f32 v143, v143, s3, v1
	v_mov_b32_e32 v199, v141
	v_cvt_pk_fp8_f32 v197, v146, v147
	v_cvt_pk_fp8_f32 v199, v140, v143
	v_max_f32_e32 v146, v200, v200
	v_max_f32_e32 v147, v201, v201
	s_waitcnt lgkmcnt(1)
	v_max_f32_e32 v140, v205, v205
	s_waitcnt lgkmcnt(0)
	v_max_f32_e32 v143, v206, v206
	v_med3_f32 v146, v146, s3, v1
	v_med3_f32 v147, v147, s3, v1
	v_med3_f32 v140, v140, s3, v1
	v_med3_f32 v143, v143, s3, v1
	v_cvt_pk_fp8_f32 v197, v146, v147 op_sel:[0,0,1]
	v_cvt_pk_fp8_f32 v199, v140, v143 op_sel:[0,0,1]
	ds_read2_b32 v[146:147], v165 offset1:32
	ds_read2_b32 v[192:193], v165 offset0:64 offset1:96
	ds_read2_b32 v[202:203], v165 offset0:128 offset1:160
	ds_read2_b32 v[204:205], v165 offset0:192 offset1:224
	ds_read_b32 v140, v166
	ds_read_b32 v143, v167
	ds_read_b32 v195, v168
	ds_read_b32 v206, v169
	ds_read_b32 v207, v170
	ds_read_b32 v208, v171
	ds_read_b32 v209, v172
	ds_read_b32 v210, v173
	s_waitcnt lgkmcnt(11)
	v_max_f32_e32 v146, v146, v146
	v_max_f32_e32 v147, v147, v147
	v_med3_f32 v146, v146, s3, v1
	v_med3_f32 v147, v147, s3, v1
	v_mov_b32_e32 v200, v141
	v_cvt_pk_fp8_f32 v200, v146, v147
	s_waitcnt lgkmcnt(10)
; #define GAS __attribute__((address_space(1)))
; __device__ __forceinline__ void p8_finish(const TItem8& t, const f32x4 (&v)[16], LAS float* scr, int lane) {
;     ...
;     const int c = lane & 7;
; #pragma unroll
;     for (int j = 0; j < 4; ++j) { const int n = (lane >> 3) + 8 * j; float x[16];
; #pragma unroll
;         for (int i = 0; i < 16; ++i) { const int k = 16 * c + i; x[i] = scr[k * 32 + ((((n >> 2) ^ ((k >> 3) & 7)) << 2) | (n & 3))]; }
;         int w[4];
; #pragma unroll
;         for (int g = 0; g < 4; ++g) { int q = 0; q = __builtin_amdgcn_cvt_pk_fp8_f32(fminf(fmaxf(x[4 * g], -448.f), 448.f), fminf(fmaxf(x[4 * g + 1], -448.f), 448.f), q, false);
;             q = __builtin_amdgcn_cvt_pk_fp8_f32(fminf(fmaxf(x[4 * g + 2], -448.f), 448.f), fminf(fmaxf(x[4 * g + 3], -448.f), 448.f), q, true); w[g] = q; }
;         v4u o; o.x = (unsigned)w[0]; o.y = (unsigned)w[1]; o.z = (unsigned)w[2]; o.w = (unsigned)w[3];
;         __builtin_nontemporal_store(o, (GAS v4u*)(t.dst + (size_t)n * t.Kd + 16 * c)); }
	v_max_f32_e32 v146, v192, v192
	v_max_f32_e32 v147, v193, v193
	v_med3_f32 v146, v146, s3, v1
	v_med3_f32 v147, v147, s3, v1
	s_waitcnt lgkmcnt(7)
	v_max_f32_e32 v140, v140, v140
	s_waitcnt lgkmcnt(6)
	v_max_f32_e32 v143, v143, v143
	v_cvt_pk_fp8_f32 v200, v146, v147 op_sel:[0,0,1]
	v_max_f32_e32 v146, v202, v202
	v_med3_f32 v140, v140, s3, v1
	v_med3_f32 v143, v143, s3, v1
	v_mov_b32_e32 v202, v141
	v_cvt_pk_fp8_f32 v202, v140, v143
	s_waitcnt lgkmcnt(5)
	v_max_f32_e32 v140, v195, v195
	s_waitcnt lgkmcnt(4)
	v_max_f32_e32 v143, v206, v206
	v_med3_f32 v140, v140, s3, v1
	v_med3_f32 v143, v143, s3, v1
	v_max_f32_e32 v147, v203, v203
	v_cvt_pk_fp8_f32 v202, v140, v143 op_sel:[0,0,1]
	s_waitcnt lgkmcnt(3)
	v_max_f32_e32 v140, v207, v207
	s_waitcnt lgkmcnt(2)
	v_max_f32_e32 v143, v208, v208
	v_med3_f32 v146, v146, s3, v1
	v_med3_f32 v147, v147, s3, v1
	v_mov_b32_e32 v201, v141
	v_med3_f32 v140, v140, s3, v1
	v_med3_f32 v143, v143, s3, v1
	v_mov_b32_e32 v203, v141
	v_cvt_pk_fp8_f32 v201, v146, v147
	v_cvt_pk_fp8_f32 v203, v140, v143
	v_max_f32_e32 v146, v204, v204
	v_max_f32_e32 v147, v205, v205
	s_waitcnt lgkmcnt(1)
	v_max_f32_e32 v140, v209, v209
	s_waitcnt lgkmcnt(0)
	v_max_f32_e32 v143, v210, v210
	v_med3_f32 v146, v146, s3, v1
	v_med3_f32 v147, v147, s3, v1
	v_med3_f32 v140, v140, s3, v1
	v_med3_f32 v143, v143, s3, v1
	v_cvt_pk_fp8_f32 v201, v146, v147 op_sel:[0,0,1]
	v_cvt_pk_fp8_f32 v203, v140, v143 op_sel:[0,0,1]
	v_lshl_add_u64 v[144:145], s[8:9], 0, v[130:131]
	v_lshl_add_u64 v[146:147], v[144:145], 0, v[132:133]
	global_store_dwordx4 v[146:147], v[196:199], off nt
	v_lshl_add_u64 v[146:147], v[144:145], 0, v[134:135]
	global_store_dwordx4 v[146:147], v[200:203], off nt
	ds_read2_b32 v[146:147], v174 offset1:32
	ds_read2_b32 v[192:193], v174 offset0:64 offset1:96
	ds_read2_b32 v[198:199], v174 offset0:128 offset1:160
	ds_read2_b32 v[200:201], v174 offset0:192 offset1:224
	ds_read_b32 v140, v175
	ds_read_b32 v143, v176
	ds_read_b32 v195, v177
	ds_read_b32 v202, v178
	ds_read_b32 v203, v179
	ds_read_b32 v204, v180
	ds_read_b32 v205, v181
	ds_read_b32 v206, v182
	s_waitcnt lgkmcnt(11)
	v_max_f32_e32 v146, v146, v146
	v_max_f32_e32 v147, v147, v147
	v_med3_f32 v146, v146, s3, v1
	v_med3_f32 v147, v147, s3, v1
	v_mov_b32_e32 v196, v141
	v_cvt_pk_fp8_f32 v196, v146, v147
	s_waitcnt lgkmcnt(10)
	v_max_f32_e32 v146, v192, v192
	v_max_f32_e32 v147, v193, v193
	v_med3_f32 v146, v146, s3, v1
	v_med3_f32 v147, v147, s3, v1
	s_waitcnt lgkmcnt(7)
	v_max_f32_e32 v140, v140, v140
	s_waitcnt lgkmcnt(6)
	v_max_f32_e32 v143, v143, v143
	v_cvt_pk_fp8_f32 v196, v146, v147 op_sel:[0,0,1]
	v_max_f32_e32 v146, v198, v198
	v_med3_f32 v140, v140, s3, v1
	v_med3_f32 v143, v143, s3, v1
	v_mov_b32_e32 v198, v141
	v_cvt_pk_fp8_f32 v198, v140, v143
	s_waitcnt lgkmcnt(5)
	v_max_f32_e32 v140, v195, v195
	s_waitcnt lgkmcnt(4)
	v_max_f32_e32 v143, v202, v202
	v_med3_f32 v140, v140, s3, v1
	v_med3_f32 v143, v143, s3, v1
	v_max_f32_e32 v147, v199, v199
	v_cvt_pk_fp8_f32 v198, v140, v143 op_sel:[0,0,1]
	s_waitcnt lgkmcnt(3)
	v_max_f32_e32 v140, v203, v203
	s_waitcnt lgkmcnt(2)
	v_max_f32_e32 v143, v204, v204
	v_med3_f32 v146, v146, s3, v1
	v_med3_f32 v147, v147, s3, v1
	v_mov_b32_e32 v197, v141
	v_med3_f32 v140, v140, s3, v1
	v_med3_f32 v143, v143, s3, v1
	v_mov_b32_e32 v199, v141
	v_cvt_pk_fp8_f32 v197, v146, v147
	v_cvt_pk_fp8_f32 v199, v140, v143
	v_max_f32_e32 v146, v200, v200
	v_max_f32_e32 v147, v201, v201
	s_waitcnt lgkmcnt(1)
	v_max_f32_e32 v140, v205, v205
	s_waitcnt lgkmcnt(0)
	v_max_f32_e32 v143, v206, v206
	v_med3_f32 v146, v146, s3, v1
	v_med3_f32 v147, v147, s3, v1
	v_med3_f32 v140, v140, s3, v1
	v_med3_f32 v143, v143, s3, v1
	v_cvt_pk_fp8_f32 v197, v146, v147 op_sel:[0,0,1]
	v_cvt_pk_fp8_f32 v199, v140, v143 op_sel:[0,0,1]
	ds_read2_b32 v[146:147], v183 offset1:32
	ds_read2_b32 v[192:193], v183 offset0:64 offset1:96
	ds_read2_b32 v[202:203], v183 offset0:128 offset1:160
	ds_read2_b32 v[204:205], v183 offset0:192 offset1:224
	ds_read_b32 v140, v184
	ds_read_b32 v143, v185
	ds_read_b32 v195, v186
	ds_read_b32 v206, v187
	ds_read_b32 v207, v188
	ds_read_b32 v208, v189
	ds_read_b32 v209, v190
	ds_read_b32 v210, v191
	s_waitcnt lgkmcnt(11)
	v_max_f32_e32 v146, v146, v146
	v_max_f32_e32 v147, v147, v147
	v_med3_f32 v146, v146, s3, v1
	v_med3_f32 v147, v147, s3, v1
	v_mov_b32_e32 v200, v141
	v_cvt_pk_fp8_f32 v200, v146, v147
	s_waitcnt lgkmcnt(10)
	v_max_f32_e32 v146, v192, v192
	v_max_f32_e32 v147, v193, v193
	v_med3_f32 v146, v146, s3, v1
	v_med3_f32 v147, v147, s3, v1
	s_waitcnt lgkmcnt(7)
	v_max_f32_e32 v140, v140, v140
	s_waitcnt lgkmcnt(6)
	v_max_f32_e32 v143, v143, v143
	v_cvt_pk_fp8_f32 v200, v146, v147 op_sel:[0,0,1]
	v_max_f32_e32 v146, v202, v202
	v_med3_f32 v140, v140, s3, v1
	v_med3_f32 v143, v143, s3, v1
	v_mov_b32_e32 v202, v141
	v_cvt_pk_fp8_f32 v202, v140, v143
	s_waitcnt lgkmcnt(5)
	v_max_f32_e32 v140, v195, v195
	s_waitcnt lgkmcnt(4)
	v_max_f32_e32 v143, v206, v206
	v_med3_f32 v140, v140, s3, v1
	v_med3_f32 v143, v143, s3, v1
	v_max_f32_e32 v147, v203, v203
	v_cvt_pk_fp8_f32 v202, v140, v143 op_sel:[0,0,1]
	s_waitcnt lgkmcnt(3)
	v_max_f32_e32 v140, v207, v207
	s_waitcnt lgkmcnt(2)
	v_max_f32_e32 v143, v208, v208
	v_med3_f32 v146, v146, s3, v1
	v_med3_f32 v147, v147, s3, v1
	v_mov_b32_e32 v201, v141
	v_med3_f32 v140, v140, s3, v1
	v_med3_f32 v143, v143, s3, v1
	v_mov_b32_e32 v203, v141
	v_cvt_pk_fp8_f32 v201, v146, v147
	v_cvt_pk_fp8_f32 v203, v140, v143
	v_max_f32_e32 v146, v204, v204
	v_max_f32_e32 v147, v205, v205
	s_waitcnt lgkmcnt(1)
	v_max_f32_e32 v140, v209, v209
	s_waitcnt lgkmcnt(0)
	v_max_f32_e32 v143, v210, v210
	v_med3_f32 v146, v146, s3, v1
	v_med3_f32 v147, v147, s3, v1
	v_med3_f32 v140, v140, s3, v1
	v_med3_f32 v143, v143, s3, v1
	v_cvt_pk_fp8_f32 v201, v146, v147 op_sel:[0,0,1]
	v_cvt_pk_fp8_f32 v203, v140, v143 op_sel:[0,0,1]
	v_lshl_add_u64 v[146:147], v[144:145], 0, v[136:137]
	v_lshl_add_u64 v[144:145], v[144:145], 0, v[138:139]
	global_store_dwordx4 v[146:147], v[196:199], off nt
	global_store_dwordx4 v[144:145], v[200:203], off nt
	s_waitcnt lgkmcnt(0)
	s_xor_b64 s[10:11], s[10:11], -1
	s_and_b64 vcc, exec, s[10:11]
	s_cbranch_vccz .LBB0_938

; #define GAS __attribute__((address_space(1)))
; #define LAS __attribute__((address_space(3)))
; __device__ __forceinline__ void p8_issue(const TItem8& t, f32x4 (&v)[16], int lane) {
;     const GAS f32x4* src = (const GAS f32x4*)((const GAS float*)t.src + (size_t)(lane >> 3) * t.N + 4 * (lane & 7));
; #pragma unroll
;     for (int i = 0; i < 16; ++i) v[i] = __builtin_nontemporal_load(src + (size_t)(2 * i) * t.N);
; }
; __device__ __forceinline__ void p8_finish(const TItem8& t, const f32x4 (&v)[16], LAS float* scr, int lane) {
; #pragma unroll
;     for (int i = 0; i < 16; ++i) *(LAS f32x4*)(scr + (8 * i + (lane >> 3)) * 32 + (((lane & 7) ^ (i & 7)) << 2)) = v[i] * W8_SCALE;
.LBB0_1427:
	s_lshl_b64 s[8:9], s[12:13], 11
	s_add_u32 s0, s18, s8
	v_mul_u32_u24_e32 v66, s22, v225
	s_addc_u32 s9, s19, s9
	v_lshlrev_b32_e32 v140, 2, v66
	s_add_u32 s8, s0, s16
	v_lshl_add_u64 v[66:67], s[14:15], 0, v[140:141]
	v_mov_b32_e32 v143, v141
	s_addc_u32 s9, s9, s17
	v_lshl_add_u64 v[66:67], v[66:67], 0, v[142:143]
	s_lshl_b32 s0, s22, 5
	v_lshl_add_u64 v[74:75], v[66:67], 0, s[0:1]
	global_load_dwordx4 v[66:69], v[66:67], off nt
	s_nop 0
	global_load_dwordx4 v[70:73], v[74:75], off nt
	v_lshl_add_u64 v[74:75], v[74:75], 0, s[0:1]
	v_lshl_add_u64 v[82:83], v[74:75], 0, s[0:1]
	global_load_dwordx4 v[74:77], v[74:75], off nt
	s_nop 0
	global_load_dwordx4 v[78:81], v[82:83], off nt
	v_lshl_add_u64 v[82:83], v[82:83], 0, s[0:1]
	v_lshl_add_u64 v[90:91], v[82:83], 0, s[0:1]
	global_load_dwordx4 v[82:85], v[82:83], off nt
	s_nop 0
	global_load_dwordx4 v[86:89], v[90:91], off nt
	v_lshl_add_u64 v[90:91], v[90:91], 0, s[0:1]
	v_lshl_add_u64 v[98:99], v[90:91], 0, s[0:1]
	v_lshl_add_u64 v[102:103], v[98:99], 0, s[0:1]
	v_lshl_add_u64 v[106:107], v[102:103], 0, s[0:1]
	v_lshl_add_u64 v[110:111], v[106:107], 0, s[0:1]
	v_lshl_add_u64 v[114:115], v[110:111], 0, s[0:1]
	v_lshl_add_u64 v[118:119], v[114:115], 0, s[0:1]
	v_lshl_add_u64 v[122:123], v[118:119], 0, s[0:1]
	v_lshl_add_u64 v[126:127], v[122:123], 0, s[0:1]
	global_load_dwordx4 v[90:93], v[90:91], off nt
	s_nop 0
	global_load_dwordx4 v[94:97], v[98:99], off nt
	s_nop 0
	global_load_dwordx4 v[98:101], v[102:103], off nt
	s_nop 0
	global_load_dwordx4 v[102:105], v[106:107], off nt
	s_nop 0
	global_load_dwordx4 v[106:109], v[110:111], off nt
	s_nop 0
	global_load_dwordx4 v[110:113], v[114:115], off nt
	s_nop 0
	global_load_dwordx4 v[114:117], v[118:119], off nt
	s_nop 0
	global_load_dwordx4 v[118:121], v[122:123], off nt
	s_nop 0
	global_load_dwordx4 v[122:125], v[126:127], off nt
	v_lshl_add_u64 v[126:127], v[126:127], 0, s[0:1]
	global_load_dwordx4 v[126:129], v[126:127], off nt
	s_waitcnt vmcnt(31)
	v_pk_mul_f32 v[194:195], v[4:5], s[4:5] op_sel_hi:[1,0]
	v_pk_mul_f32 v[192:193], v[2:3], s[4:5] op_sel_hi:[1,0]
	ds_write_b128 v1, v[192:195]
	s_waitcnt vmcnt(30)
	v_pk_mul_f32 v[194:195], v[8:9], s[4:5] op_sel_hi:[1,0]
	v_pk_mul_f32 v[192:193], v[6:7], s[4:5] op_sel_hi:[1,0]
	ds_write_b128 v146, v[192:195] offset:1024
	s_waitcnt vmcnt(29)
	v_pk_mul_f32 v[194:195], v[12:13], s[4:5] op_sel_hi:[1,0]
	v_pk_mul_f32 v[192:193], v[10:11], s[4:5] op_sel_hi:[1,0]
	ds_write_b128 v147, v[192:195] offset:2048
	s_waitcnt vmcnt(28)
	v_pk_mul_f32 v[194:195], v[16:17], s[4:5] op_sel_hi:[1,0]
	v_pk_mul_f32 v[192:193], v[14:15], s[4:5] op_sel_hi:[1,0]
	ds_write_b128 v148, v[192:195] offset:3072
	s_waitcnt vmcnt(27)
	v_pk_mul_f32 v[194:195], v[20:21], s[4:5] op_sel_hi:[1,0]
	v_pk_mul_f32 v[192:193], v[18:19], s[4:5] op_sel_hi:[1,0]
	ds_write_b128 v149, v[192:195] offset:4096
	s_waitcnt vmcnt(26)
	v_pk_mul_f32 v[194:195], v[24:25], s[4:5] op_sel_hi:[1,0]
	v_pk_mul_f32 v[192:193], v[22:23], s[4:5] op_sel_hi:[1,0]
	ds_write_b128 v150, v[192:195] offset:5120
	s_waitcnt vmcnt(25)
	v_pk_mul_f32 v[194:195], v[28:29], s[4:5] op_sel_hi:[1,0]
	v_pk_mul_f32 v[192:193], v[26:27], s[4:5] op_sel_hi:[1,0]
	ds_write_b128 v151, v[192:195] offset:6144
	s_waitcnt vmcnt(24)
	v_pk_mul_f32 v[194:195], v[32:33], s[4:5] op_sel_hi:[1,0]
	v_pk_mul_f32 v[192:193], v[30:31], s[4:5] op_sel_hi:[1,0]
	ds_write_b128 v152, v[192:195] offset:7168
	s_waitcnt vmcnt(23)
	v_pk_mul_f32 v[194:195], v[36:37], s[4:5] op_sel_hi:[1,0]
	v_pk_mul_f32 v[192:193], v[34:35], s[4:5] op_sel_hi:[1,0]
	ds_write_b128 v1, v[192:195] offset:8192
	s_waitcnt vmcnt(22)
	v_pk_mul_f32 v[194:195], v[40:41], s[4:5] op_sel_hi:[1,0]
	v_pk_mul_f32 v[192:193], v[38:39], s[4:5] op_sel_hi:[1,0]
	ds_write_b128 v146, v[192:195] offset:9216
	s_waitcnt vmcnt(21)
	v_pk_mul_f32 v[194:195], v[44:45], s[4:5] op_sel_hi:[1,0]
	v_pk_mul_f32 v[192:193], v[42:43], s[4:5] op_sel_hi:[1,0]
	ds_write_b128 v147, v[192:195] offset:10240
	s_waitcnt vmcnt(20)
	v_pk_mul_f32 v[194:195], v[48:49], s[4:5] op_sel_hi:[1,0]
	v_pk_mul_f32 v[192:193], v[46:47], s[4:5] op_sel_hi:[1,0]
	ds_write_b128 v148, v[192:195] offset:11264
	s_waitcnt vmcnt(19)
	v_pk_mul_f32 v[194:195], v[52:53], s[4:5] op_sel_hi:[1,0]
	v_pk_mul_f32 v[192:193], v[50:51], s[4:5] op_sel_hi:[1,0]
	ds_write_b128 v149, v[192:195] offset:12288
	s_waitcnt vmcnt(18)
	v_pk_mul_f32 v[194:195], v[56:57], s[4:5] op_sel_hi:[1,0]
	v_pk_mul_f32 v[192:193], v[54:55], s[4:5] op_sel_hi:[1,0]
	ds_write_b128 v150, v[192:195] offset:13312
	s_waitcnt vmcnt(17)
	v_pk_mul_f32 v[194:195], v[60:61], s[4:5] op_sel_hi:[1,0]
	v_pk_mul_f32 v[192:193], v[58:59], s[4:5] op_sel_hi:[1,0]
	ds_write_b128 v151, v[192:195] offset:14336
	s_waitcnt vmcnt(16)
	v_pk_mul_f32 v[194:195], v[64:65], s[4:5] op_sel_hi:[1,0]
	v_pk_mul_f32 v[192:193], v[62:63], s[4:5] op_sel_hi:[1,0]
	ds_write_b128 v152, v[192:195] offset:15360
	s_branch .Lcv1_2_1428

; #define GAS __attribute__((address_space(1)))
; __device__ __forceinline__ void p8_finish(const TItem8& t, const f32x4 (&v)[16], LAS float* scr, int lane) {
;     ...
;     const int c = lane & 7;
; #pragma unroll
;     for (int j = 0; j < 4; ++j) { const int n = (lane >> 3) + 8 * j; float x[16];
; #pragma unroll
;         for (int i = 0; i < 16; ++i) { const int k = 16 * c + i; x[i] = scr[k * 32 + ((((n >> 2) ^ ((k >> 3) & 7)) << 2) | (n & 3))]; }
;         int w[4];
; #pragma unroll
;         for (int g = 0; g < 4; ++g) { int q = 0; q = __builtin_amdgcn_cvt_pk_fp8_f32(fminf(fmaxf(x[4 * g], -448.f), 448.f), fminf(fmaxf(x[4 * g + 1], -448.f), 448.f), q, false);
;             q = __builtin_amdgcn_cvt_pk_fp8_f32(fminf(fmaxf(x[4 * g + 2], -448.f), 448.f), fminf(fmaxf(x[4 * g + 3], -448.f), 448.f), q, true); w[g] = q; }
;         v4u o; o.x = (unsigned)w[0]; o.y = (unsigned)w[1]; o.z = (unsigned)w[2]; o.w = (unsigned)w[3];
;         __builtin_nontemporal_store(o, (GAS v4u*)(t.dst + (size_t)n * t.Kd + 16 * c)); }
.Lcv1_2_1428:
	s_waitcnt lgkmcnt(0)
	ds_read2_b32 v[192:193], v153 offset1:32
	ds_read2_b32 v[194:195], v153 offset0:64 offset1:96
	ds_read2_b32 v[196:197], v153 offset0:128 offset1:160
	ds_read2_b32 v[198:199], v153 offset0:192 offset1:224
	ds_read_b32 v140, v154
	ds_read_b32 v143, v155
	ds_read_b32 v191, v156
	ds_read_b32 v200, v157
	ds_read_b32 v201, v158
	ds_read_b32 v202, v159
	ds_read_b32 v203, v160
	ds_read_b32 v204, v161
	s_waitcnt lgkmcnt(11)
	v_max_f32_e32 v192, v192, v192
	v_med3_f32 v205, v192, s5, v190
	v_max_f32_e32 v192, v193, v193
	v_med3_f32 v193, v192, s5, v190
	v_mov_b32_e32 v192, 0
	v_cvt_pk_fp8_f32 v192, v205, v193
	s_waitcnt lgkmcnt(10)
	v_max_f32_e32 v193, v194, v194
	v_max_f32_e32 v194, v195, v195
	v_med3_f32 v193, v193, s5, v190
	v_med3_f32 v194, v194, s5, v190
	v_cvt_pk_fp8_f32 v192, v193, v194 op_sel:[0,0,1]
	s_waitcnt lgkmcnt(9)
	v_max_f32_e32 v193, v196, v196
	v_med3_f32 v194, v193, s5, v190
	v_max_f32_e32 v193, v197, v197
	v_med3_f32 v195, v193, s5, v190
	v_mov_b32_e32 v193, 0
	v_cvt_pk_fp8_f32 v193, v194, v195
	s_waitcnt lgkmcnt(8)
	v_max_f32_e32 v194, v198, v198
	v_max_f32_e32 v195, v199, v199
	v_med3_f32 v194, v194, s5, v190
	v_med3_f32 v195, v195, s5, v190
	s_waitcnt lgkmcnt(7)
	v_max_f32_e32 v140, v140, v140
	s_waitcnt lgkmcnt(6)
	v_max_f32_e32 v143, v143, v143
	v_cvt_pk_fp8_f32 v193, v194, v195 op_sel:[0,0,1]
	v_med3_f32 v140, v140, s5, v190
	v_med3_f32 v143, v143, s5, v190
	v_mov_b32_e32 v194, 0
	v_cvt_pk_fp8_f32 v194, v140, v143
	s_waitcnt lgkmcnt(5)
	v_max_f32_e32 v140, v191, v191
	s_waitcnt lgkmcnt(4)
	v_max_f32_e32 v143, v200, v200
	v_med3_f32 v140, v140, s5, v190
	v_med3_f32 v143, v143, s5, v190
	v_cvt_pk_fp8_f32 v194, v140, v143 op_sel:[0,0,1]
	s_waitcnt lgkmcnt(3)
	v_max_f32_e32 v140, v201, v201
	s_waitcnt lgkmcnt(2)
	v_max_f32_e32 v143, v202, v202
	v_med3_f32 v140, v140, s5, v190
	v_med3_f32 v143, v143, s5, v190
	v_mov_b32_e32 v195, 0
	v_cvt_pk_fp8_f32 v195, v140, v143
	s_waitcnt lgkmcnt(1)
	v_max_f32_e32 v140, v203, v203
	s_waitcnt lgkmcnt(0)
	v_max_f32_e32 v143, v204, v204
	v_med3_f32 v140, v140, s5, v190
	v_med3_f32 v143, v143, s5, v190
	v_cvt_pk_fp8_f32 v195, v140, v143 op_sel:[0,0,1]
	ds_read2_b32 v[196:197], v162 offset1:32
	ds_read2_b32 v[198:199], v162 offset0:64 offset1:96
	ds_read2_b32 v[200:201], v162 offset0:128 offset1:160
	ds_read2_b32 v[202:203], v162 offset0:192 offset1:224
	ds_read_b32 v140, v163
	ds_read_b32 v143, v164
	ds_read_b32 v191, v165
	ds_read_b32 v204, v166
	ds_read_b32 v205, v167
	ds_read_b32 v206, v168
	ds_read_b32 v207, v169
	ds_read_b32 v208, v170
	s_waitcnt lgkmcnt(11)
	v_max_f32_e32 v196, v196, v196
	v_med3_f32 v209, v196, s5, v190
	v_max_f32_e32 v196, v197, v197
	v_med3_f32 v197, v196, s5, v190
	v_mov_b32_e32 v196, 0
	v_cvt_pk_fp8_f32 v196, v209, v197
	s_waitcnt lgkmcnt(10)
	v_max_f32_e32 v197, v198, v198
	v_max_f32_e32 v198, v199, v199
	v_med3_f32 v197, v197, s5, v190
	v_med3_f32 v198, v198, s5, v190
	v_cvt_pk_fp8_f32 v196, v197, v198 op_sel:[0,0,1]
	s_waitcnt lgkmcnt(9)
	v_max_f32_e32 v197, v200, v200
	v_med3_f32 v198, v197, s5, v190
	v_max_f32_e32 v197, v201, v201
	v_med3_f32 v199, v197, s5, v190
	v_mov_b32_e32 v197, 0
	v_cvt_pk_fp8_f32 v197, v198, v199
	s_waitcnt lgkmcnt(8)
	v_max_f32_e32 v198, v202, v202
	v_max_f32_e32 v199, v203, v203
	v_med3_f32 v198, v198, s5, v190
	v_med3_f32 v199, v199, s5, v190
	s_waitcnt lgkmcnt(7)
	v_max_f32_e32 v140, v140, v140
	s_waitcnt lgkmcnt(6)
	v_max_f32_e32 v143, v143, v143
	v_cvt_pk_fp8_f32 v197, v198, v199 op_sel:[0,0,1]
	v_med3_f32 v140, v140, s5, v190
	v_med3_f32 v143, v143, s5, v190
	v_mov_b32_e32 v198, 0
	v_cvt_pk_fp8_f32 v198, v140, v143
	s_waitcnt lgkmcnt(5)
	v_max_f32_e32 v140, v191, v191
	s_waitcnt lgkmcnt(4)
	v_max_f32_e32 v143, v204, v204
	v_med3_f32 v140, v140, s5, v190
	v_med3_f32 v143, v143, s5, v190
	v_cvt_pk_fp8_f32 v198, v140, v143 op_sel:[0,0,1]
	s_waitcnt lgkmcnt(3)
	v_max_f32_e32 v140, v205, v205
	s_waitcnt lgkmcnt(2)
	v_max_f32_e32 v143, v206, v206
	v_med3_f32 v140, v140, s5, v190
	v_med3_f32 v143, v143, s5, v190
	v_mov_b32_e32 v199, 0
	v_cvt_pk_fp8_f32 v199, v140, v143
	s_waitcnt lgkmcnt(1)
	v_max_f32_e32 v140, v207, v207
	s_waitcnt lgkmcnt(0)
	v_max_f32_e32 v143, v208, v208
	v_med3_f32 v140, v140, s5, v190
	v_med3_f32 v143, v143, s5, v190
	v_cvt_pk_fp8_f32 v199, v140, v143 op_sel:[0,0,1]
	v_lshl_add_u64 v[144:145], s[6:7], 0, v[130:131]
	v_lshl_add_u64 v[200:201], v[144:145], 0, v[132:133]
	global_store_dwordx4 v[200:201], v[192:195], off nt
	s_andn2_b64 vcc, exec, s[10:11]
	s_mov_b64 s[10:11], 0
	v_lshl_add_u64 v[192:193], v[144:145], 0, v[134:135]
	global_store_dwordx4 v[192:193], v[196:199], off nt
	ds_read2_b32 v[192:193], v171 offset1:32
	ds_read2_b32 v[194:195], v171 offset0:64 offset1:96
	ds_read2_b32 v[196:197], v171 offset0:128 offset1:160
	ds_read2_b32 v[198:199], v171 offset0:192 offset1:224
	ds_read_b32 v140, v172
	ds_read_b32 v143, v173
	ds_read_b32 v191, v174
	ds_read_b32 v200, v175
	ds_read_b32 v201, v176
	ds_read_b32 v202, v177
	ds_read_b32 v203, v178
	ds_read_b32 v204, v179
	s_waitcnt lgkmcnt(11)
; #define GAS __attribute__((address_space(1)))
; __device__ __forceinline__ TItem8 p8_decode(const Args& args, unsigned char* ws, int it) {
;     TItem8 t;
;     if (it >= P8_N) { const int j = it - P8_N; it = (P8_E0 + j / P8_DN1) * (P8_GU1 + P8_DN1) + P8_GU1 + j % P8_DN1; }
;     else if (it >= P8_E0 * (P8_GU1 + P8_DN1)) { const int r = it - P8_E0 * (P8_GU1 + P8_DN1); it = (P8_E0 + r / P8_GU1) * (P8_GU1 + P8_DN1) + r % P8_GU1; }
;     const int e = it / (P8_GU1 + P8_DN1), q = it % (P8_GU1 + P8_DN1);
; __device__ __forceinline__ void p8_finish(const TItem8& t, const f32x4 (&v)[16], LAS float* scr, int lane) {
;     ...
;     const int c = lane & 7;
; #pragma unroll
;     for (int j = 0; j < 4; ++j) { const int n = (lane >> 3) + 8 * j; float x[16];
; #pragma unroll
;         for (int i = 0; i < 16; ++i) { const int k = 16 * c + i; x[i] = scr[k * 32 + ((((n >> 2) ^ ((k >> 3) & 7)) << 2) | (n & 3))]; }
;         int w[4];
; #pragma unroll
;         for (int g = 0; g < 4; ++g) { int q = 0; q = __builtin_amdgcn_cvt_pk_fp8_f32(fminf(fmaxf(x[4 * g], -448.f), 448.f), fminf(fmaxf(x[4 * g + 1], -448.f), 448.f), q, false);
;             q = __builtin_amdgcn_cvt_pk_fp8_f32(fminf(fmaxf(x[4 * g + 2], -448.f), 448.f), fminf(fmaxf(x[4 * g + 3], -448.f), 448.f), q, true); w[g] = q; }
;         v4u o; o.x = (unsigned)w[0]; o.y = (unsigned)w[1]; o.z = (unsigned)w[2]; o.w = (unsigned)w[3];
;         __builtin_nontemporal_store(o, (GAS v4u*)(t.dst + (size_t)n * t.Kd + 16 * c)); }
	v_max_f32_e32 v192, v192, v192
	v_med3_f32 v205, v192, s5, v190
	v_max_f32_e32 v192, v193, v193
	v_med3_f32 v193, v192, s5, v190
	v_mov_b32_e32 v192, 0
	v_cvt_pk_fp8_f32 v192, v205, v193
	s_waitcnt lgkmcnt(10)
	v_max_f32_e32 v193, v194, v194
	v_max_f32_e32 v194, v195, v195
	v_med3_f32 v193, v193, s5, v190
	v_med3_f32 v194, v194, s5, v190
	v_cvt_pk_fp8_f32 v192, v193, v194 op_sel:[0,0,1]
	s_waitcnt lgkmcnt(9)
	v_max_f32_e32 v193, v196, v196
	v_med3_f32 v194, v193, s5, v190
	v_max_f32_e32 v193, v197, v197
	v_med3_f32 v195, v193, s5, v190
	v_mov_b32_e32 v193, 0
	v_cvt_pk_fp8_f32 v193, v194, v195
	s_waitcnt lgkmcnt(8)
	v_max_f32_e32 v194, v198, v198
	v_max_f32_e32 v195, v199, v199
	v_med3_f32 v194, v194, s5, v190
	v_med3_f32 v195, v195, s5, v190
	s_waitcnt lgkmcnt(7)
	v_max_f32_e32 v140, v140, v140
	s_waitcnt lgkmcnt(6)
	v_max_f32_e32 v143, v143, v143
	v_cvt_pk_fp8_f32 v193, v194, v195 op_sel:[0,0,1]
	v_med3_f32 v140, v140, s5, v190
	v_med3_f32 v143, v143, s5, v190
	v_mov_b32_e32 v194, 0
	v_cvt_pk_fp8_f32 v194, v140, v143
	s_waitcnt lgkmcnt(5)
	v_max_f32_e32 v140, v191, v191
	s_waitcnt lgkmcnt(4)
	v_max_f32_e32 v143, v200, v200
	v_med3_f32 v140, v140, s5, v190
	v_med3_f32 v143, v143, s5, v190
	v_cvt_pk_fp8_f32 v194, v140, v143 op_sel:[0,0,1]
	s_waitcnt lgkmcnt(3)
	v_max_f32_e32 v140, v201, v201
	s_waitcnt lgkmcnt(2)
	v_max_f32_e32 v143, v202, v202
	v_med3_f32 v140, v140, s5, v190
	v_med3_f32 v143, v143, s5, v190
	v_mov_b32_e32 v195, 0
	v_cvt_pk_fp8_f32 v195, v140, v143
	s_waitcnt lgkmcnt(1)
	v_max_f32_e32 v140, v203, v203
	s_waitcnt lgkmcnt(0)
	v_max_f32_e32 v143, v204, v204
	v_med3_f32 v140, v140, s5, v190
	v_med3_f32 v143, v143, s5, v190
	v_cvt_pk_fp8_f32 v195, v140, v143 op_sel:[0,0,1]
	ds_read2_b32 v[196:197], v180 offset1:32
	ds_read2_b32 v[198:199], v180 offset0:64 offset1:96
	ds_read2_b32 v[200:201], v180 offset0:128 offset1:160
	ds_read2_b32 v[202:203], v180 offset0:192 offset1:224
	ds_read_b32 v140, v181
	ds_read_b32 v143, v182
	ds_read_b32 v191, v183
	ds_read_b32 v204, v184
	ds_read_b32 v205, v185
	ds_read_b32 v206, v186
	ds_read_b32 v207, v187
	ds_read_b32 v208, v188
	s_waitcnt lgkmcnt(11)
	v_max_f32_e32 v196, v196, v196
	v_med3_f32 v209, v196, s5, v190
	v_max_f32_e32 v196, v197, v197
	v_med3_f32 v197, v196, s5, v190
	v_mov_b32_e32 v196, 0
	v_cvt_pk_fp8_f32 v196, v209, v197
	s_waitcnt lgkmcnt(10)
	v_max_f32_e32 v197, v198, v198
	v_max_f32_e32 v198, v199, v199
	v_med3_f32 v197, v197, s5, v190
	v_med3_f32 v198, v198, s5, v190
	v_cvt_pk_fp8_f32 v196, v197, v198 op_sel:[0,0,1]
	s_waitcnt lgkmcnt(9)
	v_max_f32_e32 v197, v200, v200
	v_med3_f32 v198, v197, s5, v190
	v_max_f32_e32 v197, v201, v201
	v_med3_f32 v199, v197, s5, v190
	v_mov_b32_e32 v197, 0
	v_cvt_pk_fp8_f32 v197, v198, v199
	s_waitcnt lgkmcnt(8)
	v_max_f32_e32 v198, v202, v202
	v_max_f32_e32 v199, v203, v203
	v_med3_f32 v198, v198, s5, v190
	v_med3_f32 v199, v199, s5, v190
	s_waitcnt lgkmcnt(7)
	v_max_f32_e32 v140, v140, v140
	s_waitcnt lgkmcnt(6)
	v_max_f32_e32 v143, v143, v143
	v_cvt_pk_fp8_f32 v197, v198, v199 op_sel:[0,0,1]
	v_med3_f32 v140, v140, s5, v190
	v_med3_f32 v143, v143, s5, v190
	v_mov_b32_e32 v198, 0
	v_cvt_pk_fp8_f32 v198, v140, v143
	s_waitcnt lgkmcnt(5)
	v_max_f32_e32 v140, v191, v191
	s_waitcnt lgkmcnt(4)
	v_max_f32_e32 v143, v204, v204
	v_med3_f32 v140, v140, s5, v190
	v_med3_f32 v143, v143, s5, v190
	v_cvt_pk_fp8_f32 v198, v140, v143 op_sel:[0,0,1]
	s_waitcnt lgkmcnt(3)
	v_max_f32_e32 v140, v205, v205
	s_waitcnt lgkmcnt(2)
	v_max_f32_e32 v143, v206, v206
	v_med3_f32 v140, v140, s5, v190
	v_med3_f32 v143, v143, s5, v190
	v_mov_b32_e32 v199, 0
	v_cvt_pk_fp8_f32 v199, v140, v143
	s_waitcnt lgkmcnt(1)
	v_max_f32_e32 v140, v207, v207
	s_waitcnt lgkmcnt(0)
	v_max_f32_e32 v143, v208, v208
	v_med3_f32 v140, v140, s5, v190
	v_med3_f32 v143, v143, s5, v190
	v_cvt_pk_fp8_f32 v199, v140, v143 op_sel:[0,0,1]
	v_lshl_add_u64 v[200:201], v[144:145], 0, v[136:137]
	v_lshl_add_u64 v[144:145], v[144:145], 0, v[138:139]
	global_store_dwordx4 v[200:201], v[192:195], off nt
	global_store_dwordx4 v[144:145], v[196:199], off nt
	s_waitcnt lgkmcnt(0)
	s_cbranch_vccnz .LBB0_1411
	s_add_i32 s29, s29, 2
	s_mul_i32 s12, s29, s28
	s_add_i32 s0, s12, s26
	s_cmp_lt_i32 s0, s27
	s_cselect_b64 s[10:11], -1, 0
	s_cmp_ge_i32 s0, s27
	s_cbranch_scc1 .LBB0_1445
	s_cmp_lt_i32 s0, 0x16400
	s_mov_b64 s[6:7], -1
	s_cbranch_scc0 .LBB0_1434
	s_cmp_lt_i32 s0, 0x12c00
	s_mov_b32 s13, s0
	s_cbranch_scc1 .LBB0_1433
	s_add_i32 s6, s0, 0xfffed400
	s_lshr_b32 s7, s6, 11
	s_mulk_i32 s7, 0xc00
	s_and_b32 s6, s6, 0x7ff
	s_add_i32 s6, s6, s7
	s_add_i32 s13, s6, 0x12c00

; #define GAS __attribute__((address_space(1)))
; #define LAS __attribute__((address_space(3)))
; #define LDS_WAIT() asm volatile("s_waitcnt lgkmcnt(0)" ::: "memory")
; __device__ __forceinline__ void p8_issue(const TItem8& t, f32x4 (&v)[16], int lane) {
;     const GAS f32x4* src = (const GAS f32x4*)((const GAS float*)t.src + (size_t)(lane >> 3) * t.N + 4 * (lane & 7));
; #pragma unroll
;     for (int i = 0; i < 16; ++i) v[i] = __builtin_nontemporal_load(src + (size_t)(2 * i) * t.N);
; }
; __device__ __forceinline__ void p8_finish(const TItem8& t, const f32x4 (&v)[16], LAS float* scr, int lane) {
; #pragma unroll
;     for (int i = 0; i < 16; ++i) *(LAS f32x4*)(scr + (8 * i + (lane >> 3)) * 32 + (((lane & 7) ^ (i & 7)) << 2)) = v[i] * W8_SCALE;
;     LDS_WAIT(); asm volatile("" ::: "memory");
.LBB0_1444:
	s_lshl_b64 s[6:7], s[12:13], 11
	s_add_u32 s0, s18, s6
	v_mul_u32_u24_e32 v2, s22, v225
	s_addc_u32 s7, s19, s7
	v_lshlrev_b32_e32 v140, 2, v2
	s_add_u32 s6, s0, s16
	v_lshl_add_u64 v[2:3], s[14:15], 0, v[140:141]
	v_mov_b32_e32 v143, v141
	s_addc_u32 s7, s7, s17
	v_lshl_add_u64 v[2:3], v[2:3], 0, v[142:143]
	s_lshl_b32 s0, s22, 5
	v_lshl_add_u64 v[10:11], v[2:3], 0, s[0:1]
	global_load_dwordx4 v[2:5], v[2:3], off nt
	s_nop 0
	global_load_dwordx4 v[6:9], v[10:11], off nt
	v_lshl_add_u64 v[10:11], v[10:11], 0, s[0:1]
	v_lshl_add_u64 v[18:19], v[10:11], 0, s[0:1]
	global_load_dwordx4 v[10:13], v[10:11], off nt
	s_nop 0
	global_load_dwordx4 v[14:17], v[18:19], off nt
	v_lshl_add_u64 v[18:19], v[18:19], 0, s[0:1]
	v_lshl_add_u64 v[26:27], v[18:19], 0, s[0:1]
	global_load_dwordx4 v[18:21], v[18:19], off nt
	s_nop 0
	global_load_dwordx4 v[22:25], v[26:27], off nt
	v_lshl_add_u64 v[26:27], v[26:27], 0, s[0:1]
	v_lshl_add_u64 v[34:35], v[26:27], 0, s[0:1]
	v_lshl_add_u64 v[38:39], v[34:35], 0, s[0:1]
	v_lshl_add_u64 v[42:43], v[38:39], 0, s[0:1]
	v_lshl_add_u64 v[46:47], v[42:43], 0, s[0:1]
	v_lshl_add_u64 v[50:51], v[46:47], 0, s[0:1]
	v_lshl_add_u64 v[54:55], v[50:51], 0, s[0:1]
	v_lshl_add_u64 v[58:59], v[54:55], 0, s[0:1]
	v_lshl_add_u64 v[62:63], v[58:59], 0, s[0:1]
	global_load_dwordx4 v[26:29], v[26:27], off nt
	s_nop 0
	global_load_dwordx4 v[30:33], v[34:35], off nt
	s_nop 0
	global_load_dwordx4 v[34:37], v[38:39], off nt
	s_nop 0
	global_load_dwordx4 v[38:41], v[42:43], off nt
	s_nop 0
	global_load_dwordx4 v[42:45], v[46:47], off nt
	s_nop 0
	global_load_dwordx4 v[46:49], v[50:51], off nt
	s_nop 0
	global_load_dwordx4 v[50:53], v[54:55], off nt
	s_nop 0
	global_load_dwordx4 v[54:57], v[58:59], off nt
	s_nop 0
	global_load_dwordx4 v[58:61], v[62:63], off nt
	v_lshl_add_u64 v[62:63], v[62:63], 0, s[0:1]
	global_load_dwordx4 v[62:65], v[62:63], off nt
	s_waitcnt vmcnt(35)
	v_pk_mul_f32 v[194:195], v[68:69], s[4:5] op_sel_hi:[1,0]
	v_pk_mul_f32 v[192:193], v[66:67], s[4:5] op_sel_hi:[1,0]
	ds_write_b128 v1, v[192:195]
	s_waitcnt vmcnt(34)
	v_pk_mul_f32 v[194:195], v[72:73], s[4:5] op_sel_hi:[1,0]
	v_pk_mul_f32 v[192:193], v[70:71], s[4:5] op_sel_hi:[1,0]
	ds_write_b128 v146, v[192:195] offset:1024
	s_waitcnt vmcnt(33)
	v_pk_mul_f32 v[194:195], v[76:77], s[4:5] op_sel_hi:[1,0]
	v_pk_mul_f32 v[192:193], v[74:75], s[4:5] op_sel_hi:[1,0]
	ds_write_b128 v147, v[192:195] offset:2048
	s_waitcnt vmcnt(32)
	v_pk_mul_f32 v[194:195], v[80:81], s[4:5] op_sel_hi:[1,0]
	v_pk_mul_f32 v[192:193], v[78:79], s[4:5] op_sel_hi:[1,0]
	ds_write_b128 v148, v[192:195] offset:3072
	s_waitcnt vmcnt(31)
	v_pk_mul_f32 v[194:195], v[84:85], s[4:5] op_sel_hi:[1,0]
	v_pk_mul_f32 v[192:193], v[82:83], s[4:5] op_sel_hi:[1,0]
	ds_write_b128 v149, v[192:195] offset:4096
	s_waitcnt vmcnt(30)
	v_pk_mul_f32 v[194:195], v[88:89], s[4:5] op_sel_hi:[1,0]
	v_pk_mul_f32 v[192:193], v[86:87], s[4:5] op_sel_hi:[1,0]
	ds_write_b128 v150, v[192:195] offset:5120
	s_waitcnt vmcnt(29)
	v_pk_mul_f32 v[194:195], v[92:93], s[4:5] op_sel_hi:[1,0]
	v_pk_mul_f32 v[192:193], v[90:91], s[4:5] op_sel_hi:[1,0]
	ds_write_b128 v151, v[192:195] offset:6144
	s_waitcnt vmcnt(28)
	v_pk_mul_f32 v[194:195], v[96:97], s[4:5] op_sel_hi:[1,0]
	v_pk_mul_f32 v[192:193], v[94:95], s[4:5] op_sel_hi:[1,0]
	ds_write_b128 v152, v[192:195] offset:7168
	s_waitcnt vmcnt(27)
	v_pk_mul_f32 v[194:195], v[100:101], s[4:5] op_sel_hi:[1,0]
	v_pk_mul_f32 v[192:193], v[98:99], s[4:5] op_sel_hi:[1,0]
	ds_write_b128 v1, v[192:195] offset:8192
	s_waitcnt vmcnt(26)
	v_pk_mul_f32 v[194:195], v[104:105], s[4:5] op_sel_hi:[1,0]
	v_pk_mul_f32 v[192:193], v[102:103], s[4:5] op_sel_hi:[1,0]
	ds_write_b128 v146, v[192:195] offset:9216
	s_waitcnt vmcnt(25)
	v_pk_mul_f32 v[194:195], v[108:109], s[4:5] op_sel_hi:[1,0]
	v_pk_mul_f32 v[192:193], v[106:107], s[4:5] op_sel_hi:[1,0]
	ds_write_b128 v147, v[192:195] offset:10240
	s_waitcnt vmcnt(24)
	v_pk_mul_f32 v[194:195], v[112:113], s[4:5] op_sel_hi:[1,0]
	v_pk_mul_f32 v[192:193], v[110:111], s[4:5] op_sel_hi:[1,0]
	ds_write_b128 v148, v[192:195] offset:11264
	s_waitcnt vmcnt(23)
	v_pk_mul_f32 v[194:195], v[116:117], s[4:5] op_sel_hi:[1,0]
	v_pk_mul_f32 v[192:193], v[114:115], s[4:5] op_sel_hi:[1,0]
	ds_write_b128 v149, v[192:195] offset:12288
	s_waitcnt vmcnt(22)
	v_pk_mul_f32 v[194:195], v[120:121], s[4:5] op_sel_hi:[1,0]
	v_pk_mul_f32 v[192:193], v[118:119], s[4:5] op_sel_hi:[1,0]
	ds_write_b128 v150, v[192:195] offset:13312
	s_waitcnt vmcnt(21)
	v_pk_mul_f32 v[194:195], v[124:125], s[4:5] op_sel_hi:[1,0]
	v_pk_mul_f32 v[192:193], v[122:123], s[4:5] op_sel_hi:[1,0]
	ds_write_b128 v151, v[192:195] offset:14336
	s_waitcnt vmcnt(20)
	v_pk_mul_f32 v[194:195], v[128:129], s[4:5] op_sel_hi:[1,0]
	v_pk_mul_f32 v[192:193], v[126:127], s[4:5] op_sel_hi:[1,0]
	ds_write_b128 v152, v[192:195] offset:15360
	s_branch .Lcv2_2_1428
; #define GAS __attribute__((address_space(1)))
; #define LAS __attribute__((address_space(3)))
; #define LDS_WAIT() asm volatile("s_waitcnt lgkmcnt(0)" ::: "memory")
; __device__ __forceinline__ void p8_finish(const TItem8& t, const f32x4 (&v)[16], LAS float* scr, int lane) {
; #pragma unroll
;     for (int i = 0; i < 16; ++i) *(LAS f32x4*)(scr + (8 * i + (lane >> 3)) * 32 + (((lane & 7) ^ (i & 7)) << 2)) = v[i] * W8_SCALE;
;     LDS_WAIT(); asm volatile("" ::: "memory");
;     const int c = lane & 7;
; #pragma unroll
;     for (int j = 0; j < 4; ++j) { const int n = (lane >> 3) + 8 * j; float x[16];
; #pragma unroll
;         for (int i = 0; i < 16; ++i) { const int k = 16 * c + i; x[i] = scr[k * 32 + ((((n >> 2) ^ ((k >> 3) & 7)) << 2) | (n & 3))]; }
;         int w[4];
; #pragma unroll
;         for (int g = 0; g < 4; ++g) { int q = 0; q = __builtin_amdgcn_cvt_pk_fp8_f32(fminf(fmaxf(x[4 * g], -448.f), 448.f), fminf(fmaxf(x[4 * g + 1], -448.f), 448.f), q, false);
;             q = __builtin_amdgcn_cvt_pk_fp8_f32(fminf(fmaxf(x[4 * g + 2], -448.f), 448.f), fminf(fmaxf(x[4 * g + 3], -448.f), 448.f), q, true); w[g] = q; }
;         v4u o; o.x = (unsigned)w[0]; o.y = (unsigned)w[1]; o.z = (unsigned)w[2]; o.w = (unsigned)w[3];
;         __builtin_nontemporal_store(o, (GAS v4u*)(t.dst + (size_t)n * t.Kd + 16 * c)); }
.LBB0_1445:
	s_waitcnt vmcnt(19)
	v_pk_mul_f32 v[194:195], v[68:69], s[4:5] op_sel_hi:[1,0]
	v_pk_mul_f32 v[192:193], v[66:67], s[4:5] op_sel_hi:[1,0]
	ds_write_b128 v1, v[192:195]
	s_waitcnt vmcnt(18)
	v_pk_mul_f32 v[194:195], v[72:73], s[4:5] op_sel_hi:[1,0]
	v_pk_mul_f32 v[192:193], v[70:71], s[4:5] op_sel_hi:[1,0]
	ds_write_b128 v146, v[192:195] offset:1024
	s_waitcnt vmcnt(17)
	v_pk_mul_f32 v[194:195], v[76:77], s[4:5] op_sel_hi:[1,0]
	v_pk_mul_f32 v[192:193], v[74:75], s[4:5] op_sel_hi:[1,0]
	ds_write_b128 v147, v[192:195] offset:2048
	s_waitcnt vmcnt(16)
	v_pk_mul_f32 v[194:195], v[80:81], s[4:5] op_sel_hi:[1,0]
	v_pk_mul_f32 v[192:193], v[78:79], s[4:5] op_sel_hi:[1,0]
	ds_write_b128 v148, v[192:195] offset:3072
	s_waitcnt vmcnt(15)
	v_pk_mul_f32 v[194:195], v[84:85], s[4:5] op_sel_hi:[1,0]
	v_pk_mul_f32 v[192:193], v[82:83], s[4:5] op_sel_hi:[1,0]
	ds_write_b128 v149, v[192:195] offset:4096
	s_waitcnt vmcnt(14)
	v_pk_mul_f32 v[194:195], v[88:89], s[4:5] op_sel_hi:[1,0]
	v_pk_mul_f32 v[192:193], v[86:87], s[4:5] op_sel_hi:[1,0]
	ds_write_b128 v150, v[192:195] offset:5120
	s_waitcnt vmcnt(13)
	v_pk_mul_f32 v[194:195], v[92:93], s[4:5] op_sel_hi:[1,0]
	v_pk_mul_f32 v[192:193], v[90:91], s[4:5] op_sel_hi:[1,0]
	ds_write_b128 v151, v[192:195] offset:6144
	s_waitcnt vmcnt(12)
	v_pk_mul_f32 v[194:195], v[96:97], s[4:5] op_sel_hi:[1,0]
	v_pk_mul_f32 v[192:193], v[94:95], s[4:5] op_sel_hi:[1,0]
	ds_write_b128 v152, v[192:195] offset:7168
	s_waitcnt vmcnt(11)
	v_pk_mul_f32 v[194:195], v[100:101], s[4:5] op_sel_hi:[1,0]
	v_pk_mul_f32 v[192:193], v[98:99], s[4:5] op_sel_hi:[1,0]
	ds_write_b128 v1, v[192:195] offset:8192
	s_waitcnt vmcnt(10)
	v_pk_mul_f32 v[194:195], v[104:105], s[4:5] op_sel_hi:[1,0]
	v_pk_mul_f32 v[192:193], v[102:103], s[4:5] op_sel_hi:[1,0]
	ds_write_b128 v146, v[192:195] offset:9216
	s_waitcnt vmcnt(9)
	v_pk_mul_f32 v[194:195], v[108:109], s[4:5] op_sel_hi:[1,0]
	v_pk_mul_f32 v[192:193], v[106:107], s[4:5] op_sel_hi:[1,0]
	ds_write_b128 v147, v[192:195] offset:10240
	s_waitcnt vmcnt(8)
	v_pk_mul_f32 v[194:195], v[112:113], s[4:5] op_sel_hi:[1,0]
	v_pk_mul_f32 v[192:193], v[110:111], s[4:5] op_sel_hi:[1,0]
	ds_write_b128 v148, v[192:195] offset:11264
	s_waitcnt vmcnt(7)
	v_pk_mul_f32 v[194:195], v[116:117], s[4:5] op_sel_hi:[1,0]
	v_pk_mul_f32 v[192:193], v[114:115], s[4:5] op_sel_hi:[1,0]
	ds_write_b128 v149, v[192:195] offset:12288
	s_waitcnt vmcnt(6)
	v_pk_mul_f32 v[194:195], v[120:121], s[4:5] op_sel_hi:[1,0]
	v_pk_mul_f32 v[192:193], v[118:119], s[4:5] op_sel_hi:[1,0]
	ds_write_b128 v150, v[192:195] offset:13312
	s_waitcnt vmcnt(5)
	v_pk_mul_f32 v[194:195], v[124:125], s[4:5] op_sel_hi:[1,0]
	v_pk_mul_f32 v[192:193], v[122:123], s[4:5] op_sel_hi:[1,0]
	ds_write_b128 v151, v[192:195] offset:14336
	s_waitcnt vmcnt(4)
	v_pk_mul_f32 v[194:195], v[128:129], s[4:5] op_sel_hi:[1,0]
	v_pk_mul_f32 v[192:193], v[126:127], s[4:5] op_sel_hi:[1,0]
	ds_write_b128 v152, v[192:195] offset:15360
.Lcv2_2_1428:
	s_waitcnt lgkmcnt(0)
	ds_read2_b32 v[192:193], v153 offset1:32
	ds_read2_b32 v[194:195], v153 offset0:64 offset1:96
	ds_read2_b32 v[196:197], v153 offset0:128 offset1:160
	ds_read2_b32 v[198:199], v153 offset0:192 offset1:224
	ds_read_b32 v140, v154
	ds_read_b32 v143, v155
	ds_read_b32 v191, v156
	ds_read_b32 v200, v157
	ds_read_b32 v201, v158
	ds_read_b32 v202, v159
	ds_read_b32 v203, v160
	ds_read_b32 v204, v161
	s_waitcnt lgkmcnt(11)
	v_max_f32_e32 v192, v192, v192
	v_med3_f32 v205, v192, s5, v190
	v_max_f32_e32 v192, v193, v193
	v_med3_f32 v193, v192, s5, v190
	v_mov_b32_e32 v192, v141
	v_cvt_pk_fp8_f32 v192, v205, v193
	s_waitcnt lgkmcnt(10)
	v_max_f32_e32 v193, v194, v194
	v_max_f32_e32 v194, v195, v195
	v_med3_f32 v193, v193, s5, v190
	v_med3_f32 v194, v194, s5, v190
	v_cvt_pk_fp8_f32 v192, v193, v194 op_sel:[0,0,1]
	s_waitcnt lgkmcnt(9)
	v_max_f32_e32 v193, v196, v196
	v_med3_f32 v194, v193, s5, v190
	v_max_f32_e32 v193, v197, v197
	v_med3_f32 v195, v193, s5, v190
	v_mov_b32_e32 v193, v141
	v_cvt_pk_fp8_f32 v193, v194, v195
	s_waitcnt lgkmcnt(8)
	v_max_f32_e32 v194, v198, v198
	v_max_f32_e32 v195, v199, v199
	v_med3_f32 v194, v194, s5, v190
	v_med3_f32 v195, v195, s5, v190
	s_waitcnt lgkmcnt(7)
	v_max_f32_e32 v140, v140, v140
	s_waitcnt lgkmcnt(6)
	v_max_f32_e32 v143, v143, v143
	v_cvt_pk_fp8_f32 v193, v194, v195 op_sel:[0,0,1]
	v_med3_f32 v140, v140, s5, v190
	v_med3_f32 v143, v143, s5, v190
	v_mov_b32_e32 v194, v141
	v_cvt_pk_fp8_f32 v194, v140, v143
	s_waitcnt lgkmcnt(5)
	v_max_f32_e32 v140, v191, v191
	s_waitcnt lgkmcnt(4)
	v_max_f32_e32 v143, v200, v200
	v_med3_f32 v140, v140, s5, v190
	v_med3_f32 v143, v143, s5, v190
	v_cvt_pk_fp8_f32 v194, v140, v143 op_sel:[0,0,1]
	s_waitcnt lgkmcnt(3)
	v_max_f32_e32 v140, v201, v201
	s_waitcnt lgkmcnt(2)
	v_max_f32_e32 v143, v202, v202
	v_med3_f32 v140, v140, s5, v190
	v_med3_f32 v143, v143, s5, v190
	v_mov_b32_e32 v195, v141
	v_cvt_pk_fp8_f32 v195, v140, v143
	s_waitcnt lgkmcnt(1)
	v_max_f32_e32 v140, v203, v203
	s_waitcnt lgkmcnt(0)
	v_max_f32_e32 v143, v204, v204
	v_med3_f32 v140, v140, s5, v190
	v_med3_f32 v143, v143, s5, v190
	v_cvt_pk_fp8_f32 v195, v140, v143 op_sel:[0,0,1]
	ds_read2_b32 v[196:197], v162 offset1:32
	ds_read2_b32 v[198:199], v162 offset0:64 offset1:96
	ds_read2_b32 v[200:201], v162 offset0:128 offset1:160
	ds_read2_b32 v[202:203], v162 offset0:192 offset1:224
	ds_read_b32 v140, v163
	ds_read_b32 v143, v164
	ds_read_b32 v191, v165
	ds_read_b32 v204, v166
	ds_read_b32 v205, v167
	ds_read_b32 v206, v168
	ds_read_b32 v207, v169
	ds_read_b32 v208, v170
	s_waitcnt lgkmcnt(11)
; #define GAS __attribute__((address_space(1)))
; #define LDS_WAIT() asm volatile("s_waitcnt lgkmcnt(0)" ::: "memory")
; __device__ __forceinline__ void p8_finish(const TItem8& t, const f32x4 (&v)[16], LAS float* scr, int lane) {
;     ...
;     const int c = lane & 7;
; #pragma unroll
;     for (int j = 0; j < 4; ++j) { const int n = (lane >> 3) + 8 * j; float x[16];
; #pragma unroll
;         for (int i = 0; i < 16; ++i) { const int k = 16 * c + i; x[i] = scr[k * 32 + ((((n >> 2) ^ ((k >> 3) & 7)) << 2) | (n & 3))]; }
;         int w[4];
; #pragma unroll
;         for (int g = 0; g < 4; ++g) { int q = 0; q = __builtin_amdgcn_cvt_pk_fp8_f32(fminf(fmaxf(x[4 * g], -448.f), 448.f), fminf(fmaxf(x[4 * g + 1], -448.f), 448.f), q, false);
;             q = __builtin_amdgcn_cvt_pk_fp8_f32(fminf(fmaxf(x[4 * g + 2], -448.f), 448.f), fminf(fmaxf(x[4 * g + 3], -448.f), 448.f), q, true); w[g] = q; }
;         v4u o; o.x = (unsigned)w[0]; o.y = (unsigned)w[1]; o.z = (unsigned)w[2]; o.w = (unsigned)w[3];
;         __builtin_nontemporal_store(o, (GAS v4u*)(t.dst + (size_t)n * t.Kd + 16 * c)); }
;     LDS_WAIT(); asm volatile("" ::: "memory");
	v_max_f32_e32 v196, v196, v196
	v_med3_f32 v209, v196, s5, v190
	v_max_f32_e32 v196, v197, v197
	v_med3_f32 v197, v196, s5, v190
	v_mov_b32_e32 v196, v141
	v_cvt_pk_fp8_f32 v196, v209, v197
	s_waitcnt lgkmcnt(10)
	v_max_f32_e32 v197, v198, v198
	v_max_f32_e32 v198, v199, v199
	v_med3_f32 v197, v197, s5, v190
	v_med3_f32 v198, v198, s5, v190
	v_cvt_pk_fp8_f32 v196, v197, v198 op_sel:[0,0,1]
	s_waitcnt lgkmcnt(9)
	v_max_f32_e32 v197, v200, v200
	v_med3_f32 v198, v197, s5, v190
	v_max_f32_e32 v197, v201, v201
	v_med3_f32 v199, v197, s5, v190
	v_mov_b32_e32 v197, v141
	v_cvt_pk_fp8_f32 v197, v198, v199
	s_waitcnt lgkmcnt(8)
	v_max_f32_e32 v198, v202, v202
	v_max_f32_e32 v199, v203, v203
	v_med3_f32 v198, v198, s5, v190
	v_med3_f32 v199, v199, s5, v190
	s_waitcnt lgkmcnt(7)
	v_max_f32_e32 v140, v140, v140
	s_waitcnt lgkmcnt(6)
	v_max_f32_e32 v143, v143, v143
	v_cvt_pk_fp8_f32 v197, v198, v199 op_sel:[0,0,1]
	v_med3_f32 v140, v140, s5, v190
	v_med3_f32 v143, v143, s5, v190
	v_mov_b32_e32 v198, v141
	v_cvt_pk_fp8_f32 v198, v140, v143
	s_waitcnt lgkmcnt(5)
	v_max_f32_e32 v140, v191, v191
	s_waitcnt lgkmcnt(4)
	v_max_f32_e32 v143, v204, v204
	v_med3_f32 v140, v140, s5, v190
	v_med3_f32 v143, v143, s5, v190
	v_cvt_pk_fp8_f32 v198, v140, v143 op_sel:[0,0,1]
	s_waitcnt lgkmcnt(3)
	v_max_f32_e32 v140, v205, v205
	s_waitcnt lgkmcnt(2)
	v_max_f32_e32 v143, v206, v206
	v_med3_f32 v140, v140, s5, v190
	v_med3_f32 v143, v143, s5, v190
	v_mov_b32_e32 v199, v141
	v_cvt_pk_fp8_f32 v199, v140, v143
	s_waitcnt lgkmcnt(1)
	v_max_f32_e32 v140, v207, v207
	s_waitcnt lgkmcnt(0)
	v_max_f32_e32 v143, v208, v208
	v_med3_f32 v140, v140, s5, v190
	v_med3_f32 v143, v143, s5, v190
	v_cvt_pk_fp8_f32 v199, v140, v143 op_sel:[0,0,1]
	v_lshl_add_u64 v[144:145], s[8:9], 0, v[130:131]
	v_lshl_add_u64 v[200:201], v[144:145], 0, v[132:133]
	global_store_dwordx4 v[200:201], v[192:195], off nt
	s_nop 1
	v_lshl_add_u64 v[192:193], v[144:145], 0, v[134:135]
	global_store_dwordx4 v[192:193], v[196:199], off nt
	ds_read2_b32 v[192:193], v171 offset1:32
	ds_read2_b32 v[194:195], v171 offset0:64 offset1:96
	ds_read2_b32 v[196:197], v171 offset0:128 offset1:160
	ds_read2_b32 v[198:199], v171 offset0:192 offset1:224
	ds_read_b32 v140, v172
	ds_read_b32 v143, v173
	ds_read_b32 v191, v174
	ds_read_b32 v200, v175
	ds_read_b32 v201, v176
	ds_read_b32 v202, v177
	ds_read_b32 v203, v178
	ds_read_b32 v204, v179
	s_waitcnt lgkmcnt(11)
	v_max_f32_e32 v192, v192, v192
	v_med3_f32 v205, v192, s5, v190
	v_max_f32_e32 v192, v193, v193
	v_med3_f32 v193, v192, s5, v190
	v_mov_b32_e32 v192, v141
	v_cvt_pk_fp8_f32 v192, v205, v193
	s_waitcnt lgkmcnt(10)
	v_max_f32_e32 v193, v194, v194
	v_max_f32_e32 v194, v195, v195
	v_med3_f32 v193, v193, s5, v190
	v_med3_f32 v194, v194, s5, v190
	v_cvt_pk_fp8_f32 v192, v193, v194 op_sel:[0,0,1]
	s_waitcnt lgkmcnt(9)
	v_max_f32_e32 v193, v196, v196
	v_med3_f32 v194, v193, s5, v190
	v_max_f32_e32 v193, v197, v197
	v_med3_f32 v195, v193, s5, v190
	v_mov_b32_e32 v193, v141
	v_cvt_pk_fp8_f32 v193, v194, v195
	s_waitcnt lgkmcnt(8)
	v_max_f32_e32 v194, v198, v198
	v_max_f32_e32 v195, v199, v199
	v_med3_f32 v194, v194, s5, v190
	v_med3_f32 v195, v195, s5, v190
	s_waitcnt lgkmcnt(7)
	v_max_f32_e32 v140, v140, v140
	s_waitcnt lgkmcnt(6)
	v_max_f32_e32 v143, v143, v143
	v_cvt_pk_fp8_f32 v193, v194, v195 op_sel:[0,0,1]
	v_med3_f32 v140, v140, s5, v190
	v_med3_f32 v143, v143, s5, v190
	v_mov_b32_e32 v194, v141
	v_cvt_pk_fp8_f32 v194, v140, v143
	s_waitcnt lgkmcnt(5)
	v_max_f32_e32 v140, v191, v191
	s_waitcnt lgkmcnt(4)
	v_max_f32_e32 v143, v200, v200
	v_med3_f32 v140, v140, s5, v190
	v_med3_f32 v143, v143, s5, v190
	v_cvt_pk_fp8_f32 v194, v140, v143 op_sel:[0,0,1]
	s_waitcnt lgkmcnt(3)
	v_max_f32_e32 v140, v201, v201
	s_waitcnt lgkmcnt(2)
	v_max_f32_e32 v143, v202, v202
	v_med3_f32 v140, v140, s5, v190
	v_med3_f32 v143, v143, s5, v190
	v_mov_b32_e32 v195, v141
	v_cvt_pk_fp8_f32 v195, v140, v143
	s_waitcnt lgkmcnt(1)
	v_max_f32_e32 v140, v203, v203
	s_waitcnt lgkmcnt(0)
	v_max_f32_e32 v143, v204, v204
	v_med3_f32 v140, v140, s5, v190
	v_med3_f32 v143, v143, s5, v190
	v_cvt_pk_fp8_f32 v195, v140, v143 op_sel:[0,0,1]
	ds_read2_b32 v[196:197], v180 offset1:32
	ds_read2_b32 v[198:199], v180 offset0:64 offset1:96
	ds_read2_b32 v[200:201], v180 offset0:128 offset1:160
	ds_read2_b32 v[202:203], v180 offset0:192 offset1:224
	ds_read_b32 v140, v181
	ds_read_b32 v143, v182
	ds_read_b32 v191, v183
	ds_read_b32 v204, v184
	ds_read_b32 v205, v185
	ds_read_b32 v206, v186
	ds_read_b32 v207, v187
	ds_read_b32 v208, v188
	s_waitcnt lgkmcnt(11)
	v_max_f32_e32 v196, v196, v196
	v_med3_f32 v209, v196, s5, v190
	v_max_f32_e32 v196, v197, v197
	v_med3_f32 v197, v196, s5, v190
	v_mov_b32_e32 v196, v141
	v_cvt_pk_fp8_f32 v196, v209, v197
	s_waitcnt lgkmcnt(10)
	v_max_f32_e32 v197, v198, v198
	v_max_f32_e32 v198, v199, v199
	v_med3_f32 v197, v197, s5, v190
	v_med3_f32 v198, v198, s5, v190
	v_cvt_pk_fp8_f32 v196, v197, v198 op_sel:[0,0,1]
	s_waitcnt lgkmcnt(9)
	v_max_f32_e32 v197, v200, v200
	v_med3_f32 v198, v197, s5, v190
	v_max_f32_e32 v197, v201, v201
	v_med3_f32 v199, v197, s5, v190
	v_mov_b32_e32 v197, v141
	v_cvt_pk_fp8_f32 v197, v198, v199
	s_waitcnt lgkmcnt(8)
	v_max_f32_e32 v198, v202, v202
	v_max_f32_e32 v199, v203, v203
	v_med3_f32 v198, v198, s5, v190
	v_med3_f32 v199, v199, s5, v190
	s_waitcnt lgkmcnt(7)
	v_max_f32_e32 v140, v140, v140
	s_waitcnt lgkmcnt(6)
	v_max_f32_e32 v143, v143, v143
	v_cvt_pk_fp8_f32 v197, v198, v199 op_sel:[0,0,1]
	v_med3_f32 v140, v140, s5, v190
	v_med3_f32 v143, v143, s5, v190
	v_mov_b32_e32 v198, v141
	v_cvt_pk_fp8_f32 v198, v140, v143
	s_waitcnt lgkmcnt(5)
	v_max_f32_e32 v140, v191, v191
	s_waitcnt lgkmcnt(4)
	v_max_f32_e32 v143, v204, v204
	v_med3_f32 v140, v140, s5, v190
	v_med3_f32 v143, v143, s5, v190
	v_cvt_pk_fp8_f32 v198, v140, v143 op_sel:[0,0,1]
	s_waitcnt lgkmcnt(3)
	v_max_f32_e32 v140, v205, v205
	s_waitcnt lgkmcnt(2)
	v_max_f32_e32 v143, v206, v206
	v_med3_f32 v140, v140, s5, v190
	v_med3_f32 v143, v143, s5, v190
	v_mov_b32_e32 v199, v141
	v_cvt_pk_fp8_f32 v199, v140, v143
	s_waitcnt lgkmcnt(1)
	v_max_f32_e32 v140, v207, v207
	s_waitcnt lgkmcnt(0)
	v_max_f32_e32 v143, v208, v208
	v_med3_f32 v140, v140, s5, v190
	v_med3_f32 v143, v143, s5, v190
	v_cvt_pk_fp8_f32 v199, v140, v143 op_sel:[0,0,1]
	v_lshl_add_u64 v[200:201], v[144:145], 0, v[136:137]
	v_lshl_add_u64 v[144:145], v[144:145], 0, v[138:139]
	global_store_dwordx4 v[200:201], v[192:195], off nt
	global_store_dwordx4 v[144:145], v[196:199], off nt
	s_waitcnt lgkmcnt(0)
	s_xor_b64 s[10:11], s[10:11], -1
	s_andn2_b64 vcc, exec, s[10:11]
	s_cbranch_vccnz .LBB0_1412

; #define GAS __attribute__((address_space(1)))
; #define LAS __attribute__((address_space(3)))
; #define LDS_WAIT() asm volatile("s_waitcnt lgkmcnt(0)" ::: "memory")
; __device__ __forceinline__ void p8_issue(const TItem8& t, f32x4 (&v)[16], int lane) {
;     const GAS f32x4* src = (const GAS f32x4*)((const GAS float*)t.src + (size_t)(lane >> 3) * t.N + 4 * (lane & 7));
; #pragma unroll
;     for (int i = 0; i < 16; ++i) v[i] = __builtin_nontemporal_load(src + (size_t)(2 * i) * t.N);
; }
; __device__ __forceinline__ void p8_finish(const TItem8& t, const f32x4 (&v)[16], LAS float* scr, int lane) {
; #pragma unroll
;     for (int i = 0; i < 16; ++i) *(LAS f32x4*)(scr + (8 * i + (lane >> 3)) * 32 + (((lane & 7) ^ (i & 7)) << 2)) = v[i] * W8_SCALE;
;     LDS_WAIT(); asm volatile("" ::: "memory");
.LBB0_1480:
	s_lshl_b64 s[8:9], s[12:13], 11
	s_add_u32 s0, s18, s8
	v_mul_u32_u24_e32 v66, s22, v225
	s_addc_u32 s9, s19, s9
	v_lshlrev_b32_e32 v140, 2, v66
	s_add_u32 s8, s0, s16
	v_lshl_add_u64 v[66:67], s[14:15], 0, v[140:141]
	v_mov_b32_e32 v143, v141
	s_addc_u32 s9, s9, s17
	v_lshl_add_u64 v[66:67], v[66:67], 0, v[142:143]
	s_lshl_b32 s0, s22, 5
	v_lshl_add_u64 v[74:75], v[66:67], 0, s[0:1]
	global_load_dwordx4 v[66:69], v[66:67], off nt
	s_nop 0
	global_load_dwordx4 v[70:73], v[74:75], off nt
	v_lshl_add_u64 v[74:75], v[74:75], 0, s[0:1]
	v_lshl_add_u64 v[82:83], v[74:75], 0, s[0:1]
	global_load_dwordx4 v[74:77], v[74:75], off nt
	s_nop 0
	global_load_dwordx4 v[78:81], v[82:83], off nt
	v_lshl_add_u64 v[82:83], v[82:83], 0, s[0:1]
	v_lshl_add_u64 v[90:91], v[82:83], 0, s[0:1]
	global_load_dwordx4 v[82:85], v[82:83], off nt
	s_nop 0
	global_load_dwordx4 v[86:89], v[90:91], off nt
	v_lshl_add_u64 v[90:91], v[90:91], 0, s[0:1]
	v_lshl_add_u64 v[98:99], v[90:91], 0, s[0:1]
	v_lshl_add_u64 v[102:103], v[98:99], 0, s[0:1]
	v_lshl_add_u64 v[106:107], v[102:103], 0, s[0:1]
	v_lshl_add_u64 v[110:111], v[106:107], 0, s[0:1]
	v_lshl_add_u64 v[114:115], v[110:111], 0, s[0:1]
	v_lshl_add_u64 v[118:119], v[114:115], 0, s[0:1]
	v_lshl_add_u64 v[122:123], v[118:119], 0, s[0:1]
	v_lshl_add_u64 v[126:127], v[122:123], 0, s[0:1]
	global_load_dwordx4 v[90:93], v[90:91], off nt
	s_nop 0
	global_load_dwordx4 v[94:97], v[98:99], off nt
	s_nop 0
	global_load_dwordx4 v[98:101], v[102:103], off nt
	s_nop 0
	global_load_dwordx4 v[102:105], v[106:107], off nt
	s_nop 0
	global_load_dwordx4 v[106:109], v[110:111], off nt
	s_nop 0
	global_load_dwordx4 v[110:113], v[114:115], off nt
	s_nop 0
	global_load_dwordx4 v[114:117], v[118:119], off nt
	s_nop 0
	global_load_dwordx4 v[118:121], v[122:123], off nt
	s_nop 0
	global_load_dwordx4 v[122:125], v[126:127], off nt
	v_lshl_add_u64 v[126:127], v[126:127], 0, s[0:1]
	global_load_dwordx4 v[126:129], v[126:127], off nt
	s_waitcnt vmcnt(31)
	v_pk_mul_f32 v[192:193], v[4:5], s[4:5] op_sel_hi:[1,0]
	v_pk_mul_f32 v[190:191], v[2:3], s[4:5] op_sel_hi:[1,0]
	ds_write_b128 v1, v[190:193]
	s_waitcnt vmcnt(30)
	v_pk_mul_f32 v[192:193], v[8:9], s[4:5] op_sel_hi:[1,0]
	v_pk_mul_f32 v[190:191], v[6:7], s[4:5] op_sel_hi:[1,0]
	ds_write_b128 v146, v[190:193] offset:1024
	s_waitcnt vmcnt(29)
	v_pk_mul_f32 v[192:193], v[12:13], s[4:5] op_sel_hi:[1,0]
	v_pk_mul_f32 v[190:191], v[10:11], s[4:5] op_sel_hi:[1,0]
	ds_write_b128 v147, v[190:193] offset:2048
	s_waitcnt vmcnt(28)
	v_pk_mul_f32 v[192:193], v[16:17], s[4:5] op_sel_hi:[1,0]
	v_pk_mul_f32 v[190:191], v[14:15], s[4:5] op_sel_hi:[1,0]
	ds_write_b128 v148, v[190:193] offset:3072
	s_waitcnt vmcnt(27)
	v_pk_mul_f32 v[192:193], v[20:21], s[4:5] op_sel_hi:[1,0]
	v_pk_mul_f32 v[190:191], v[18:19], s[4:5] op_sel_hi:[1,0]
	ds_write_b128 v149, v[190:193] offset:4096
	s_waitcnt vmcnt(26)
	v_pk_mul_f32 v[192:193], v[24:25], s[4:5] op_sel_hi:[1,0]
	v_pk_mul_f32 v[190:191], v[22:23], s[4:5] op_sel_hi:[1,0]
	ds_write_b128 v150, v[190:193] offset:5120
	s_waitcnt vmcnt(25)
	v_pk_mul_f32 v[192:193], v[28:29], s[4:5] op_sel_hi:[1,0]
	v_pk_mul_f32 v[190:191], v[26:27], s[4:5] op_sel_hi:[1,0]
	ds_write_b128 v151, v[190:193] offset:6144
	s_waitcnt vmcnt(24)
	v_pk_mul_f32 v[192:193], v[32:33], s[4:5] op_sel_hi:[1,0]
	v_pk_mul_f32 v[190:191], v[30:31], s[4:5] op_sel_hi:[1,0]
	ds_write_b128 v152, v[190:193] offset:7168
	s_waitcnt vmcnt(23)
	v_pk_mul_f32 v[192:193], v[36:37], s[4:5] op_sel_hi:[1,0]
	v_pk_mul_f32 v[190:191], v[34:35], s[4:5] op_sel_hi:[1,0]
	ds_write_b128 v1, v[190:193] offset:8192
	s_waitcnt vmcnt(22)
	v_pk_mul_f32 v[192:193], v[40:41], s[4:5] op_sel_hi:[1,0]
	v_pk_mul_f32 v[190:191], v[38:39], s[4:5] op_sel_hi:[1,0]
	ds_write_b128 v146, v[190:193] offset:9216
	s_waitcnt vmcnt(21)
	v_pk_mul_f32 v[192:193], v[44:45], s[4:5] op_sel_hi:[1,0]
	v_pk_mul_f32 v[190:191], v[42:43], s[4:5] op_sel_hi:[1,0]
	ds_write_b128 v147, v[190:193] offset:10240
	s_waitcnt vmcnt(20)
	v_pk_mul_f32 v[192:193], v[48:49], s[4:5] op_sel_hi:[1,0]
	v_pk_mul_f32 v[190:191], v[46:47], s[4:5] op_sel_hi:[1,0]
	ds_write_b128 v148, v[190:193] offset:11264
	s_waitcnt vmcnt(19)
	v_pk_mul_f32 v[192:193], v[52:53], s[4:5] op_sel_hi:[1,0]
	v_pk_mul_f32 v[190:191], v[50:51], s[4:5] op_sel_hi:[1,0]
	ds_write_b128 v149, v[190:193] offset:12288
	s_waitcnt vmcnt(18)
	v_pk_mul_f32 v[192:193], v[56:57], s[4:5] op_sel_hi:[1,0]
	v_pk_mul_f32 v[190:191], v[54:55], s[4:5] op_sel_hi:[1,0]
	ds_write_b128 v150, v[190:193] offset:13312
	s_waitcnt vmcnt(17)
	v_pk_mul_f32 v[192:193], v[60:61], s[4:5] op_sel_hi:[1,0]
	v_pk_mul_f32 v[190:191], v[58:59], s[4:5] op_sel_hi:[1,0]
	ds_write_b128 v151, v[190:193] offset:14336
	s_waitcnt vmcnt(16)
	v_pk_mul_f32 v[192:193], v[64:65], s[4:5] op_sel_hi:[1,0]
	v_pk_mul_f32 v[190:191], v[62:63], s[4:5] op_sel_hi:[1,0]
	ds_write_b128 v152, v[190:193] offset:15360
	s_branch .Lcv1_1_1481

; #define GAS __attribute__((address_space(1)))
; #define LDS_WAIT() asm volatile("s_waitcnt lgkmcnt(0)" ::: "memory")
; __device__ __forceinline__ void p8_finish(const TItem8& t, const f32x4 (&v)[16], LAS float* scr, int lane) {
;     ...
;     LDS_WAIT(); asm volatile("" ::: "memory");
;     const int c = lane & 7;
; #pragma unroll
;     for (int j = 0; j < 4; ++j) { const int n = (lane >> 3) + 8 * j; float x[16];
; #pragma unroll
;         for (int i = 0; i < 16; ++i) { const int k = 16 * c + i; x[i] = scr[k * 32 + ((((n >> 2) ^ ((k >> 3) & 7)) << 2) | (n & 3))]; }
;         int w[4];
; #pragma unroll
;         for (int g = 0; g < 4; ++g) { int q = 0; q = __builtin_amdgcn_cvt_pk_fp8_f32(fminf(fmaxf(x[4 * g], -448.f), 448.f), fminf(fmaxf(x[4 * g + 1], -448.f), 448.f), q, false);
;             q = __builtin_amdgcn_cvt_pk_fp8_f32(fminf(fmaxf(x[4 * g + 2], -448.f), 448.f), fminf(fmaxf(x[4 * g + 3], -448.f), 448.f), q, true); w[g] = q; }
;         v4u o; o.x = (unsigned)w[0]; o.y = (unsigned)w[1]; o.z = (unsigned)w[2]; o.w = (unsigned)w[3];
;         __builtin_nontemporal_store(o, (GAS v4u*)(t.dst + (size_t)n * t.Kd + 16 * c)); }
.Lcv1_1_1481:
	s_waitcnt lgkmcnt(0)
	ds_read2_b32 v[190:191], v153 offset1:32
	ds_read2_b32 v[192:193], v153 offset0:64 offset1:96
	ds_read2_b32 v[194:195], v153 offset0:128 offset1:160
	ds_read2_b32 v[196:197], v153 offset0:192 offset1:224
	ds_read_b32 v140, v154
	ds_read_b32 v143, v155
	ds_read_b32 v198, v156
	ds_read_b32 v199, v157
	ds_read_b32 v200, v158
	ds_read_b32 v201, v159
	ds_read_b32 v202, v160
	ds_read_b32 v203, v161
	s_waitcnt lgkmcnt(11)
	v_max_f32_e32 v190, v190, v190
	v_med3_f32 v204, v190, s5, v189
	v_max_f32_e32 v190, v191, v191
	v_med3_f32 v191, v190, s5, v189
	v_mov_b32_e32 v190, 0
	v_cvt_pk_fp8_f32 v190, v204, v191
	s_waitcnt lgkmcnt(10)
	v_max_f32_e32 v191, v192, v192
	v_max_f32_e32 v192, v193, v193
	v_med3_f32 v191, v191, s5, v189
	v_med3_f32 v192, v192, s5, v189
	v_cvt_pk_fp8_f32 v190, v191, v192 op_sel:[0,0,1]
	s_waitcnt lgkmcnt(9)
	v_max_f32_e32 v191, v194, v194
	v_med3_f32 v192, v191, s5, v189
	v_max_f32_e32 v191, v195, v195
	v_med3_f32 v193, v191, s5, v189
	v_mov_b32_e32 v191, 0
	v_cvt_pk_fp8_f32 v191, v192, v193
	s_waitcnt lgkmcnt(8)
	v_max_f32_e32 v192, v196, v196
	v_max_f32_e32 v193, v197, v197
	v_med3_f32 v192, v192, s5, v189
	v_med3_f32 v193, v193, s5, v189
	s_waitcnt lgkmcnt(7)
	v_max_f32_e32 v140, v140, v140
	s_waitcnt lgkmcnt(6)
	v_max_f32_e32 v143, v143, v143
	v_cvt_pk_fp8_f32 v191, v192, v193 op_sel:[0,0,1]
	v_med3_f32 v140, v140, s5, v189
	v_med3_f32 v143, v143, s5, v189
	v_mov_b32_e32 v192, 0
	v_cvt_pk_fp8_f32 v192, v140, v143
	s_waitcnt lgkmcnt(5)
	v_max_f32_e32 v140, v198, v198
	s_waitcnt lgkmcnt(4)
	v_max_f32_e32 v143, v199, v199
	v_med3_f32 v140, v140, s5, v189
	v_med3_f32 v143, v143, s5, v189
	v_cvt_pk_fp8_f32 v192, v140, v143 op_sel:[0,0,1]
	s_waitcnt lgkmcnt(3)
	v_max_f32_e32 v140, v200, v200
	s_waitcnt lgkmcnt(2)
	v_max_f32_e32 v143, v201, v201
	v_med3_f32 v140, v140, s5, v189
	v_med3_f32 v143, v143, s5, v189
	v_mov_b32_e32 v193, 0
	v_cvt_pk_fp8_f32 v193, v140, v143
	s_waitcnt lgkmcnt(1)
	v_max_f32_e32 v140, v202, v202
	s_waitcnt lgkmcnt(0)
	v_max_f32_e32 v143, v203, v203
	v_med3_f32 v140, v140, s5, v189
	v_med3_f32 v143, v143, s5, v189
	v_cvt_pk_fp8_f32 v193, v140, v143 op_sel:[0,0,1]
	ds_read2_b32 v[194:195], v162 offset1:32
	ds_read2_b32 v[196:197], v162 offset0:64 offset1:96
	ds_read2_b32 v[198:199], v162 offset0:128 offset1:160
	ds_read2_b32 v[200:201], v162 offset0:192 offset1:224
	ds_read_b32 v140, v163
	ds_read_b32 v143, v164
	ds_read_b32 v202, v165
	ds_read_b32 v203, v166
	ds_read_b32 v204, v167
	ds_read_b32 v205, v168
	ds_read_b32 v206, v169
	ds_read_b32 v207, v170
	s_waitcnt lgkmcnt(11)
	v_max_f32_e32 v194, v194, v194
	v_med3_f32 v208, v194, s5, v189
	v_max_f32_e32 v194, v195, v195
	v_med3_f32 v195, v194, s5, v189
	v_mov_b32_e32 v194, 0
	v_cvt_pk_fp8_f32 v194, v208, v195
	s_waitcnt lgkmcnt(10)
	v_max_f32_e32 v195, v196, v196
	v_max_f32_e32 v196, v197, v197
	v_med3_f32 v195, v195, s5, v189
	v_med3_f32 v196, v196, s5, v189
	v_cvt_pk_fp8_f32 v194, v195, v196 op_sel:[0,0,1]
	s_waitcnt lgkmcnt(9)
	v_max_f32_e32 v195, v198, v198
	v_med3_f32 v196, v195, s5, v189
	v_max_f32_e32 v195, v199, v199
	v_med3_f32 v197, v195, s5, v189
	v_mov_b32_e32 v195, 0
	v_cvt_pk_fp8_f32 v195, v196, v197
	s_waitcnt lgkmcnt(8)
	v_max_f32_e32 v196, v200, v200
	v_max_f32_e32 v197, v201, v201
	v_med3_f32 v196, v196, s5, v189
	v_med3_f32 v197, v197, s5, v189
	s_waitcnt lgkmcnt(7)
	v_max_f32_e32 v140, v140, v140
	s_waitcnt lgkmcnt(6)
	v_max_f32_e32 v143, v143, v143
	v_cvt_pk_fp8_f32 v195, v196, v197 op_sel:[0,0,1]
	v_med3_f32 v140, v140, s5, v189
	v_med3_f32 v143, v143, s5, v189
	v_mov_b32_e32 v196, 0
	v_cvt_pk_fp8_f32 v196, v140, v143
	s_waitcnt lgkmcnt(5)
	v_max_f32_e32 v140, v202, v202
	s_waitcnt lgkmcnt(4)
	v_max_f32_e32 v143, v203, v203
	v_med3_f32 v140, v140, s5, v189
	v_med3_f32 v143, v143, s5, v189
	v_cvt_pk_fp8_f32 v196, v140, v143 op_sel:[0,0,1]
	s_waitcnt lgkmcnt(3)
	v_max_f32_e32 v140, v204, v204
	s_waitcnt lgkmcnt(2)
	v_max_f32_e32 v143, v205, v205
	v_med3_f32 v140, v140, s5, v189
	v_med3_f32 v143, v143, s5, v189
	v_mov_b32_e32 v197, 0
	v_cvt_pk_fp8_f32 v197, v140, v143
	s_waitcnt lgkmcnt(1)
	v_max_f32_e32 v140, v206, v206
	s_waitcnt lgkmcnt(0)
	v_max_f32_e32 v143, v207, v207
	v_med3_f32 v140, v140, s5, v189
	v_med3_f32 v143, v143, s5, v189
	v_cvt_pk_fp8_f32 v197, v140, v143 op_sel:[0,0,1]
	v_lshl_add_u64 v[144:145], s[6:7], 0, v[130:131]
	v_lshl_add_u64 v[198:199], v[144:145], 0, v[132:133]
	global_store_dwordx4 v[198:199], v[190:193], off nt
	s_andn2_b64 vcc, exec, s[10:11]
	s_mov_b64 s[10:11], 0
	v_lshl_add_u64 v[190:191], v[144:145], 0, v[134:135]
	global_store_dwordx4 v[190:191], v[194:197], off nt
	ds_read2_b32 v[190:191], v171 offset1:32
	ds_read2_b32 v[192:193], v171 offset0:64 offset1:96
	ds_read2_b32 v[194:195], v171 offset0:128 offset1:160
	ds_read2_b32 v[196:197], v171 offset0:192 offset1:224
	ds_read_b32 v140, v172
	ds_read_b32 v143, v173
	ds_read_b32 v198, v174
	ds_read_b32 v199, v175
	ds_read_b32 v200, v176
	ds_read_b32 v201, v177
	ds_read_b32 v202, v178
	ds_read_b32 v203, v179
	s_waitcnt lgkmcnt(11)
; #define GAS __attribute__((address_space(1)))
; #define LDS_WAIT() asm volatile("s_waitcnt lgkmcnt(0)" ::: "memory")
; __device__ __forceinline__ TItem8 p8_decode(const Args& args, unsigned char* ws, int it) {
;     TItem8 t;
;     if (it >= P8_N) { const int j = it - P8_N; it = (P8_E0 + j / P8_DN1) * (P8_GU1 + P8_DN1) + P8_GU1 + j % P8_DN1; }
;     else if (it >= P8_E0 * (P8_GU1 + P8_DN1)) { const int r = it - P8_E0 * (P8_GU1 + P8_DN1); it = (P8_E0 + r / P8_GU1) * (P8_GU1 + P8_DN1) + r % P8_GU1; }
;     const int e = it / (P8_GU1 + P8_DN1), q = it % (P8_GU1 + P8_DN1);
;     if (q < P8_GU1) { const int kb = q / 128, nb = q % 128, n0 = nb * 32;
;         const int dr = (n0 < DE) ? (256 * (n0 / 128) + (n0 % 128)) : (256 * ((n0 - DE) / 128) + 128 + ((n0 - DE) % 128));
;         t.src = args.in[25] + (size_t)e * D * 2 * DE + (size_t)(kb * 128) * (2 * DE) + n0; t.N = 2 * DE; t.dst = ws + WS_WGU + (size_t)e * 2 * DE * D + (size_t)dr * D + kb * 128; t.Kd = D; }
; __device__ __forceinline__ void p8_finish(const TItem8& t, const f32x4 (&v)[16], LAS float* scr, int lane) {
;     ...
;     for (int j = 0; j < 4; ++j) { const int n = (lane >> 3) + 8 * j; float x[16];
; #pragma unroll
;         for (int i = 0; i < 16; ++i) { const int k = 16 * c + i; x[i] = scr[k * 32 + ((((n >> 2) ^ ((k >> 3) & 7)) << 2) | (n & 3))]; }
;         int w[4];
; #pragma unroll
;         for (int g = 0; g < 4; ++g) { int q = 0; q = __builtin_amdgcn_cvt_pk_fp8_f32(fminf(fmaxf(x[4 * g], -448.f), 448.f), fminf(fmaxf(x[4 * g + 1], -448.f), 448.f), q, false);
;             q = __builtin_amdgcn_cvt_pk_fp8_f32(fminf(fmaxf(x[4 * g + 2], -448.f), 448.f), fminf(fmaxf(x[4 * g + 3], -448.f), 448.f), q, true); w[g] = q; }
;         v4u o; o.x = (unsigned)w[0]; o.y = (unsigned)w[1]; o.z = (unsigned)w[2]; o.w = (unsigned)w[3];
;         __builtin_nontemporal_store(o, (GAS v4u*)(t.dst + (size_t)n * t.Kd + 16 * c)); }
;     LDS_WAIT(); asm volatile("" ::: "memory");
	v_max_f32_e32 v190, v190, v190
	v_med3_f32 v204, v190, s5, v189
	v_max_f32_e32 v190, v191, v191
	v_med3_f32 v191, v190, s5, v189
	v_mov_b32_e32 v190, 0
	v_cvt_pk_fp8_f32 v190, v204, v191
	s_waitcnt lgkmcnt(10)
	v_max_f32_e32 v191, v192, v192
	v_max_f32_e32 v192, v193, v193
	v_med3_f32 v191, v191, s5, v189
	v_med3_f32 v192, v192, s5, v189
	v_cvt_pk_fp8_f32 v190, v191, v192 op_sel:[0,0,1]
	s_waitcnt lgkmcnt(9)
	v_max_f32_e32 v191, v194, v194
	v_med3_f32 v192, v191, s5, v189
	v_max_f32_e32 v191, v195, v195
	v_med3_f32 v193, v191, s5, v189
	v_mov_b32_e32 v191, 0
	v_cvt_pk_fp8_f32 v191, v192, v193
	s_waitcnt lgkmcnt(8)
	v_max_f32_e32 v192, v196, v196
	v_max_f32_e32 v193, v197, v197
	v_med3_f32 v192, v192, s5, v189
	v_med3_f32 v193, v193, s5, v189
	s_waitcnt lgkmcnt(7)
	v_max_f32_e32 v140, v140, v140
	s_waitcnt lgkmcnt(6)
	v_max_f32_e32 v143, v143, v143
	v_cvt_pk_fp8_f32 v191, v192, v193 op_sel:[0,0,1]
	v_med3_f32 v140, v140, s5, v189
	v_med3_f32 v143, v143, s5, v189
	v_mov_b32_e32 v192, 0
	v_cvt_pk_fp8_f32 v192, v140, v143
	s_waitcnt lgkmcnt(5)
	v_max_f32_e32 v140, v198, v198
	s_waitcnt lgkmcnt(4)
	v_max_f32_e32 v143, v199, v199
	v_med3_f32 v140, v140, s5, v189
	v_med3_f32 v143, v143, s5, v189
	v_cvt_pk_fp8_f32 v192, v140, v143 op_sel:[0,0,1]
	s_waitcnt lgkmcnt(3)
	v_max_f32_e32 v140, v200, v200
	s_waitcnt lgkmcnt(2)
	v_max_f32_e32 v143, v201, v201
	v_med3_f32 v140, v140, s5, v189
	v_med3_f32 v143, v143, s5, v189
	v_mov_b32_e32 v193, 0
	v_cvt_pk_fp8_f32 v193, v140, v143
	s_waitcnt lgkmcnt(1)
	v_max_f32_e32 v140, v202, v202
	s_waitcnt lgkmcnt(0)
	v_max_f32_e32 v143, v203, v203
	v_med3_f32 v140, v140, s5, v189
	v_med3_f32 v143, v143, s5, v189
	v_cvt_pk_fp8_f32 v193, v140, v143 op_sel:[0,0,1]
	ds_read2_b32 v[194:195], v180 offset1:32
	ds_read2_b32 v[196:197], v180 offset0:64 offset1:96
	ds_read2_b32 v[198:199], v180 offset0:128 offset1:160
	ds_read2_b32 v[200:201], v180 offset0:192 offset1:224
	ds_read_b32 v140, v181
	ds_read_b32 v143, v182
	ds_read_b32 v202, v183
	ds_read_b32 v203, v184
	ds_read_b32 v204, v185
	ds_read_b32 v205, v186
	ds_read_b32 v206, v187
	ds_read_b32 v207, v188
	s_waitcnt lgkmcnt(11)
	v_max_f32_e32 v194, v194, v194
	v_med3_f32 v208, v194, s5, v189
	v_max_f32_e32 v194, v195, v195
	v_med3_f32 v195, v194, s5, v189
	v_mov_b32_e32 v194, 0
	v_cvt_pk_fp8_f32 v194, v208, v195
	s_waitcnt lgkmcnt(10)
	v_max_f32_e32 v195, v196, v196
	v_max_f32_e32 v196, v197, v197
	v_med3_f32 v195, v195, s5, v189
	v_med3_f32 v196, v196, s5, v189
	v_cvt_pk_fp8_f32 v194, v195, v196 op_sel:[0,0,1]
	s_waitcnt lgkmcnt(9)
	v_max_f32_e32 v195, v198, v198
	v_med3_f32 v196, v195, s5, v189
	v_max_f32_e32 v195, v199, v199
	v_med3_f32 v197, v195, s5, v189
	v_mov_b32_e32 v195, 0
	v_cvt_pk_fp8_f32 v195, v196, v197
	s_waitcnt lgkmcnt(8)
	v_max_f32_e32 v196, v200, v200
	v_max_f32_e32 v197, v201, v201
	v_med3_f32 v196, v196, s5, v189
	v_med3_f32 v197, v197, s5, v189
	s_waitcnt lgkmcnt(7)
	v_max_f32_e32 v140, v140, v140
	s_waitcnt lgkmcnt(6)
	v_max_f32_e32 v143, v143, v143
	v_cvt_pk_fp8_f32 v195, v196, v197 op_sel:[0,0,1]
	v_med3_f32 v140, v140, s5, v189
	v_med3_f32 v143, v143, s5, v189
	v_mov_b32_e32 v196, 0
	v_cvt_pk_fp8_f32 v196, v140, v143
	s_waitcnt lgkmcnt(5)
	v_max_f32_e32 v140, v202, v202
	s_waitcnt lgkmcnt(4)
	v_max_f32_e32 v143, v203, v203
	v_med3_f32 v140, v140, s5, v189
	v_med3_f32 v143, v143, s5, v189
	v_cvt_pk_fp8_f32 v196, v140, v143 op_sel:[0,0,1]
	s_waitcnt lgkmcnt(3)
	v_max_f32_e32 v140, v204, v204
	s_waitcnt lgkmcnt(2)
	v_max_f32_e32 v143, v205, v205
	v_med3_f32 v140, v140, s5, v189
	v_med3_f32 v143, v143, s5, v189
	v_mov_b32_e32 v197, 0
	v_cvt_pk_fp8_f32 v197, v140, v143
	s_waitcnt lgkmcnt(1)
	v_max_f32_e32 v140, v206, v206
	s_waitcnt lgkmcnt(0)
	v_max_f32_e32 v143, v207, v207
	v_med3_f32 v140, v140, s5, v189
	v_med3_f32 v143, v143, s5, v189
	v_cvt_pk_fp8_f32 v197, v140, v143 op_sel:[0,0,1]
	v_lshl_add_u64 v[198:199], v[144:145], 0, v[136:137]
	v_lshl_add_u64 v[144:145], v[144:145], 0, v[138:139]
	global_store_dwordx4 v[198:199], v[190:193], off nt
	global_store_dwordx4 v[144:145], v[194:197], off nt
	s_waitcnt lgkmcnt(0)
	s_cbranch_vccnz .LBB0_1464
	s_add_i32 s26, s26, 2
	s_mul_i32 s0, s26, s25
	s_add_i32 s0, s0, s24
	s_cmp_lt_i32 s0, 0x18000
	s_cselect_b64 s[10:11], -1, 0
	s_cmp_gt_i32 s0, 0x17fff
	s_cbranch_scc1 .LBB0_1498
	s_cmp_lt_i32 s0, 0x16400
	s_mov_b64 s[6:7], -1
	s_cbranch_scc0 .LBB0_1487
	s_cmp_lt_i32 s0, 0x12c00
	s_mov_b32 s12, s0
	s_cbranch_scc1 .LBB0_1486
	s_add_i32 s6, s0, 0xfffed400
	s_lshr_b32 s7, s6, 11
	s_mulk_i32 s7, 0xc00
	s_and_b32 s6, s6, 0x7ff
	s_add_i32 s6, s6, s7
	s_add_i32 s12, s6, 0x12c00

; #define GAS __attribute__((address_space(1)))
; #define LAS __attribute__((address_space(3)))
; #define LDS_WAIT() asm volatile("s_waitcnt lgkmcnt(0)" ::: "memory")
; __device__ __forceinline__ void p8_issue(const TItem8& t, f32x4 (&v)[16], int lane) {
;     const GAS f32x4* src = (const GAS f32x4*)((const GAS float*)t.src + (size_t)(lane >> 3) * t.N + 4 * (lane & 7));
; #pragma unroll
;     for (int i = 0; i < 16; ++i) v[i] = __builtin_nontemporal_load(src + (size_t)(2 * i) * t.N);
; }
; __device__ __forceinline__ void p8_finish(const TItem8& t, const f32x4 (&v)[16], LAS float* scr, int lane) {
; #pragma unroll
;     for (int i = 0; i < 16; ++i) *(LAS f32x4*)(scr + (8 * i + (lane >> 3)) * 32 + (((lane & 7) ^ (i & 7)) << 2)) = v[i] * W8_SCALE;
;     LDS_WAIT(); asm volatile("" ::: "memory");
.LBB0_1497:
	s_lshl_b64 s[6:7], s[12:13], 11
	s_add_u32 s0, s18, s6
	v_mul_u32_u24_e32 v2, s22, v225
	s_addc_u32 s7, s19, s7
	v_lshlrev_b32_e32 v140, 2, v2
	s_add_u32 s6, s0, s16
	v_lshl_add_u64 v[2:3], s[14:15], 0, v[140:141]
	v_mov_b32_e32 v143, v141
	s_addc_u32 s7, s7, s17
	v_lshl_add_u64 v[2:3], v[2:3], 0, v[142:143]
	s_lshl_b32 s0, s22, 5
	v_lshl_add_u64 v[10:11], v[2:3], 0, s[0:1]
	global_load_dwordx4 v[2:5], v[2:3], off nt
	s_nop 0
	global_load_dwordx4 v[6:9], v[10:11], off nt
	v_lshl_add_u64 v[10:11], v[10:11], 0, s[0:1]
	v_lshl_add_u64 v[18:19], v[10:11], 0, s[0:1]
	global_load_dwordx4 v[10:13], v[10:11], off nt
	s_nop 0
	global_load_dwordx4 v[14:17], v[18:19], off nt
	v_lshl_add_u64 v[18:19], v[18:19], 0, s[0:1]
	v_lshl_add_u64 v[26:27], v[18:19], 0, s[0:1]
	global_load_dwordx4 v[18:21], v[18:19], off nt
	s_nop 0
	global_load_dwordx4 v[22:25], v[26:27], off nt
	v_lshl_add_u64 v[26:27], v[26:27], 0, s[0:1]
	v_lshl_add_u64 v[34:35], v[26:27], 0, s[0:1]
	v_lshl_add_u64 v[38:39], v[34:35], 0, s[0:1]
	v_lshl_add_u64 v[42:43], v[38:39], 0, s[0:1]
	v_lshl_add_u64 v[46:47], v[42:43], 0, s[0:1]
	v_lshl_add_u64 v[50:51], v[46:47], 0, s[0:1]
	v_lshl_add_u64 v[54:55], v[50:51], 0, s[0:1]
	v_lshl_add_u64 v[58:59], v[54:55], 0, s[0:1]
	v_lshl_add_u64 v[62:63], v[58:59], 0, s[0:1]
	global_load_dwordx4 v[26:29], v[26:27], off nt
	s_nop 0
	global_load_dwordx4 v[30:33], v[34:35], off nt
	s_nop 0
	global_load_dwordx4 v[34:37], v[38:39], off nt
	s_nop 0
	global_load_dwordx4 v[38:41], v[42:43], off nt
	s_nop 0
	global_load_dwordx4 v[42:45], v[46:47], off nt
	s_nop 0
	global_load_dwordx4 v[46:49], v[50:51], off nt
	s_nop 0
	global_load_dwordx4 v[50:53], v[54:55], off nt
	s_nop 0
	global_load_dwordx4 v[54:57], v[58:59], off nt
	s_nop 0
	global_load_dwordx4 v[58:61], v[62:63], off nt
	v_lshl_add_u64 v[62:63], v[62:63], 0, s[0:1]
	global_load_dwordx4 v[62:65], v[62:63], off nt
	s_waitcnt vmcnt(35)
	v_pk_mul_f32 v[192:193], v[68:69], s[4:5] op_sel_hi:[1,0]
	v_pk_mul_f32 v[190:191], v[66:67], s[4:5] op_sel_hi:[1,0]
	ds_write_b128 v1, v[190:193]
	s_waitcnt vmcnt(34)
	v_pk_mul_f32 v[192:193], v[72:73], s[4:5] op_sel_hi:[1,0]
	v_pk_mul_f32 v[190:191], v[70:71], s[4:5] op_sel_hi:[1,0]
	ds_write_b128 v146, v[190:193] offset:1024
	s_waitcnt vmcnt(33)
	v_pk_mul_f32 v[192:193], v[76:77], s[4:5] op_sel_hi:[1,0]
	v_pk_mul_f32 v[190:191], v[74:75], s[4:5] op_sel_hi:[1,0]
	ds_write_b128 v147, v[190:193] offset:2048
	s_waitcnt vmcnt(32)
	v_pk_mul_f32 v[192:193], v[80:81], s[4:5] op_sel_hi:[1,0]
	v_pk_mul_f32 v[190:191], v[78:79], s[4:5] op_sel_hi:[1,0]
	ds_write_b128 v148, v[190:193] offset:3072
	s_waitcnt vmcnt(31)
	v_pk_mul_f32 v[192:193], v[84:85], s[4:5] op_sel_hi:[1,0]
	v_pk_mul_f32 v[190:191], v[82:83], s[4:5] op_sel_hi:[1,0]
	ds_write_b128 v149, v[190:193] offset:4096
	s_waitcnt vmcnt(30)
	v_pk_mul_f32 v[192:193], v[88:89], s[4:5] op_sel_hi:[1,0]
	v_pk_mul_f32 v[190:191], v[86:87], s[4:5] op_sel_hi:[1,0]
	ds_write_b128 v150, v[190:193] offset:5120
	s_waitcnt vmcnt(29)
	v_pk_mul_f32 v[192:193], v[92:93], s[4:5] op_sel_hi:[1,0]
	v_pk_mul_f32 v[190:191], v[90:91], s[4:5] op_sel_hi:[1,0]
	ds_write_b128 v151, v[190:193] offset:6144
	s_waitcnt vmcnt(28)
	v_pk_mul_f32 v[192:193], v[96:97], s[4:5] op_sel_hi:[1,0]
	v_pk_mul_f32 v[190:191], v[94:95], s[4:5] op_sel_hi:[1,0]
	ds_write_b128 v152, v[190:193] offset:7168
	s_waitcnt vmcnt(27)
	v_pk_mul_f32 v[192:193], v[100:101], s[4:5] op_sel_hi:[1,0]
	v_pk_mul_f32 v[190:191], v[98:99], s[4:5] op_sel_hi:[1,0]
	ds_write_b128 v1, v[190:193] offset:8192
	s_waitcnt vmcnt(26)
	v_pk_mul_f32 v[192:193], v[104:105], s[4:5] op_sel_hi:[1,0]
	v_pk_mul_f32 v[190:191], v[102:103], s[4:5] op_sel_hi:[1,0]
	ds_write_b128 v146, v[190:193] offset:9216
	s_waitcnt vmcnt(25)
	v_pk_mul_f32 v[192:193], v[108:109], s[4:5] op_sel_hi:[1,0]
	v_pk_mul_f32 v[190:191], v[106:107], s[4:5] op_sel_hi:[1,0]
	ds_write_b128 v147, v[190:193] offset:10240
	s_waitcnt vmcnt(24)
	v_pk_mul_f32 v[192:193], v[112:113], s[4:5] op_sel_hi:[1,0]
	v_pk_mul_f32 v[190:191], v[110:111], s[4:5] op_sel_hi:[1,0]
	ds_write_b128 v148, v[190:193] offset:11264
	s_waitcnt vmcnt(23)
	v_pk_mul_f32 v[192:193], v[116:117], s[4:5] op_sel_hi:[1,0]
	v_pk_mul_f32 v[190:191], v[114:115], s[4:5] op_sel_hi:[1,0]
	ds_write_b128 v149, v[190:193] offset:12288
	s_waitcnt vmcnt(22)
	v_pk_mul_f32 v[192:193], v[120:121], s[4:5] op_sel_hi:[1,0]
	v_pk_mul_f32 v[190:191], v[118:119], s[4:5] op_sel_hi:[1,0]
	ds_write_b128 v150, v[190:193] offset:13312
	s_waitcnt vmcnt(21)
	v_pk_mul_f32 v[192:193], v[124:125], s[4:5] op_sel_hi:[1,0]
	v_pk_mul_f32 v[190:191], v[122:123], s[4:5] op_sel_hi:[1,0]
	ds_write_b128 v151, v[190:193] offset:14336
	s_waitcnt vmcnt(20)
	v_pk_mul_f32 v[192:193], v[128:129], s[4:5] op_sel_hi:[1,0]
	v_pk_mul_f32 v[190:191], v[126:127], s[4:5] op_sel_hi:[1,0]
	ds_write_b128 v152, v[190:193] offset:15360
	s_branch .Lcv2_1_1481
; #define GAS __attribute__((address_space(1)))
; #define LAS __attribute__((address_space(3)))
; #define LDS_WAIT() asm volatile("s_waitcnt lgkmcnt(0)" ::: "memory")
; __device__ __forceinline__ void p8_finish(const TItem8& t, const f32x4 (&v)[16], LAS float* scr, int lane) {
; #pragma unroll
;     for (int i = 0; i < 16; ++i) *(LAS f32x4*)(scr + (8 * i + (lane >> 3)) * 32 + (((lane & 7) ^ (i & 7)) << 2)) = v[i] * W8_SCALE;
;     LDS_WAIT(); asm volatile("" ::: "memory");
;     const int c = lane & 7;
; #pragma unroll
;     for (int j = 0; j < 4; ++j) { const int n = (lane >> 3) + 8 * j; float x[16];
; #pragma unroll
;         for (int i = 0; i < 16; ++i) { const int k = 16 * c + i; x[i] = scr[k * 32 + ((((n >> 2) ^ ((k >> 3) & 7)) << 2) | (n & 3))]; }
;         int w[4];
; #pragma unroll
;         for (int g = 0; g < 4; ++g) { int q = 0; q = __builtin_amdgcn_cvt_pk_fp8_f32(fminf(fmaxf(x[4 * g], -448.f), 448.f), fminf(fmaxf(x[4 * g + 1], -448.f), 448.f), q, false);
;             q = __builtin_amdgcn_cvt_pk_fp8_f32(fminf(fmaxf(x[4 * g + 2], -448.f), 448.f), fminf(fmaxf(x[4 * g + 3], -448.f), 448.f), q, true); w[g] = q; }
;         v4u o; o.x = (unsigned)w[0]; o.y = (unsigned)w[1]; o.z = (unsigned)w[2]; o.w = (unsigned)w[3];
;         __builtin_nontemporal_store(o, (GAS v4u*)(t.dst + (size_t)n * t.Kd + 16 * c)); }
.LBB0_1498:
	s_waitcnt vmcnt(19)
	v_pk_mul_f32 v[192:193], v[68:69], s[4:5] op_sel_hi:[1,0]
	v_pk_mul_f32 v[190:191], v[66:67], s[4:5] op_sel_hi:[1,0]
	ds_write_b128 v1, v[190:193]
	s_waitcnt vmcnt(18)
	v_pk_mul_f32 v[192:193], v[72:73], s[4:5] op_sel_hi:[1,0]
	v_pk_mul_f32 v[190:191], v[70:71], s[4:5] op_sel_hi:[1,0]
	ds_write_b128 v146, v[190:193] offset:1024
	s_waitcnt vmcnt(17)
	v_pk_mul_f32 v[192:193], v[76:77], s[4:5] op_sel_hi:[1,0]
	v_pk_mul_f32 v[190:191], v[74:75], s[4:5] op_sel_hi:[1,0]
	ds_write_b128 v147, v[190:193] offset:2048
	s_waitcnt vmcnt(16)
	v_pk_mul_f32 v[192:193], v[80:81], s[4:5] op_sel_hi:[1,0]
	v_pk_mul_f32 v[190:191], v[78:79], s[4:5] op_sel_hi:[1,0]
	ds_write_b128 v148, v[190:193] offset:3072
	s_waitcnt vmcnt(15)
	v_pk_mul_f32 v[192:193], v[84:85], s[4:5] op_sel_hi:[1,0]
	v_pk_mul_f32 v[190:191], v[82:83], s[4:5] op_sel_hi:[1,0]
	ds_write_b128 v149, v[190:193] offset:4096
	s_waitcnt vmcnt(14)
	v_pk_mul_f32 v[192:193], v[88:89], s[4:5] op_sel_hi:[1,0]
	v_pk_mul_f32 v[190:191], v[86:87], s[4:5] op_sel_hi:[1,0]
	ds_write_b128 v150, v[190:193] offset:5120
	s_waitcnt vmcnt(13)
	v_pk_mul_f32 v[192:193], v[92:93], s[4:5] op_sel_hi:[1,0]
	v_pk_mul_f32 v[190:191], v[90:91], s[4:5] op_sel_hi:[1,0]
	ds_write_b128 v151, v[190:193] offset:6144
	s_waitcnt vmcnt(12)
	v_pk_mul_f32 v[192:193], v[96:97], s[4:5] op_sel_hi:[1,0]
	v_pk_mul_f32 v[190:191], v[94:95], s[4:5] op_sel_hi:[1,0]
	ds_write_b128 v152, v[190:193] offset:7168
	s_waitcnt vmcnt(11)
	v_pk_mul_f32 v[192:193], v[100:101], s[4:5] op_sel_hi:[1,0]
	v_pk_mul_f32 v[190:191], v[98:99], s[4:5] op_sel_hi:[1,0]
	ds_write_b128 v1, v[190:193] offset:8192
	s_waitcnt vmcnt(10)
	v_pk_mul_f32 v[192:193], v[104:105], s[4:5] op_sel_hi:[1,0]
	v_pk_mul_f32 v[190:191], v[102:103], s[4:5] op_sel_hi:[1,0]
	ds_write_b128 v146, v[190:193] offset:9216
	s_waitcnt vmcnt(9)
	v_pk_mul_f32 v[192:193], v[108:109], s[4:5] op_sel_hi:[1,0]
	v_pk_mul_f32 v[190:191], v[106:107], s[4:5] op_sel_hi:[1,0]
	ds_write_b128 v147, v[190:193] offset:10240
	s_waitcnt vmcnt(8)
	v_pk_mul_f32 v[192:193], v[112:113], s[4:5] op_sel_hi:[1,0]
	v_pk_mul_f32 v[190:191], v[110:111], s[4:5] op_sel_hi:[1,0]
	ds_write_b128 v148, v[190:193] offset:11264
	s_waitcnt vmcnt(7)
	v_pk_mul_f32 v[192:193], v[116:117], s[4:5] op_sel_hi:[1,0]
	v_pk_mul_f32 v[190:191], v[114:115], s[4:5] op_sel_hi:[1,0]
	ds_write_b128 v149, v[190:193] offset:12288
	s_waitcnt vmcnt(6)
	v_pk_mul_f32 v[192:193], v[120:121], s[4:5] op_sel_hi:[1,0]
	v_pk_mul_f32 v[190:191], v[118:119], s[4:5] op_sel_hi:[1,0]
	ds_write_b128 v150, v[190:193] offset:13312
	s_waitcnt vmcnt(5)
	v_pk_mul_f32 v[192:193], v[124:125], s[4:5] op_sel_hi:[1,0]
	v_pk_mul_f32 v[190:191], v[122:123], s[4:5] op_sel_hi:[1,0]
	ds_write_b128 v151, v[190:193] offset:14336
	s_waitcnt vmcnt(4)
	v_pk_mul_f32 v[192:193], v[128:129], s[4:5] op_sel_hi:[1,0]
	v_pk_mul_f32 v[190:191], v[126:127], s[4:5] op_sel_hi:[1,0]
	ds_write_b128 v152, v[190:193] offset:15360
.Lcv2_1_1481:
	s_waitcnt lgkmcnt(0)
	ds_read2_b32 v[190:191], v153 offset1:32
	ds_read2_b32 v[192:193], v153 offset0:64 offset1:96
	ds_read2_b32 v[194:195], v153 offset0:128 offset1:160
	ds_read2_b32 v[196:197], v153 offset0:192 offset1:224
	ds_read_b32 v140, v154
	ds_read_b32 v143, v155
	ds_read_b32 v198, v156
	ds_read_b32 v199, v157
	ds_read_b32 v200, v158
	ds_read_b32 v201, v159
	ds_read_b32 v202, v160
	ds_read_b32 v203, v161
	s_waitcnt lgkmcnt(11)
	v_max_f32_e32 v190, v190, v190
	v_med3_f32 v204, v190, s5, v189
	v_max_f32_e32 v190, v191, v191
	v_med3_f32 v191, v190, s5, v189
	v_mov_b32_e32 v190, v141
	v_cvt_pk_fp8_f32 v190, v204, v191
	s_waitcnt lgkmcnt(10)
	v_max_f32_e32 v191, v192, v192
	v_max_f32_e32 v192, v193, v193
	v_med3_f32 v191, v191, s5, v189
	v_med3_f32 v192, v192, s5, v189
	v_cvt_pk_fp8_f32 v190, v191, v192 op_sel:[0,0,1]
	s_waitcnt lgkmcnt(9)
	v_max_f32_e32 v191, v194, v194
	v_med3_f32 v192, v191, s5, v189
	v_max_f32_e32 v191, v195, v195
	v_med3_f32 v193, v191, s5, v189
	v_mov_b32_e32 v191, v141
	v_cvt_pk_fp8_f32 v191, v192, v193
	s_waitcnt lgkmcnt(8)
	v_max_f32_e32 v192, v196, v196
	v_max_f32_e32 v193, v197, v197
	v_med3_f32 v192, v192, s5, v189
	v_med3_f32 v193, v193, s5, v189
	s_waitcnt lgkmcnt(7)
	v_max_f32_e32 v140, v140, v140
	s_waitcnt lgkmcnt(6)
	v_max_f32_e32 v143, v143, v143
	v_cvt_pk_fp8_f32 v191, v192, v193 op_sel:[0,0,1]
	v_med3_f32 v140, v140, s5, v189
	v_med3_f32 v143, v143, s5, v189
	v_mov_b32_e32 v192, v141
	v_cvt_pk_fp8_f32 v192, v140, v143
	s_waitcnt lgkmcnt(5)
	v_max_f32_e32 v140, v198, v198
	s_waitcnt lgkmcnt(4)
	v_max_f32_e32 v143, v199, v199
	v_med3_f32 v140, v140, s5, v189
	v_med3_f32 v143, v143, s5, v189
	v_cvt_pk_fp8_f32 v192, v140, v143 op_sel:[0,0,1]
	s_waitcnt lgkmcnt(3)
	v_max_f32_e32 v140, v200, v200
	s_waitcnt lgkmcnt(2)
	v_max_f32_e32 v143, v201, v201
	v_med3_f32 v140, v140, s5, v189
	v_med3_f32 v143, v143, s5, v189
	v_mov_b32_e32 v193, v141
	v_cvt_pk_fp8_f32 v193, v140, v143
	s_waitcnt lgkmcnt(1)
	v_max_f32_e32 v140, v202, v202
	s_waitcnt lgkmcnt(0)
	v_max_f32_e32 v143, v203, v203
	v_med3_f32 v140, v140, s5, v189
	v_med3_f32 v143, v143, s5, v189
	v_cvt_pk_fp8_f32 v193, v140, v143 op_sel:[0,0,1]
	ds_read2_b32 v[194:195], v162 offset1:32
	ds_read2_b32 v[196:197], v162 offset0:64 offset1:96
	ds_read2_b32 v[198:199], v162 offset0:128 offset1:160
	ds_read2_b32 v[200:201], v162 offset0:192 offset1:224
	ds_read_b32 v140, v163
	ds_read_b32 v143, v164
	ds_read_b32 v202, v165
	ds_read_b32 v203, v166
	ds_read_b32 v204, v167
	ds_read_b32 v205, v168
	ds_read_b32 v206, v169
	ds_read_b32 v207, v170
	s_waitcnt lgkmcnt(11)
; #define GAS __attribute__((address_space(1)))
; #define LDS_WAIT() asm volatile("s_waitcnt lgkmcnt(0)" ::: "memory")
; __device__ __forceinline__ void p8_finish(const TItem8& t, const f32x4 (&v)[16], LAS float* scr, int lane) {
;     ...
;     const int c = lane & 7;
; #pragma unroll
;     for (int j = 0; j < 4; ++j) { const int n = (lane >> 3) + 8 * j; float x[16];
; #pragma unroll
;         for (int i = 0; i < 16; ++i) { const int k = 16 * c + i; x[i] = scr[k * 32 + ((((n >> 2) ^ ((k >> 3) & 7)) << 2) | (n & 3))]; }
;         int w[4];
; #pragma unroll
;         for (int g = 0; g < 4; ++g) { int q = 0; q = __builtin_amdgcn_cvt_pk_fp8_f32(fminf(fmaxf(x[4 * g], -448.f), 448.f), fminf(fmaxf(x[4 * g + 1], -448.f), 448.f), q, false);
;             q = __builtin_amdgcn_cvt_pk_fp8_f32(fminf(fmaxf(x[4 * g + 2], -448.f), 448.f), fminf(fmaxf(x[4 * g + 3], -448.f), 448.f), q, true); w[g] = q; }
;         v4u o; o.x = (unsigned)w[0]; o.y = (unsigned)w[1]; o.z = (unsigned)w[2]; o.w = (unsigned)w[3];
;         __builtin_nontemporal_store(o, (GAS v4u*)(t.dst + (size_t)n * t.Kd + 16 * c)); }
;     LDS_WAIT(); asm volatile("" ::: "memory");
	v_max_f32_e32 v194, v194, v194
	v_med3_f32 v208, v194, s5, v189
	v_max_f32_e32 v194, v195, v195
	v_med3_f32 v195, v194, s5, v189
	v_mov_b32_e32 v194, v141
	v_cvt_pk_fp8_f32 v194, v208, v195
	s_waitcnt lgkmcnt(10)
	v_max_f32_e32 v195, v196, v196
	v_max_f32_e32 v196, v197, v197
	v_med3_f32 v195, v195, s5, v189
	v_med3_f32 v196, v196, s5, v189
	v_cvt_pk_fp8_f32 v194, v195, v196 op_sel:[0,0,1]
	s_waitcnt lgkmcnt(9)
	v_max_f32_e32 v195, v198, v198
	v_med3_f32 v196, v195, s5, v189
	v_max_f32_e32 v195, v199, v199
	v_med3_f32 v197, v195, s5, v189
	v_mov_b32_e32 v195, v141
	v_cvt_pk_fp8_f32 v195, v196, v197
	s_waitcnt lgkmcnt(8)
	v_max_f32_e32 v196, v200, v200
	v_max_f32_e32 v197, v201, v201
	v_med3_f32 v196, v196, s5, v189
	v_med3_f32 v197, v197, s5, v189
	s_waitcnt lgkmcnt(7)
	v_max_f32_e32 v140, v140, v140
	s_waitcnt lgkmcnt(6)
	v_max_f32_e32 v143, v143, v143
	v_cvt_pk_fp8_f32 v195, v196, v197 op_sel:[0,0,1]
	v_med3_f32 v140, v140, s5, v189
	v_med3_f32 v143, v143, s5, v189
	v_mov_b32_e32 v196, v141
	v_cvt_pk_fp8_f32 v196, v140, v143
	s_waitcnt lgkmcnt(5)
	v_max_f32_e32 v140, v202, v202
	s_waitcnt lgkmcnt(4)
	v_max_f32_e32 v143, v203, v203
	v_med3_f32 v140, v140, s5, v189
	v_med3_f32 v143, v143, s5, v189
	v_cvt_pk_fp8_f32 v196, v140, v143 op_sel:[0,0,1]
	s_waitcnt lgkmcnt(3)
	v_max_f32_e32 v140, v204, v204
	s_waitcnt lgkmcnt(2)
	v_max_f32_e32 v143, v205, v205
	v_med3_f32 v140, v140, s5, v189
	v_med3_f32 v143, v143, s5, v189
	v_mov_b32_e32 v197, v141
	v_cvt_pk_fp8_f32 v197, v140, v143
	s_waitcnt lgkmcnt(1)
	v_max_f32_e32 v140, v206, v206
	s_waitcnt lgkmcnt(0)
	v_max_f32_e32 v143, v207, v207
	v_med3_f32 v140, v140, s5, v189
	v_med3_f32 v143, v143, s5, v189
	v_cvt_pk_fp8_f32 v197, v140, v143 op_sel:[0,0,1]
	v_lshl_add_u64 v[144:145], s[8:9], 0, v[130:131]
	v_lshl_add_u64 v[198:199], v[144:145], 0, v[132:133]
	global_store_dwordx4 v[198:199], v[190:193], off nt
	s_nop 1
	v_lshl_add_u64 v[190:191], v[144:145], 0, v[134:135]
	global_store_dwordx4 v[190:191], v[194:197], off nt
	ds_read2_b32 v[190:191], v171 offset1:32
	ds_read2_b32 v[192:193], v171 offset0:64 offset1:96
	ds_read2_b32 v[194:195], v171 offset0:128 offset1:160
	ds_read2_b32 v[196:197], v171 offset0:192 offset1:224
	ds_read_b32 v140, v172
	ds_read_b32 v143, v173
	ds_read_b32 v198, v174
	ds_read_b32 v199, v175
	ds_read_b32 v200, v176
	ds_read_b32 v201, v177
	ds_read_b32 v202, v178
	ds_read_b32 v203, v179
	s_waitcnt lgkmcnt(11)
	v_max_f32_e32 v190, v190, v190
	v_med3_f32 v204, v190, s5, v189
	v_max_f32_e32 v190, v191, v191
	v_med3_f32 v191, v190, s5, v189
	v_mov_b32_e32 v190, v141
	v_cvt_pk_fp8_f32 v190, v204, v191
	s_waitcnt lgkmcnt(10)
	v_max_f32_e32 v191, v192, v192
	v_max_f32_e32 v192, v193, v193
	v_med3_f32 v191, v191, s5, v189
	v_med3_f32 v192, v192, s5, v189
	v_cvt_pk_fp8_f32 v190, v191, v192 op_sel:[0,0,1]
	s_waitcnt lgkmcnt(9)
	v_max_f32_e32 v191, v194, v194
	v_med3_f32 v192, v191, s5, v189
	v_max_f32_e32 v191, v195, v195
	v_med3_f32 v193, v191, s5, v189
	v_mov_b32_e32 v191, v141
	v_cvt_pk_fp8_f32 v191, v192, v193
	s_waitcnt lgkmcnt(8)
	v_max_f32_e32 v192, v196, v196
	v_max_f32_e32 v193, v197, v197
	v_med3_f32 v192, v192, s5, v189
	v_med3_f32 v193, v193, s5, v189
	s_waitcnt lgkmcnt(7)
	v_max_f32_e32 v140, v140, v140
	s_waitcnt lgkmcnt(6)
	v_max_f32_e32 v143, v143, v143
	v_cvt_pk_fp8_f32 v191, v192, v193 op_sel:[0,0,1]
	v_med3_f32 v140, v140, s5, v189
	v_med3_f32 v143, v143, s5, v189
	v_mov_b32_e32 v192, v141
	v_cvt_pk_fp8_f32 v192, v140, v143
	s_waitcnt lgkmcnt(5)
	v_max_f32_e32 v140, v198, v198
	s_waitcnt lgkmcnt(4)
	v_max_f32_e32 v143, v199, v199
	v_med3_f32 v140, v140, s5, v189
	v_med3_f32 v143, v143, s5, v189
	v_cvt_pk_fp8_f32 v192, v140, v143 op_sel:[0,0,1]
	s_waitcnt lgkmcnt(3)
	v_max_f32_e32 v140, v200, v200
	s_waitcnt lgkmcnt(2)
	v_max_f32_e32 v143, v201, v201
	v_med3_f32 v140, v140, s5, v189
	v_med3_f32 v143, v143, s5, v189
	v_mov_b32_e32 v193, v141
	v_cvt_pk_fp8_f32 v193, v140, v143
	s_waitcnt lgkmcnt(1)
	v_max_f32_e32 v140, v202, v202
	s_waitcnt lgkmcnt(0)
	v_max_f32_e32 v143, v203, v203
	v_med3_f32 v140, v140, s5, v189
	v_med3_f32 v143, v143, s5, v189
	v_cvt_pk_fp8_f32 v193, v140, v143 op_sel:[0,0,1]
	ds_read2_b32 v[194:195], v180 offset1:32
	ds_read2_b32 v[196:197], v180 offset0:64 offset1:96
	ds_read2_b32 v[198:199], v180 offset0:128 offset1:160
	ds_read2_b32 v[200:201], v180 offset0:192 offset1:224
	ds_read_b32 v140, v181
	ds_read_b32 v143, v182
	ds_read_b32 v202, v183
	ds_read_b32 v203, v184
	ds_read_b32 v204, v185
	ds_read_b32 v205, v186
	ds_read_b32 v206, v187
	ds_read_b32 v207, v188
	s_waitcnt lgkmcnt(11)
	v_max_f32_e32 v194, v194, v194
	v_med3_f32 v208, v194, s5, v189
	v_max_f32_e32 v194, v195, v195
	v_med3_f32 v195, v194, s5, v189
	v_mov_b32_e32 v194, v141
	v_cvt_pk_fp8_f32 v194, v208, v195
	s_waitcnt lgkmcnt(10)
	v_max_f32_e32 v195, v196, v196
	v_max_f32_e32 v196, v197, v197
	v_med3_f32 v195, v195, s5, v189
	v_med3_f32 v196, v196, s5, v189
	v_cvt_pk_fp8_f32 v194, v195, v196 op_sel:[0,0,1]
	s_waitcnt lgkmcnt(9)
	v_max_f32_e32 v195, v198, v198
	v_med3_f32 v196, v195, s5, v189
	v_max_f32_e32 v195, v199, v199
	v_med3_f32 v197, v195, s5, v189
	v_mov_b32_e32 v195, v141
	v_cvt_pk_fp8_f32 v195, v196, v197
	s_waitcnt lgkmcnt(8)
	v_max_f32_e32 v196, v200, v200
	v_max_f32_e32 v197, v201, v201
	v_med3_f32 v196, v196, s5, v189
	v_med3_f32 v197, v197, s5, v189
	s_waitcnt lgkmcnt(7)
	v_max_f32_e32 v140, v140, v140
	s_waitcnt lgkmcnt(6)
	v_max_f32_e32 v143, v143, v143
	v_cvt_pk_fp8_f32 v195, v196, v197 op_sel:[0,0,1]
	v_med3_f32 v140, v140, s5, v189
	v_med3_f32 v143, v143, s5, v189
	v_mov_b32_e32 v196, v141
	v_cvt_pk_fp8_f32 v196, v140, v143
	s_waitcnt lgkmcnt(5)
	v_max_f32_e32 v140, v202, v202
	s_waitcnt lgkmcnt(4)
	v_max_f32_e32 v143, v203, v203
	v_med3_f32 v140, v140, s5, v189
	v_med3_f32 v143, v143, s5, v189
	v_cvt_pk_fp8_f32 v196, v140, v143 op_sel:[0,0,1]
	s_waitcnt lgkmcnt(3)
	v_max_f32_e32 v140, v204, v204
	s_waitcnt lgkmcnt(2)
	v_max_f32_e32 v143, v205, v205
	v_med3_f32 v140, v140, s5, v189
	v_med3_f32 v143, v143, s5, v189
	v_mov_b32_e32 v197, v141
	v_cvt_pk_fp8_f32 v197, v140, v143
	s_waitcnt lgkmcnt(1)
	v_max_f32_e32 v140, v206, v206
	s_waitcnt lgkmcnt(0)
	v_max_f32_e32 v143, v207, v207
	v_med3_f32 v140, v140, s5, v189
	v_med3_f32 v143, v143, s5, v189
	v_cvt_pk_fp8_f32 v197, v140, v143 op_sel:[0,0,1]
	v_lshl_add_u64 v[198:199], v[144:145], 0, v[136:137]
	v_lshl_add_u64 v[144:145], v[144:145], 0, v[138:139]
	global_store_dwordx4 v[198:199], v[190:193], off nt
	global_store_dwordx4 v[144:145], v[194:197], off nt
	s_waitcnt lgkmcnt(0)
	s_xor_b64 s[10:11], s[10:11], -1
	s_andn2_b64 vcc, exec, s[10:11]
	s_cbranch_vccnz .LBB0_1465
